# baseline (speedup 1.0000x reference)
_Z7k_stageILi0ELi8EEv8AttnArgsPKDF16_PKfPDF16_iii:
	s_load_dwordx2 s[86:87], s[0:1], 0x70
	s_load_dwordx2 s[82:83], s[0:1], 0x88
	s_mov_b32 s81, s3
	s_load_dwordx16 s[64:79], s[0:1], 0x0
	v_readfirstlane_b32 s94, v0
	s_nop 0
	s_lshr_b32 s94, s94, 6
	s_load_dwordx4 s[8:11], s[0:1], 0x88
	s_lshl_b32 s4, s2, 4
	s_and_b32 s4, s4, 0x70
	s_lshr_b32 s5, s2, 3
	s_add_i32 s4, s4, s5
	s_lshr_b32 s7, s4, 5
	s_lshl_b32 s6, s4, 1
	s_waitcnt lgkmcnt(0)
	s_lshl_b32 s11, s2, 1
	s_cmp_gt_i32 s10, 0
	v_readfirstlane_b32 s24, v0
	s_cbranch_scc1 .LBB3_2
	s_lshl_b32 s31, s7, 12
	s_ashr_i32 s2, s3, 31
	s_mov_b64 s[4:5], 0
	s_branch .LBB3_3

.LBB3_5:
	s_waitcnt lgkmcnt(0)
	v_cvt_f16_f32_e32 v180, s7
	v_cvt_f16_f32_e32 v182, s6
	v_cvt_f16_f32_e32 v181, s28
	s_waitcnt vmcnt(3)
	v_pk_mul_f16 v183, v182, v184 op_sel_hi:[0,1]
	v_pk_mul_f16 v190, v182, v187 op_sel_hi:[0,1]
	v_pk_mul_f16 v194, v180, v187 op_sel_hi:[0,1]
	v_pk_mul_f16 v198, v181, v187 op_sel_hi:[0,1]
	v_pk_mul_f16 v188, v182, v185 op_sel_hi:[0,1]
	v_pk_mul_f16 v189, v182, v186 op_sel_hi:[0,1]
	v_pk_mul_f16 v191, v180, v184 op_sel_hi:[0,1]
	s_mov_b64 exec, s[64:65]
	buffer_load_dwordx4 v[18:21], v249, s[16:19], 0 offen
	buffer_load_dwordx4 v[6:9], v249, s[16:19], 0 offen offset:512
	s_mov_b64 exec, -1
	v_pk_mul_f16 v192, v180, v185 op_sel_hi:[0,1]
	v_pk_mul_f16 v193, v180, v186 op_sel_hi:[0,1]
	v_pk_mul_f16 v195, v181, v184 op_sel_hi:[0,1]
	v_pk_mul_f16 v196, v181, v185 op_sel_hi:[0,1]
	v_pk_mul_f16 v197, v181, v186 op_sel_hi:[0,1]
	v_pk_fma_f16 v113, v113, v187, v190
	v_pk_fma_f16 v110, v110, v184, v183
	v_pk_fma_f16 v129, v129, v187, v190
	v_pk_fma_f16 v126, v126, v184, v183
	v_pk_fma_f16 v141, v141, v187, v190
	v_pk_fma_f16 v138, v138, v184, v183
	v_pk_fma_f16 v183, v89, v187, v194
	v_pk_fma_f16 v199, v109, v187, v194
	buffer_load_dwordx4 v[30:33], v250, s[16:19], 0 offen offset:512
	buffer_load_dwordx4 v[10:13], v250, s[16:19], 0 offen offset:1024
	v_pk_fma_f16 v194, v125, v187, v194
	v_pk_fma_f16 v203, v53, v187, v198
	v_pk_fma_f16 v207, v69, v187, v198
	v_pk_fma_f16 v187, v97, v187, v198
	v_pk_maximum3_f16 v198, v113, v129, v141
	v_pk_fma_f16 v112, v112, v186, v189
	v_pk_fma_f16 v111, v111, v185, v188
	v_pk_fma_f16 v128, v128, v186, v189
	v_pk_fma_f16 v127, v127, v185, v188
	v_pk_fma_f16 v140, v140, v186, v189
	v_pk_fma_f16 v139, v139, v185, v188
	v_pk_fma_f16 v188, v88, v186, v193
	v_pk_fma_f16 v189, v87, v185, v192
	v_pk_fma_f16 v190, v86, v184, v191
	v_pk_fma_f16 v200, v108, v186, v193
	v_pk_fma_f16 v201, v107, v185, v192
	s_mov_b64 exec, s[66:67]
	buffer_load_dwordx4 v[54:57], v250, s[16:19], 0 offen offset:2048
	buffer_load_dwordx4 v[14:17], v250, s[16:19], 0 offen offset:2560
	s_mov_b64 exec, -1
	v_pk_fma_f16 v202, v106, v184, v191
	v_pk_fma_f16 v193, v124, v186, v193
	v_pk_fma_f16 v192, v123, v185, v192
	v_pk_fma_f16 v191, v122, v184, v191
	v_pk_fma_f16 v204, v52, v186, v197
	v_pk_fma_f16 v205, v51, v185, v196
	v_pk_fma_f16 v206, v50, v184, v195
	v_pk_fma_f16 v208, v68, v186, v197
	v_pk_fma_f16 v209, v67, v185, v196
	v_pk_fma_f16 v210, v66, v184, v195
	v_pk_fma_f16 v186, v96, v186, v197
	v_pk_fma_f16 v185, v95, v185, v196
	v_pk_fma_f16 v184, v94, v184, v195
	v_pk_maximum3_f16 v195, v110, v126, v138
	v_pk_maximum3_f16 v196, v111, v127, v139
	v_pk_maximum3_f16 v197, v112, v128, v140
	v_pk_maximum3_f16 v214, v183, v199, v194
	v_pk_maximum3_f16 v218, v203, v207, v187
	v_pk_maximum3_f16 v211, v190, v202, v191
	v_pk_maximum3_f16 v212, v189, v201, v192
	v_pk_maximum3_f16 v213, v188, v200, v193
	v_pk_maximum3_f16 v215, v206, v210, v184
	v_pk_maximum3_f16 v216, v205, v209, v185
	v_pk_maximum3_f16 v198, v198, v214, v218
	v_pk_maximum3_f16 v217, v204, v208, v186
	v_pk_maximum3_f16 v195, v195, v211, v215
	v_pk_maximum3_f16 v196, v196, v212, v216
	v_pk_maximum3_f16 v197, v197, v213, v217
	v_pk_add_f16 v113, v113, v198 neg_lo:[0,1] neg_hi:[0,1]
	s_mov_b64 exec, s[64:65]
	buffer_load_dwordx4 v[74:77], v251, s[16:19], 0 offen
	buffer_load_dwordx4 v[26:29], v251, s[16:19], 0 offen offset:512
	s_mov_b64 exec, -1
	v_pk_add_f16 v110, v110, v195 neg_lo:[0,1] neg_hi:[0,1]
	v_pk_add_f16 v111, v111, v196 neg_lo:[0,1] neg_hi:[0,1]
	v_pk_add_f16 v112, v112, v197 neg_lo:[0,1] neg_hi:[0,1]
	v_pk_add_f16 v126, v126, v195 neg_lo:[0,1] neg_hi:[0,1]
	v_exp_f16_sdwa v211, v110 dst_sel:WORD_0 dst_unused:UNUSED_PAD src0_sel:WORD_0
	v_exp_f16_sdwa v212, v111 dst_sel:WORD_0 dst_unused:UNUSED_PAD src0_sel:WORD_0
	v_exp_f16_sdwa v213, v112 dst_sel:WORD_0 dst_unused:UNUSED_PAD src0_sel:WORD_0
	v_exp_f16_sdwa v214, v113 dst_sel:WORD_0 dst_unused:UNUSED_PAD src0_sel:WORD_0
	v_exp_f16_sdwa v211, v110 dst_sel:WORD_1 dst_unused:UNUSED_PRESERVE src0_sel:WORD_1
	v_exp_f16_sdwa v212, v111 dst_sel:WORD_1 dst_unused:UNUSED_PRESERVE src0_sel:WORD_1
	v_exp_f16_sdwa v213, v112 dst_sel:WORD_1 dst_unused:UNUSED_PRESERVE src0_sel:WORD_1
	v_exp_f16_sdwa v214, v113 dst_sel:WORD_1 dst_unused:UNUSED_PRESERVE src0_sel:WORD_1
	v_pk_add_f16 v127, v127, v196 neg_lo:[0,1] neg_hi:[0,1]
	v_pk_add_f16 v113, v211, 0
	v_pk_fma_f16 v81, v81, v214, 0
	v_pk_add_f16 v110, v214, 0
	v_pk_add_f16 v111, v213, 0
	v_pk_add_f16 v112, v212, 0
	v_pk_fma_f16 v80, v80, v213, 0
	v_pk_fma_f16 v79, v79, v212, 0
	v_pk_fma_f16 v78, v78, v211, 0
	v_pk_add_f16 v128, v128, v197 neg_lo:[0,1] neg_hi:[0,1]
	buffer_load_dwordx4 v[98:101], v252, s[16:19], 0 offen offset:512
	buffer_load_dwordx4 v[38:41], v252, s[16:19], 0 offen offset:1024
	v_pk_add_f16 v129, v129, v198 neg_lo:[0,1] neg_hi:[0,1]
	v_exp_f16_sdwa v211, v126 dst_sel:WORD_0 dst_unused:UNUSED_PAD src0_sel:WORD_0
	v_exp_f16_sdwa v212, v127 dst_sel:WORD_0 dst_unused:UNUSED_PAD src0_sel:WORD_0
	v_exp_f16_sdwa v213, v128 dst_sel:WORD_0 dst_unused:UNUSED_PAD src0_sel:WORD_0
	v_exp_f16_sdwa v214, v129 dst_sel:WORD_0 dst_unused:UNUSED_PAD src0_sel:WORD_0
	v_exp_f16_sdwa v211, v126 dst_sel:WORD_1 dst_unused:UNUSED_PRESERVE src0_sel:WORD_1
	v_exp_f16_sdwa v212, v127 dst_sel:WORD_1 dst_unused:UNUSED_PRESERVE src0_sel:WORD_1
	v_exp_f16_sdwa v213, v128 dst_sel:WORD_1 dst_unused:UNUSED_PRESERVE src0_sel:WORD_1
	v_exp_f16_sdwa v214, v129 dst_sel:WORD_1 dst_unused:UNUSED_PRESERVE src0_sel:WORD_1
	v_pk_add_f16 v113, v113, v211
	v_pk_fma_f16 v81, v105, v214, v81
	v_pk_add_f16 v105, v141, v198 neg_lo:[0,1] neg_hi:[0,1]
	v_pk_add_f16 v112, v112, v212
	v_pk_add_f16 v111, v111, v213
	v_pk_add_f16 v110, v110, v214
	v_pk_fma_f16 v78, v102, v211, v78
	v_pk_fma_f16 v79, v103, v212, v79
	v_pk_fma_f16 v80, v104, v213, v80
	v_pk_add_f16 v102, v138, v195 neg_lo:[0,1] neg_hi:[0,1]
	v_pk_add_f16 v103, v139, v196 neg_lo:[0,1] neg_hi:[0,1]
	v_pk_add_f16 v104, v140, v197 neg_lo:[0,1] neg_hi:[0,1]
	v_exp_f16_sdwa v126, v102 dst_sel:WORD_0 dst_unused:UNUSED_PAD src0_sel:WORD_0
	v_exp_f16_sdwa v127, v103 dst_sel:WORD_0 dst_unused:UNUSED_PAD src0_sel:WORD_0
	v_exp_f16_sdwa v128, v104 dst_sel:WORD_0 dst_unused:UNUSED_PAD src0_sel:WORD_0
	v_exp_f16_sdwa v129, v105 dst_sel:WORD_0 dst_unused:UNUSED_PAD src0_sel:WORD_0
	v_exp_f16_sdwa v126, v102 dst_sel:WORD_1 dst_unused:UNUSED_PRESERVE src0_sel:WORD_1
	v_exp_f16_sdwa v127, v103 dst_sel:WORD_1 dst_unused:UNUSED_PRESERVE src0_sel:WORD_1
	v_exp_f16_sdwa v128, v104 dst_sel:WORD_1 dst_unused:UNUSED_PRESERVE src0_sel:WORD_1
	v_exp_f16_sdwa v129, v105 dst_sel:WORD_1 dst_unused:UNUSED_PRESERVE src0_sel:WORD_1
	v_pk_add_f16 v105, v113, v126
	v_pk_add_f16 v102, v110, v129
	s_mov_b64 exec, s[66:67]
	buffer_load_dwordx4 v[114:117], v252, s[16:19], 0 offen offset:2048
	buffer_load_dwordx4 v[58:61], v252, s[16:19], 0 offen offset:2560
	s_mov_b64 exec, -1
	v_pk_add_f16 v103, v111, v128
	v_pk_add_f16 v104, v112, v127
	v_pk_fma_f16 v81, v121, v129, v81
	v_pk_fma_f16 v80, v120, v128, v80
	v_pk_fma_f16 v79, v119, v127, v79
	v_pk_fma_f16 v78, v118, v126, v78
	v_pk_add_f16 v110, v190, v195 neg_lo:[0,1] neg_hi:[0,1]
	v_pk_add_f16 v111, v189, v196 neg_lo:[0,1] neg_hi:[0,1]
	v_pk_add_f16 v112, v188, v197 neg_lo:[0,1] neg_hi:[0,1]
	v_pk_add_f16 v113, v183, v198 neg_lo:[0,1] neg_hi:[0,1]
	v_exp_f16_sdwa v118, v110 dst_sel:WORD_0 dst_unused:UNUSED_PAD src0_sel:WORD_0
	v_exp_f16_sdwa v119, v111 dst_sel:WORD_0 dst_unused:UNUSED_PAD src0_sel:WORD_0
	v_exp_f16_sdwa v120, v112 dst_sel:WORD_0 dst_unused:UNUSED_PAD src0_sel:WORD_0
	v_exp_f16_sdwa v121, v113 dst_sel:WORD_0 dst_unused:UNUSED_PAD src0_sel:WORD_0
	v_exp_f16_sdwa v118, v110 dst_sel:WORD_1 dst_unused:UNUSED_PRESERVE src0_sel:WORD_1
	v_exp_f16_sdwa v119, v111 dst_sel:WORD_1 dst_unused:UNUSED_PRESERVE src0_sel:WORD_1
	v_exp_f16_sdwa v120, v112 dst_sel:WORD_1 dst_unused:UNUSED_PRESERVE src0_sel:WORD_1
	v_exp_f16_sdwa v121, v113 dst_sel:WORD_1 dst_unused:UNUSED_PRESERVE src0_sel:WORD_1
	v_pk_add_f16 v110, v202, v195 neg_lo:[0,1] neg_hi:[0,1]
	v_pk_add_f16 v105, v105, v118
	v_pk_add_f16 v104, v104, v119
	v_pk_add_f16 v103, v103, v120
	s_mov_b64 exec, s[76:77]
	buffer_load_dwordx4 v[130:133], v253, s[16:19], 0 offen
	buffer_load_dwordx4 v[70:73], v253, s[16:19], 0 offen offset:512
	s_mov_b64 exec, -1
	v_pk_add_f16 v102, v102, v121
	v_pk_fma_f16 v78, v46, v118, v78
	v_pk_fma_f16 v79, v47, v119, v79
	v_pk_fma_f16 v80, v48, v120, v80
	v_pk_fma_f16 v81, v49, v121, v81
	v_pk_add_f16 v111, v201, v196 neg_lo:[0,1] neg_hi:[0,1]
	v_pk_add_f16 v112, v200, v197 neg_lo:[0,1] neg_hi:[0,1]
	v_pk_add_f16 v113, v199, v198 neg_lo:[0,1] neg_hi:[0,1]
	v_exp_f16_sdwa v118, v110 dst_sel:WORD_0 dst_unused:UNUSED_PAD src0_sel:WORD_0
	v_exp_f16_sdwa v119, v111 dst_sel:WORD_0 dst_unused:UNUSED_PAD src0_sel:WORD_0
	v_exp_f16_sdwa v120, v112 dst_sel:WORD_0 dst_unused:UNUSED_PAD src0_sel:WORD_0
	v_exp_f16_sdwa v121, v113 dst_sel:WORD_0 dst_unused:UNUSED_PAD src0_sel:WORD_0
	v_exp_f16_sdwa v118, v110 dst_sel:WORD_1 dst_unused:UNUSED_PRESERVE src0_sel:WORD_1
	v_exp_f16_sdwa v119, v111 dst_sel:WORD_1 dst_unused:UNUSED_PRESERVE src0_sel:WORD_1
	v_exp_f16_sdwa v120, v112 dst_sel:WORD_1 dst_unused:UNUSED_PRESERVE src0_sel:WORD_1
	v_exp_f16_sdwa v121, v113 dst_sel:WORD_1 dst_unused:UNUSED_PRESERVE src0_sel:WORD_1
	v_pk_add_f16 v110, v191, v195 neg_lo:[0,1] neg_hi:[0,1]
	v_pk_add_f16 v105, v105, v118
	v_pk_add_f16 v102, v102, v121
	v_pk_add_f16 v103, v103, v120
	v_pk_add_f16 v104, v104, v119
	v_pk_fma_f16 v81, v65, v121, v81
	v_pk_fma_f16 v80, v64, v120, v80
	s_mov_b64 exec, s[70:71]
	buffer_load_dwordx4 v[134:137], v254, s[16:19], 0 offen offset:512
	buffer_load_dwordx4 v[90:93], v254, s[16:19], 0 offen offset:1024
	s_mov_b64 exec, -1
	v_pk_fma_f16 v79, v63, v119, v79
	v_pk_fma_f16 v78, v62, v118, v78
	v_pk_add_f16 v111, v192, v196 neg_lo:[0,1] neg_hi:[0,1]
	v_pk_add_f16 v112, v193, v197 neg_lo:[0,1] neg_hi:[0,1]
	v_pk_add_f16 v113, v194, v198 neg_lo:[0,1] neg_hi:[0,1]
	v_exp_f16_sdwa v118, v110 dst_sel:WORD_0 dst_unused:UNUSED_PAD src0_sel:WORD_0
	v_exp_f16_sdwa v119, v111 dst_sel:WORD_0 dst_unused:UNUSED_PAD src0_sel:WORD_0
	v_exp_f16_sdwa v120, v112 dst_sel:WORD_0 dst_unused:UNUSED_PAD src0_sel:WORD_0
	v_exp_f16_sdwa v121, v113 dst_sel:WORD_0 dst_unused:UNUSED_PAD src0_sel:WORD_0
	v_exp_f16_sdwa v118, v110 dst_sel:WORD_1 dst_unused:UNUSED_PRESERVE src0_sel:WORD_1
	v_exp_f16_sdwa v119, v111 dst_sel:WORD_1 dst_unused:UNUSED_PRESERVE src0_sel:WORD_1
	v_exp_f16_sdwa v120, v112 dst_sel:WORD_1 dst_unused:UNUSED_PRESERVE src0_sel:WORD_1
	v_exp_f16_sdwa v121, v113 dst_sel:WORD_1 dst_unused:UNUSED_PRESERVE src0_sel:WORD_1
	v_pk_add_f16 v110, v206, v195 neg_lo:[0,1] neg_hi:[0,1]
	v_pk_add_f16 v105, v105, v118
	v_pk_add_f16 v104, v104, v119
	v_pk_add_f16 v103, v103, v120
	v_pk_add_f16 v102, v102, v121
	v_pk_fma_f16 v78, v82, v118, v78
	v_pk_fma_f16 v79, v83, v119, v79
	v_pk_fma_f16 v80, v84, v120, v80
	v_pk_fma_f16 v81, v85, v121, v81
	s_mov_b64 exec, s[78:79]
	buffer_load_dwordx4 v[142:145], v254, s[16:19], 0 offen offset:2048
	buffer_load_dwordx4 v[2:5], v254, s[16:19], 0 offen offset:2560
	s_mov_b64 exec, -1
	v_pk_add_f16 v111, v205, v196 neg_lo:[0,1] neg_hi:[0,1]
	v_pk_add_f16 v112, v204, v197 neg_lo:[0,1] neg_hi:[0,1]
	v_pk_add_f16 v113, v203, v198 neg_lo:[0,1] neg_hi:[0,1]
	v_exp_f16_sdwa v118, v110 dst_sel:WORD_0 dst_unused:UNUSED_PAD src0_sel:WORD_0
	v_exp_f16_sdwa v119, v111 dst_sel:WORD_0 dst_unused:UNUSED_PAD src0_sel:WORD_0
	v_exp_f16_sdwa v120, v112 dst_sel:WORD_0 dst_unused:UNUSED_PAD src0_sel:WORD_0
	v_exp_f16_sdwa v121, v113 dst_sel:WORD_0 dst_unused:UNUSED_PAD src0_sel:WORD_0
	v_exp_f16_sdwa v118, v110 dst_sel:WORD_1 dst_unused:UNUSED_PRESERVE src0_sel:WORD_1
	v_exp_f16_sdwa v119, v111 dst_sel:WORD_1 dst_unused:UNUSED_PRESERVE src0_sel:WORD_1
	v_exp_f16_sdwa v120, v112 dst_sel:WORD_1 dst_unused:UNUSED_PRESERVE src0_sel:WORD_1
	v_exp_f16_sdwa v121, v113 dst_sel:WORD_1 dst_unused:UNUSED_PRESERVE src0_sel:WORD_1
	v_pk_add_f16 v110, v210, v195 neg_lo:[0,1] neg_hi:[0,1]
	v_pk_add_f16 v105, v105, v118
	v_pk_add_f16 v102, v102, v121
	v_pk_add_f16 v103, v103, v120
	v_pk_add_f16 v104, v104, v119
	v_pk_fma_f16 v81, v25, v121, v81
	v_pk_fma_f16 v80, v24, v120, v80
	v_pk_fma_f16 v79, v23, v119, v79
	v_pk_fma_f16 v78, v22, v118, v78
	v_pk_add_f16 v111, v209, v196 neg_lo:[0,1] neg_hi:[0,1]
	v_pk_add_f16 v112, v208, v197 neg_lo:[0,1] neg_hi:[0,1]
	v_pk_add_f16 v113, v207, v198 neg_lo:[0,1] neg_hi:[0,1]
	v_exp_f16_sdwa v118, v110 dst_sel:WORD_0 dst_unused:UNUSED_PAD src0_sel:WORD_0
	v_exp_f16_sdwa v119, v111 dst_sel:WORD_0 dst_unused:UNUSED_PAD src0_sel:WORD_0
	v_exp_f16_sdwa v120, v112 dst_sel:WORD_0 dst_unused:UNUSED_PAD src0_sel:WORD_0
	v_exp_f16_sdwa v121, v113 dst_sel:WORD_0 dst_unused:UNUSED_PAD src0_sel:WORD_0
	v_exp_f16_sdwa v118, v110 dst_sel:WORD_1 dst_unused:UNUSED_PRESERVE src0_sel:WORD_1
	v_exp_f16_sdwa v119, v111 dst_sel:WORD_1 dst_unused:UNUSED_PRESERVE src0_sel:WORD_1
	v_exp_f16_sdwa v120, v112 dst_sel:WORD_1 dst_unused:UNUSED_PRESERVE src0_sel:WORD_1
	v_exp_f16_sdwa v121, v113 dst_sel:WORD_1 dst_unused:UNUSED_PRESERVE src0_sel:WORD_1
	v_pk_add_f16 v110, v184, v195 neg_lo:[0,1] neg_hi:[0,1]
	v_pk_add_f16 v105, v105, v118
	v_pk_add_f16 v104, v104, v119
	v_pk_add_f16 v103, v103, v120
	v_pk_add_f16 v102, v102, v121
	v_pk_fma_f16 v78, v34, v118, v78
	v_pk_fma_f16 v79, v35, v119, v79
	v_pk_fma_f16 v80, v36, v120, v80
	v_pk_fma_f16 v81, v37, v121, v81
	v_pk_add_f16 v111, v185, v196 neg_lo:[0,1] neg_hi:[0,1]
	v_pk_add_f16 v112, v186, v197 neg_lo:[0,1] neg_hi:[0,1]
	v_pk_add_f16 v113, v187, v198 neg_lo:[0,1] neg_hi:[0,1]
	v_exp_f16_sdwa v118, v110 dst_sel:WORD_0 dst_unused:UNUSED_PAD src0_sel:WORD_0
	v_exp_f16_sdwa v119, v111 dst_sel:WORD_0 dst_unused:UNUSED_PAD src0_sel:WORD_0
	v_exp_f16_sdwa v120, v112 dst_sel:WORD_0 dst_unused:UNUSED_PAD src0_sel:WORD_0
	v_exp_f16_sdwa v121, v113 dst_sel:WORD_0 dst_unused:UNUSED_PAD src0_sel:WORD_0
	v_exp_f16_sdwa v118, v110 dst_sel:WORD_1 dst_unused:UNUSED_PRESERVE src0_sel:WORD_1
	v_exp_f16_sdwa v119, v111 dst_sel:WORD_1 dst_unused:UNUSED_PRESERVE src0_sel:WORD_1
	v_exp_f16_sdwa v120, v112 dst_sel:WORD_1 dst_unused:UNUSED_PRESERVE src0_sel:WORD_1
	v_exp_f16_sdwa v121, v113 dst_sel:WORD_1 dst_unused:UNUSED_PRESERVE src0_sel:WORD_1
	v_pk_add_f16 v105, v105, v118
	v_pk_add_f16 v104, v104, v119
	v_rcp_f16_e32 v110, v105
	v_rcp_f16_sdwa v105, v105 dst_sel:DWORD dst_unused:UNUSED_PAD src0_sel:WORD_1
	v_pk_add_f16 v103, v103, v120
	v_rcp_f16_e32 v111, v104
	v_rcp_f16_sdwa v104, v104 dst_sel:DWORD dst_unused:UNUSED_PAD src0_sel:WORD_1
	v_pk_add_f16 v102, v102, v121
	v_rcp_f16_e32 v112, v103
	v_rcp_f16_sdwa v103, v103 dst_sel:DWORD dst_unused:UNUSED_PAD src0_sel:WORD_1
	v_rcp_f16_e32 v113, v102
	v_rcp_f16_sdwa v102, v102 dst_sel:DWORD dst_unused:UNUSED_PAD src0_sel:WORD_1
	v_pk_fma_f16 v78, v42, v118, v78
	v_pack_b32_f16 v105, v110, v105
	v_pk_fma_f16 v79, v43, v119, v79
	v_pk_mul_f16 v110, v78, v105
	v_pack_b32_f16 v78, v111, v104
	v_pk_fma_f16 v80, v44, v120, v80
	v_pk_mul_f16 v111, v79, v78
	v_pack_b32_f16 v78, v112, v103
	v_pk_fma_f16 v81, v45, v121, v81
	v_pk_mul_f16 v112, v80, v78
	v_pack_b32_f16 v78, v113, v102
	v_pk_mul_f16 v113, v81, v78
	s_waitcnt vmcnt(12)
	v_pk_mul_f16 v78, v182, v154 op_sel_hi:[0,1]
	v_pk_mul_f16 v81, v182, v157 op_sel_hi:[0,1]
	v_pk_mul_f16 v105, v180, v157 op_sel_hi:[0,1]
	v_pk_mul_f16 v121, v181, v157 op_sel_hi:[0,1]
	v_pk_mul_f16 v79, v182, v155 op_sel_hi:[0,1]
	v_pk_mul_f16 v80, v182, v156 op_sel_hi:[0,1]
	v_pk_mul_f16 v102, v180, v154 op_sel_hi:[0,1]
	v_pk_mul_f16 v103, v180, v155 op_sel_hi:[0,1]
	v_pk_mul_f16 v104, v180, v156 op_sel_hi:[0,1]
	v_pk_mul_f16 v118, v181, v154 op_sel_hi:[0,1]
	v_pk_mul_f16 v119, v181, v155 op_sel_hi:[0,1]
	v_pk_mul_f16 v120, v181, v156 op_sel_hi:[0,1]
	v_pk_fma_f16 v89, v89, v157, v81
	v_pk_fma_f16 v86, v86, v154, v78
	v_pk_fma_f16 v109, v109, v157, v81
	v_pk_fma_f16 v106, v106, v154, v78
	v_pk_fma_f16 v81, v125, v157, v81
	v_pk_fma_f16 v78, v122, v154, v78
	v_pk_fma_f16 v122, v53, v157, v105
	v_pk_fma_f16 v126, v69, v157, v105
	v_pk_fma_f16 v105, v97, v157, v105
	v_pk_fma_f16 v138, v21, v157, v121
	v_pk_fma_f16 v183, v33, v157, v121
	v_pk_fma_f16 v121, v57, v157, v121
	v_pk_maximum3_f16 v157, v89, v109, v81
	v_pk_fma_f16 v88, v88, v156, v80
	v_pk_fma_f16 v87, v87, v155, v79
	v_pk_fma_f16 v108, v108, v156, v80
	v_pk_fma_f16 v107, v107, v155, v79
	v_pk_fma_f16 v80, v124, v156, v80
	v_pk_fma_f16 v79, v123, v155, v79
	v_pk_fma_f16 v123, v52, v156, v104
	v_pk_fma_f16 v124, v51, v155, v103
	v_pk_fma_f16 v125, v50, v154, v102
	v_pk_fma_f16 v127, v68, v156, v104
	v_pk_fma_f16 v128, v67, v155, v103
	v_pk_fma_f16 v129, v66, v154, v102
	v_pk_fma_f16 v104, v96, v156, v104
	v_pk_fma_f16 v103, v95, v155, v103
	v_pk_fma_f16 v102, v94, v154, v102
	v_pk_fma_f16 v139, v20, v156, v120
	v_pk_fma_f16 v140, v19, v155, v119
	v_pk_fma_f16 v141, v18, v154, v118
	v_pk_fma_f16 v184, v32, v156, v120
	v_pk_fma_f16 v185, v31, v155, v119
	v_pk_fma_f16 v186, v30, v154, v118
	v_pk_fma_f16 v120, v56, v156, v120
	v_pk_fma_f16 v119, v55, v155, v119
	v_pk_fma_f16 v118, v54, v154, v118
	v_pk_maximum3_f16 v154, v86, v106, v78
	v_pk_maximum3_f16 v155, v87, v107, v79
	v_pk_maximum3_f16 v156, v88, v108, v80
	v_pk_maximum3_f16 v190, v122, v126, v105
	v_pk_maximum3_f16 v194, v138, v183, v121
	v_pk_maximum3_f16 v187, v125, v129, v102
	v_pk_maximum3_f16 v188, v124, v128, v103
	v_pk_maximum3_f16 v189, v123, v127, v104
	v_pk_maximum3_f16 v191, v141, v186, v118
	v_pk_maximum3_f16 v192, v140, v185, v119
	v_pk_maximum3_f16 v157, v157, v190, v194
	v_pk_maximum3_f16 v193, v139, v184, v120
	v_pk_maximum3_f16 v154, v154, v187, v191
	v_pk_maximum3_f16 v155, v155, v188, v192
	v_pk_maximum3_f16 v156, v156, v189, v193
	v_pk_add_f16 v89, v89, v157 neg_lo:[0,1] neg_hi:[0,1]
	v_pk_add_f16 v86, v86, v154 neg_lo:[0,1] neg_hi:[0,1]
	v_pk_add_f16 v87, v87, v155 neg_lo:[0,1] neg_hi:[0,1]
	v_pk_add_f16 v88, v88, v156 neg_lo:[0,1] neg_hi:[0,1]
	v_pk_add_f16 v106, v106, v154 neg_lo:[0,1] neg_hi:[0,1]
	v_exp_f16_sdwa v187, v86 dst_sel:WORD_0 dst_unused:UNUSED_PAD src0_sel:WORD_0
	v_exp_f16_sdwa v188, v87 dst_sel:WORD_0 dst_unused:UNUSED_PAD src0_sel:WORD_0
	v_exp_f16_sdwa v189, v88 dst_sel:WORD_0 dst_unused:UNUSED_PAD src0_sel:WORD_0
	v_exp_f16_sdwa v190, v89 dst_sel:WORD_0 dst_unused:UNUSED_PAD src0_sel:WORD_0
	v_exp_f16_sdwa v187, v86 dst_sel:WORD_1 dst_unused:UNUSED_PRESERVE src0_sel:WORD_1
	v_exp_f16_sdwa v188, v87 dst_sel:WORD_1 dst_unused:UNUSED_PRESERVE src0_sel:WORD_1
	v_exp_f16_sdwa v189, v88 dst_sel:WORD_1 dst_unused:UNUSED_PRESERVE src0_sel:WORD_1
	v_exp_f16_sdwa v190, v89 dst_sel:WORD_1 dst_unused:UNUSED_PRESERVE src0_sel:WORD_1
	v_pk_add_f16 v107, v107, v155 neg_lo:[0,1] neg_hi:[0,1]
	v_pk_add_f16 v89, v187, 0
	v_pk_fma_f16 v49, v49, v190, 0
	v_pk_add_f16 v86, v190, 0
	v_pk_add_f16 v87, v189, 0
	v_pk_add_f16 v88, v188, 0
	v_pk_fma_f16 v48, v48, v189, 0
	v_pk_fma_f16 v47, v47, v188, 0
	v_pk_fma_f16 v46, v46, v187, 0
	v_pk_add_f16 v108, v108, v156 neg_lo:[0,1] neg_hi:[0,1]
	v_pk_add_f16 v109, v109, v157 neg_lo:[0,1] neg_hi:[0,1]
	v_exp_f16_sdwa v187, v106 dst_sel:WORD_0 dst_unused:UNUSED_PAD src0_sel:WORD_0
	v_exp_f16_sdwa v188, v107 dst_sel:WORD_0 dst_unused:UNUSED_PAD src0_sel:WORD_0
	v_exp_f16_sdwa v189, v108 dst_sel:WORD_0 dst_unused:UNUSED_PAD src0_sel:WORD_0
	v_exp_f16_sdwa v190, v109 dst_sel:WORD_0 dst_unused:UNUSED_PAD src0_sel:WORD_0
	v_exp_f16_sdwa v187, v106 dst_sel:WORD_1 dst_unused:UNUSED_PRESERVE src0_sel:WORD_1
	v_exp_f16_sdwa v188, v107 dst_sel:WORD_1 dst_unused:UNUSED_PRESERVE src0_sel:WORD_1
	v_exp_f16_sdwa v189, v108 dst_sel:WORD_1 dst_unused:UNUSED_PRESERVE src0_sel:WORD_1
	v_exp_f16_sdwa v190, v109 dst_sel:WORD_1 dst_unused:UNUSED_PRESERVE src0_sel:WORD_1
	v_pk_add_f16 v89, v89, v187
	v_pk_fma_f16 v49, v65, v190, v49
	v_pk_add_f16 v65, v81, v157 neg_lo:[0,1] neg_hi:[0,1]
	v_pk_add_f16 v88, v88, v188
	v_pk_add_f16 v87, v87, v189
	v_pk_add_f16 v86, v86, v190
	v_pk_fma_f16 v46, v62, v187, v46
	v_pk_fma_f16 v47, v63, v188, v47
	v_pk_fma_f16 v48, v64, v189, v48
	v_pk_add_f16 v62, v78, v154 neg_lo:[0,1] neg_hi:[0,1]
	v_pk_add_f16 v63, v79, v155 neg_lo:[0,1] neg_hi:[0,1]
	v_pk_add_f16 v64, v80, v156 neg_lo:[0,1] neg_hi:[0,1]
	v_exp_f16_sdwa v78, v62 dst_sel:WORD_0 dst_unused:UNUSED_PAD src0_sel:WORD_0
	v_exp_f16_sdwa v79, v63 dst_sel:WORD_0 dst_unused:UNUSED_PAD src0_sel:WORD_0
	v_exp_f16_sdwa v80, v64 dst_sel:WORD_0 dst_unused:UNUSED_PAD src0_sel:WORD_0
	v_exp_f16_sdwa v81, v65 dst_sel:WORD_0 dst_unused:UNUSED_PAD src0_sel:WORD_0
	v_exp_f16_sdwa v78, v62 dst_sel:WORD_1 dst_unused:UNUSED_PRESERVE src0_sel:WORD_1
	v_exp_f16_sdwa v79, v63 dst_sel:WORD_1 dst_unused:UNUSED_PRESERVE src0_sel:WORD_1
	v_exp_f16_sdwa v80, v64 dst_sel:WORD_1 dst_unused:UNUSED_PRESERVE src0_sel:WORD_1
	v_exp_f16_sdwa v81, v65 dst_sel:WORD_1 dst_unused:UNUSED_PRESERVE src0_sel:WORD_1
	v_pk_add_f16 v65, v89, v78
	v_pk_add_f16 v62, v86, v81
	v_pk_add_f16 v63, v87, v80
	v_pk_add_f16 v64, v88, v79
	v_pk_fma_f16 v49, v85, v81, v49
	v_pk_fma_f16 v48, v84, v80, v48
	v_pk_fma_f16 v47, v83, v79, v47
	v_pk_fma_f16 v46, v82, v78, v46
	v_pk_add_f16 v78, v125, v154 neg_lo:[0,1] neg_hi:[0,1]
	v_pk_add_f16 v79, v124, v155 neg_lo:[0,1] neg_hi:[0,1]
	v_pk_add_f16 v80, v123, v156 neg_lo:[0,1] neg_hi:[0,1]
	v_pk_add_f16 v81, v122, v157 neg_lo:[0,1] neg_hi:[0,1]
	v_exp_f16_sdwa v82, v78 dst_sel:WORD_0 dst_unused:UNUSED_PAD src0_sel:WORD_0
	v_exp_f16_sdwa v83, v79 dst_sel:WORD_0 dst_unused:UNUSED_PAD src0_sel:WORD_0
	v_exp_f16_sdwa v84, v80 dst_sel:WORD_0 dst_unused:UNUSED_PAD src0_sel:WORD_0
	v_exp_f16_sdwa v85, v81 dst_sel:WORD_0 dst_unused:UNUSED_PAD src0_sel:WORD_0
	v_exp_f16_sdwa v82, v78 dst_sel:WORD_1 dst_unused:UNUSED_PRESERVE src0_sel:WORD_1
	v_exp_f16_sdwa v83, v79 dst_sel:WORD_1 dst_unused:UNUSED_PRESERVE src0_sel:WORD_1
	v_exp_f16_sdwa v84, v80 dst_sel:WORD_1 dst_unused:UNUSED_PRESERVE src0_sel:WORD_1
	v_exp_f16_sdwa v85, v81 dst_sel:WORD_1 dst_unused:UNUSED_PRESERVE src0_sel:WORD_1
	v_pk_add_f16 v78, v129, v154 neg_lo:[0,1] neg_hi:[0,1]
	v_pk_add_f16 v65, v65, v82
	v_pk_add_f16 v64, v64, v83
	v_pk_add_f16 v63, v63, v84
	v_pk_add_f16 v62, v62, v85
	v_pk_fma_f16 v46, v22, v82, v46
	v_pk_fma_f16 v47, v23, v83, v47
	v_pk_fma_f16 v48, v24, v84, v48
	v_pk_fma_f16 v49, v25, v85, v49
	v_pk_add_f16 v79, v128, v155 neg_lo:[0,1] neg_hi:[0,1]
	v_pk_add_f16 v80, v127, v156 neg_lo:[0,1] neg_hi:[0,1]
	v_pk_add_f16 v81, v126, v157 neg_lo:[0,1] neg_hi:[0,1]
	v_exp_f16_sdwa v82, v78 dst_sel:WORD_0 dst_unused:UNUSED_PAD src0_sel:WORD_0
	v_exp_f16_sdwa v83, v79 dst_sel:WORD_0 dst_unused:UNUSED_PAD src0_sel:WORD_0
	v_exp_f16_sdwa v84, v80 dst_sel:WORD_0 dst_unused:UNUSED_PAD src0_sel:WORD_0
	v_exp_f16_sdwa v85, v81 dst_sel:WORD_0 dst_unused:UNUSED_PAD src0_sel:WORD_0
	v_exp_f16_sdwa v82, v78 dst_sel:WORD_1 dst_unused:UNUSED_PRESERVE src0_sel:WORD_1
	v_exp_f16_sdwa v83, v79 dst_sel:WORD_1 dst_unused:UNUSED_PRESERVE src0_sel:WORD_1
	v_exp_f16_sdwa v84, v80 dst_sel:WORD_1 dst_unused:UNUSED_PRESERVE src0_sel:WORD_1
	v_exp_f16_sdwa v85, v81 dst_sel:WORD_1 dst_unused:UNUSED_PRESERVE src0_sel:WORD_1
	v_pk_add_f16 v78, v102, v154 neg_lo:[0,1] neg_hi:[0,1]
	v_pk_add_f16 v65, v65, v82
	v_pk_add_f16 v62, v62, v85
	v_pk_add_f16 v63, v63, v84
	v_pk_add_f16 v64, v64, v83
	v_pk_fma_f16 v49, v37, v85, v49
	v_pk_fma_f16 v48, v36, v84, v48
	v_pk_fma_f16 v47, v35, v83, v47
	v_pk_fma_f16 v46, v34, v82, v46
	v_pk_add_f16 v79, v103, v155 neg_lo:[0,1] neg_hi:[0,1]
	v_pk_add_f16 v80, v104, v156 neg_lo:[0,1] neg_hi:[0,1]
	v_pk_add_f16 v81, v105, v157 neg_lo:[0,1] neg_hi:[0,1]
	v_exp_f16_sdwa v82, v78 dst_sel:WORD_0 dst_unused:UNUSED_PAD src0_sel:WORD_0
	v_exp_f16_sdwa v83, v79 dst_sel:WORD_0 dst_unused:UNUSED_PAD src0_sel:WORD_0
	v_exp_f16_sdwa v84, v80 dst_sel:WORD_0 dst_unused:UNUSED_PAD src0_sel:WORD_0
	v_exp_f16_sdwa v85, v81 dst_sel:WORD_0 dst_unused:UNUSED_PAD src0_sel:WORD_0
	v_exp_f16_sdwa v82, v78 dst_sel:WORD_1 dst_unused:UNUSED_PRESERVE src0_sel:WORD_1
	v_exp_f16_sdwa v83, v79 dst_sel:WORD_1 dst_unused:UNUSED_PRESERVE src0_sel:WORD_1
	v_exp_f16_sdwa v84, v80 dst_sel:WORD_1 dst_unused:UNUSED_PRESERVE src0_sel:WORD_1
	v_exp_f16_sdwa v85, v81 dst_sel:WORD_1 dst_unused:UNUSED_PRESERVE src0_sel:WORD_1
	v_pk_add_f16 v78, v141, v154 neg_lo:[0,1] neg_hi:[0,1]
	v_pk_add_f16 v65, v65, v82
	v_pk_add_f16 v64, v64, v83
	v_pk_add_f16 v63, v63, v84
	v_pk_add_f16 v62, v62, v85
	v_pk_fma_f16 v46, v42, v82, v46
	v_pk_fma_f16 v47, v43, v83, v47
	v_pk_fma_f16 v48, v44, v84, v48
	v_pk_fma_f16 v49, v45, v85, v49
	v_pk_add_f16 v79, v140, v155 neg_lo:[0,1] neg_hi:[0,1]
	v_pk_add_f16 v80, v139, v156 neg_lo:[0,1] neg_hi:[0,1]
	v_pk_add_f16 v81, v138, v157 neg_lo:[0,1] neg_hi:[0,1]
	v_exp_f16_sdwa v82, v78 dst_sel:WORD_0 dst_unused:UNUSED_PAD src0_sel:WORD_0
	v_exp_f16_sdwa v83, v79 dst_sel:WORD_0 dst_unused:UNUSED_PAD src0_sel:WORD_0
	v_exp_f16_sdwa v84, v80 dst_sel:WORD_0 dst_unused:UNUSED_PAD src0_sel:WORD_0
	v_exp_f16_sdwa v85, v81 dst_sel:WORD_0 dst_unused:UNUSED_PAD src0_sel:WORD_0
	v_exp_f16_sdwa v82, v78 dst_sel:WORD_1 dst_unused:UNUSED_PRESERVE src0_sel:WORD_1
	v_exp_f16_sdwa v83, v79 dst_sel:WORD_1 dst_unused:UNUSED_PRESERVE src0_sel:WORD_1
	v_exp_f16_sdwa v84, v80 dst_sel:WORD_1 dst_unused:UNUSED_PRESERVE src0_sel:WORD_1
	v_exp_f16_sdwa v85, v81 dst_sel:WORD_1 dst_unused:UNUSED_PRESERVE src0_sel:WORD_1
	v_pk_add_f16 v78, v186, v154 neg_lo:[0,1] neg_hi:[0,1]
	v_pk_add_f16 v65, v65, v82
	v_pk_add_f16 v62, v62, v85
	v_pk_add_f16 v63, v63, v84
	v_pk_add_f16 v64, v64, v83
	v_pk_fma_f16 v49, v9, v85, v49
	v_pk_fma_f16 v48, v8, v84, v48
	v_pk_fma_f16 v47, v7, v83, v47
	v_pk_fma_f16 v46, v6, v82, v46
	v_pk_add_f16 v79, v185, v155 neg_lo:[0,1] neg_hi:[0,1]
	v_pk_add_f16 v80, v184, v156 neg_lo:[0,1] neg_hi:[0,1]
	v_pk_add_f16 v81, v183, v157 neg_lo:[0,1] neg_hi:[0,1]
	v_exp_f16_sdwa v82, v78 dst_sel:WORD_0 dst_unused:UNUSED_PAD src0_sel:WORD_0
	v_exp_f16_sdwa v83, v79 dst_sel:WORD_0 dst_unused:UNUSED_PAD src0_sel:WORD_0
	v_exp_f16_sdwa v84, v80 dst_sel:WORD_0 dst_unused:UNUSED_PAD src0_sel:WORD_0
	v_exp_f16_sdwa v85, v81 dst_sel:WORD_0 dst_unused:UNUSED_PAD src0_sel:WORD_0
	v_exp_f16_sdwa v82, v78 dst_sel:WORD_1 dst_unused:UNUSED_PRESERVE src0_sel:WORD_1
	v_exp_f16_sdwa v83, v79 dst_sel:WORD_1 dst_unused:UNUSED_PRESERVE src0_sel:WORD_1
	v_exp_f16_sdwa v84, v80 dst_sel:WORD_1 dst_unused:UNUSED_PRESERVE src0_sel:WORD_1
	v_exp_f16_sdwa v85, v81 dst_sel:WORD_1 dst_unused:UNUSED_PRESERVE src0_sel:WORD_1
	v_pk_add_f16 v78, v118, v154 neg_lo:[0,1] neg_hi:[0,1]
	v_pk_add_f16 v65, v65, v82
	v_pk_add_f16 v64, v64, v83
	v_pk_add_f16 v63, v63, v84
	v_pk_add_f16 v62, v62, v85
	v_pk_fma_f16 v46, v10, v82, v46
	v_pk_fma_f16 v47, v11, v83, v47
	v_pk_fma_f16 v48, v12, v84, v48
	v_pk_fma_f16 v49, v13, v85, v49
	v_pk_add_f16 v79, v119, v155 neg_lo:[0,1] neg_hi:[0,1]
	v_pk_add_f16 v80, v120, v156 neg_lo:[0,1] neg_hi:[0,1]
	v_pk_add_f16 v81, v121, v157 neg_lo:[0,1] neg_hi:[0,1]
	v_exp_f16_sdwa v82, v78 dst_sel:WORD_0 dst_unused:UNUSED_PAD src0_sel:WORD_0
	v_exp_f16_sdwa v83, v79 dst_sel:WORD_0 dst_unused:UNUSED_PAD src0_sel:WORD_0
	v_exp_f16_sdwa v84, v80 dst_sel:WORD_0 dst_unused:UNUSED_PAD src0_sel:WORD_0
	v_exp_f16_sdwa v85, v81 dst_sel:WORD_0 dst_unused:UNUSED_PAD src0_sel:WORD_0
	v_exp_f16_sdwa v82, v78 dst_sel:WORD_1 dst_unused:UNUSED_PRESERVE src0_sel:WORD_1
	v_exp_f16_sdwa v83, v79 dst_sel:WORD_1 dst_unused:UNUSED_PRESERVE src0_sel:WORD_1
	v_exp_f16_sdwa v84, v80 dst_sel:WORD_1 dst_unused:UNUSED_PRESERVE src0_sel:WORD_1
	v_exp_f16_sdwa v85, v81 dst_sel:WORD_1 dst_unused:UNUSED_PRESERVE src0_sel:WORD_1
	v_pk_add_f16 v65, v65, v82
	v_pk_add_f16 v64, v64, v83
	v_rcp_f16_e32 v78, v65
	v_rcp_f16_sdwa v65, v65 dst_sel:DWORD dst_unused:UNUSED_PAD src0_sel:WORD_1
	v_pk_add_f16 v63, v63, v84
	v_rcp_f16_e32 v79, v64
	v_rcp_f16_sdwa v64, v64 dst_sel:DWORD dst_unused:UNUSED_PAD src0_sel:WORD_1
	v_pk_add_f16 v62, v62, v85
	v_rcp_f16_e32 v80, v63
	v_rcp_f16_sdwa v81, v63 dst_sel:DWORD dst_unused:UNUSED_PAD src0_sel:WORD_1
	v_pk_fma_f16 v47, v15, v83, v47
	v_pk_fma_f16 v46, v14, v82, v46
	v_rcp_f16_e32 v82, v62
	v_rcp_f16_sdwa v83, v62 dst_sel:DWORD dst_unused:UNUSED_PAD src0_sel:WORD_1
	v_pack_b32_f16 v62, v78, v65
	v_pk_mul_f16 v62, v46, v62
	v_pack_b32_f16 v46, v79, v64
	v_pk_fma_f16 v48, v16, v84, v48
	v_pk_mul_f16 v63, v47, v46
	v_pack_b32_f16 v46, v80, v81
	v_pk_fma_f16 v49, v17, v85, v49
	v_pk_mul_f16 v64, v48, v46
	v_pack_b32_f16 v46, v82, v83
	v_pk_mul_f16 v65, v49, v46
	s_waitcnt vmcnt(6)
	v_pk_mul_f16 v46, v182, v150 op_sel_hi:[0,1]
	v_pk_mul_f16 v47, v182, v151 op_sel_hi:[0,1]
	v_pk_mul_f16 v48, v182, v152 op_sel_hi:[0,1]
	v_pk_mul_f16 v49, v182, v153 op_sel_hi:[0,1]
	v_pk_mul_f16 v78, v180, v150 op_sel_hi:[0,1]
	v_pk_mul_f16 v82, v181, v150 op_sel_hi:[0,1]
	v_pk_fma_f16 v50, v50, v150, v46
	v_pk_fma_f16 v66, v66, v150, v46
	v_pk_fma_f16 v46, v94, v150, v46
	v_pk_mul_f16 v79, v180, v151 op_sel_hi:[0,1]
	v_pk_maximum3_f16 v118, v50, v66, v46
	v_pk_mul_f16 v80, v180, v152 op_sel_hi:[0,1]
	v_pk_mul_f16 v81, v180, v153 op_sel_hi:[0,1]
	v_pk_mul_f16 v83, v181, v151 op_sel_hi:[0,1]
	v_pk_mul_f16 v84, v181, v152 op_sel_hi:[0,1]
	v_pk_mul_f16 v85, v181, v153 op_sel_hi:[0,1]
	v_pk_fma_f16 v53, v53, v153, v49
	v_pk_fma_f16 v52, v52, v152, v48
	v_pk_fma_f16 v51, v51, v151, v47
	v_pk_fma_f16 v69, v69, v153, v49
	v_pk_fma_f16 v68, v68, v152, v48
	v_pk_fma_f16 v67, v67, v151, v47
	v_pk_fma_f16 v49, v97, v153, v49
	v_pk_fma_f16 v48, v96, v152, v48
	v_pk_fma_f16 v47, v95, v151, v47
	v_pk_fma_f16 v89, v18, v150, v78
	v_pk_fma_f16 v97, v30, v150, v78
	v_pk_fma_f16 v78, v54, v150, v78
	v_pk_fma_f16 v105, v74, v150, v82
	v_pk_fma_f16 v109, v98, v150, v82
	v_pk_fma_f16 v82, v114, v150, v82
	v_pk_maximum3_f16 v119, v51, v67, v47
	v_pk_maximum3_f16 v120, v52, v68, v48
	v_pk_maximum3_f16 v121, v53, v69, v49
	v_pk_maximum3_f16 v122, v89, v97, v78
	v_pk_fma_f16 v86, v21, v153, v81
	v_pk_maximum3_f16 v126, v105, v109, v82
	v_pk_fma_f16 v87, v20, v152, v80
	v_pk_maximum3_f16 v118, v118, v122, v126
	v_pk_fma_f16 v88, v19, v151, v79
	v_pk_fma_f16 v94, v33, v153, v81
	v_pk_fma_f16 v95, v32, v152, v80
	v_pk_fma_f16 v96, v31, v151, v79
	v_pk_fma_f16 v81, v57, v153, v81
	v_pk_fma_f16 v80, v56, v152, v80
	v_pk_fma_f16 v79, v55, v151, v79
	v_pk_fma_f16 v102, v77, v153, v85
	v_pk_fma_f16 v103, v76, v152, v84
	v_pk_fma_f16 v104, v75, v151, v83
	v_pk_fma_f16 v106, v101, v153, v85
	v_pk_fma_f16 v107, v100, v152, v84
	v_pk_fma_f16 v108, v99, v151, v83
	v_pk_fma_f16 v85, v117, v153, v85
	v_pk_fma_f16 v84, v116, v152, v84
	v_pk_fma_f16 v83, v115, v151, v83
	v_pk_maximum3_f16 v123, v88, v96, v79
	v_pk_maximum3_f16 v124, v87, v95, v80
	v_pk_maximum3_f16 v125, v86, v94, v81
	v_pk_maximum3_f16 v128, v103, v107, v84
	v_pk_maximum3_f16 v129, v102, v106, v85
	v_pk_maximum3_f16 v127, v104, v108, v83
	v_pk_maximum3_f16 v119, v119, v123, v127
	v_pk_maximum3_f16 v120, v120, v124, v128
	v_pk_maximum3_f16 v121, v121, v125, v129
	v_pk_add_f16 v50, v50, v118 neg_lo:[0,1] neg_hi:[0,1]
	v_pk_add_f16 v51, v51, v119 neg_lo:[0,1] neg_hi:[0,1]
	v_pk_add_f16 v52, v52, v120 neg_lo:[0,1] neg_hi:[0,1]
	v_pk_add_f16 v53, v53, v121 neg_lo:[0,1] neg_hi:[0,1]
	v_pk_add_f16 v66, v66, v118 neg_lo:[0,1] neg_hi:[0,1]
	v_exp_f16_sdwa v122, v50 dst_sel:WORD_0 dst_unused:UNUSED_PAD src0_sel:WORD_0
	v_exp_f16_sdwa v123, v51 dst_sel:WORD_0 dst_unused:UNUSED_PAD src0_sel:WORD_0
	v_exp_f16_sdwa v124, v52 dst_sel:WORD_0 dst_unused:UNUSED_PAD src0_sel:WORD_0
	v_exp_f16_sdwa v125, v53 dst_sel:WORD_0 dst_unused:UNUSED_PAD src0_sel:WORD_0
	v_exp_f16_sdwa v122, v50 dst_sel:WORD_1 dst_unused:UNUSED_PRESERVE src0_sel:WORD_1
	v_exp_f16_sdwa v123, v51 dst_sel:WORD_1 dst_unused:UNUSED_PRESERVE src0_sel:WORD_1
	v_exp_f16_sdwa v124, v52 dst_sel:WORD_1 dst_unused:UNUSED_PRESERVE src0_sel:WORD_1
	v_exp_f16_sdwa v125, v53 dst_sel:WORD_1 dst_unused:UNUSED_PRESERVE src0_sel:WORD_1
	v_pk_add_f16 v67, v67, v119 neg_lo:[0,1] neg_hi:[0,1]
	v_pk_add_f16 v50, v125, 0
	v_pk_fma_f16 v22, v22, v122, 0
	v_pk_add_f16 v51, v124, 0
	v_pk_add_f16 v52, v123, 0
	v_pk_add_f16 v53, v122, 0
	v_pk_fma_f16 v23, v23, v123, 0
	v_pk_fma_f16 v24, v24, v124, 0
	v_pk_fma_f16 v25, v25, v125, 0
	v_pk_add_f16 v68, v68, v120 neg_lo:[0,1] neg_hi:[0,1]
	v_pk_add_f16 v69, v69, v121 neg_lo:[0,1] neg_hi:[0,1]
	v_exp_f16_sdwa v122, v66 dst_sel:WORD_0 dst_unused:UNUSED_PAD src0_sel:WORD_0
	v_exp_f16_sdwa v123, v67 dst_sel:WORD_0 dst_unused:UNUSED_PAD src0_sel:WORD_0
	v_exp_f16_sdwa v124, v68 dst_sel:WORD_0 dst_unused:UNUSED_PAD src0_sel:WORD_0
	v_exp_f16_sdwa v125, v69 dst_sel:WORD_0 dst_unused:UNUSED_PAD src0_sel:WORD_0
	v_exp_f16_sdwa v122, v66 dst_sel:WORD_1 dst_unused:UNUSED_PRESERVE src0_sel:WORD_1
	v_exp_f16_sdwa v123, v67 dst_sel:WORD_1 dst_unused:UNUSED_PRESERVE src0_sel:WORD_1
	v_exp_f16_sdwa v124, v68 dst_sel:WORD_1 dst_unused:UNUSED_PRESERVE src0_sel:WORD_1
	v_exp_f16_sdwa v125, v69 dst_sel:WORD_1 dst_unused:UNUSED_PRESERVE src0_sel:WORD_1
	s_nop 0
	v_pk_add_f16 v50, v50, v125
	v_pk_fma_f16 v22, v34, v122, v22
	v_pk_add_f16 v34, v46, v118 neg_lo:[0,1] neg_hi:[0,1]
	v_pk_add_f16 v53, v53, v122
	v_pk_add_f16 v52, v52, v123
	v_pk_add_f16 v51, v51, v124
	v_pk_fma_f16 v25, v37, v125, v25
	v_pk_fma_f16 v24, v36, v124, v24
	v_pk_fma_f16 v23, v35, v123, v23
	v_pk_add_f16 v35, v47, v119 neg_lo:[0,1] neg_hi:[0,1]
	v_pk_add_f16 v36, v48, v120 neg_lo:[0,1] neg_hi:[0,1]
	v_pk_add_f16 v37, v49, v121 neg_lo:[0,1] neg_hi:[0,1]
	v_exp_f16_sdwa v46, v34 dst_sel:WORD_0 dst_unused:UNUSED_PAD src0_sel:WORD_0
	v_exp_f16_sdwa v47, v35 dst_sel:WORD_0 dst_unused:UNUSED_PAD src0_sel:WORD_0
	v_exp_f16_sdwa v48, v36 dst_sel:WORD_0 dst_unused:UNUSED_PAD src0_sel:WORD_0
	v_exp_f16_sdwa v49, v37 dst_sel:WORD_0 dst_unused:UNUSED_PAD src0_sel:WORD_0
	v_exp_f16_sdwa v46, v34 dst_sel:WORD_1 dst_unused:UNUSED_PRESERVE src0_sel:WORD_1
	v_exp_f16_sdwa v47, v35 dst_sel:WORD_1 dst_unused:UNUSED_PRESERVE src0_sel:WORD_1
	v_exp_f16_sdwa v48, v36 dst_sel:WORD_1 dst_unused:UNUSED_PRESERVE src0_sel:WORD_1
	v_exp_f16_sdwa v49, v37 dst_sel:WORD_1 dst_unused:UNUSED_PRESERVE src0_sel:WORD_1
	s_nop 0
	v_pk_add_f16 v34, v50, v49
	v_pk_add_f16 v35, v51, v48
	v_pk_add_f16 v36, v52, v47
	v_pk_add_f16 v37, v53, v46
	v_pk_fma_f16 v22, v42, v46, v22
	v_pk_fma_f16 v23, v43, v47, v23
	v_pk_fma_f16 v24, v44, v48, v24
	v_pk_fma_f16 v25, v45, v49, v25
	v_pk_add_f16 v42, v89, v118 neg_lo:[0,1] neg_hi:[0,1]
	v_pk_add_f16 v43, v88, v119 neg_lo:[0,1] neg_hi:[0,1]
	v_pk_add_f16 v44, v87, v120 neg_lo:[0,1] neg_hi:[0,1]
	v_pk_add_f16 v45, v86, v121 neg_lo:[0,1] neg_hi:[0,1]
	v_exp_f16_sdwa v46, v42 dst_sel:WORD_0 dst_unused:UNUSED_PAD src0_sel:WORD_0
	v_exp_f16_sdwa v47, v43 dst_sel:WORD_0 dst_unused:UNUSED_PAD src0_sel:WORD_0
	v_exp_f16_sdwa v48, v44 dst_sel:WORD_0 dst_unused:UNUSED_PAD src0_sel:WORD_0
	v_exp_f16_sdwa v49, v45 dst_sel:WORD_0 dst_unused:UNUSED_PAD src0_sel:WORD_0
	v_exp_f16_sdwa v46, v42 dst_sel:WORD_1 dst_unused:UNUSED_PRESERVE src0_sel:WORD_1
	v_exp_f16_sdwa v47, v43 dst_sel:WORD_1 dst_unused:UNUSED_PRESERVE src0_sel:WORD_1
	v_exp_f16_sdwa v48, v44 dst_sel:WORD_1 dst_unused:UNUSED_PRESERVE src0_sel:WORD_1
	v_exp_f16_sdwa v49, v45 dst_sel:WORD_1 dst_unused:UNUSED_PRESERVE src0_sel:WORD_1
	v_pk_add_f16 v42, v97, v118 neg_lo:[0,1] neg_hi:[0,1]
	v_pk_add_f16 v34, v34, v49
	v_pk_add_f16 v37, v37, v46
	v_pk_add_f16 v36, v36, v47
	v_pk_add_f16 v35, v35, v48
	v_pk_fma_f16 v25, v9, v49, v25
	v_pk_fma_f16 v24, v8, v48, v24
	v_pk_fma_f16 v23, v7, v47, v23
	v_pk_fma_f16 v22, v6, v46, v22
	v_pk_add_f16 v43, v96, v119 neg_lo:[0,1] neg_hi:[0,1]
	v_pk_add_f16 v44, v95, v120 neg_lo:[0,1] neg_hi:[0,1]
	v_pk_add_f16 v45, v94, v121 neg_lo:[0,1] neg_hi:[0,1]
	v_exp_f16_sdwa v46, v42 dst_sel:WORD_0 dst_unused:UNUSED_PAD src0_sel:WORD_0
	v_exp_f16_sdwa v47, v43 dst_sel:WORD_0 dst_unused:UNUSED_PAD src0_sel:WORD_0
	v_exp_f16_sdwa v48, v44 dst_sel:WORD_0 dst_unused:UNUSED_PAD src0_sel:WORD_0
	v_exp_f16_sdwa v49, v45 dst_sel:WORD_0 dst_unused:UNUSED_PAD src0_sel:WORD_0
	v_exp_f16_sdwa v46, v42 dst_sel:WORD_1 dst_unused:UNUSED_PRESERVE src0_sel:WORD_1
	v_exp_f16_sdwa v47, v43 dst_sel:WORD_1 dst_unused:UNUSED_PRESERVE src0_sel:WORD_1
	v_exp_f16_sdwa v48, v44 dst_sel:WORD_1 dst_unused:UNUSED_PRESERVE src0_sel:WORD_1
	v_exp_f16_sdwa v49, v45 dst_sel:WORD_1 dst_unused:UNUSED_PRESERVE src0_sel:WORD_1
	v_pk_add_f16 v42, v78, v118 neg_lo:[0,1] neg_hi:[0,1]
	v_pk_add_f16 v34, v34, v49
	v_pk_add_f16 v35, v35, v48
	v_pk_add_f16 v36, v36, v47
	v_pk_add_f16 v37, v37, v46
	v_pk_fma_f16 v22, v10, v46, v22
	v_pk_fma_f16 v23, v11, v47, v23
	v_pk_fma_f16 v24, v12, v48, v24
	v_pk_fma_f16 v25, v13, v49, v25
	v_pk_add_f16 v43, v79, v119 neg_lo:[0,1] neg_hi:[0,1]
	v_pk_add_f16 v44, v80, v120 neg_lo:[0,1] neg_hi:[0,1]
	v_pk_add_f16 v45, v81, v121 neg_lo:[0,1] neg_hi:[0,1]
	v_exp_f16_sdwa v46, v42 dst_sel:WORD_0 dst_unused:UNUSED_PAD src0_sel:WORD_0
	v_exp_f16_sdwa v47, v43 dst_sel:WORD_0 dst_unused:UNUSED_PAD src0_sel:WORD_0
	v_exp_f16_sdwa v48, v44 dst_sel:WORD_0 dst_unused:UNUSED_PAD src0_sel:WORD_0
	v_exp_f16_sdwa v49, v45 dst_sel:WORD_0 dst_unused:UNUSED_PAD src0_sel:WORD_0
	v_exp_f16_sdwa v46, v42 dst_sel:WORD_1 dst_unused:UNUSED_PRESERVE src0_sel:WORD_1
	v_exp_f16_sdwa v47, v43 dst_sel:WORD_1 dst_unused:UNUSED_PRESERVE src0_sel:WORD_1
	v_exp_f16_sdwa v48, v44 dst_sel:WORD_1 dst_unused:UNUSED_PRESERVE src0_sel:WORD_1
	v_exp_f16_sdwa v49, v45 dst_sel:WORD_1 dst_unused:UNUSED_PRESERVE src0_sel:WORD_1
	v_pk_add_f16 v42, v105, v118 neg_lo:[0,1] neg_hi:[0,1]
	v_pk_add_f16 v34, v34, v49
	v_pk_add_f16 v37, v37, v46
	v_pk_add_f16 v36, v36, v47
	v_pk_add_f16 v35, v35, v48
	v_pk_fma_f16 v25, v17, v49, v25
	v_pk_fma_f16 v24, v16, v48, v24
	v_pk_fma_f16 v23, v15, v47, v23
	v_pk_fma_f16 v22, v14, v46, v22
	v_pk_add_f16 v43, v104, v119 neg_lo:[0,1] neg_hi:[0,1]
	v_pk_add_f16 v44, v103, v120 neg_lo:[0,1] neg_hi:[0,1]
	v_pk_add_f16 v45, v102, v121 neg_lo:[0,1] neg_hi:[0,1]
	v_exp_f16_sdwa v46, v42 dst_sel:WORD_0 dst_unused:UNUSED_PAD src0_sel:WORD_0
	v_exp_f16_sdwa v47, v43 dst_sel:WORD_0 dst_unused:UNUSED_PAD src0_sel:WORD_0
	v_exp_f16_sdwa v48, v44 dst_sel:WORD_0 dst_unused:UNUSED_PAD src0_sel:WORD_0
	v_exp_f16_sdwa v49, v45 dst_sel:WORD_0 dst_unused:UNUSED_PAD src0_sel:WORD_0
	v_exp_f16_sdwa v46, v42 dst_sel:WORD_1 dst_unused:UNUSED_PRESERVE src0_sel:WORD_1
	v_exp_f16_sdwa v47, v43 dst_sel:WORD_1 dst_unused:UNUSED_PRESERVE src0_sel:WORD_1
	v_exp_f16_sdwa v48, v44 dst_sel:WORD_1 dst_unused:UNUSED_PRESERVE src0_sel:WORD_1
	v_exp_f16_sdwa v49, v45 dst_sel:WORD_1 dst_unused:UNUSED_PRESERVE src0_sel:WORD_1
	v_pk_add_f16 v42, v109, v118 neg_lo:[0,1] neg_hi:[0,1]
	v_pk_add_f16 v34, v34, v49
	v_pk_add_f16 v35, v35, v48
	v_pk_add_f16 v36, v36, v47
	v_pk_add_f16 v37, v37, v46
	v_pk_fma_f16 v22, v26, v46, v22
	v_pk_fma_f16 v23, v27, v47, v23
	v_pk_fma_f16 v24, v28, v48, v24
	v_pk_fma_f16 v25, v29, v49, v25
	v_pk_add_f16 v43, v108, v119 neg_lo:[0,1] neg_hi:[0,1]
	v_pk_add_f16 v44, v107, v120 neg_lo:[0,1] neg_hi:[0,1]
	v_pk_add_f16 v45, v106, v121 neg_lo:[0,1] neg_hi:[0,1]
	v_exp_f16_sdwa v46, v42 dst_sel:WORD_0 dst_unused:UNUSED_PAD src0_sel:WORD_0
	v_exp_f16_sdwa v47, v43 dst_sel:WORD_0 dst_unused:UNUSED_PAD src0_sel:WORD_0
	v_exp_f16_sdwa v48, v44 dst_sel:WORD_0 dst_unused:UNUSED_PAD src0_sel:WORD_0
	v_exp_f16_sdwa v49, v45 dst_sel:WORD_0 dst_unused:UNUSED_PAD src0_sel:WORD_0
	v_exp_f16_sdwa v46, v42 dst_sel:WORD_1 dst_unused:UNUSED_PRESERVE src0_sel:WORD_1
	v_exp_f16_sdwa v47, v43 dst_sel:WORD_1 dst_unused:UNUSED_PRESERVE src0_sel:WORD_1
	v_exp_f16_sdwa v48, v44 dst_sel:WORD_1 dst_unused:UNUSED_PRESERVE src0_sel:WORD_1
	v_exp_f16_sdwa v49, v45 dst_sel:WORD_1 dst_unused:UNUSED_PRESERVE src0_sel:WORD_1
	v_pk_add_f16 v42, v82, v118 neg_lo:[0,1] neg_hi:[0,1]
	v_pk_add_f16 v34, v34, v49
	v_pk_add_f16 v37, v37, v46
	v_pk_add_f16 v36, v36, v47
	v_pk_add_f16 v35, v35, v48
	v_pk_fma_f16 v25, v41, v49, v25
	v_pk_fma_f16 v24, v40, v48, v24
	v_pk_fma_f16 v23, v39, v47, v23
	v_pk_fma_f16 v22, v38, v46, v22
	v_pk_add_f16 v43, v83, v119 neg_lo:[0,1] neg_hi:[0,1]
	v_pk_add_f16 v44, v84, v120 neg_lo:[0,1] neg_hi:[0,1]
	v_pk_add_f16 v45, v85, v121 neg_lo:[0,1] neg_hi:[0,1]
	v_exp_f16_sdwa v46, v42 dst_sel:WORD_0 dst_unused:UNUSED_PAD src0_sel:WORD_0
	v_exp_f16_sdwa v47, v43 dst_sel:WORD_0 dst_unused:UNUSED_PAD src0_sel:WORD_0
	v_exp_f16_sdwa v48, v44 dst_sel:WORD_0 dst_unused:UNUSED_PAD src0_sel:WORD_0
	v_exp_f16_sdwa v49, v45 dst_sel:WORD_0 dst_unused:UNUSED_PAD src0_sel:WORD_0
	v_exp_f16_sdwa v46, v42 dst_sel:WORD_1 dst_unused:UNUSED_PRESERVE src0_sel:WORD_1
	v_exp_f16_sdwa v47, v43 dst_sel:WORD_1 dst_unused:UNUSED_PRESERVE src0_sel:WORD_1
	v_exp_f16_sdwa v48, v44 dst_sel:WORD_1 dst_unused:UNUSED_PRESERVE src0_sel:WORD_1
	v_exp_f16_sdwa v49, v45 dst_sel:WORD_1 dst_unused:UNUSED_PRESERVE src0_sel:WORD_1
	s_nop 0
	v_pk_add_f16 v34, v34, v49
	v_pk_add_f16 v35, v35, v48
	v_rcp_f16_e32 v44, v34
	v_rcp_f16_sdwa v34, v34 dst_sel:DWORD dst_unused:UNUSED_PAD src0_sel:WORD_1
	v_pk_add_f16 v36, v36, v47
	v_rcp_f16_e32 v45, v35
	v_rcp_f16_sdwa v35, v35 dst_sel:DWORD dst_unused:UNUSED_PAD src0_sel:WORD_1
	v_pk_add_f16 v37, v37, v46
	v_rcp_f16_e32 v43, v36
	v_rcp_f16_sdwa v36, v36 dst_sel:DWORD dst_unused:UNUSED_PAD src0_sel:WORD_1
	v_rcp_f16_e32 v42, v37
	v_rcp_f16_sdwa v37, v37 dst_sel:DWORD dst_unused:UNUSED_PAD src0_sel:WORD_1
	v_pk_fma_f16 v25, v61, v49, v25
	v_pack_b32_f16 v34, v44, v34
	v_pk_fma_f16 v24, v60, v48, v24
	v_pk_mul_f16 v25, v25, v34
	v_pack_b32_f16 v34, v45, v35
	v_pk_fma_f16 v23, v59, v47, v23
	v_pk_mul_f16 v24, v24, v34
	v_pack_b32_f16 v34, v43, v36
	v_pk_fma_f16 v22, v58, v46, v22
	v_pk_mul_f16 v23, v23, v34
	v_pack_b32_f16 v34, v42, v37
	v_pk_mul_f16 v22, v22, v34
	s_waitcnt vmcnt(0)
	s_cmp_lg_u32 s10, 1
	s_cbranch_scc1 .Lmywd3_1
	s_mul_i32 s84, s81, s83
	s_add_i32 s84, s84, s82
	s_mul_i32 s84, s84, 0x60000
	s_mul_i32 s85, s94, 0x6000
	s_add_u32 s84, s84, s85
	s_add_u32 s88, s86, s84
	s_addc_u32 s89, s87, 0
	v_mbcnt_lo_u32_b32 v251, -1, 0
	v_mbcnt_hi_u32_b32 v251, -1, v251
	v_lshlrev_b32_e32 v251, 4, v251
	global_load_dwordx4 v[252:255], v251, s[88:89]
	global_load_dwordx4 v[252:255], v251, s[88:89] offset:1024
	global_load_dwordx4 v[252:255], v251, s[88:89] offset:2048
	global_load_dwordx4 v[252:255], v251, s[88:89] offset:3072
	s_add_u32 s88, s88, 0x1000
	s_addc_u32 s89, s89, 0
	global_load_dwordx4 v[252:255], v251, s[88:89]
	global_load_dwordx4 v[252:255], v251, s[88:89] offset:1024
	global_load_dwordx4 v[252:255], v251, s[88:89] offset:2048
	global_load_dwordx4 v[252:255], v251, s[88:89] offset:3072
	s_add_u32 s88, s88, 0x1000
	s_addc_u32 s89, s89, 0
	global_load_dwordx4 v[252:255], v251, s[88:89]
	global_load_dwordx4 v[252:255], v251, s[88:89] offset:1024
	global_load_dwordx4 v[252:255], v251, s[88:89] offset:2048
	global_load_dwordx4 v[252:255], v251, s[88:89] offset:3072

.Lmyf_B1_7:
	s_mov_b64 exec, -1
	s_waitcnt lgkmcnt(0)
	v_cvt_f16_f32_e32 v183, s27
	v_cvt_f16_f32_e32 v185, s26
	v_cvt_f16_f32_e32 v184, s34
	s_mov_b64 s[4:5], 0
	s_waitcnt vmcnt(3)
	v_pk_mul_f16 v193, v185, v189 op_sel_hi:[0,1]
	v_pk_mul_f16 v197, v183, v189 op_sel_hi:[0,1]
	v_pk_mul_f16 v201, v184, v189 op_sel_hi:[0,1]
	v_pk_mul_f16 v190, v185, v186 op_sel_hi:[0,1]
	v_pk_mul_f16 v191, v185, v187 op_sel_hi:[0,1]
	v_pk_mul_f16 v192, v185, v188 op_sel_hi:[0,1]
	v_pk_mul_f16 v194, v183, v186 op_sel_hi:[0,1]
	s_mov_b64 exec, s[64:65]
	buffer_load_dwordx4 v[18:21], v249, s[16:19], 0 offen
	buffer_load_dwordx4 v[6:9], v249, s[16:19], 0 offen offset:512
	s_mov_b64 exec, -1
	v_pk_mul_f16 v195, v183, v187 op_sel_hi:[0,1]
	v_pk_mul_f16 v196, v183, v188 op_sel_hi:[0,1]
	v_pk_mul_f16 v198, v184, v186 op_sel_hi:[0,1]
	v_pk_mul_f16 v199, v184, v187 op_sel_hi:[0,1]
	v_pk_mul_f16 v200, v184, v188 op_sel_hi:[0,1]
	v_pk_fma_f16 v113, v113, v189, v193
	v_pk_fma_f16 v129, v129, v189, v197
	v_pk_fma_f16 v137, v137, v189, v201
	v_pk_fma_f16 v202, v85, v189, v193
	v_pk_fma_f16 v206, v109, v189, v197
	v_pk_fma_f16 v210, v125, v189, v201
	v_pk_fma_f16 v193, v53, v189, v193
	v_pk_fma_f16 v197, v69, v189, v197
	buffer_load_dwordx4 v[34:37], v250, s[16:19], 0 offen offset:512
	buffer_load_dwordx4 v[10:13], v250, s[16:19], 0 offen offset:1024
	v_pk_fma_f16 v189, v97, v189, v201
	v_pk_maximum3_f16 v201, v113, v129, v137
	v_pk_fma_f16 v112, v112, v188, v192
	v_pk_fma_f16 v111, v111, v187, v191
	v_pk_fma_f16 v110, v110, v186, v190
	v_pk_fma_f16 v128, v128, v188, v196
	v_pk_fma_f16 v127, v127, v187, v195
	v_pk_fma_f16 v126, v126, v186, v194
	v_pk_fma_f16 v136, v136, v188, v200
	v_pk_fma_f16 v135, v135, v187, v199
	v_pk_fma_f16 v134, v134, v186, v198
	v_pk_fma_f16 v203, v84, v188, v192
	v_pk_fma_f16 v204, v83, v187, v191
	v_pk_fma_f16 v205, v82, v186, v190
	v_pk_fma_f16 v207, v108, v188, v196
	v_pk_fma_f16 v208, v107, v187, v195
	s_mov_b64 exec, s[66:67]
	buffer_load_dwordx4 v[54:57], v250, s[16:19], 0 offen offset:2048
	buffer_load_dwordx4 v[14:17], v250, s[16:19], 0 offen offset:2560
	s_mov_b64 exec, -1
	v_pk_fma_f16 v209, v106, v186, v194
	v_pk_fma_f16 v211, v124, v188, v200
	v_pk_fma_f16 v212, v123, v187, v199
	v_pk_fma_f16 v213, v122, v186, v198
	v_pk_fma_f16 v192, v52, v188, v192
	v_pk_fma_f16 v191, v51, v187, v191
	v_pk_fma_f16 v190, v50, v186, v190
	v_pk_fma_f16 v196, v68, v188, v196
	v_pk_fma_f16 v195, v67, v187, v195
	v_pk_fma_f16 v194, v66, v186, v194
	v_pk_fma_f16 v188, v96, v188, v200
	v_pk_fma_f16 v187, v95, v187, v199
	v_pk_fma_f16 v186, v94, v186, v198
	v_pk_maximum3_f16 v198, v110, v126, v134
	v_pk_maximum3_f16 v199, v111, v127, v135
	v_pk_maximum3_f16 v200, v112, v128, v136
	v_pk_maximum3_f16 v217, v202, v206, v210
	v_pk_maximum3_f16 v221, v193, v197, v189
	v_pk_maximum3_f16 v214, v205, v209, v213
	v_pk_maximum3_f16 v215, v204, v208, v212
	v_pk_maximum3_f16 v216, v203, v207, v211
	v_pk_maximum3_f16 v218, v190, v194, v186
	v_pk_maximum3_f16 v219, v191, v195, v187
	v_pk_maximum3_f16 v201, v201, v217, v221
	v_pk_maximum3_f16 v220, v192, v196, v188
	v_pk_maximum3_f16 v198, v198, v214, v218
	v_pk_maximum3_f16 v199, v199, v215, v219
	v_pk_maximum3_f16 v200, v200, v216, v220
	v_pk_add_f16 v113, v113, v201 neg_lo:[0,1] neg_hi:[0,1]
	s_mov_b64 exec, s[64:65]
	buffer_load_dwordx4 v[74:77], v251, s[16:19], 0 offen
	buffer_load_dwordx4 v[26:29], v251, s[16:19], 0 offen offset:512
	s_mov_b64 exec, -1
	v_pk_add_f16 v110, v110, v198 neg_lo:[0,1] neg_hi:[0,1]
	v_pk_add_f16 v111, v111, v199 neg_lo:[0,1] neg_hi:[0,1]
	v_pk_add_f16 v112, v112, v200 neg_lo:[0,1] neg_hi:[0,1]
	v_pk_add_f16 v126, v126, v198 neg_lo:[0,1] neg_hi:[0,1]
	v_exp_f16_sdwa v214, v110 dst_sel:WORD_0 dst_unused:UNUSED_PAD src0_sel:WORD_0
	v_exp_f16_sdwa v215, v111 dst_sel:WORD_0 dst_unused:UNUSED_PAD src0_sel:WORD_0
	v_exp_f16_sdwa v216, v112 dst_sel:WORD_0 dst_unused:UNUSED_PAD src0_sel:WORD_0
	v_exp_f16_sdwa v217, v113 dst_sel:WORD_0 dst_unused:UNUSED_PAD src0_sel:WORD_0
	v_exp_f16_sdwa v214, v110 dst_sel:WORD_1 dst_unused:UNUSED_PRESERVE src0_sel:WORD_1
	v_exp_f16_sdwa v215, v111 dst_sel:WORD_1 dst_unused:UNUSED_PRESERVE src0_sel:WORD_1
	v_exp_f16_sdwa v216, v112 dst_sel:WORD_1 dst_unused:UNUSED_PRESERVE src0_sel:WORD_1
	v_exp_f16_sdwa v217, v113 dst_sel:WORD_1 dst_unused:UNUSED_PRESERVE src0_sel:WORD_1
	v_pk_add_f16 v127, v127, v199 neg_lo:[0,1] neg_hi:[0,1]
	v_pk_add_f16 v113, v214, 0
	v_pk_fma_f16 v73, v73, v217, 0
	v_pk_add_f16 v110, v217, 0
	v_pk_add_f16 v111, v216, 0
	v_pk_add_f16 v112, v215, 0
	v_pk_fma_f16 v72, v72, v216, 0
	v_pk_fma_f16 v71, v71, v215, 0
	v_pk_fma_f16 v70, v70, v214, 0
	v_pk_add_f16 v128, v128, v200 neg_lo:[0,1] neg_hi:[0,1]
	buffer_load_dwordx4 v[102:105], v252, s[16:19], 0 offen offset:512
	buffer_load_dwordx4 v[38:41], v252, s[16:19], 0 offen offset:1024
	v_pk_add_f16 v129, v129, v201 neg_lo:[0,1] neg_hi:[0,1]
	v_exp_f16_sdwa v214, v126 dst_sel:WORD_0 dst_unused:UNUSED_PAD src0_sel:WORD_0
	v_exp_f16_sdwa v215, v127 dst_sel:WORD_0 dst_unused:UNUSED_PAD src0_sel:WORD_0
	v_exp_f16_sdwa v216, v128 dst_sel:WORD_0 dst_unused:UNUSED_PAD src0_sel:WORD_0
	v_exp_f16_sdwa v217, v129 dst_sel:WORD_0 dst_unused:UNUSED_PAD src0_sel:WORD_0
	v_exp_f16_sdwa v214, v126 dst_sel:WORD_1 dst_unused:UNUSED_PRESERVE src0_sel:WORD_1
	v_exp_f16_sdwa v215, v127 dst_sel:WORD_1 dst_unused:UNUSED_PRESERVE src0_sel:WORD_1
	v_exp_f16_sdwa v216, v128 dst_sel:WORD_1 dst_unused:UNUSED_PRESERVE src0_sel:WORD_1
	v_exp_f16_sdwa v217, v129 dst_sel:WORD_1 dst_unused:UNUSED_PRESERVE src0_sel:WORD_1
	v_pk_add_f16 v113, v113, v214
	v_pk_fma_f16 v73, v101, v217, v73
	v_pk_add_f16 v101, v137, v201 neg_lo:[0,1] neg_hi:[0,1]
	v_pk_add_f16 v112, v112, v215
	v_pk_add_f16 v111, v111, v216
	v_pk_add_f16 v110, v110, v217
	v_pk_fma_f16 v70, v98, v214, v70
	v_pk_fma_f16 v71, v99, v215, v71
	v_pk_fma_f16 v72, v100, v216, v72
	v_pk_add_f16 v98, v134, v198 neg_lo:[0,1] neg_hi:[0,1]
	v_pk_add_f16 v99, v135, v199 neg_lo:[0,1] neg_hi:[0,1]
	v_pk_add_f16 v100, v136, v200 neg_lo:[0,1] neg_hi:[0,1]
	v_exp_f16_sdwa v126, v98 dst_sel:WORD_0 dst_unused:UNUSED_PAD src0_sel:WORD_0
	v_exp_f16_sdwa v127, v99 dst_sel:WORD_0 dst_unused:UNUSED_PAD src0_sel:WORD_0
	v_exp_f16_sdwa v128, v100 dst_sel:WORD_0 dst_unused:UNUSED_PAD src0_sel:WORD_0
	v_exp_f16_sdwa v129, v101 dst_sel:WORD_0 dst_unused:UNUSED_PAD src0_sel:WORD_0
	v_exp_f16_sdwa v126, v98 dst_sel:WORD_1 dst_unused:UNUSED_PRESERVE src0_sel:WORD_1
	v_exp_f16_sdwa v127, v99 dst_sel:WORD_1 dst_unused:UNUSED_PRESERVE src0_sel:WORD_1
	v_exp_f16_sdwa v128, v100 dst_sel:WORD_1 dst_unused:UNUSED_PRESERVE src0_sel:WORD_1
	v_exp_f16_sdwa v129, v101 dst_sel:WORD_1 dst_unused:UNUSED_PRESERVE src0_sel:WORD_1
	v_pk_add_f16 v101, v113, v126
	v_pk_add_f16 v98, v110, v129
	s_mov_b64 exec, s[66:67]
	buffer_load_dwordx4 v[118:121], v252, s[16:19], 0 offen offset:2048
	buffer_load_dwordx4 v[58:61], v252, s[16:19], 0 offen offset:2560
	s_mov_b64 exec, -1
	v_pk_add_f16 v99, v111, v128
	v_pk_add_f16 v100, v112, v127
	v_pk_fma_f16 v73, v117, v129, v73
	v_pk_fma_f16 v72, v116, v128, v72
	v_pk_fma_f16 v71, v115, v127, v71
	v_pk_fma_f16 v70, v114, v126, v70
	v_pk_add_f16 v110, v205, v198 neg_lo:[0,1] neg_hi:[0,1]
	v_pk_add_f16 v111, v204, v199 neg_lo:[0,1] neg_hi:[0,1]
	v_pk_add_f16 v112, v203, v200 neg_lo:[0,1] neg_hi:[0,1]
	v_pk_add_f16 v113, v202, v201 neg_lo:[0,1] neg_hi:[0,1]
	v_exp_f16_sdwa v114, v110 dst_sel:WORD_0 dst_unused:UNUSED_PAD src0_sel:WORD_0
	v_exp_f16_sdwa v115, v111 dst_sel:WORD_0 dst_unused:UNUSED_PAD src0_sel:WORD_0
	v_exp_f16_sdwa v116, v112 dst_sel:WORD_0 dst_unused:UNUSED_PAD src0_sel:WORD_0
	v_exp_f16_sdwa v117, v113 dst_sel:WORD_0 dst_unused:UNUSED_PAD src0_sel:WORD_0
	v_exp_f16_sdwa v114, v110 dst_sel:WORD_1 dst_unused:UNUSED_PRESERVE src0_sel:WORD_1
	v_exp_f16_sdwa v115, v111 dst_sel:WORD_1 dst_unused:UNUSED_PRESERVE src0_sel:WORD_1
	v_exp_f16_sdwa v116, v112 dst_sel:WORD_1 dst_unused:UNUSED_PRESERVE src0_sel:WORD_1
	v_exp_f16_sdwa v117, v113 dst_sel:WORD_1 dst_unused:UNUSED_PRESERVE src0_sel:WORD_1
	v_pk_add_f16 v110, v209, v198 neg_lo:[0,1] neg_hi:[0,1]
	v_pk_add_f16 v101, v101, v114
	v_pk_add_f16 v100, v100, v115
	v_pk_add_f16 v99, v99, v116
	s_mov_b64 exec, s[76:77]
	buffer_load_dwordx4 v[130:133], v253, s[16:19], 0 offen
	buffer_load_dwordx4 v[78:81], v253, s[16:19], 0 offen offset:512
	s_mov_b64 exec, -1
	v_pk_add_f16 v98, v98, v117
	v_pk_fma_f16 v70, v42, v114, v70
	v_pk_fma_f16 v71, v43, v115, v71
	v_pk_fma_f16 v72, v44, v116, v72
	v_pk_fma_f16 v73, v45, v117, v73
	v_pk_add_f16 v111, v208, v199 neg_lo:[0,1] neg_hi:[0,1]
	v_pk_add_f16 v112, v207, v200 neg_lo:[0,1] neg_hi:[0,1]
	v_pk_add_f16 v113, v206, v201 neg_lo:[0,1] neg_hi:[0,1]
	v_exp_f16_sdwa v114, v110 dst_sel:WORD_0 dst_unused:UNUSED_PAD src0_sel:WORD_0
	v_exp_f16_sdwa v115, v111 dst_sel:WORD_0 dst_unused:UNUSED_PAD src0_sel:WORD_0
	v_exp_f16_sdwa v116, v112 dst_sel:WORD_0 dst_unused:UNUSED_PAD src0_sel:WORD_0
	v_exp_f16_sdwa v117, v113 dst_sel:WORD_0 dst_unused:UNUSED_PAD src0_sel:WORD_0
	v_exp_f16_sdwa v114, v110 dst_sel:WORD_1 dst_unused:UNUSED_PRESERVE src0_sel:WORD_1
	v_exp_f16_sdwa v115, v111 dst_sel:WORD_1 dst_unused:UNUSED_PRESERVE src0_sel:WORD_1
	v_exp_f16_sdwa v116, v112 dst_sel:WORD_1 dst_unused:UNUSED_PRESERVE src0_sel:WORD_1
	v_exp_f16_sdwa v117, v113 dst_sel:WORD_1 dst_unused:UNUSED_PRESERVE src0_sel:WORD_1
	v_pk_add_f16 v110, v213, v198 neg_lo:[0,1] neg_hi:[0,1]
	v_pk_add_f16 v101, v101, v114
	v_pk_add_f16 v98, v98, v117
	v_pk_add_f16 v99, v99, v116
	v_pk_add_f16 v100, v100, v115
	v_pk_fma_f16 v73, v65, v117, v73
	v_pk_fma_f16 v72, v64, v116, v72
	s_mov_b64 exec, s[70:71]
	buffer_load_dwordx4 v[138:141], v254, s[16:19], 0 offen offset:512
	buffer_load_dwordx4 v[90:93], v254, s[16:19], 0 offen offset:1024
	s_mov_b64 exec, -1
	v_pk_fma_f16 v71, v63, v115, v71
	v_pk_fma_f16 v70, v62, v114, v70
	v_pk_add_f16 v111, v212, v199 neg_lo:[0,1] neg_hi:[0,1]
	v_pk_add_f16 v112, v211, v200 neg_lo:[0,1] neg_hi:[0,1]
	v_pk_add_f16 v113, v210, v201 neg_lo:[0,1] neg_hi:[0,1]
	v_exp_f16_sdwa v114, v110 dst_sel:WORD_0 dst_unused:UNUSED_PAD src0_sel:WORD_0
	v_exp_f16_sdwa v115, v111 dst_sel:WORD_0 dst_unused:UNUSED_PAD src0_sel:WORD_0
	v_exp_f16_sdwa v116, v112 dst_sel:WORD_0 dst_unused:UNUSED_PAD src0_sel:WORD_0
	v_exp_f16_sdwa v117, v113 dst_sel:WORD_0 dst_unused:UNUSED_PAD src0_sel:WORD_0
	v_exp_f16_sdwa v114, v110 dst_sel:WORD_1 dst_unused:UNUSED_PRESERVE src0_sel:WORD_1
	v_exp_f16_sdwa v115, v111 dst_sel:WORD_1 dst_unused:UNUSED_PRESERVE src0_sel:WORD_1
	v_exp_f16_sdwa v116, v112 dst_sel:WORD_1 dst_unused:UNUSED_PRESERVE src0_sel:WORD_1
	v_exp_f16_sdwa v117, v113 dst_sel:WORD_1 dst_unused:UNUSED_PRESERVE src0_sel:WORD_1
	v_pk_add_f16 v110, v190, v198 neg_lo:[0,1] neg_hi:[0,1]
	v_pk_add_f16 v101, v101, v114
	v_pk_add_f16 v100, v100, v115
	v_pk_add_f16 v99, v99, v116
	v_pk_add_f16 v98, v98, v117
	v_pk_fma_f16 v70, v86, v114, v70
	v_pk_fma_f16 v71, v87, v115, v71
	v_pk_fma_f16 v72, v88, v116, v72
	v_pk_fma_f16 v73, v89, v117, v73
	s_mov_b64 exec, s[78:79]
	buffer_load_dwordx4 v[142:145], v254, s[16:19], 0 offen offset:2048
	buffer_load_dwordx4 v[2:5], v254, s[16:19], 0 offen offset:2560
	s_mov_b64 exec, -1
	v_pk_add_f16 v111, v191, v199 neg_lo:[0,1] neg_hi:[0,1]
	v_pk_add_f16 v112, v192, v200 neg_lo:[0,1] neg_hi:[0,1]
	v_pk_add_f16 v113, v193, v201 neg_lo:[0,1] neg_hi:[0,1]
	v_exp_f16_sdwa v114, v110 dst_sel:WORD_0 dst_unused:UNUSED_PAD src0_sel:WORD_0
	v_exp_f16_sdwa v115, v111 dst_sel:WORD_0 dst_unused:UNUSED_PAD src0_sel:WORD_0
	v_exp_f16_sdwa v116, v112 dst_sel:WORD_0 dst_unused:UNUSED_PAD src0_sel:WORD_0
	v_exp_f16_sdwa v117, v113 dst_sel:WORD_0 dst_unused:UNUSED_PAD src0_sel:WORD_0
	v_exp_f16_sdwa v114, v110 dst_sel:WORD_1 dst_unused:UNUSED_PRESERVE src0_sel:WORD_1
	v_exp_f16_sdwa v115, v111 dst_sel:WORD_1 dst_unused:UNUSED_PRESERVE src0_sel:WORD_1
	v_exp_f16_sdwa v116, v112 dst_sel:WORD_1 dst_unused:UNUSED_PRESERVE src0_sel:WORD_1
	v_exp_f16_sdwa v117, v113 dst_sel:WORD_1 dst_unused:UNUSED_PRESERVE src0_sel:WORD_1
	v_pk_add_f16 v110, v194, v198 neg_lo:[0,1] neg_hi:[0,1]
	v_pk_add_f16 v101, v101, v114
	v_pk_add_f16 v98, v98, v117
	v_pk_add_f16 v99, v99, v116
	v_pk_add_f16 v100, v100, v115
	v_pk_fma_f16 v73, v25, v117, v73
	v_pk_fma_f16 v72, v24, v116, v72
	v_pk_fma_f16 v71, v23, v115, v71
	v_pk_fma_f16 v70, v22, v114, v70
	v_pk_add_f16 v111, v195, v199 neg_lo:[0,1] neg_hi:[0,1]
	v_pk_add_f16 v112, v196, v200 neg_lo:[0,1] neg_hi:[0,1]
	v_pk_add_f16 v113, v197, v201 neg_lo:[0,1] neg_hi:[0,1]
	v_exp_f16_sdwa v114, v110 dst_sel:WORD_0 dst_unused:UNUSED_PAD src0_sel:WORD_0
	v_exp_f16_sdwa v115, v111 dst_sel:WORD_0 dst_unused:UNUSED_PAD src0_sel:WORD_0
	v_exp_f16_sdwa v116, v112 dst_sel:WORD_0 dst_unused:UNUSED_PAD src0_sel:WORD_0
	v_exp_f16_sdwa v117, v113 dst_sel:WORD_0 dst_unused:UNUSED_PAD src0_sel:WORD_0
	v_exp_f16_sdwa v114, v110 dst_sel:WORD_1 dst_unused:UNUSED_PRESERVE src0_sel:WORD_1
	v_exp_f16_sdwa v115, v111 dst_sel:WORD_1 dst_unused:UNUSED_PRESERVE src0_sel:WORD_1
	v_exp_f16_sdwa v116, v112 dst_sel:WORD_1 dst_unused:UNUSED_PRESERVE src0_sel:WORD_1
	v_exp_f16_sdwa v117, v113 dst_sel:WORD_1 dst_unused:UNUSED_PRESERVE src0_sel:WORD_1
	v_pk_add_f16 v110, v186, v198 neg_lo:[0,1] neg_hi:[0,1]
	v_pk_add_f16 v101, v101, v114
	v_pk_add_f16 v100, v100, v115
	v_pk_add_f16 v99, v99, v116
	v_pk_add_f16 v98, v98, v117
	v_pk_fma_f16 v70, v30, v114, v70
	v_pk_fma_f16 v71, v31, v115, v71
	v_pk_fma_f16 v72, v32, v116, v72
	v_pk_fma_f16 v73, v33, v117, v73
	v_pk_add_f16 v111, v187, v199 neg_lo:[0,1] neg_hi:[0,1]
	v_pk_add_f16 v112, v188, v200 neg_lo:[0,1] neg_hi:[0,1]
	v_pk_add_f16 v113, v189, v201 neg_lo:[0,1] neg_hi:[0,1]
	v_exp_f16_sdwa v114, v110 dst_sel:WORD_0 dst_unused:UNUSED_PAD src0_sel:WORD_0
	v_exp_f16_sdwa v115, v111 dst_sel:WORD_0 dst_unused:UNUSED_PAD src0_sel:WORD_0
	v_exp_f16_sdwa v116, v112 dst_sel:WORD_0 dst_unused:UNUSED_PAD src0_sel:WORD_0
	v_exp_f16_sdwa v117, v113 dst_sel:WORD_0 dst_unused:UNUSED_PAD src0_sel:WORD_0
	v_exp_f16_sdwa v114, v110 dst_sel:WORD_1 dst_unused:UNUSED_PRESERVE src0_sel:WORD_1
	v_exp_f16_sdwa v115, v111 dst_sel:WORD_1 dst_unused:UNUSED_PRESERVE src0_sel:WORD_1
	v_exp_f16_sdwa v116, v112 dst_sel:WORD_1 dst_unused:UNUSED_PRESERVE src0_sel:WORD_1
	v_exp_f16_sdwa v117, v113 dst_sel:WORD_1 dst_unused:UNUSED_PRESERVE src0_sel:WORD_1
	v_pk_add_f16 v101, v101, v114
	v_pk_add_f16 v100, v100, v115
	v_rcp_f16_e32 v110, v101
	v_rcp_f16_sdwa v101, v101 dst_sel:DWORD dst_unused:UNUSED_PAD src0_sel:WORD_1
	v_pk_add_f16 v99, v99, v116
	v_rcp_f16_e32 v111, v100
	v_rcp_f16_sdwa v100, v100 dst_sel:DWORD dst_unused:UNUSED_PAD src0_sel:WORD_1
	v_pk_add_f16 v98, v98, v117
	v_rcp_f16_e32 v112, v99
	v_rcp_f16_sdwa v99, v99 dst_sel:DWORD dst_unused:UNUSED_PAD src0_sel:WORD_1
	v_rcp_f16_e32 v113, v98
	v_rcp_f16_sdwa v98, v98 dst_sel:DWORD dst_unused:UNUSED_PAD src0_sel:WORD_1
	v_pk_fma_f16 v70, v46, v114, v70
	v_pack_b32_f16 v101, v110, v101
	v_pk_fma_f16 v71, v47, v115, v71
	v_pk_mul_f16 v110, v70, v101
	v_pack_b32_f16 v70, v111, v100
	v_pk_fma_f16 v72, v48, v116, v72
	v_pk_mul_f16 v111, v71, v70
	v_pack_b32_f16 v70, v112, v99
	v_pk_fma_f16 v73, v49, v117, v73
	v_pk_mul_f16 v112, v72, v70
	v_pack_b32_f16 v70, v113, v98
	v_pk_mul_f16 v113, v73, v70
	s_waitcnt vmcnt(12)
	v_pk_mul_f16 v73, v185, v157 op_sel_hi:[0,1]
	v_pk_mul_f16 v101, v183, v157 op_sel_hi:[0,1]
	v_pk_mul_f16 v117, v184, v157 op_sel_hi:[0,1]
	v_pk_mul_f16 v70, v185, v154 op_sel_hi:[0,1]
	v_pk_mul_f16 v71, v185, v155 op_sel_hi:[0,1]
	v_pk_mul_f16 v72, v185, v156 op_sel_hi:[0,1]
	v_pk_mul_f16 v98, v183, v154 op_sel_hi:[0,1]
	v_pk_mul_f16 v99, v183, v155 op_sel_hi:[0,1]
	v_pk_mul_f16 v100, v183, v156 op_sel_hi:[0,1]
	v_pk_mul_f16 v114, v184, v154 op_sel_hi:[0,1]
	v_pk_mul_f16 v115, v184, v155 op_sel_hi:[0,1]
	v_pk_mul_f16 v116, v184, v156 op_sel_hi:[0,1]
	v_pk_fma_f16 v85, v85, v157, v73
	v_pk_fma_f16 v109, v109, v157, v101
	v_pk_fma_f16 v125, v125, v157, v117
	v_pk_fma_f16 v126, v53, v157, v73
	v_pk_fma_f16 v134, v69, v157, v101
	v_pk_fma_f16 v186, v97, v157, v117
	v_pk_fma_f16 v73, v21, v157, v73
	v_pk_fma_f16 v101, v37, v157, v101
	v_pk_fma_f16 v117, v57, v157, v117
	v_pk_maximum3_f16 v157, v85, v109, v125
	v_pk_fma_f16 v84, v84, v156, v72
	v_pk_fma_f16 v83, v83, v155, v71
	v_pk_fma_f16 v82, v82, v154, v70
	v_pk_fma_f16 v108, v108, v156, v100
	v_pk_fma_f16 v107, v107, v155, v99
	v_pk_fma_f16 v106, v106, v154, v98
	v_pk_fma_f16 v124, v124, v156, v116
	v_pk_fma_f16 v123, v123, v155, v115
	v_pk_fma_f16 v122, v122, v154, v114
	v_pk_fma_f16 v127, v52, v156, v72
	v_pk_fma_f16 v128, v51, v155, v71
	v_pk_fma_f16 v129, v50, v154, v70
	v_pk_fma_f16 v135, v68, v156, v100
	v_pk_fma_f16 v136, v67, v155, v99
	v_pk_fma_f16 v137, v66, v154, v98
	v_pk_fma_f16 v187, v96, v156, v116
	v_pk_fma_f16 v188, v95, v155, v115
	v_pk_fma_f16 v189, v94, v154, v114
	v_pk_fma_f16 v72, v20, v156, v72
	v_pk_fma_f16 v71, v19, v155, v71
	v_pk_fma_f16 v70, v18, v154, v70
	v_pk_fma_f16 v100, v36, v156, v100
	v_pk_fma_f16 v99, v35, v155, v99
	v_pk_fma_f16 v98, v34, v154, v98
	v_pk_fma_f16 v116, v56, v156, v116
	v_pk_fma_f16 v115, v55, v155, v115
	v_pk_fma_f16 v114, v54, v154, v114
	v_pk_maximum3_f16 v154, v82, v106, v122
	v_pk_maximum3_f16 v155, v83, v107, v123
	v_pk_maximum3_f16 v156, v84, v108, v124
	v_pk_maximum3_f16 v193, v126, v134, v186
	v_pk_maximum3_f16 v197, v73, v101, v117
	v_pk_maximum3_f16 v190, v129, v137, v189
	v_pk_maximum3_f16 v191, v128, v136, v188
	v_pk_maximum3_f16 v192, v127, v135, v187
	v_pk_maximum3_f16 v194, v70, v98, v114
	v_pk_maximum3_f16 v195, v71, v99, v115
	v_pk_maximum3_f16 v157, v157, v193, v197
	v_pk_maximum3_f16 v196, v72, v100, v116
	v_pk_maximum3_f16 v154, v154, v190, v194
	v_pk_maximum3_f16 v155, v155, v191, v195
	v_pk_maximum3_f16 v156, v156, v192, v196
	v_pk_add_f16 v85, v85, v157 neg_lo:[0,1] neg_hi:[0,1]
	v_pk_add_f16 v82, v82, v154 neg_lo:[0,1] neg_hi:[0,1]
	v_pk_add_f16 v83, v83, v155 neg_lo:[0,1] neg_hi:[0,1]
	v_pk_add_f16 v84, v84, v156 neg_lo:[0,1] neg_hi:[0,1]
	v_pk_add_f16 v106, v106, v154 neg_lo:[0,1] neg_hi:[0,1]
	v_exp_f16_sdwa v190, v82 dst_sel:WORD_0 dst_unused:UNUSED_PAD src0_sel:WORD_0
	v_exp_f16_sdwa v191, v83 dst_sel:WORD_0 dst_unused:UNUSED_PAD src0_sel:WORD_0
	v_exp_f16_sdwa v192, v84 dst_sel:WORD_0 dst_unused:UNUSED_PAD src0_sel:WORD_0
	v_exp_f16_sdwa v193, v85 dst_sel:WORD_0 dst_unused:UNUSED_PAD src0_sel:WORD_0
	v_exp_f16_sdwa v190, v82 dst_sel:WORD_1 dst_unused:UNUSED_PRESERVE src0_sel:WORD_1
	v_exp_f16_sdwa v191, v83 dst_sel:WORD_1 dst_unused:UNUSED_PRESERVE src0_sel:WORD_1
	v_exp_f16_sdwa v192, v84 dst_sel:WORD_1 dst_unused:UNUSED_PRESERVE src0_sel:WORD_1
	v_exp_f16_sdwa v193, v85 dst_sel:WORD_1 dst_unused:UNUSED_PRESERVE src0_sel:WORD_1
	v_pk_add_f16 v107, v107, v155 neg_lo:[0,1] neg_hi:[0,1]
	v_pk_add_f16 v85, v190, 0
	v_pk_fma_f16 v45, v45, v193, 0
	v_pk_add_f16 v82, v193, 0
	v_pk_add_f16 v83, v192, 0
	v_pk_add_f16 v84, v191, 0
	v_pk_fma_f16 v44, v44, v192, 0
	v_pk_fma_f16 v43, v43, v191, 0
	v_pk_fma_f16 v42, v42, v190, 0
	v_pk_add_f16 v108, v108, v156 neg_lo:[0,1] neg_hi:[0,1]
	v_pk_add_f16 v109, v109, v157 neg_lo:[0,1] neg_hi:[0,1]
	v_pk_add_f16 v70, v70, v154 neg_lo:[0,1] neg_hi:[0,1]
	v_exp_f16_sdwa v190, v106 dst_sel:WORD_0 dst_unused:UNUSED_PAD src0_sel:WORD_0
	v_exp_f16_sdwa v191, v107 dst_sel:WORD_0 dst_unused:UNUSED_PAD src0_sel:WORD_0
	v_exp_f16_sdwa v192, v108 dst_sel:WORD_0 dst_unused:UNUSED_PAD src0_sel:WORD_0
	v_exp_f16_sdwa v193, v109 dst_sel:WORD_0 dst_unused:UNUSED_PAD src0_sel:WORD_0
	v_exp_f16_sdwa v190, v106 dst_sel:WORD_1 dst_unused:UNUSED_PRESERVE src0_sel:WORD_1
	v_exp_f16_sdwa v191, v107 dst_sel:WORD_1 dst_unused:UNUSED_PRESERVE src0_sel:WORD_1
	v_exp_f16_sdwa v192, v108 dst_sel:WORD_1 dst_unused:UNUSED_PRESERVE src0_sel:WORD_1
	v_exp_f16_sdwa v193, v109 dst_sel:WORD_1 dst_unused:UNUSED_PRESERVE src0_sel:WORD_1
	v_pk_add_f16 v71, v71, v155 neg_lo:[0,1] neg_hi:[0,1]
	v_pk_add_f16 v85, v85, v190
	v_pk_fma_f16 v45, v65, v193, v45
	v_pk_add_f16 v65, v125, v157 neg_lo:[0,1] neg_hi:[0,1]
	v_pk_add_f16 v84, v84, v191
	v_pk_add_f16 v83, v83, v192
	v_pk_add_f16 v82, v82, v193
	v_pk_fma_f16 v42, v62, v190, v42
	v_pk_fma_f16 v43, v63, v191, v43
	v_pk_fma_f16 v44, v64, v192, v44
	v_pk_add_f16 v62, v122, v154 neg_lo:[0,1] neg_hi:[0,1]
	v_pk_add_f16 v63, v123, v155 neg_lo:[0,1] neg_hi:[0,1]
	v_pk_add_f16 v64, v124, v156 neg_lo:[0,1] neg_hi:[0,1]
	v_pk_add_f16 v72, v72, v156 neg_lo:[0,1] neg_hi:[0,1]
	v_exp_f16_sdwa v106, v62 dst_sel:WORD_0 dst_unused:UNUSED_PAD src0_sel:WORD_0
	v_exp_f16_sdwa v107, v63 dst_sel:WORD_0 dst_unused:UNUSED_PAD src0_sel:WORD_0
	v_exp_f16_sdwa v108, v64 dst_sel:WORD_0 dst_unused:UNUSED_PAD src0_sel:WORD_0
	v_exp_f16_sdwa v109, v65 dst_sel:WORD_0 dst_unused:UNUSED_PAD src0_sel:WORD_0
	v_exp_f16_sdwa v106, v62 dst_sel:WORD_1 dst_unused:UNUSED_PRESERVE src0_sel:WORD_1
	v_exp_f16_sdwa v107, v63 dst_sel:WORD_1 dst_unused:UNUSED_PRESERVE src0_sel:WORD_1
	v_exp_f16_sdwa v108, v64 dst_sel:WORD_1 dst_unused:UNUSED_PRESERVE src0_sel:WORD_1
	v_exp_f16_sdwa v109, v65 dst_sel:WORD_1 dst_unused:UNUSED_PRESERVE src0_sel:WORD_1
	v_pk_add_f16 v73, v73, v157 neg_lo:[0,1] neg_hi:[0,1]
	v_pk_add_f16 v65, v85, v106
	v_pk_add_f16 v62, v82, v109
	v_pk_add_f16 v63, v83, v108
	v_pk_add_f16 v64, v84, v107
	v_pk_fma_f16 v45, v89, v109, v45
	v_pk_fma_f16 v44, v88, v108, v44
	v_pk_fma_f16 v43, v87, v107, v43
	v_pk_fma_f16 v42, v86, v106, v42
	v_pk_add_f16 v82, v129, v154 neg_lo:[0,1] neg_hi:[0,1]
	v_pk_add_f16 v83, v128, v155 neg_lo:[0,1] neg_hi:[0,1]
	v_pk_add_f16 v84, v127, v156 neg_lo:[0,1] neg_hi:[0,1]
	v_pk_add_f16 v85, v126, v157 neg_lo:[0,1] neg_hi:[0,1]
	v_exp_f16_sdwa v86, v82 dst_sel:WORD_0 dst_unused:UNUSED_PAD src0_sel:WORD_0
	v_exp_f16_sdwa v87, v83 dst_sel:WORD_0 dst_unused:UNUSED_PAD src0_sel:WORD_0
	v_exp_f16_sdwa v88, v84 dst_sel:WORD_0 dst_unused:UNUSED_PAD src0_sel:WORD_0
	v_exp_f16_sdwa v89, v85 dst_sel:WORD_0 dst_unused:UNUSED_PAD src0_sel:WORD_0
	v_exp_f16_sdwa v86, v82 dst_sel:WORD_1 dst_unused:UNUSED_PRESERVE src0_sel:WORD_1
	v_exp_f16_sdwa v87, v83 dst_sel:WORD_1 dst_unused:UNUSED_PRESERVE src0_sel:WORD_1
	v_exp_f16_sdwa v88, v84 dst_sel:WORD_1 dst_unused:UNUSED_PRESERVE src0_sel:WORD_1
	v_exp_f16_sdwa v89, v85 dst_sel:WORD_1 dst_unused:UNUSED_PRESERVE src0_sel:WORD_1
	v_pk_add_f16 v82, v137, v154 neg_lo:[0,1] neg_hi:[0,1]
	v_pk_add_f16 v65, v65, v86
	v_pk_add_f16 v64, v64, v87
	v_pk_add_f16 v63, v63, v88
	v_pk_add_f16 v62, v62, v89
	v_pk_fma_f16 v42, v22, v86, v42
	v_pk_fma_f16 v43, v23, v87, v43
	v_pk_fma_f16 v44, v24, v88, v44
	v_pk_fma_f16 v45, v25, v89, v45
	v_pk_add_f16 v83, v136, v155 neg_lo:[0,1] neg_hi:[0,1]
	v_pk_add_f16 v84, v135, v156 neg_lo:[0,1] neg_hi:[0,1]
	v_pk_add_f16 v85, v134, v157 neg_lo:[0,1] neg_hi:[0,1]
	v_exp_f16_sdwa v86, v82 dst_sel:WORD_0 dst_unused:UNUSED_PAD src0_sel:WORD_0
	v_exp_f16_sdwa v87, v83 dst_sel:WORD_0 dst_unused:UNUSED_PAD src0_sel:WORD_0
	v_exp_f16_sdwa v88, v84 dst_sel:WORD_0 dst_unused:UNUSED_PAD src0_sel:WORD_0
	v_exp_f16_sdwa v89, v85 dst_sel:WORD_0 dst_unused:UNUSED_PAD src0_sel:WORD_0
	v_exp_f16_sdwa v86, v82 dst_sel:WORD_1 dst_unused:UNUSED_PRESERVE src0_sel:WORD_1
	v_exp_f16_sdwa v87, v83 dst_sel:WORD_1 dst_unused:UNUSED_PRESERVE src0_sel:WORD_1
	v_exp_f16_sdwa v88, v84 dst_sel:WORD_1 dst_unused:UNUSED_PRESERVE src0_sel:WORD_1
	v_exp_f16_sdwa v89, v85 dst_sel:WORD_1 dst_unused:UNUSED_PRESERVE src0_sel:WORD_1
	v_pk_add_f16 v82, v189, v154 neg_lo:[0,1] neg_hi:[0,1]
	v_pk_add_f16 v65, v65, v86
	v_pk_add_f16 v62, v62, v89
	v_pk_add_f16 v63, v63, v88
	v_pk_add_f16 v64, v64, v87
	v_pk_fma_f16 v45, v33, v89, v45
	v_pk_fma_f16 v44, v32, v88, v44
	v_pk_fma_f16 v43, v31, v87, v43
	v_pk_fma_f16 v42, v30, v86, v42
	v_pk_add_f16 v83, v188, v155 neg_lo:[0,1] neg_hi:[0,1]
	v_pk_add_f16 v84, v187, v156 neg_lo:[0,1] neg_hi:[0,1]
	v_pk_add_f16 v85, v186, v157 neg_lo:[0,1] neg_hi:[0,1]
	v_exp_f16_sdwa v86, v82 dst_sel:WORD_0 dst_unused:UNUSED_PAD src0_sel:WORD_0
	v_exp_f16_sdwa v87, v83 dst_sel:WORD_0 dst_unused:UNUSED_PAD src0_sel:WORD_0
	v_exp_f16_sdwa v88, v84 dst_sel:WORD_0 dst_unused:UNUSED_PAD src0_sel:WORD_0
	v_exp_f16_sdwa v89, v85 dst_sel:WORD_0 dst_unused:UNUSED_PAD src0_sel:WORD_0
	v_exp_f16_sdwa v86, v82 dst_sel:WORD_1 dst_unused:UNUSED_PRESERVE src0_sel:WORD_1
	v_exp_f16_sdwa v87, v83 dst_sel:WORD_1 dst_unused:UNUSED_PRESERVE src0_sel:WORD_1
	v_exp_f16_sdwa v88, v84 dst_sel:WORD_1 dst_unused:UNUSED_PRESERVE src0_sel:WORD_1
	v_exp_f16_sdwa v89, v85 dst_sel:WORD_1 dst_unused:UNUSED_PRESERVE src0_sel:WORD_1
	v_exp_f16_sdwa v82, v70 dst_sel:WORD_0 dst_unused:UNUSED_PAD src0_sel:WORD_0
	v_exp_f16_sdwa v83, v71 dst_sel:WORD_0 dst_unused:UNUSED_PAD src0_sel:WORD_0
	v_exp_f16_sdwa v84, v72 dst_sel:WORD_0 dst_unused:UNUSED_PAD src0_sel:WORD_0
	v_exp_f16_sdwa v85, v73 dst_sel:WORD_0 dst_unused:UNUSED_PAD src0_sel:WORD_0
	v_exp_f16_sdwa v82, v70 dst_sel:WORD_1 dst_unused:UNUSED_PRESERVE src0_sel:WORD_1
	v_exp_f16_sdwa v83, v71 dst_sel:WORD_1 dst_unused:UNUSED_PRESERVE src0_sel:WORD_1
	v_exp_f16_sdwa v84, v72 dst_sel:WORD_1 dst_unused:UNUSED_PRESERVE src0_sel:WORD_1
	v_exp_f16_sdwa v85, v73 dst_sel:WORD_1 dst_unused:UNUSED_PRESERVE src0_sel:WORD_1
	v_pk_add_f16 v70, v98, v154 neg_lo:[0,1] neg_hi:[0,1]
	v_pk_add_f16 v65, v65, v86
	v_pk_add_f16 v64, v64, v87
	v_pk_add_f16 v63, v63, v88
	v_pk_add_f16 v62, v62, v89
	v_pk_fma_f16 v42, v46, v86, v42
	v_pk_fma_f16 v43, v47, v87, v43
	v_pk_fma_f16 v44, v48, v88, v44
	v_pk_fma_f16 v45, v49, v89, v45
	v_pk_add_f16 v65, v65, v82
	v_pk_add_f16 v62, v62, v85
	v_pk_add_f16 v63, v63, v84
	v_pk_add_f16 v64, v64, v83
	v_pk_fma_f16 v45, v9, v85, v45
	v_pk_fma_f16 v44, v8, v84, v44
	v_pk_fma_f16 v43, v7, v83, v43
	v_pk_fma_f16 v42, v6, v82, v42
	v_pk_add_f16 v71, v99, v155 neg_lo:[0,1] neg_hi:[0,1]
	v_pk_add_f16 v72, v100, v156 neg_lo:[0,1] neg_hi:[0,1]
	v_pk_add_f16 v73, v101, v157 neg_lo:[0,1] neg_hi:[0,1]
	v_exp_f16_sdwa v82, v70 dst_sel:WORD_0 dst_unused:UNUSED_PAD src0_sel:WORD_0
	v_exp_f16_sdwa v83, v71 dst_sel:WORD_0 dst_unused:UNUSED_PAD src0_sel:WORD_0
	v_exp_f16_sdwa v84, v72 dst_sel:WORD_0 dst_unused:UNUSED_PAD src0_sel:WORD_0
	v_exp_f16_sdwa v85, v73 dst_sel:WORD_0 dst_unused:UNUSED_PAD src0_sel:WORD_0
	v_exp_f16_sdwa v82, v70 dst_sel:WORD_1 dst_unused:UNUSED_PRESERVE src0_sel:WORD_1
	v_exp_f16_sdwa v83, v71 dst_sel:WORD_1 dst_unused:UNUSED_PRESERVE src0_sel:WORD_1
	v_exp_f16_sdwa v84, v72 dst_sel:WORD_1 dst_unused:UNUSED_PRESERVE src0_sel:WORD_1
	v_exp_f16_sdwa v85, v73 dst_sel:WORD_1 dst_unused:UNUSED_PRESERVE src0_sel:WORD_1
	v_pk_add_f16 v70, v114, v154 neg_lo:[0,1] neg_hi:[0,1]
	v_pk_add_f16 v65, v65, v82
	v_pk_add_f16 v64, v64, v83
	v_pk_add_f16 v63, v63, v84
	v_pk_add_f16 v62, v62, v85
	v_pk_fma_f16 v42, v10, v82, v42
	v_pk_fma_f16 v43, v11, v83, v43
	v_pk_fma_f16 v44, v12, v84, v44
	v_pk_fma_f16 v45, v13, v85, v45
	v_pk_add_f16 v71, v115, v155 neg_lo:[0,1] neg_hi:[0,1]
	v_pk_add_f16 v72, v116, v156 neg_lo:[0,1] neg_hi:[0,1]
	v_pk_add_f16 v73, v117, v157 neg_lo:[0,1] neg_hi:[0,1]
	v_exp_f16_sdwa v82, v70 dst_sel:WORD_0 dst_unused:UNUSED_PAD src0_sel:WORD_0
	v_exp_f16_sdwa v83, v71 dst_sel:WORD_0 dst_unused:UNUSED_PAD src0_sel:WORD_0
	v_exp_f16_sdwa v84, v72 dst_sel:WORD_0 dst_unused:UNUSED_PAD src0_sel:WORD_0
	v_exp_f16_sdwa v85, v73 dst_sel:WORD_0 dst_unused:UNUSED_PAD src0_sel:WORD_0
	v_exp_f16_sdwa v82, v70 dst_sel:WORD_1 dst_unused:UNUSED_PRESERVE src0_sel:WORD_1
	v_exp_f16_sdwa v83, v71 dst_sel:WORD_1 dst_unused:UNUSED_PRESERVE src0_sel:WORD_1
	v_exp_f16_sdwa v84, v72 dst_sel:WORD_1 dst_unused:UNUSED_PRESERVE src0_sel:WORD_1
	v_exp_f16_sdwa v85, v73 dst_sel:WORD_1 dst_unused:UNUSED_PRESERVE src0_sel:WORD_1
	v_pk_add_f16 v65, v65, v82
	v_pk_add_f16 v64, v64, v83
	v_rcp_f16_e32 v70, v65
	v_rcp_f16_sdwa v65, v65 dst_sel:DWORD dst_unused:UNUSED_PAD src0_sel:WORD_1
	v_pk_add_f16 v63, v63, v84
	v_rcp_f16_e32 v71, v64
	v_rcp_f16_sdwa v64, v64 dst_sel:DWORD dst_unused:UNUSED_PAD src0_sel:WORD_1
	v_pk_add_f16 v62, v62, v85
	v_rcp_f16_e32 v72, v63
	v_rcp_f16_sdwa v73, v63 dst_sel:DWORD dst_unused:UNUSED_PAD src0_sel:WORD_1
	v_pk_fma_f16 v43, v15, v83, v43
	v_pk_fma_f16 v42, v14, v82, v42
	v_rcp_f16_e32 v82, v62
	v_rcp_f16_sdwa v83, v62 dst_sel:DWORD dst_unused:UNUSED_PAD src0_sel:WORD_1
	v_pack_b32_f16 v62, v70, v65
	v_pk_mul_f16 v62, v42, v62
	v_pack_b32_f16 v42, v71, v64
	v_pk_fma_f16 v44, v16, v84, v44
	v_pk_mul_f16 v63, v43, v42
	v_pack_b32_f16 v42, v72, v73
	v_pk_fma_f16 v45, v17, v85, v45
	v_pk_mul_f16 v64, v44, v42
	v_pack_b32_f16 v42, v82, v83
	v_pk_mul_f16 v65, v45, v42
	s_waitcnt vmcnt(6)
	v_pk_mul_f16 v42, v185, v150 op_sel_hi:[0,1]
	v_pk_mul_f16 v70, v183, v150 op_sel_hi:[0,1]
	v_pk_mul_f16 v82, v184, v150 op_sel_hi:[0,1]
	v_pk_mul_f16 v43, v185, v151 op_sel_hi:[0,1]
	v_pk_mul_f16 v44, v185, v152 op_sel_hi:[0,1]
	v_pk_mul_f16 v45, v185, v153 op_sel_hi:[0,1]
	v_pk_mul_f16 v71, v183, v151 op_sel_hi:[0,1]
	v_pk_mul_f16 v72, v183, v152 op_sel_hi:[0,1]
	v_pk_mul_f16 v73, v183, v153 op_sel_hi:[0,1]
	v_pk_mul_f16 v83, v184, v151 op_sel_hi:[0,1]
	v_pk_mul_f16 v84, v184, v152 op_sel_hi:[0,1]
	v_pk_mul_f16 v85, v184, v153 op_sel_hi:[0,1]
	v_pk_fma_f16 v50, v50, v150, v42
	v_pk_fma_f16 v66, v66, v150, v70
	v_pk_fma_f16 v89, v94, v150, v82
	v_pk_fma_f16 v53, v53, v153, v45
	v_pk_maximum3_f16 v114, v50, v66, v89
	v_pk_fma_f16 v52, v52, v152, v44
	v_pk_fma_f16 v51, v51, v151, v43
	v_pk_fma_f16 v69, v69, v153, v73
	v_pk_fma_f16 v68, v68, v152, v72
	v_pk_fma_f16 v67, v67, v151, v71
	v_pk_fma_f16 v86, v97, v153, v85
	v_pk_fma_f16 v87, v96, v152, v84
	v_pk_fma_f16 v88, v95, v151, v83
	v_pk_fma_f16 v97, v18, v150, v42
	v_pk_fma_f16 v101, v34, v150, v70
	v_pk_fma_f16 v109, v54, v150, v82
	v_pk_fma_f16 v42, v74, v150, v42
	v_pk_fma_f16 v70, v102, v150, v70
	v_pk_fma_f16 v82, v118, v150, v82
	v_pk_maximum3_f16 v115, v51, v67, v88
	v_pk_maximum3_f16 v116, v52, v68, v87
	v_pk_maximum3_f16 v117, v53, v69, v86
	v_pk_maximum3_f16 v122, v97, v101, v109
	v_pk_fma_f16 v94, v21, v153, v45
	v_pk_maximum3_f16 v126, v42, v70, v82
	v_pk_fma_f16 v95, v20, v152, v44
	v_pk_maximum3_f16 v114, v114, v122, v126
	v_pk_fma_f16 v96, v19, v151, v43
	v_pk_fma_f16 v98, v37, v153, v73
	v_pk_fma_f16 v99, v36, v152, v72
	v_pk_fma_f16 v100, v35, v151, v71
	v_pk_fma_f16 v106, v57, v153, v85
	v_pk_fma_f16 v107, v56, v152, v84
	v_pk_fma_f16 v108, v55, v151, v83
	v_pk_fma_f16 v45, v77, v153, v45
	v_pk_fma_f16 v44, v76, v152, v44
	v_pk_fma_f16 v43, v75, v151, v43
	v_pk_fma_f16 v73, v105, v153, v73
	v_pk_fma_f16 v72, v104, v152, v72
	v_pk_fma_f16 v71, v103, v151, v71
	v_pk_fma_f16 v85, v121, v153, v85
	v_pk_fma_f16 v84, v120, v152, v84
	v_pk_fma_f16 v83, v119, v151, v83
	v_pk_maximum3_f16 v123, v96, v100, v108
	v_pk_maximum3_f16 v124, v95, v99, v107
	v_pk_maximum3_f16 v125, v94, v98, v106
	v_pk_maximum3_f16 v128, v44, v72, v84
	v_pk_maximum3_f16 v129, v45, v73, v85
	v_pk_maximum3_f16 v127, v43, v71, v83
	v_pk_maximum3_f16 v115, v115, v123, v127
	v_pk_maximum3_f16 v116, v116, v124, v128
	v_pk_maximum3_f16 v117, v117, v125, v129
	v_pk_add_f16 v50, v50, v114 neg_lo:[0,1] neg_hi:[0,1]
	v_pk_add_f16 v51, v51, v115 neg_lo:[0,1] neg_hi:[0,1]
	v_pk_add_f16 v52, v52, v116 neg_lo:[0,1] neg_hi:[0,1]
	v_pk_add_f16 v53, v53, v117 neg_lo:[0,1] neg_hi:[0,1]
	v_pk_add_f16 v66, v66, v114 neg_lo:[0,1] neg_hi:[0,1]
	v_exp_f16_sdwa v122, v50 dst_sel:WORD_0 dst_unused:UNUSED_PAD src0_sel:WORD_0
	v_exp_f16_sdwa v123, v51 dst_sel:WORD_0 dst_unused:UNUSED_PAD src0_sel:WORD_0
	v_exp_f16_sdwa v124, v52 dst_sel:WORD_0 dst_unused:UNUSED_PAD src0_sel:WORD_0
	v_exp_f16_sdwa v125, v53 dst_sel:WORD_0 dst_unused:UNUSED_PAD src0_sel:WORD_0
	v_exp_f16_sdwa v122, v50 dst_sel:WORD_1 dst_unused:UNUSED_PRESERVE src0_sel:WORD_1
	v_exp_f16_sdwa v123, v51 dst_sel:WORD_1 dst_unused:UNUSED_PRESERVE src0_sel:WORD_1
	v_exp_f16_sdwa v124, v52 dst_sel:WORD_1 dst_unused:UNUSED_PRESERVE src0_sel:WORD_1
	v_exp_f16_sdwa v125, v53 dst_sel:WORD_1 dst_unused:UNUSED_PRESERVE src0_sel:WORD_1
	v_pk_add_f16 v67, v67, v115 neg_lo:[0,1] neg_hi:[0,1]
	v_pk_add_f16 v50, v125, 0
	v_pk_fma_f16 v22, v22, v122, 0
	v_pk_add_f16 v51, v124, 0
	v_pk_add_f16 v52, v123, 0
	v_pk_add_f16 v53, v122, 0
	v_pk_fma_f16 v23, v23, v123, 0
	v_pk_fma_f16 v24, v24, v124, 0
	v_pk_fma_f16 v25, v25, v125, 0
	v_pk_add_f16 v68, v68, v116 neg_lo:[0,1] neg_hi:[0,1]
	v_pk_add_f16 v69, v69, v117 neg_lo:[0,1] neg_hi:[0,1]
	v_pk_add_f16 v42, v42, v114 neg_lo:[0,1] neg_hi:[0,1]
	v_exp_f16_sdwa v122, v66 dst_sel:WORD_0 dst_unused:UNUSED_PAD src0_sel:WORD_0
	v_exp_f16_sdwa v123, v67 dst_sel:WORD_0 dst_unused:UNUSED_PAD src0_sel:WORD_0
	v_exp_f16_sdwa v124, v68 dst_sel:WORD_0 dst_unused:UNUSED_PAD src0_sel:WORD_0
	v_exp_f16_sdwa v125, v69 dst_sel:WORD_0 dst_unused:UNUSED_PAD src0_sel:WORD_0
	v_exp_f16_sdwa v122, v66 dst_sel:WORD_1 dst_unused:UNUSED_PRESERVE src0_sel:WORD_1
	v_exp_f16_sdwa v123, v67 dst_sel:WORD_1 dst_unused:UNUSED_PRESERVE src0_sel:WORD_1
	v_exp_f16_sdwa v124, v68 dst_sel:WORD_1 dst_unused:UNUSED_PRESERVE src0_sel:WORD_1
	v_exp_f16_sdwa v125, v69 dst_sel:WORD_1 dst_unused:UNUSED_PRESERVE src0_sel:WORD_1
	v_pk_add_f16 v43, v43, v115 neg_lo:[0,1] neg_hi:[0,1]
	v_pk_add_f16 v50, v50, v125
	v_pk_fma_f16 v22, v30, v122, v22
	v_pk_add_f16 v30, v89, v114 neg_lo:[0,1] neg_hi:[0,1]
	v_pk_add_f16 v53, v53, v122
	v_pk_add_f16 v52, v52, v123
	v_pk_add_f16 v51, v51, v124
	v_pk_fma_f16 v25, v33, v125, v25
	v_pk_fma_f16 v24, v32, v124, v24
	v_pk_fma_f16 v23, v31, v123, v23
	v_pk_add_f16 v31, v88, v115 neg_lo:[0,1] neg_hi:[0,1]
	v_pk_add_f16 v32, v87, v116 neg_lo:[0,1] neg_hi:[0,1]
	v_pk_add_f16 v33, v86, v117 neg_lo:[0,1] neg_hi:[0,1]
	v_pk_add_f16 v44, v44, v116 neg_lo:[0,1] neg_hi:[0,1]
	v_exp_f16_sdwa v66, v30 dst_sel:WORD_0 dst_unused:UNUSED_PAD src0_sel:WORD_0
	v_exp_f16_sdwa v67, v31 dst_sel:WORD_0 dst_unused:UNUSED_PAD src0_sel:WORD_0
	v_exp_f16_sdwa v68, v32 dst_sel:WORD_0 dst_unused:UNUSED_PAD src0_sel:WORD_0
	v_exp_f16_sdwa v69, v33 dst_sel:WORD_0 dst_unused:UNUSED_PAD src0_sel:WORD_0
	v_exp_f16_sdwa v66, v30 dst_sel:WORD_1 dst_unused:UNUSED_PRESERVE src0_sel:WORD_1
	v_exp_f16_sdwa v67, v31 dst_sel:WORD_1 dst_unused:UNUSED_PRESERVE src0_sel:WORD_1
	v_exp_f16_sdwa v68, v32 dst_sel:WORD_1 dst_unused:UNUSED_PRESERVE src0_sel:WORD_1
	v_exp_f16_sdwa v69, v33 dst_sel:WORD_1 dst_unused:UNUSED_PRESERVE src0_sel:WORD_1
	v_pk_add_f16 v45, v45, v117 neg_lo:[0,1] neg_hi:[0,1]
	v_pk_add_f16 v30, v50, v69
	v_pk_add_f16 v31, v51, v68
	v_pk_add_f16 v32, v52, v67
	v_pk_add_f16 v33, v53, v66
	v_pk_fma_f16 v22, v46, v66, v22
	v_pk_fma_f16 v23, v47, v67, v23
	v_pk_fma_f16 v24, v48, v68, v24
	v_pk_fma_f16 v25, v49, v69, v25
	v_pk_add_f16 v46, v97, v114 neg_lo:[0,1] neg_hi:[0,1]
	v_pk_add_f16 v47, v96, v115 neg_lo:[0,1] neg_hi:[0,1]
	v_pk_add_f16 v48, v95, v116 neg_lo:[0,1] neg_hi:[0,1]
	v_pk_add_f16 v49, v94, v117 neg_lo:[0,1] neg_hi:[0,1]
	v_exp_f16_sdwa v50, v46 dst_sel:WORD_0 dst_unused:UNUSED_PAD src0_sel:WORD_0
	v_exp_f16_sdwa v51, v47 dst_sel:WORD_0 dst_unused:UNUSED_PAD src0_sel:WORD_0
	v_exp_f16_sdwa v52, v48 dst_sel:WORD_0 dst_unused:UNUSED_PAD src0_sel:WORD_0
	v_exp_f16_sdwa v53, v49 dst_sel:WORD_0 dst_unused:UNUSED_PAD src0_sel:WORD_0
	v_exp_f16_sdwa v50, v46 dst_sel:WORD_1 dst_unused:UNUSED_PRESERVE src0_sel:WORD_1
	v_exp_f16_sdwa v51, v47 dst_sel:WORD_1 dst_unused:UNUSED_PRESERVE src0_sel:WORD_1
	v_exp_f16_sdwa v52, v48 dst_sel:WORD_1 dst_unused:UNUSED_PRESERVE src0_sel:WORD_1
	v_exp_f16_sdwa v53, v49 dst_sel:WORD_1 dst_unused:UNUSED_PRESERVE src0_sel:WORD_1
	v_pk_add_f16 v46, v101, v114 neg_lo:[0,1] neg_hi:[0,1]
	v_pk_add_f16 v30, v30, v53
	v_pk_add_f16 v33, v33, v50
	v_pk_add_f16 v32, v32, v51
	v_pk_add_f16 v31, v31, v52
	v_pk_fma_f16 v25, v9, v53, v25
	v_pk_fma_f16 v24, v8, v52, v24
	v_pk_fma_f16 v23, v7, v51, v23
	v_pk_fma_f16 v22, v6, v50, v22
	v_pk_add_f16 v47, v100, v115 neg_lo:[0,1] neg_hi:[0,1]
	v_pk_add_f16 v48, v99, v116 neg_lo:[0,1] neg_hi:[0,1]
	v_pk_add_f16 v49, v98, v117 neg_lo:[0,1] neg_hi:[0,1]
	v_exp_f16_sdwa v50, v46 dst_sel:WORD_0 dst_unused:UNUSED_PAD src0_sel:WORD_0
	v_exp_f16_sdwa v51, v47 dst_sel:WORD_0 dst_unused:UNUSED_PAD src0_sel:WORD_0
	v_exp_f16_sdwa v52, v48 dst_sel:WORD_0 dst_unused:UNUSED_PAD src0_sel:WORD_0
	v_exp_f16_sdwa v53, v49 dst_sel:WORD_0 dst_unused:UNUSED_PAD src0_sel:WORD_0
	v_exp_f16_sdwa v50, v46 dst_sel:WORD_1 dst_unused:UNUSED_PRESERVE src0_sel:WORD_1
	v_exp_f16_sdwa v51, v47 dst_sel:WORD_1 dst_unused:UNUSED_PRESERVE src0_sel:WORD_1
	v_exp_f16_sdwa v52, v48 dst_sel:WORD_1 dst_unused:UNUSED_PRESERVE src0_sel:WORD_1
	v_exp_f16_sdwa v53, v49 dst_sel:WORD_1 dst_unused:UNUSED_PRESERVE src0_sel:WORD_1
	v_pk_add_f16 v46, v109, v114 neg_lo:[0,1] neg_hi:[0,1]
	v_pk_add_f16 v30, v30, v53
	v_pk_add_f16 v31, v31, v52
	v_pk_add_f16 v32, v32, v51
	v_pk_add_f16 v33, v33, v50
	v_pk_fma_f16 v22, v10, v50, v22
	v_pk_fma_f16 v23, v11, v51, v23
	v_pk_fma_f16 v24, v12, v52, v24
	v_pk_fma_f16 v25, v13, v53, v25
	v_pk_add_f16 v47, v108, v115 neg_lo:[0,1] neg_hi:[0,1]
	v_pk_add_f16 v48, v107, v116 neg_lo:[0,1] neg_hi:[0,1]
	v_pk_add_f16 v49, v106, v117 neg_lo:[0,1] neg_hi:[0,1]
	v_exp_f16_sdwa v50, v46 dst_sel:WORD_0 dst_unused:UNUSED_PAD src0_sel:WORD_0
	v_exp_f16_sdwa v51, v47 dst_sel:WORD_0 dst_unused:UNUSED_PAD src0_sel:WORD_0
	v_exp_f16_sdwa v52, v48 dst_sel:WORD_0 dst_unused:UNUSED_PAD src0_sel:WORD_0
	v_exp_f16_sdwa v53, v49 dst_sel:WORD_0 dst_unused:UNUSED_PAD src0_sel:WORD_0
	v_exp_f16_sdwa v50, v46 dst_sel:WORD_1 dst_unused:UNUSED_PRESERVE src0_sel:WORD_1
	v_exp_f16_sdwa v51, v47 dst_sel:WORD_1 dst_unused:UNUSED_PRESERVE src0_sel:WORD_1
	v_exp_f16_sdwa v52, v48 dst_sel:WORD_1 dst_unused:UNUSED_PRESERVE src0_sel:WORD_1
	v_exp_f16_sdwa v53, v49 dst_sel:WORD_1 dst_unused:UNUSED_PRESERVE src0_sel:WORD_1
	v_exp_f16_sdwa v46, v42 dst_sel:WORD_0 dst_unused:UNUSED_PAD src0_sel:WORD_0
	v_exp_f16_sdwa v47, v43 dst_sel:WORD_0 dst_unused:UNUSED_PAD src0_sel:WORD_0
	v_exp_f16_sdwa v48, v44 dst_sel:WORD_0 dst_unused:UNUSED_PAD src0_sel:WORD_0
	v_exp_f16_sdwa v49, v45 dst_sel:WORD_0 dst_unused:UNUSED_PAD src0_sel:WORD_0
	v_exp_f16_sdwa v46, v42 dst_sel:WORD_1 dst_unused:UNUSED_PRESERVE src0_sel:WORD_1
	v_exp_f16_sdwa v47, v43 dst_sel:WORD_1 dst_unused:UNUSED_PRESERVE src0_sel:WORD_1
	v_exp_f16_sdwa v48, v44 dst_sel:WORD_1 dst_unused:UNUSED_PRESERVE src0_sel:WORD_1
	v_exp_f16_sdwa v49, v45 dst_sel:WORD_1 dst_unused:UNUSED_PRESERVE src0_sel:WORD_1
	v_pk_add_f16 v42, v70, v114 neg_lo:[0,1] neg_hi:[0,1]
	v_pk_add_f16 v30, v30, v53
	v_pk_add_f16 v33, v33, v50
	v_pk_add_f16 v32, v32, v51
	v_pk_add_f16 v31, v31, v52
	v_pk_fma_f16 v25, v17, v53, v25
	v_pk_fma_f16 v24, v16, v52, v24
	v_pk_fma_f16 v23, v15, v51, v23
	v_pk_fma_f16 v22, v14, v50, v22
	v_pk_add_f16 v30, v30, v49
	v_pk_add_f16 v31, v31, v48
	v_pk_add_f16 v32, v32, v47
	v_pk_add_f16 v33, v33, v46
	v_pk_fma_f16 v22, v26, v46, v22
	v_pk_fma_f16 v23, v27, v47, v23
	v_pk_fma_f16 v24, v28, v48, v24
	v_pk_fma_f16 v25, v29, v49, v25
	v_pk_add_f16 v43, v71, v115 neg_lo:[0,1] neg_hi:[0,1]
	v_pk_add_f16 v44, v72, v116 neg_lo:[0,1] neg_hi:[0,1]
	v_pk_add_f16 v45, v73, v117 neg_lo:[0,1] neg_hi:[0,1]
	v_exp_f16_sdwa v46, v42 dst_sel:WORD_0 dst_unused:UNUSED_PAD src0_sel:WORD_0
	v_exp_f16_sdwa v47, v43 dst_sel:WORD_0 dst_unused:UNUSED_PAD src0_sel:WORD_0
	v_exp_f16_sdwa v48, v44 dst_sel:WORD_0 dst_unused:UNUSED_PAD src0_sel:WORD_0
	v_exp_f16_sdwa v49, v45 dst_sel:WORD_0 dst_unused:UNUSED_PAD src0_sel:WORD_0
	v_exp_f16_sdwa v46, v42 dst_sel:WORD_1 dst_unused:UNUSED_PRESERVE src0_sel:WORD_1
	v_exp_f16_sdwa v47, v43 dst_sel:WORD_1 dst_unused:UNUSED_PRESERVE src0_sel:WORD_1
	v_exp_f16_sdwa v48, v44 dst_sel:WORD_1 dst_unused:UNUSED_PRESERVE src0_sel:WORD_1
	v_exp_f16_sdwa v49, v45 dst_sel:WORD_1 dst_unused:UNUSED_PRESERVE src0_sel:WORD_1
	v_pk_add_f16 v42, v82, v114 neg_lo:[0,1] neg_hi:[0,1]
	v_pk_add_f16 v30, v30, v49
	v_pk_add_f16 v33, v33, v46
	v_pk_add_f16 v32, v32, v47
	v_pk_add_f16 v31, v31, v48
	v_pk_fma_f16 v25, v41, v49, v25
	v_pk_fma_f16 v24, v40, v48, v24
	v_pk_fma_f16 v23, v39, v47, v23
	v_pk_fma_f16 v22, v38, v46, v22
	v_pk_add_f16 v43, v83, v115 neg_lo:[0,1] neg_hi:[0,1]
	v_pk_add_f16 v44, v84, v116 neg_lo:[0,1] neg_hi:[0,1]
	v_pk_add_f16 v45, v85, v117 neg_lo:[0,1] neg_hi:[0,1]
	v_exp_f16_sdwa v46, v42 dst_sel:WORD_0 dst_unused:UNUSED_PAD src0_sel:WORD_0
	v_exp_f16_sdwa v47, v43 dst_sel:WORD_0 dst_unused:UNUSED_PAD src0_sel:WORD_0
	v_exp_f16_sdwa v48, v44 dst_sel:WORD_0 dst_unused:UNUSED_PAD src0_sel:WORD_0
	v_exp_f16_sdwa v49, v45 dst_sel:WORD_0 dst_unused:UNUSED_PAD src0_sel:WORD_0
	v_exp_f16_sdwa v46, v42 dst_sel:WORD_1 dst_unused:UNUSED_PRESERVE src0_sel:WORD_1
	v_exp_f16_sdwa v47, v43 dst_sel:WORD_1 dst_unused:UNUSED_PRESERVE src0_sel:WORD_1
	v_exp_f16_sdwa v48, v44 dst_sel:WORD_1 dst_unused:UNUSED_PRESERVE src0_sel:WORD_1
	v_exp_f16_sdwa v49, v45 dst_sel:WORD_1 dst_unused:UNUSED_PRESERVE src0_sel:WORD_1
	s_nop 0
	v_pk_add_f16 v30, v30, v49
	v_pk_add_f16 v31, v31, v48
	v_rcp_f16_e32 v44, v30
	v_rcp_f16_sdwa v30, v30 dst_sel:DWORD dst_unused:UNUSED_PAD src0_sel:WORD_1
	v_pk_add_f16 v32, v32, v47
	v_rcp_f16_e32 v45, v31
	v_rcp_f16_sdwa v31, v31 dst_sel:DWORD dst_unused:UNUSED_PAD src0_sel:WORD_1
	v_pk_add_f16 v33, v33, v46
	v_rcp_f16_e32 v43, v32
	v_rcp_f16_sdwa v32, v32 dst_sel:DWORD dst_unused:UNUSED_PAD src0_sel:WORD_1
	v_rcp_f16_e32 v42, v33
	v_rcp_f16_sdwa v33, v33 dst_sel:DWORD dst_unused:UNUSED_PAD src0_sel:WORD_1
	v_pk_fma_f16 v25, v61, v49, v25
	v_pack_b32_f16 v30, v44, v30
	v_pk_fma_f16 v24, v60, v48, v24
	v_pk_mul_f16 v25, v25, v30
	v_pack_b32_f16 v30, v45, v31
	v_pk_fma_f16 v23, v59, v47, v23
	v_pk_mul_f16 v24, v24, v30
	v_pack_b32_f16 v30, v43, v32
	v_pk_fma_f16 v22, v58, v46, v22
	v_pk_mul_f16 v23, v23, v30
	v_pack_b32_f16 v30, v42, v33
	v_pk_mul_f16 v22, v22, v30
	s_waitcnt vmcnt(0)
	s_cmp_lg_u32 s10, 1
	s_cbranch_scc1 .Lmywd3_0
	s_mul_i32 s84, s81, s83
	s_add_i32 s84, s84, s82
	s_mul_i32 s84, s84, 0x60000
	s_mul_i32 s85, s94, 0x6000
	s_add_u32 s84, s84, s85
	s_add_u32 s88, s86, s84
	s_addc_u32 s89, s87, 0
	v_mbcnt_lo_u32_b32 v251, -1, 0
	v_mbcnt_hi_u32_b32 v251, -1, v251
	v_lshlrev_b32_e32 v251, 4, v251
	global_load_dwordx4 v[252:255], v251, s[88:89]
	global_load_dwordx4 v[252:255], v251, s[88:89] offset:1024
	global_load_dwordx4 v[252:255], v251, s[88:89] offset:2048
	global_load_dwordx4 v[252:255], v251, s[88:89] offset:3072
	s_add_u32 s88, s88, 0x1000
	s_addc_u32 s89, s89, 0
	global_load_dwordx4 v[252:255], v251, s[88:89]
	global_load_dwordx4 v[252:255], v251, s[88:89] offset:1024
	global_load_dwordx4 v[252:255], v251, s[88:89] offset:2048
	global_load_dwordx4 v[252:255], v251, s[88:89] offset:3072
	s_add_u32 s88, s88, 0x1000
	s_addc_u32 s89, s89, 0
	global_load_dwordx4 v[252:255], v251, s[88:89]
	global_load_dwordx4 v[252:255], v251, s[88:89] offset:1024
	global_load_dwordx4 v[252:255], v251, s[88:89] offset:2048
	global_load_dwordx4 v[252:255], v251, s[88:89] offset:3072

_Z7k_stageILi1ELi4EEv8AttnArgsPKDF16_PKfPDF16_iii:
	s_load_dwordx2 s[86:87], s[0:1], 0x70
	s_load_dwordx2 s[82:83], s[0:1], 0x88
	s_mov_b32 s81, s3
	s_load_dwordx16 s[64:79], s[0:1], 0x0
	v_readfirstlane_b32 s94, v0
	s_nop 0
	s_lshr_b32 s94, s94, 6
	s_load_dwordx4 s[28:31], s[0:1], 0x70
	s_load_dwordx2 s[24:25], s[0:1], 0x80
	s_load_dword s33, s[0:1], 0x90
	s_lshl_b32 s4, s2, 5
	s_and_b32 s45, s4, 0xe0
	s_lshr_b32 s4, s2, 3
	s_add_i32 s45, s45, s4
	s_and_b32 s44, s2, 56
	v_readfirstlane_b32 s3, v0
	v_and_b32_e32 v1, 15, v0
	s_waitcnt lgkmcnt(0)
	s_cmp_lt_i32 s33, 1
	v_bfe_u32 v167, v0, 4, 2
	s_cbranch_scc1 .LBB4_155
	s_lshr_b32 s2, s3, 2
	v_lshrrev_b32_e32 v7, 7, v0
	v_lshrrev_b32_e32 v2, 5, v0
	v_lshrrev_b32_e32 v3, 4, v0
	s_and_b32 s2, s2, 16
	v_lshrrev_b32_e32 v4, 6, v0
	v_and_b32_e32 v7, 1, v7
	v_and_b32_e32 v2, 4, v2
	v_or_b32_e32 v179, s2, v1
	v_and_b32_e32 v5, 4, v4
	s_load_dwordx2 s[40:41], s[0:1], 0x60
	s_bitcmp1_b32 s3, 6
	v_lshlrev_b16_e32 v7, 2, v7
	v_and_b32_e32 v8, 3, v3
	s_load_dwordx4 s[36:39], s[0:1], 0x0
	s_load_dwordx2 s[4:5], s[0:1], 0x10
	s_load_dwordx8 s[8:15], s[0:1], 0x18
	s_load_dwordx2 s[6:7], s[0:1], 0x38
	s_load_dwordx8 s[16:23], s[0:1], 0x40
	v_or_b32_e32 v178, v2, v167
	v_and_or_b32 v180, s45, 56, v5
	s_cselect_b64 s[26:27], -1, 0
	s_and_b32 s3, s45, 0x3ffffc0
	v_bitop3_b16 v3, v7, v3, 3 bitop3:0xf8
	v_bitop3_b16 v7, v7, 8, v8 bitop3:0xfe
	v_lshlrev_b32_e32 v8, 12, v5
	v_bitop3_b32 v2, v2, v179, v167 bitop3:0x36
	v_or_b32_e32 v6, s3, v180
	s_and_b32 s3, s45, 0x1ffc0
	v_and_b32_e32 v3, 0xffff, v3
	v_lshl_or_b32 v184, v2, 4, v8
	v_lshlrev_b32_e32 v2, 3, v5
	v_mov_b32_e32 v169, 0
	v_lshlrev_b32_e32 v168, 5, v179
	v_lshlrev_b32_e32 v181, 6, v6
	v_or_b32_e32 v6, s3, v180
	v_and_b32_e32 v7, 0xffff, v7
	v_or_b32_e32 v186, 8, v2
	v_or_b32_e32 v188, 16, v2
	v_bitop3_b32 v2, s2, v3, v1 bitop3:0x36
	v_lshlrev_b32_e32 v166, 3, v179
	s_waitcnt lgkmcnt(0)
	v_lshl_add_u64 v[170:171], s[38:39], 0, v[168:169]
	s_mov_b32 s39, 0x20000
	v_lshlrev_b32_e32 v189, 4, v2
	v_bitop3_b32 v2, s2, v7, v1 bitop3:0x36
	v_lshlrev_b32_e32 v193, 15, v6
	v_lshl_add_u64 v[172:173], s[4:5], 0, v[168:169]
	s_and_b32 s37, s37, 0xffff
	s_mov_b32 s38, 0x1800000
	v_add_u32_e32 v182, -1, v180
	v_add_u32_e32 v183, 4, v180
	v_lshl_add_u64 v[174:175], s[14:15], 0, v[168:169]
	v_lshl_add_u64 v[176:177], s[6:7], 0, v[168:169]
	s_and_b32 s13, s13, 0xffff
	s_mov_b32 s42, 0x800000
	s_mov_b32 s43, s39
	s_and_b32 s41, s41, 0xffff
	v_or_b32_e32 v185, 64, v181
	v_or_b32_e32 v187, 0x80, v181
	v_or_b32_e32 v190, 0xc0, v181
	v_lshl_or_b32 v191, v4, 3, 24
	v_lshlrev_b32_e32 v192, 4, v2
	v_lshlrev_b32_e32 v194, 4, v179
	v_or_b32_e32 v195, 0x8000, v193
	v_or_b32_e32 v196, 0x10000, v193
	v_or_b32_e32 v197, 0x18000, v193
	s_mov_b32 s46, 0
	s_movk_i32 s47, 0x300
	v_lshlrev_b32_e32 v198, 1, v166
	s_branch .LBB4_4
.LBB4_2:
	s_waitcnt vmcnt(3)
	v_pk_mul_f16 v161, v160, v162 op_sel_hi:[0,1]
	v_pk_mul_f16 v206, v160, v165 op_sel_hi:[0,1]
	v_pk_mul_f16 v210, v158, v165 op_sel_hi:[0,1]
	v_pk_mul_f16 v214, v159, v165 op_sel_hi:[0,1]
	v_pk_mul_f16 v200, v160, v163 op_sel_hi:[0,1]
	v_pk_mul_f16 v201, v160, v164 op_sel_hi:[0,1]
	v_pk_mul_f16 v207, v158, v162 op_sel_hi:[0,1]
	s_mov_b64 exec, s[64:65]
	buffer_load_dwordx4 v[26:29], v245, s[12:15], 0 offen
	buffer_load_dwordx4 v[10:13], v245, s[12:15], 0 offen offset:512
	s_mov_b64 exec, -1
	v_pk_mul_f16 v208, v158, v163 op_sel_hi:[0,1]
	v_pk_mul_f16 v209, v158, v164 op_sel_hi:[0,1]
	v_pk_mul_f16 v211, v159, v162 op_sel_hi:[0,1]
	v_pk_mul_f16 v212, v159, v163 op_sel_hi:[0,1]
	v_pk_mul_f16 v213, v159, v164 op_sel_hi:[0,1]
	v_pk_fma_f16 v117, v117, v165, v206
	v_pk_fma_f16 v114, v114, v162, v161
	v_pk_fma_f16 v133, v133, v165, v206
	v_pk_fma_f16 v130, v130, v162, v161
	v_pk_fma_f16 v141, v141, v165, v206
	v_pk_fma_f16 v138, v138, v162, v161
	v_pk_fma_f16 v161, v89, v165, v210
	v_pk_fma_f16 v215, v113, v165, v210
	buffer_load_dwordx4 v[38:41], v246, s[12:15], 0 offen offset:512
	buffer_load_dwordx4 v[14:17], v246, s[12:15], 0 offen offset:1024
	v_pk_fma_f16 v210, v129, v165, v210
	v_pk_fma_f16 v219, v57, v165, v214
	v_pk_fma_f16 v223, v77, v165, v214
	v_pk_fma_f16 v165, v101, v165, v214
	v_pk_maximum3_f16 v214, v117, v133, v141
	v_pk_fma_f16 v116, v116, v164, v201
	v_pk_fma_f16 v115, v115, v163, v200
	v_pk_fma_f16 v132, v132, v164, v201
	v_pk_fma_f16 v131, v131, v163, v200
	v_pk_fma_f16 v140, v140, v164, v201
	v_pk_fma_f16 v139, v139, v163, v200
	v_pk_fma_f16 v200, v88, v164, v209
	v_pk_fma_f16 v201, v87, v163, v208
	v_pk_fma_f16 v206, v86, v162, v207
	v_pk_fma_f16 v216, v112, v164, v209
	v_pk_fma_f16 v217, v111, v163, v208
	s_mov_b64 exec, s[66:67]
	buffer_load_dwordx4 v[58:61], v246, s[12:15], 0 offen offset:2048
	buffer_load_dwordx4 v[18:21], v246, s[12:15], 0 offen offset:2560
	s_mov_b64 exec, -1
	v_pk_fma_f16 v218, v110, v162, v207
	v_pk_fma_f16 v209, v128, v164, v209
	v_pk_fma_f16 v208, v127, v163, v208
	v_pk_fma_f16 v207, v126, v162, v207
	v_pk_fma_f16 v220, v56, v164, v213
	v_pk_fma_f16 v221, v55, v163, v212
	v_pk_fma_f16 v222, v54, v162, v211
	v_pk_fma_f16 v224, v76, v164, v213
	v_pk_fma_f16 v225, v75, v163, v212
	v_pk_fma_f16 v226, v74, v162, v211
	v_pk_fma_f16 v164, v100, v164, v213
	v_pk_fma_f16 v163, v99, v163, v212
	v_pk_fma_f16 v162, v98, v162, v211
	v_pk_maximum3_f16 v211, v114, v130, v138
	v_pk_maximum3_f16 v212, v115, v131, v139
	v_pk_maximum3_f16 v213, v116, v132, v140
	v_pk_maximum3_f16 v230, v161, v215, v210
	v_pk_maximum3_f16 v234, v219, v223, v165
	v_pk_maximum3_f16 v227, v206, v218, v207
	v_pk_maximum3_f16 v228, v201, v217, v208
	v_pk_maximum3_f16 v229, v200, v216, v209
	v_pk_maximum3_f16 v231, v222, v226, v162
	v_pk_maximum3_f16 v232, v221, v225, v163
	v_pk_maximum3_f16 v214, v214, v230, v234
	v_pk_maximum3_f16 v233, v220, v224, v164
	v_pk_maximum3_f16 v211, v211, v227, v231
	v_pk_maximum3_f16 v212, v212, v228, v232
	v_pk_maximum3_f16 v213, v213, v229, v233
	v_pk_add_f16 v117, v117, v214 neg_lo:[0,1] neg_hi:[0,1]
	s_mov_b64 exec, s[64:65]
	buffer_load_dwordx4 v[78:81], v247, s[12:15], 0 offen
	buffer_load_dwordx4 v[30:33], v247, s[12:15], 0 offen offset:512
	s_mov_b64 exec, -1
	v_pk_add_f16 v114, v114, v211 neg_lo:[0,1] neg_hi:[0,1]
	v_pk_add_f16 v115, v115, v212 neg_lo:[0,1] neg_hi:[0,1]
	v_pk_add_f16 v116, v116, v213 neg_lo:[0,1] neg_hi:[0,1]
	v_pk_add_f16 v130, v130, v211 neg_lo:[0,1] neg_hi:[0,1]
	v_exp_f16_sdwa v227, v114 dst_sel:WORD_0 dst_unused:UNUSED_PAD src0_sel:WORD_0
	v_exp_f16_sdwa v228, v115 dst_sel:WORD_0 dst_unused:UNUSED_PAD src0_sel:WORD_0
	v_exp_f16_sdwa v229, v116 dst_sel:WORD_0 dst_unused:UNUSED_PAD src0_sel:WORD_0
	v_exp_f16_sdwa v230, v117 dst_sel:WORD_0 dst_unused:UNUSED_PAD src0_sel:WORD_0
	v_exp_f16_sdwa v227, v114 dst_sel:WORD_1 dst_unused:UNUSED_PRESERVE src0_sel:WORD_1
	v_exp_f16_sdwa v228, v115 dst_sel:WORD_1 dst_unused:UNUSED_PRESERVE src0_sel:WORD_1
	v_exp_f16_sdwa v229, v116 dst_sel:WORD_1 dst_unused:UNUSED_PRESERVE src0_sel:WORD_1
	v_exp_f16_sdwa v230, v117 dst_sel:WORD_1 dst_unused:UNUSED_PRESERVE src0_sel:WORD_1
	v_pk_add_f16 v131, v131, v212 neg_lo:[0,1] neg_hi:[0,1]
	v_pk_add_f16 v117, v227, 0
	v_pk_fma_f16 v73, v73, v230, 0
	v_pk_add_f16 v114, v230, 0
	v_pk_add_f16 v115, v229, 0
	v_pk_add_f16 v116, v228, 0
	v_pk_fma_f16 v72, v72, v229, 0
	v_pk_fma_f16 v71, v71, v228, 0
	v_pk_fma_f16 v70, v70, v227, 0
	v_pk_add_f16 v132, v132, v213 neg_lo:[0,1] neg_hi:[0,1]
	buffer_load_dwordx4 v[106:109], v248, s[12:15], 0 offen offset:512
	buffer_load_dwordx4 v[46:49], v248, s[12:15], 0 offen offset:1024
	v_pk_add_f16 v133, v133, v214 neg_lo:[0,1] neg_hi:[0,1]
	v_exp_f16_sdwa v227, v130 dst_sel:WORD_0 dst_unused:UNUSED_PAD src0_sel:WORD_0
	v_exp_f16_sdwa v228, v131 dst_sel:WORD_0 dst_unused:UNUSED_PAD src0_sel:WORD_0
	v_exp_f16_sdwa v229, v132 dst_sel:WORD_0 dst_unused:UNUSED_PAD src0_sel:WORD_0
	v_exp_f16_sdwa v230, v133 dst_sel:WORD_0 dst_unused:UNUSED_PAD src0_sel:WORD_0
	v_exp_f16_sdwa v227, v130 dst_sel:WORD_1 dst_unused:UNUSED_PRESERVE src0_sel:WORD_1
	v_exp_f16_sdwa v228, v131 dst_sel:WORD_1 dst_unused:UNUSED_PRESERVE src0_sel:WORD_1
	v_exp_f16_sdwa v229, v132 dst_sel:WORD_1 dst_unused:UNUSED_PRESERVE src0_sel:WORD_1
	v_exp_f16_sdwa v230, v133 dst_sel:WORD_1 dst_unused:UNUSED_PRESERVE src0_sel:WORD_1
	v_pk_add_f16 v117, v117, v227
	v_pk_fma_f16 v73, v97, v230, v73
	v_pk_add_f16 v97, v141, v214 neg_lo:[0,1] neg_hi:[0,1]
	v_pk_add_f16 v116, v116, v228
	v_pk_add_f16 v115, v115, v229
	v_pk_add_f16 v114, v114, v230
	v_pk_fma_f16 v70, v94, v227, v70
	v_pk_fma_f16 v71, v95, v228, v71
	v_pk_fma_f16 v72, v96, v229, v72
	v_pk_add_f16 v94, v138, v211 neg_lo:[0,1] neg_hi:[0,1]
	v_pk_add_f16 v95, v139, v212 neg_lo:[0,1] neg_hi:[0,1]
	v_pk_add_f16 v96, v140, v213 neg_lo:[0,1] neg_hi:[0,1]
	v_exp_f16_sdwa v130, v94 dst_sel:WORD_0 dst_unused:UNUSED_PAD src0_sel:WORD_0
	v_exp_f16_sdwa v131, v95 dst_sel:WORD_0 dst_unused:UNUSED_PAD src0_sel:WORD_0
	v_exp_f16_sdwa v132, v96 dst_sel:WORD_0 dst_unused:UNUSED_PAD src0_sel:WORD_0
	v_exp_f16_sdwa v133, v97 dst_sel:WORD_0 dst_unused:UNUSED_PAD src0_sel:WORD_0
	v_exp_f16_sdwa v130, v94 dst_sel:WORD_1 dst_unused:UNUSED_PRESERVE src0_sel:WORD_1
	v_exp_f16_sdwa v131, v95 dst_sel:WORD_1 dst_unused:UNUSED_PRESERVE src0_sel:WORD_1
	v_exp_f16_sdwa v132, v96 dst_sel:WORD_1 dst_unused:UNUSED_PRESERVE src0_sel:WORD_1
	v_exp_f16_sdwa v133, v97 dst_sel:WORD_1 dst_unused:UNUSED_PRESERVE src0_sel:WORD_1
	v_pk_add_f16 v97, v117, v130
	v_pk_add_f16 v94, v114, v133
	s_mov_b64 exec, s[66:67]
	buffer_load_dwordx4 v[122:125], v248, s[12:15], 0 offen offset:2048
	buffer_load_dwordx4 v[62:65], v248, s[12:15], 0 offen offset:2560
	s_mov_b64 exec, -1
	v_pk_add_f16 v95, v115, v132
	v_pk_add_f16 v96, v116, v131
	v_pk_fma_f16 v73, v121, v133, v73
	v_pk_fma_f16 v72, v120, v132, v72
	v_pk_fma_f16 v71, v119, v131, v71
	v_pk_fma_f16 v70, v118, v130, v70
	v_pk_add_f16 v114, v206, v211 neg_lo:[0,1] neg_hi:[0,1]
	v_pk_add_f16 v115, v201, v212 neg_lo:[0,1] neg_hi:[0,1]
	v_pk_add_f16 v116, v200, v213 neg_lo:[0,1] neg_hi:[0,1]
	v_pk_add_f16 v117, v161, v214 neg_lo:[0,1] neg_hi:[0,1]
	v_exp_f16_sdwa v118, v114 dst_sel:WORD_0 dst_unused:UNUSED_PAD src0_sel:WORD_0
	v_exp_f16_sdwa v119, v115 dst_sel:WORD_0 dst_unused:UNUSED_PAD src0_sel:WORD_0
	v_exp_f16_sdwa v120, v116 dst_sel:WORD_0 dst_unused:UNUSED_PAD src0_sel:WORD_0
	v_exp_f16_sdwa v121, v117 dst_sel:WORD_0 dst_unused:UNUSED_PAD src0_sel:WORD_0
	v_exp_f16_sdwa v118, v114 dst_sel:WORD_1 dst_unused:UNUSED_PRESERVE src0_sel:WORD_1
	v_exp_f16_sdwa v119, v115 dst_sel:WORD_1 dst_unused:UNUSED_PRESERVE src0_sel:WORD_1
	v_exp_f16_sdwa v120, v116 dst_sel:WORD_1 dst_unused:UNUSED_PRESERVE src0_sel:WORD_1
	v_exp_f16_sdwa v121, v117 dst_sel:WORD_1 dst_unused:UNUSED_PRESERVE src0_sel:WORD_1
	v_pk_add_f16 v114, v218, v211 neg_lo:[0,1] neg_hi:[0,1]
	v_pk_add_f16 v97, v97, v118
	v_pk_add_f16 v96, v96, v119
	v_pk_add_f16 v95, v95, v120
	s_mov_b64 exec, s[76:77]
	buffer_load_dwordx4 v[134:137], v249, s[12:15], 0 offen
	buffer_load_dwordx4 v[82:85], v249, s[12:15], 0 offen offset:512
	s_mov_b64 exec, -1
	v_pk_add_f16 v94, v94, v121
	v_pk_fma_f16 v70, v42, v118, v70
	v_pk_fma_f16 v71, v43, v119, v71
	v_pk_fma_f16 v72, v44, v120, v72
	v_pk_fma_f16 v73, v45, v121, v73
	v_pk_add_f16 v115, v217, v212 neg_lo:[0,1] neg_hi:[0,1]
	v_pk_add_f16 v116, v216, v213 neg_lo:[0,1] neg_hi:[0,1]
	v_pk_add_f16 v117, v215, v214 neg_lo:[0,1] neg_hi:[0,1]
	v_exp_f16_sdwa v118, v114 dst_sel:WORD_0 dst_unused:UNUSED_PAD src0_sel:WORD_0
	v_exp_f16_sdwa v119, v115 dst_sel:WORD_0 dst_unused:UNUSED_PAD src0_sel:WORD_0
	v_exp_f16_sdwa v120, v116 dst_sel:WORD_0 dst_unused:UNUSED_PAD src0_sel:WORD_0
	v_exp_f16_sdwa v121, v117 dst_sel:WORD_0 dst_unused:UNUSED_PAD src0_sel:WORD_0
	v_exp_f16_sdwa v118, v114 dst_sel:WORD_1 dst_unused:UNUSED_PRESERVE src0_sel:WORD_1
	v_exp_f16_sdwa v119, v115 dst_sel:WORD_1 dst_unused:UNUSED_PRESERVE src0_sel:WORD_1
	v_exp_f16_sdwa v120, v116 dst_sel:WORD_1 dst_unused:UNUSED_PRESERVE src0_sel:WORD_1
	v_exp_f16_sdwa v121, v117 dst_sel:WORD_1 dst_unused:UNUSED_PRESERVE src0_sel:WORD_1
	v_pk_add_f16 v114, v207, v211 neg_lo:[0,1] neg_hi:[0,1]
	v_pk_add_f16 v97, v97, v118
	v_pk_add_f16 v94, v94, v121
	v_pk_add_f16 v95, v95, v120
	v_pk_add_f16 v96, v96, v119
	v_pk_fma_f16 v73, v69, v121, v73
	v_pk_fma_f16 v72, v68, v120, v72
	s_mov_b64 exec, s[70:71]
	buffer_load_dwordx4 v[142:145], v250, s[12:15], 0 offen offset:512
	buffer_load_dwordx4 v[102:105], v250, s[12:15], 0 offen offset:1024
	s_mov_b64 exec, -1
	v_pk_fma_f16 v71, v67, v119, v71
	v_pk_fma_f16 v70, v66, v118, v70
	v_pk_add_f16 v115, v208, v212 neg_lo:[0,1] neg_hi:[0,1]
	v_pk_add_f16 v116, v209, v213 neg_lo:[0,1] neg_hi:[0,1]
	v_pk_add_f16 v117, v210, v214 neg_lo:[0,1] neg_hi:[0,1]
	v_exp_f16_sdwa v118, v114 dst_sel:WORD_0 dst_unused:UNUSED_PAD src0_sel:WORD_0
	v_exp_f16_sdwa v119, v115 dst_sel:WORD_0 dst_unused:UNUSED_PAD src0_sel:WORD_0
	v_exp_f16_sdwa v120, v116 dst_sel:WORD_0 dst_unused:UNUSED_PAD src0_sel:WORD_0
	v_exp_f16_sdwa v121, v117 dst_sel:WORD_0 dst_unused:UNUSED_PAD src0_sel:WORD_0
	v_exp_f16_sdwa v118, v114 dst_sel:WORD_1 dst_unused:UNUSED_PRESERVE src0_sel:WORD_1
	v_exp_f16_sdwa v119, v115 dst_sel:WORD_1 dst_unused:UNUSED_PRESERVE src0_sel:WORD_1
	v_exp_f16_sdwa v120, v116 dst_sel:WORD_1 dst_unused:UNUSED_PRESERVE src0_sel:WORD_1
	v_exp_f16_sdwa v121, v117 dst_sel:WORD_1 dst_unused:UNUSED_PRESERVE src0_sel:WORD_1
	v_pk_add_f16 v114, v222, v211 neg_lo:[0,1] neg_hi:[0,1]
	v_pk_add_f16 v97, v97, v118
	v_pk_add_f16 v96, v96, v119
	v_pk_add_f16 v95, v95, v120
	v_pk_add_f16 v94, v94, v121
	v_pk_fma_f16 v70, v90, v118, v70
	v_pk_fma_f16 v71, v91, v119, v71
	v_pk_fma_f16 v72, v92, v120, v72
	v_pk_fma_f16 v73, v93, v121, v73
	s_mov_b64 exec, s[78:79]
	buffer_load_dwordx4 v[6:9], v250, s[12:15], 0 offen offset:2048
	buffer_load_dwordx4 v[2:5], v250, s[12:15], 0 offen offset:2560
	s_mov_b64 exec, -1
	v_pk_add_f16 v115, v221, v212 neg_lo:[0,1] neg_hi:[0,1]
	v_pk_add_f16 v116, v220, v213 neg_lo:[0,1] neg_hi:[0,1]
	v_pk_add_f16 v117, v219, v214 neg_lo:[0,1] neg_hi:[0,1]
	v_exp_f16_sdwa v118, v114 dst_sel:WORD_0 dst_unused:UNUSED_PAD src0_sel:WORD_0
	v_exp_f16_sdwa v119, v115 dst_sel:WORD_0 dst_unused:UNUSED_PAD src0_sel:WORD_0
	v_exp_f16_sdwa v120, v116 dst_sel:WORD_0 dst_unused:UNUSED_PAD src0_sel:WORD_0
	v_exp_f16_sdwa v121, v117 dst_sel:WORD_0 dst_unused:UNUSED_PAD src0_sel:WORD_0
	v_exp_f16_sdwa v118, v114 dst_sel:WORD_1 dst_unused:UNUSED_PRESERVE src0_sel:WORD_1
	v_exp_f16_sdwa v119, v115 dst_sel:WORD_1 dst_unused:UNUSED_PRESERVE src0_sel:WORD_1
	v_exp_f16_sdwa v120, v116 dst_sel:WORD_1 dst_unused:UNUSED_PRESERVE src0_sel:WORD_1
	v_exp_f16_sdwa v121, v117 dst_sel:WORD_1 dst_unused:UNUSED_PRESERVE src0_sel:WORD_1
	v_pk_add_f16 v114, v226, v211 neg_lo:[0,1] neg_hi:[0,1]
	v_pk_add_f16 v97, v97, v118
	v_pk_add_f16 v94, v94, v121
	v_pk_add_f16 v95, v95, v120
	v_pk_add_f16 v96, v96, v119
	v_pk_fma_f16 v73, v25, v121, v73
	v_pk_fma_f16 v72, v24, v120, v72
	v_pk_fma_f16 v71, v23, v119, v71
	v_pk_fma_f16 v70, v22, v118, v70
	v_pk_add_f16 v115, v225, v212 neg_lo:[0,1] neg_hi:[0,1]
	v_pk_add_f16 v116, v224, v213 neg_lo:[0,1] neg_hi:[0,1]
	v_pk_add_f16 v117, v223, v214 neg_lo:[0,1] neg_hi:[0,1]
	v_exp_f16_sdwa v118, v114 dst_sel:WORD_0 dst_unused:UNUSED_PAD src0_sel:WORD_0
	v_exp_f16_sdwa v119, v115 dst_sel:WORD_0 dst_unused:UNUSED_PAD src0_sel:WORD_0
	v_exp_f16_sdwa v120, v116 dst_sel:WORD_0 dst_unused:UNUSED_PAD src0_sel:WORD_0
	v_exp_f16_sdwa v121, v117 dst_sel:WORD_0 dst_unused:UNUSED_PAD src0_sel:WORD_0
	v_exp_f16_sdwa v118, v114 dst_sel:WORD_1 dst_unused:UNUSED_PRESERVE src0_sel:WORD_1
	v_exp_f16_sdwa v119, v115 dst_sel:WORD_1 dst_unused:UNUSED_PRESERVE src0_sel:WORD_1
	v_exp_f16_sdwa v120, v116 dst_sel:WORD_1 dst_unused:UNUSED_PRESERVE src0_sel:WORD_1
	v_exp_f16_sdwa v121, v117 dst_sel:WORD_1 dst_unused:UNUSED_PRESERVE src0_sel:WORD_1
	v_pk_add_f16 v114, v162, v211 neg_lo:[0,1] neg_hi:[0,1]
	v_pk_add_f16 v97, v97, v118
	v_pk_add_f16 v96, v96, v119
	v_pk_add_f16 v95, v95, v120
	v_pk_add_f16 v94, v94, v121
	v_pk_fma_f16 v70, v34, v118, v70
	v_pk_fma_f16 v71, v35, v119, v71
	v_pk_fma_f16 v72, v36, v120, v72
	v_pk_fma_f16 v73, v37, v121, v73
	v_pk_add_f16 v115, v163, v212 neg_lo:[0,1] neg_hi:[0,1]
	v_pk_add_f16 v116, v164, v213 neg_lo:[0,1] neg_hi:[0,1]
	v_pk_add_f16 v117, v165, v214 neg_lo:[0,1] neg_hi:[0,1]
	v_exp_f16_sdwa v118, v114 dst_sel:WORD_0 dst_unused:UNUSED_PAD src0_sel:WORD_0
	v_exp_f16_sdwa v119, v115 dst_sel:WORD_0 dst_unused:UNUSED_PAD src0_sel:WORD_0
	v_exp_f16_sdwa v120, v116 dst_sel:WORD_0 dst_unused:UNUSED_PAD src0_sel:WORD_0
	v_exp_f16_sdwa v121, v117 dst_sel:WORD_0 dst_unused:UNUSED_PAD src0_sel:WORD_0
	v_exp_f16_sdwa v118, v114 dst_sel:WORD_1 dst_unused:UNUSED_PRESERVE src0_sel:WORD_1
	v_exp_f16_sdwa v119, v115 dst_sel:WORD_1 dst_unused:UNUSED_PRESERVE src0_sel:WORD_1
	v_exp_f16_sdwa v120, v116 dst_sel:WORD_1 dst_unused:UNUSED_PRESERVE src0_sel:WORD_1
	v_exp_f16_sdwa v121, v117 dst_sel:WORD_1 dst_unused:UNUSED_PRESERVE src0_sel:WORD_1
	v_pk_add_f16 v97, v97, v118
	v_pk_add_f16 v96, v96, v119
	v_rcp_f16_e32 v114, v97
	v_rcp_f16_sdwa v97, v97 dst_sel:DWORD dst_unused:UNUSED_PAD src0_sel:WORD_1
	v_pk_add_f16 v95, v95, v120
	v_rcp_f16_e32 v115, v96
	v_rcp_f16_sdwa v96, v96 dst_sel:DWORD dst_unused:UNUSED_PAD src0_sel:WORD_1
	v_pk_add_f16 v94, v94, v121
	v_rcp_f16_e32 v116, v95
	v_rcp_f16_sdwa v95, v95 dst_sel:DWORD dst_unused:UNUSED_PAD src0_sel:WORD_1
	v_rcp_f16_e32 v117, v94
	v_rcp_f16_sdwa v94, v94 dst_sel:DWORD dst_unused:UNUSED_PAD src0_sel:WORD_1
	v_pk_fma_f16 v70, v50, v118, v70
	v_pack_b32_f16 v97, v114, v97
	v_pk_fma_f16 v71, v51, v119, v71
	v_pk_mul_f16 v141, v70, v97
	v_pack_b32_f16 v70, v115, v96
	v_pk_fma_f16 v72, v52, v120, v72
	v_pk_mul_f16 v140, v71, v70
	v_pack_b32_f16 v70, v116, v95
	v_pk_fma_f16 v73, v53, v121, v73
	v_pk_mul_f16 v139, v72, v70
	v_pack_b32_f16 v70, v117, v94
	v_pk_mul_f16 v138, v73, v70
	s_waitcnt vmcnt(12)
	v_pk_mul_f16 v70, v160, v154 op_sel_hi:[0,1]
	v_pk_mul_f16 v73, v160, v157 op_sel_hi:[0,1]
	v_pk_mul_f16 v97, v158, v157 op_sel_hi:[0,1]
	v_pk_mul_f16 v117, v159, v157 op_sel_hi:[0,1]
	v_pk_mul_f16 v71, v160, v155 op_sel_hi:[0,1]
	v_pk_mul_f16 v72, v160, v156 op_sel_hi:[0,1]
	v_pk_mul_f16 v94, v158, v154 op_sel_hi:[0,1]
	v_pk_mul_f16 v95, v158, v155 op_sel_hi:[0,1]
	v_pk_mul_f16 v96, v158, v156 op_sel_hi:[0,1]
	v_pk_mul_f16 v114, v159, v154 op_sel_hi:[0,1]
	v_pk_mul_f16 v115, v159, v155 op_sel_hi:[0,1]
	v_pk_mul_f16 v116, v159, v156 op_sel_hi:[0,1]
	v_pk_fma_f16 v89, v89, v157, v73
	v_pk_fma_f16 v86, v86, v154, v70
	v_pk_fma_f16 v113, v113, v157, v73
	v_pk_fma_f16 v110, v110, v154, v70
	v_pk_fma_f16 v73, v129, v157, v73
	v_pk_fma_f16 v70, v126, v154, v70
	v_pk_fma_f16 v118, v57, v157, v97
	v_pk_fma_f16 v126, v77, v157, v97
	v_pk_fma_f16 v97, v101, v157, v97
	v_pk_fma_f16 v130, v29, v157, v117
	v_pk_fma_f16 v161, v41, v157, v117
	v_pk_fma_f16 v117, v61, v157, v117
	v_pk_maximum3_f16 v157, v89, v113, v73
	v_pk_fma_f16 v88, v88, v156, v72
	v_pk_fma_f16 v87, v87, v155, v71
	v_pk_fma_f16 v112, v112, v156, v72
	v_pk_fma_f16 v111, v111, v155, v71
	v_pk_fma_f16 v72, v128, v156, v72
	v_pk_fma_f16 v71, v127, v155, v71
	v_pk_fma_f16 v119, v56, v156, v96
	v_pk_fma_f16 v120, v55, v155, v95
	v_pk_fma_f16 v121, v54, v154, v94
	v_pk_fma_f16 v127, v76, v156, v96
	v_pk_fma_f16 v128, v75, v155, v95
	v_pk_fma_f16 v129, v74, v154, v94
	v_pk_fma_f16 v96, v100, v156, v96
	v_pk_fma_f16 v95, v99, v155, v95
	v_pk_fma_f16 v94, v98, v154, v94
	v_pk_fma_f16 v131, v28, v156, v116
	v_pk_fma_f16 v132, v27, v155, v115
	v_pk_fma_f16 v133, v26, v154, v114
	v_pk_fma_f16 v162, v40, v156, v116
	v_pk_fma_f16 v163, v39, v155, v115
	v_pk_fma_f16 v164, v38, v154, v114
	v_pk_fma_f16 v116, v60, v156, v116
	v_pk_fma_f16 v115, v59, v155, v115
	v_pk_fma_f16 v114, v58, v154, v114
	v_pk_maximum3_f16 v154, v86, v110, v70
	v_pk_maximum3_f16 v155, v87, v111, v71
	v_pk_maximum3_f16 v156, v88, v112, v72
	v_pk_maximum3_f16 v206, v118, v126, v97
	v_pk_maximum3_f16 v210, v130, v161, v117
	v_pk_maximum3_f16 v165, v121, v129, v94
	v_pk_maximum3_f16 v200, v120, v128, v95
	v_pk_maximum3_f16 v201, v119, v127, v96
	v_pk_maximum3_f16 v207, v133, v164, v114
	v_pk_maximum3_f16 v208, v132, v163, v115
	v_pk_maximum3_f16 v157, v157, v206, v210
	v_pk_maximum3_f16 v209, v131, v162, v116
	v_pk_maximum3_f16 v154, v154, v165, v207
	v_pk_maximum3_f16 v155, v155, v200, v208
	v_pk_maximum3_f16 v156, v156, v201, v209
	v_pk_add_f16 v89, v89, v157 neg_lo:[0,1] neg_hi:[0,1]
	v_pk_add_f16 v86, v86, v154 neg_lo:[0,1] neg_hi:[0,1]
	v_pk_add_f16 v87, v87, v155 neg_lo:[0,1] neg_hi:[0,1]
	v_pk_add_f16 v88, v88, v156 neg_lo:[0,1] neg_hi:[0,1]
	v_pk_add_f16 v110, v110, v154 neg_lo:[0,1] neg_hi:[0,1]
	v_exp_f16_sdwa v165, v86 dst_sel:WORD_0 dst_unused:UNUSED_PAD src0_sel:WORD_0
	v_exp_f16_sdwa v200, v87 dst_sel:WORD_0 dst_unused:UNUSED_PAD src0_sel:WORD_0
	v_exp_f16_sdwa v201, v88 dst_sel:WORD_0 dst_unused:UNUSED_PAD src0_sel:WORD_0
	v_exp_f16_sdwa v206, v89 dst_sel:WORD_0 dst_unused:UNUSED_PAD src0_sel:WORD_0
	v_exp_f16_sdwa v165, v86 dst_sel:WORD_1 dst_unused:UNUSED_PRESERVE src0_sel:WORD_1
	v_exp_f16_sdwa v200, v87 dst_sel:WORD_1 dst_unused:UNUSED_PRESERVE src0_sel:WORD_1
	v_exp_f16_sdwa v201, v88 dst_sel:WORD_1 dst_unused:UNUSED_PRESERVE src0_sel:WORD_1
	v_exp_f16_sdwa v206, v89 dst_sel:WORD_1 dst_unused:UNUSED_PRESERVE src0_sel:WORD_1
	v_pk_add_f16 v111, v111, v155 neg_lo:[0,1] neg_hi:[0,1]
	v_pk_add_f16 v89, v165, 0
	v_pk_fma_f16 v45, v45, v206, 0
	v_pk_add_f16 v86, v206, 0
	v_pk_add_f16 v87, v201, 0
	v_pk_add_f16 v88, v200, 0
	v_pk_fma_f16 v44, v44, v201, 0
	v_pk_fma_f16 v43, v43, v200, 0
	v_pk_fma_f16 v42, v42, v165, 0
	v_pk_add_f16 v112, v112, v156 neg_lo:[0,1] neg_hi:[0,1]
	v_pk_add_f16 v113, v113, v157 neg_lo:[0,1] neg_hi:[0,1]
	v_exp_f16_sdwa v165, v110 dst_sel:WORD_0 dst_unused:UNUSED_PAD src0_sel:WORD_0
	v_exp_f16_sdwa v200, v111 dst_sel:WORD_0 dst_unused:UNUSED_PAD src0_sel:WORD_0
	v_exp_f16_sdwa v201, v112 dst_sel:WORD_0 dst_unused:UNUSED_PAD src0_sel:WORD_0
	v_exp_f16_sdwa v206, v113 dst_sel:WORD_0 dst_unused:UNUSED_PAD src0_sel:WORD_0
	v_exp_f16_sdwa v165, v110 dst_sel:WORD_1 dst_unused:UNUSED_PRESERVE src0_sel:WORD_1
	v_exp_f16_sdwa v200, v111 dst_sel:WORD_1 dst_unused:UNUSED_PRESERVE src0_sel:WORD_1
	v_exp_f16_sdwa v201, v112 dst_sel:WORD_1 dst_unused:UNUSED_PRESERVE src0_sel:WORD_1
	v_exp_f16_sdwa v206, v113 dst_sel:WORD_1 dst_unused:UNUSED_PRESERVE src0_sel:WORD_1
	v_pk_add_f16 v89, v89, v165
	v_pk_fma_f16 v45, v69, v206, v45
	v_pk_add_f16 v69, v73, v157 neg_lo:[0,1] neg_hi:[0,1]
	v_pk_add_f16 v88, v88, v200
	v_pk_add_f16 v87, v87, v201
	v_pk_add_f16 v86, v86, v206
	v_pk_fma_f16 v42, v66, v165, v42
	v_pk_fma_f16 v43, v67, v200, v43
	v_pk_fma_f16 v44, v68, v201, v44
	v_pk_add_f16 v66, v70, v154 neg_lo:[0,1] neg_hi:[0,1]
	v_pk_add_f16 v67, v71, v155 neg_lo:[0,1] neg_hi:[0,1]
	v_pk_add_f16 v68, v72, v156 neg_lo:[0,1] neg_hi:[0,1]
	v_exp_f16_sdwa v70, v66 dst_sel:WORD_0 dst_unused:UNUSED_PAD src0_sel:WORD_0
	v_exp_f16_sdwa v71, v67 dst_sel:WORD_0 dst_unused:UNUSED_PAD src0_sel:WORD_0
	v_exp_f16_sdwa v72, v68 dst_sel:WORD_0 dst_unused:UNUSED_PAD src0_sel:WORD_0
	v_exp_f16_sdwa v73, v69 dst_sel:WORD_0 dst_unused:UNUSED_PAD src0_sel:WORD_0
	v_exp_f16_sdwa v70, v66 dst_sel:WORD_1 dst_unused:UNUSED_PRESERVE src0_sel:WORD_1
	v_exp_f16_sdwa v71, v67 dst_sel:WORD_1 dst_unused:UNUSED_PRESERVE src0_sel:WORD_1
	v_exp_f16_sdwa v72, v68 dst_sel:WORD_1 dst_unused:UNUSED_PRESERVE src0_sel:WORD_1
	v_exp_f16_sdwa v73, v69 dst_sel:WORD_1 dst_unused:UNUSED_PRESERVE src0_sel:WORD_1
	v_pk_add_f16 v69, v89, v70
	v_pk_add_f16 v66, v86, v73
	v_pk_add_f16 v67, v87, v72
	v_pk_add_f16 v68, v88, v71
	v_pk_fma_f16 v45, v93, v73, v45
	v_pk_fma_f16 v44, v92, v72, v44
	v_pk_fma_f16 v43, v91, v71, v43
	v_pk_fma_f16 v42, v90, v70, v42
	v_pk_add_f16 v70, v121, v154 neg_lo:[0,1] neg_hi:[0,1]
	v_pk_add_f16 v71, v120, v155 neg_lo:[0,1] neg_hi:[0,1]
	v_pk_add_f16 v72, v119, v156 neg_lo:[0,1] neg_hi:[0,1]
	v_pk_add_f16 v73, v118, v157 neg_lo:[0,1] neg_hi:[0,1]
	v_exp_f16_sdwa v86, v70 dst_sel:WORD_0 dst_unused:UNUSED_PAD src0_sel:WORD_0
	v_exp_f16_sdwa v87, v71 dst_sel:WORD_0 dst_unused:UNUSED_PAD src0_sel:WORD_0
	v_exp_f16_sdwa v88, v72 dst_sel:WORD_0 dst_unused:UNUSED_PAD src0_sel:WORD_0
	v_exp_f16_sdwa v89, v73 dst_sel:WORD_0 dst_unused:UNUSED_PAD src0_sel:WORD_0
	v_exp_f16_sdwa v86, v70 dst_sel:WORD_1 dst_unused:UNUSED_PRESERVE src0_sel:WORD_1
	v_exp_f16_sdwa v87, v71 dst_sel:WORD_1 dst_unused:UNUSED_PRESERVE src0_sel:WORD_1
	v_exp_f16_sdwa v88, v72 dst_sel:WORD_1 dst_unused:UNUSED_PRESERVE src0_sel:WORD_1
	v_exp_f16_sdwa v89, v73 dst_sel:WORD_1 dst_unused:UNUSED_PRESERVE src0_sel:WORD_1
	v_pk_add_f16 v70, v129, v154 neg_lo:[0,1] neg_hi:[0,1]
	v_pk_add_f16 v69, v69, v86
	v_pk_add_f16 v68, v68, v87
	v_pk_add_f16 v67, v67, v88
	v_pk_add_f16 v66, v66, v89
	v_pk_fma_f16 v42, v22, v86, v42
	v_pk_fma_f16 v43, v23, v87, v43
	v_pk_fma_f16 v44, v24, v88, v44
	v_pk_fma_f16 v45, v25, v89, v45
	v_pk_add_f16 v71, v128, v155 neg_lo:[0,1] neg_hi:[0,1]
	v_pk_add_f16 v72, v127, v156 neg_lo:[0,1] neg_hi:[0,1]
	v_pk_add_f16 v73, v126, v157 neg_lo:[0,1] neg_hi:[0,1]
	v_exp_f16_sdwa v86, v70 dst_sel:WORD_0 dst_unused:UNUSED_PAD src0_sel:WORD_0
	v_exp_f16_sdwa v87, v71 dst_sel:WORD_0 dst_unused:UNUSED_PAD src0_sel:WORD_0
	v_exp_f16_sdwa v88, v72 dst_sel:WORD_0 dst_unused:UNUSED_PAD src0_sel:WORD_0
	v_exp_f16_sdwa v89, v73 dst_sel:WORD_0 dst_unused:UNUSED_PAD src0_sel:WORD_0
	v_exp_f16_sdwa v86, v70 dst_sel:WORD_1 dst_unused:UNUSED_PRESERVE src0_sel:WORD_1
	v_exp_f16_sdwa v87, v71 dst_sel:WORD_1 dst_unused:UNUSED_PRESERVE src0_sel:WORD_1
	v_exp_f16_sdwa v88, v72 dst_sel:WORD_1 dst_unused:UNUSED_PRESERVE src0_sel:WORD_1
	v_exp_f16_sdwa v89, v73 dst_sel:WORD_1 dst_unused:UNUSED_PRESERVE src0_sel:WORD_1
	v_pk_add_f16 v70, v94, v154 neg_lo:[0,1] neg_hi:[0,1]
	v_pk_add_f16 v69, v69, v86
	v_pk_add_f16 v66, v66, v89
	v_pk_add_f16 v67, v67, v88
	v_pk_add_f16 v68, v68, v87
	v_pk_fma_f16 v45, v37, v89, v45
	v_pk_fma_f16 v44, v36, v88, v44
	v_pk_fma_f16 v43, v35, v87, v43
	v_pk_fma_f16 v42, v34, v86, v42
	v_pk_add_f16 v71, v95, v155 neg_lo:[0,1] neg_hi:[0,1]
	v_pk_add_f16 v72, v96, v156 neg_lo:[0,1] neg_hi:[0,1]
	v_pk_add_f16 v73, v97, v157 neg_lo:[0,1] neg_hi:[0,1]
	v_exp_f16_sdwa v86, v70 dst_sel:WORD_0 dst_unused:UNUSED_PAD src0_sel:WORD_0
	v_exp_f16_sdwa v87, v71 dst_sel:WORD_0 dst_unused:UNUSED_PAD src0_sel:WORD_0
	v_exp_f16_sdwa v88, v72 dst_sel:WORD_0 dst_unused:UNUSED_PAD src0_sel:WORD_0
	v_exp_f16_sdwa v89, v73 dst_sel:WORD_0 dst_unused:UNUSED_PAD src0_sel:WORD_0
	v_exp_f16_sdwa v86, v70 dst_sel:WORD_1 dst_unused:UNUSED_PRESERVE src0_sel:WORD_1
	v_exp_f16_sdwa v87, v71 dst_sel:WORD_1 dst_unused:UNUSED_PRESERVE src0_sel:WORD_1
	v_exp_f16_sdwa v88, v72 dst_sel:WORD_1 dst_unused:UNUSED_PRESERVE src0_sel:WORD_1
	v_exp_f16_sdwa v89, v73 dst_sel:WORD_1 dst_unused:UNUSED_PRESERVE src0_sel:WORD_1
	v_pk_add_f16 v70, v133, v154 neg_lo:[0,1] neg_hi:[0,1]
	v_pk_add_f16 v69, v69, v86
	v_pk_add_f16 v68, v68, v87
	v_pk_add_f16 v67, v67, v88
	v_pk_add_f16 v66, v66, v89
	v_pk_fma_f16 v42, v50, v86, v42
	v_pk_fma_f16 v43, v51, v87, v43
	v_pk_fma_f16 v44, v52, v88, v44
	v_pk_fma_f16 v45, v53, v89, v45
	v_pk_add_f16 v71, v132, v155 neg_lo:[0,1] neg_hi:[0,1]
	v_pk_add_f16 v72, v131, v156 neg_lo:[0,1] neg_hi:[0,1]
	v_pk_add_f16 v73, v130, v157 neg_lo:[0,1] neg_hi:[0,1]
	v_exp_f16_sdwa v86, v70 dst_sel:WORD_0 dst_unused:UNUSED_PAD src0_sel:WORD_0
	v_exp_f16_sdwa v87, v71 dst_sel:WORD_0 dst_unused:UNUSED_PAD src0_sel:WORD_0
	v_exp_f16_sdwa v88, v72 dst_sel:WORD_0 dst_unused:UNUSED_PAD src0_sel:WORD_0
	v_exp_f16_sdwa v89, v73 dst_sel:WORD_0 dst_unused:UNUSED_PAD src0_sel:WORD_0
	v_exp_f16_sdwa v86, v70 dst_sel:WORD_1 dst_unused:UNUSED_PRESERVE src0_sel:WORD_1
	v_exp_f16_sdwa v87, v71 dst_sel:WORD_1 dst_unused:UNUSED_PRESERVE src0_sel:WORD_1
	v_exp_f16_sdwa v88, v72 dst_sel:WORD_1 dst_unused:UNUSED_PRESERVE src0_sel:WORD_1
	v_exp_f16_sdwa v89, v73 dst_sel:WORD_1 dst_unused:UNUSED_PRESERVE src0_sel:WORD_1
	v_pk_add_f16 v70, v164, v154 neg_lo:[0,1] neg_hi:[0,1]
	v_pk_add_f16 v69, v69, v86
	v_pk_add_f16 v66, v66, v89
	v_pk_add_f16 v67, v67, v88
	v_pk_add_f16 v68, v68, v87
	v_pk_fma_f16 v45, v13, v89, v45
	v_pk_fma_f16 v44, v12, v88, v44
	v_pk_fma_f16 v43, v11, v87, v43
	v_pk_fma_f16 v42, v10, v86, v42
	v_pk_add_f16 v71, v163, v155 neg_lo:[0,1] neg_hi:[0,1]
	v_pk_add_f16 v72, v162, v156 neg_lo:[0,1] neg_hi:[0,1]
	v_pk_add_f16 v73, v161, v157 neg_lo:[0,1] neg_hi:[0,1]
	v_exp_f16_sdwa v86, v70 dst_sel:WORD_0 dst_unused:UNUSED_PAD src0_sel:WORD_0
	v_exp_f16_sdwa v87, v71 dst_sel:WORD_0 dst_unused:UNUSED_PAD src0_sel:WORD_0
	v_exp_f16_sdwa v88, v72 dst_sel:WORD_0 dst_unused:UNUSED_PAD src0_sel:WORD_0
	v_exp_f16_sdwa v89, v73 dst_sel:WORD_0 dst_unused:UNUSED_PAD src0_sel:WORD_0
	v_exp_f16_sdwa v86, v70 dst_sel:WORD_1 dst_unused:UNUSED_PRESERVE src0_sel:WORD_1
	v_exp_f16_sdwa v87, v71 dst_sel:WORD_1 dst_unused:UNUSED_PRESERVE src0_sel:WORD_1
	v_exp_f16_sdwa v88, v72 dst_sel:WORD_1 dst_unused:UNUSED_PRESERVE src0_sel:WORD_1
	v_exp_f16_sdwa v89, v73 dst_sel:WORD_1 dst_unused:UNUSED_PRESERVE src0_sel:WORD_1
	v_pk_add_f16 v70, v114, v154 neg_lo:[0,1] neg_hi:[0,1]
	v_pk_add_f16 v69, v69, v86
	v_pk_add_f16 v68, v68, v87
	v_pk_add_f16 v67, v67, v88
	v_pk_add_f16 v66, v66, v89
	v_pk_fma_f16 v42, v14, v86, v42
	v_pk_fma_f16 v43, v15, v87, v43
	v_pk_fma_f16 v44, v16, v88, v44
	v_pk_fma_f16 v45, v17, v89, v45
	v_pk_add_f16 v71, v115, v155 neg_lo:[0,1] neg_hi:[0,1]
	v_pk_add_f16 v72, v116, v156 neg_lo:[0,1] neg_hi:[0,1]
	v_pk_add_f16 v73, v117, v157 neg_lo:[0,1] neg_hi:[0,1]
	v_exp_f16_sdwa v86, v70 dst_sel:WORD_0 dst_unused:UNUSED_PAD src0_sel:WORD_0
	v_exp_f16_sdwa v87, v71 dst_sel:WORD_0 dst_unused:UNUSED_PAD src0_sel:WORD_0
	v_exp_f16_sdwa v88, v72 dst_sel:WORD_0 dst_unused:UNUSED_PAD src0_sel:WORD_0
	v_exp_f16_sdwa v89, v73 dst_sel:WORD_0 dst_unused:UNUSED_PAD src0_sel:WORD_0
	v_exp_f16_sdwa v86, v70 dst_sel:WORD_1 dst_unused:UNUSED_PRESERVE src0_sel:WORD_1
	v_exp_f16_sdwa v87, v71 dst_sel:WORD_1 dst_unused:UNUSED_PRESERVE src0_sel:WORD_1
	v_exp_f16_sdwa v88, v72 dst_sel:WORD_1 dst_unused:UNUSED_PRESERVE src0_sel:WORD_1
	v_exp_f16_sdwa v89, v73 dst_sel:WORD_1 dst_unused:UNUSED_PRESERVE src0_sel:WORD_1
	v_pk_add_f16 v69, v69, v86
	v_pk_add_f16 v68, v68, v87
	v_rcp_f16_e32 v70, v69
	v_rcp_f16_sdwa v69, v69 dst_sel:DWORD dst_unused:UNUSED_PAD src0_sel:WORD_1
	v_pk_add_f16 v67, v67, v88
	v_rcp_f16_e32 v71, v68
	v_rcp_f16_sdwa v68, v68 dst_sel:DWORD dst_unused:UNUSED_PAD src0_sel:WORD_1
	v_pk_add_f16 v66, v66, v89
	v_rcp_f16_e32 v72, v67
	v_rcp_f16_sdwa v67, v67 dst_sel:DWORD dst_unused:UNUSED_PAD src0_sel:WORD_1
	v_rcp_f16_e32 v73, v66
	v_rcp_f16_sdwa v66, v66 dst_sel:DWORD dst_unused:UNUSED_PAD src0_sel:WORD_1
	v_pk_fma_f16 v42, v18, v86, v42
	v_pack_b32_f16 v69, v70, v69
	v_pk_fma_f16 v43, v19, v87, v43
	v_pk_mul_f16 v97, v42, v69
	v_pack_b32_f16 v42, v71, v68
	v_pk_fma_f16 v44, v20, v88, v44
	v_pk_mul_f16 v96, v43, v42
	v_pack_b32_f16 v42, v72, v67
	v_pk_fma_f16 v45, v21, v89, v45
	v_pk_mul_f16 v95, v44, v42
	v_pack_b32_f16 v42, v73, v66
	v_pk_mul_f16 v94, v45, v42
	s_waitcnt vmcnt(6)
	v_pk_mul_f16 v45, v160, v153 op_sel_hi:[0,1]
	v_pk_mul_f16 v42, v160, v150 op_sel_hi:[0,1]
	v_pk_mul_f16 v43, v160, v151 op_sel_hi:[0,1]
	v_pk_mul_f16 v44, v160, v152 op_sel_hi:[0,1]
	v_pk_mul_f16 v69, v158, v153 op_sel_hi:[0,1]
	v_pk_mul_f16 v73, v159, v153 op_sel_hi:[0,1]
	v_pk_fma_f16 v57, v57, v153, v45
	v_pk_fma_f16 v77, v77, v153, v45
	v_pk_fma_f16 v45, v101, v153, v45
	v_pk_mul_f16 v66, v158, v150 op_sel_hi:[0,1]
	v_pk_maximum3_f16 v117, v57, v77, v45
	v_pk_mul_f16 v67, v158, v151 op_sel_hi:[0,1]
	v_pk_mul_f16 v68, v158, v152 op_sel_hi:[0,1]
	v_pk_mul_f16 v70, v159, v150 op_sel_hi:[0,1]
	v_pk_mul_f16 v71, v159, v151 op_sel_hi:[0,1]
	v_pk_mul_f16 v72, v159, v152 op_sel_hi:[0,1]
	v_pk_fma_f16 v56, v56, v152, v44
	v_pk_fma_f16 v55, v55, v151, v43
	v_pk_fma_f16 v54, v54, v150, v42
	v_pk_fma_f16 v76, v76, v152, v44
	v_pk_fma_f16 v75, v75, v151, v43
	v_pk_fma_f16 v74, v74, v150, v42
	v_pk_fma_f16 v44, v100, v152, v44
	v_pk_fma_f16 v43, v99, v151, v43
	v_pk_fma_f16 v42, v98, v150, v42
	v_pk_fma_f16 v86, v29, v153, v69
	v_pk_fma_f16 v90, v41, v153, v69
	v_pk_fma_f16 v69, v61, v153, v69
	v_pk_fma_f16 v98, v81, v153, v73
	v_pk_fma_f16 v110, v109, v153, v73
	v_pk_fma_f16 v73, v125, v153, v73
	v_pk_maximum3_f16 v114, v54, v74, v42
	v_pk_maximum3_f16 v115, v55, v75, v43
	v_pk_maximum3_f16 v116, v56, v76, v44
	v_pk_maximum3_f16 v121, v86, v90, v69
	v_pk_fma_f16 v87, v28, v152, v68
	v_pk_maximum3_f16 v129, v98, v110, v73
	v_pk_fma_f16 v88, v27, v151, v67
	v_pk_maximum3_f16 v117, v117, v121, v129
	v_pk_fma_f16 v89, v26, v150, v66
	v_pk_fma_f16 v91, v40, v152, v68
	v_pk_fma_f16 v92, v39, v151, v67
	v_pk_fma_f16 v93, v38, v150, v66
	v_pk_fma_f16 v68, v60, v152, v68
	v_pk_fma_f16 v67, v59, v151, v67
	v_pk_fma_f16 v66, v58, v150, v66
	v_pk_fma_f16 v99, v80, v152, v72
	v_pk_fma_f16 v100, v79, v151, v71
	v_pk_fma_f16 v101, v78, v150, v70
	v_pk_fma_f16 v111, v108, v152, v72
	v_pk_fma_f16 v112, v107, v151, v71
	v_pk_fma_f16 v113, v106, v150, v70
	v_pk_fma_f16 v72, v124, v152, v72
	v_pk_fma_f16 v71, v123, v151, v71
	v_pk_fma_f16 v70, v122, v150, v70
	v_pk_maximum3_f16 v118, v89, v93, v66
	v_pk_maximum3_f16 v119, v88, v92, v67
	v_pk_maximum3_f16 v120, v87, v91, v68
	v_pk_maximum3_f16 v127, v100, v112, v71
	v_pk_maximum3_f16 v128, v99, v111, v72
	v_pk_maximum3_f16 v126, v101, v113, v70
	v_pk_maximum3_f16 v114, v114, v118, v126
	v_pk_maximum3_f16 v115, v115, v119, v127
	v_pk_maximum3_f16 v116, v116, v120, v128
	v_pk_add_f16 v57, v57, v117 neg_lo:[0,1] neg_hi:[0,1]
	v_pk_add_f16 v54, v54, v114 neg_lo:[0,1] neg_hi:[0,1]
	v_pk_add_f16 v55, v55, v115 neg_lo:[0,1] neg_hi:[0,1]
	v_pk_add_f16 v56, v56, v116 neg_lo:[0,1] neg_hi:[0,1]
	v_pk_add_f16 v74, v74, v114 neg_lo:[0,1] neg_hi:[0,1]
	v_exp_f16_sdwa v118, v54 dst_sel:WORD_0 dst_unused:UNUSED_PAD src0_sel:WORD_0
	v_exp_f16_sdwa v119, v55 dst_sel:WORD_0 dst_unused:UNUSED_PAD src0_sel:WORD_0
	v_exp_f16_sdwa v120, v56 dst_sel:WORD_0 dst_unused:UNUSED_PAD src0_sel:WORD_0
	v_exp_f16_sdwa v121, v57 dst_sel:WORD_0 dst_unused:UNUSED_PAD src0_sel:WORD_0
	v_exp_f16_sdwa v118, v54 dst_sel:WORD_1 dst_unused:UNUSED_PRESERVE src0_sel:WORD_1
	v_exp_f16_sdwa v119, v55 dst_sel:WORD_1 dst_unused:UNUSED_PRESERVE src0_sel:WORD_1
	v_exp_f16_sdwa v120, v56 dst_sel:WORD_1 dst_unused:UNUSED_PRESERVE src0_sel:WORD_1
	v_exp_f16_sdwa v121, v57 dst_sel:WORD_1 dst_unused:UNUSED_PRESERVE src0_sel:WORD_1
	v_pk_add_f16 v75, v75, v115 neg_lo:[0,1] neg_hi:[0,1]
	v_pk_add_f16 v57, v118, 0
	v_pk_fma_f16 v25, v25, v121, 0
	v_pk_add_f16 v54, v121, 0
	v_pk_add_f16 v55, v120, 0
	v_pk_add_f16 v56, v119, 0
	v_pk_fma_f16 v24, v24, v120, 0
	v_pk_fma_f16 v23, v23, v119, 0
	v_pk_fma_f16 v22, v22, v118, 0
	v_pk_add_f16 v76, v76, v116 neg_lo:[0,1] neg_hi:[0,1]
	v_pk_add_f16 v77, v77, v117 neg_lo:[0,1] neg_hi:[0,1]
	v_exp_f16_sdwa v118, v74 dst_sel:WORD_0 dst_unused:UNUSED_PAD src0_sel:WORD_0
	v_exp_f16_sdwa v119, v75 dst_sel:WORD_0 dst_unused:UNUSED_PAD src0_sel:WORD_0
	v_exp_f16_sdwa v120, v76 dst_sel:WORD_0 dst_unused:UNUSED_PAD src0_sel:WORD_0
	v_exp_f16_sdwa v121, v77 dst_sel:WORD_0 dst_unused:UNUSED_PAD src0_sel:WORD_0
	v_exp_f16_sdwa v118, v74 dst_sel:WORD_1 dst_unused:UNUSED_PRESERVE src0_sel:WORD_1
	v_exp_f16_sdwa v119, v75 dst_sel:WORD_1 dst_unused:UNUSED_PRESERVE src0_sel:WORD_1
	v_exp_f16_sdwa v120, v76 dst_sel:WORD_1 dst_unused:UNUSED_PRESERVE src0_sel:WORD_1
	v_exp_f16_sdwa v121, v77 dst_sel:WORD_1 dst_unused:UNUSED_PRESERVE src0_sel:WORD_1
	v_pk_add_f16 v57, v57, v118
	v_pk_fma_f16 v25, v37, v121, v25
	v_pk_add_f16 v37, v45, v117 neg_lo:[0,1] neg_hi:[0,1]
	v_pk_add_f16 v56, v56, v119
	v_pk_add_f16 v55, v55, v120
	v_pk_add_f16 v54, v54, v121
	v_pk_fma_f16 v22, v34, v118, v22
	v_pk_fma_f16 v23, v35, v119, v23
	v_pk_fma_f16 v24, v36, v120, v24
	v_pk_add_f16 v34, v42, v114 neg_lo:[0,1] neg_hi:[0,1]
	v_pk_add_f16 v35, v43, v115 neg_lo:[0,1] neg_hi:[0,1]
	v_pk_add_f16 v36, v44, v116 neg_lo:[0,1] neg_hi:[0,1]
	v_exp_f16_sdwa v42, v34 dst_sel:WORD_0 dst_unused:UNUSED_PAD src0_sel:WORD_0
	v_exp_f16_sdwa v43, v35 dst_sel:WORD_0 dst_unused:UNUSED_PAD src0_sel:WORD_0
	v_exp_f16_sdwa v44, v36 dst_sel:WORD_0 dst_unused:UNUSED_PAD src0_sel:WORD_0
	v_exp_f16_sdwa v45, v37 dst_sel:WORD_0 dst_unused:UNUSED_PAD src0_sel:WORD_0
	v_exp_f16_sdwa v42, v34 dst_sel:WORD_1 dst_unused:UNUSED_PRESERVE src0_sel:WORD_1
	v_exp_f16_sdwa v43, v35 dst_sel:WORD_1 dst_unused:UNUSED_PRESERVE src0_sel:WORD_1
	v_exp_f16_sdwa v44, v36 dst_sel:WORD_1 dst_unused:UNUSED_PRESERVE src0_sel:WORD_1
	v_exp_f16_sdwa v45, v37 dst_sel:WORD_1 dst_unused:UNUSED_PRESERVE src0_sel:WORD_1
	v_pk_add_f16 v37, v57, v42
	v_pk_add_f16 v34, v54, v45
	v_pk_add_f16 v35, v55, v44
	v_pk_add_f16 v36, v56, v43
	v_pk_fma_f16 v25, v53, v45, v25
	v_pk_fma_f16 v24, v52, v44, v24
	v_pk_fma_f16 v23, v51, v43, v23
	v_pk_fma_f16 v22, v50, v42, v22
	v_pk_add_f16 v42, v89, v114 neg_lo:[0,1] neg_hi:[0,1]
	v_pk_add_f16 v43, v88, v115 neg_lo:[0,1] neg_hi:[0,1]
	v_pk_add_f16 v44, v87, v116 neg_lo:[0,1] neg_hi:[0,1]
	v_pk_add_f16 v45, v86, v117 neg_lo:[0,1] neg_hi:[0,1]
	v_exp_f16_sdwa v50, v42 dst_sel:WORD_0 dst_unused:UNUSED_PAD src0_sel:WORD_0
	v_exp_f16_sdwa v51, v43 dst_sel:WORD_0 dst_unused:UNUSED_PAD src0_sel:WORD_0
	v_exp_f16_sdwa v52, v44 dst_sel:WORD_0 dst_unused:UNUSED_PAD src0_sel:WORD_0
	v_exp_f16_sdwa v53, v45 dst_sel:WORD_0 dst_unused:UNUSED_PAD src0_sel:WORD_0
	v_exp_f16_sdwa v50, v42 dst_sel:WORD_1 dst_unused:UNUSED_PRESERVE src0_sel:WORD_1
	v_exp_f16_sdwa v51, v43 dst_sel:WORD_1 dst_unused:UNUSED_PRESERVE src0_sel:WORD_1
	v_exp_f16_sdwa v52, v44 dst_sel:WORD_1 dst_unused:UNUSED_PRESERVE src0_sel:WORD_1
	v_exp_f16_sdwa v53, v45 dst_sel:WORD_1 dst_unused:UNUSED_PRESERVE src0_sel:WORD_1
	v_pk_add_f16 v42, v93, v114 neg_lo:[0,1] neg_hi:[0,1]
	v_pk_add_f16 v37, v37, v50
	v_pk_add_f16 v36, v36, v51
	v_pk_add_f16 v35, v35, v52
	v_pk_add_f16 v34, v34, v53
	v_pk_fma_f16 v22, v10, v50, v22
	v_pk_fma_f16 v23, v11, v51, v23
	v_pk_fma_f16 v24, v12, v52, v24
	v_pk_fma_f16 v25, v13, v53, v25
	v_pk_add_f16 v43, v92, v115 neg_lo:[0,1] neg_hi:[0,1]
	v_pk_add_f16 v44, v91, v116 neg_lo:[0,1] neg_hi:[0,1]
	v_pk_add_f16 v45, v90, v117 neg_lo:[0,1] neg_hi:[0,1]
	v_exp_f16_sdwa v50, v42 dst_sel:WORD_0 dst_unused:UNUSED_PAD src0_sel:WORD_0
	v_exp_f16_sdwa v51, v43 dst_sel:WORD_0 dst_unused:UNUSED_PAD src0_sel:WORD_0
	v_exp_f16_sdwa v52, v44 dst_sel:WORD_0 dst_unused:UNUSED_PAD src0_sel:WORD_0
	v_exp_f16_sdwa v53, v45 dst_sel:WORD_0 dst_unused:UNUSED_PAD src0_sel:WORD_0
	v_exp_f16_sdwa v50, v42 dst_sel:WORD_1 dst_unused:UNUSED_PRESERVE src0_sel:WORD_1
	v_exp_f16_sdwa v51, v43 dst_sel:WORD_1 dst_unused:UNUSED_PRESERVE src0_sel:WORD_1
	v_exp_f16_sdwa v52, v44 dst_sel:WORD_1 dst_unused:UNUSED_PRESERVE src0_sel:WORD_1
	v_exp_f16_sdwa v53, v45 dst_sel:WORD_1 dst_unused:UNUSED_PRESERVE src0_sel:WORD_1
	v_pk_add_f16 v42, v66, v114 neg_lo:[0,1] neg_hi:[0,1]
	v_pk_add_f16 v37, v37, v50
	v_pk_add_f16 v34, v34, v53
	v_pk_add_f16 v35, v35, v52
	v_pk_add_f16 v36, v36, v51
	v_pk_fma_f16 v25, v17, v53, v25
	v_pk_fma_f16 v24, v16, v52, v24
	v_pk_fma_f16 v23, v15, v51, v23
	v_pk_fma_f16 v22, v14, v50, v22
	v_pk_add_f16 v43, v67, v115 neg_lo:[0,1] neg_hi:[0,1]
	v_pk_add_f16 v44, v68, v116 neg_lo:[0,1] neg_hi:[0,1]
	v_pk_add_f16 v45, v69, v117 neg_lo:[0,1] neg_hi:[0,1]
	v_exp_f16_sdwa v50, v42 dst_sel:WORD_0 dst_unused:UNUSED_PAD src0_sel:WORD_0
	v_exp_f16_sdwa v51, v43 dst_sel:WORD_0 dst_unused:UNUSED_PAD src0_sel:WORD_0
	v_exp_f16_sdwa v52, v44 dst_sel:WORD_0 dst_unused:UNUSED_PAD src0_sel:WORD_0
	v_exp_f16_sdwa v53, v45 dst_sel:WORD_0 dst_unused:UNUSED_PAD src0_sel:WORD_0
	v_exp_f16_sdwa v50, v42 dst_sel:WORD_1 dst_unused:UNUSED_PRESERVE src0_sel:WORD_1
	v_exp_f16_sdwa v51, v43 dst_sel:WORD_1 dst_unused:UNUSED_PRESERVE src0_sel:WORD_1
	v_exp_f16_sdwa v52, v44 dst_sel:WORD_1 dst_unused:UNUSED_PRESERVE src0_sel:WORD_1
	v_exp_f16_sdwa v53, v45 dst_sel:WORD_1 dst_unused:UNUSED_PRESERVE src0_sel:WORD_1
	v_pk_add_f16 v42, v101, v114 neg_lo:[0,1] neg_hi:[0,1]
	v_pk_add_f16 v37, v37, v50
	v_pk_add_f16 v36, v36, v51
	v_pk_add_f16 v35, v35, v52
	v_pk_add_f16 v34, v34, v53
	v_pk_fma_f16 v22, v18, v50, v22
	v_pk_fma_f16 v23, v19, v51, v23
	v_pk_fma_f16 v24, v20, v52, v24
	v_pk_fma_f16 v25, v21, v53, v25
	v_pk_add_f16 v43, v100, v115 neg_lo:[0,1] neg_hi:[0,1]
	v_pk_add_f16 v44, v99, v116 neg_lo:[0,1] neg_hi:[0,1]
	v_pk_add_f16 v45, v98, v117 neg_lo:[0,1] neg_hi:[0,1]
	v_exp_f16_sdwa v50, v42 dst_sel:WORD_0 dst_unused:UNUSED_PAD src0_sel:WORD_0
	v_exp_f16_sdwa v51, v43 dst_sel:WORD_0 dst_unused:UNUSED_PAD src0_sel:WORD_0
	v_exp_f16_sdwa v52, v44 dst_sel:WORD_0 dst_unused:UNUSED_PAD src0_sel:WORD_0
	v_exp_f16_sdwa v53, v45 dst_sel:WORD_0 dst_unused:UNUSED_PAD src0_sel:WORD_0
	v_exp_f16_sdwa v50, v42 dst_sel:WORD_1 dst_unused:UNUSED_PRESERVE src0_sel:WORD_1
	v_exp_f16_sdwa v51, v43 dst_sel:WORD_1 dst_unused:UNUSED_PRESERVE src0_sel:WORD_1
	v_exp_f16_sdwa v52, v44 dst_sel:WORD_1 dst_unused:UNUSED_PRESERVE src0_sel:WORD_1
	v_exp_f16_sdwa v53, v45 dst_sel:WORD_1 dst_unused:UNUSED_PRESERVE src0_sel:WORD_1
	v_pk_add_f16 v42, v113, v114 neg_lo:[0,1] neg_hi:[0,1]
	v_pk_add_f16 v37, v37, v50
	v_pk_add_f16 v34, v34, v53
	v_pk_add_f16 v35, v35, v52
	v_pk_add_f16 v36, v36, v51
	v_pk_fma_f16 v25, v33, v53, v25
	v_pk_fma_f16 v24, v32, v52, v24
	v_pk_fma_f16 v23, v31, v51, v23
	v_pk_fma_f16 v22, v30, v50, v22
	v_pk_add_f16 v43, v112, v115 neg_lo:[0,1] neg_hi:[0,1]
	v_pk_add_f16 v44, v111, v116 neg_lo:[0,1] neg_hi:[0,1]
	v_pk_add_f16 v45, v110, v117 neg_lo:[0,1] neg_hi:[0,1]
	v_exp_f16_sdwa v50, v42 dst_sel:WORD_0 dst_unused:UNUSED_PAD src0_sel:WORD_0
	v_exp_f16_sdwa v51, v43 dst_sel:WORD_0 dst_unused:UNUSED_PAD src0_sel:WORD_0
	v_exp_f16_sdwa v52, v44 dst_sel:WORD_0 dst_unused:UNUSED_PAD src0_sel:WORD_0
	v_exp_f16_sdwa v53, v45 dst_sel:WORD_0 dst_unused:UNUSED_PAD src0_sel:WORD_0
	v_exp_f16_sdwa v50, v42 dst_sel:WORD_1 dst_unused:UNUSED_PRESERVE src0_sel:WORD_1
	v_exp_f16_sdwa v51, v43 dst_sel:WORD_1 dst_unused:UNUSED_PRESERVE src0_sel:WORD_1
	v_exp_f16_sdwa v52, v44 dst_sel:WORD_1 dst_unused:UNUSED_PRESERVE src0_sel:WORD_1
	v_exp_f16_sdwa v53, v45 dst_sel:WORD_1 dst_unused:UNUSED_PRESERVE src0_sel:WORD_1
	v_pk_add_f16 v42, v70, v114 neg_lo:[0,1] neg_hi:[0,1]
	v_pk_add_f16 v37, v37, v50
	v_pk_add_f16 v36, v36, v51
	v_pk_add_f16 v35, v35, v52
	v_pk_add_f16 v34, v34, v53
	v_pk_fma_f16 v22, v46, v50, v22
	v_pk_fma_f16 v23, v47, v51, v23
	v_pk_fma_f16 v24, v48, v52, v24
	v_pk_fma_f16 v25, v49, v53, v25
	v_pk_add_f16 v43, v71, v115 neg_lo:[0,1] neg_hi:[0,1]
	v_pk_add_f16 v44, v72, v116 neg_lo:[0,1] neg_hi:[0,1]
	v_pk_add_f16 v45, v73, v117 neg_lo:[0,1] neg_hi:[0,1]
	v_exp_f16_sdwa v50, v42 dst_sel:WORD_0 dst_unused:UNUSED_PAD src0_sel:WORD_0
	v_exp_f16_sdwa v51, v43 dst_sel:WORD_0 dst_unused:UNUSED_PAD src0_sel:WORD_0
	v_exp_f16_sdwa v52, v44 dst_sel:WORD_0 dst_unused:UNUSED_PAD src0_sel:WORD_0
	v_exp_f16_sdwa v53, v45 dst_sel:WORD_0 dst_unused:UNUSED_PAD src0_sel:WORD_0
	v_exp_f16_sdwa v50, v42 dst_sel:WORD_1 dst_unused:UNUSED_PRESERVE src0_sel:WORD_1
	v_exp_f16_sdwa v51, v43 dst_sel:WORD_1 dst_unused:UNUSED_PRESERVE src0_sel:WORD_1
	v_exp_f16_sdwa v52, v44 dst_sel:WORD_1 dst_unused:UNUSED_PRESERVE src0_sel:WORD_1
	v_exp_f16_sdwa v53, v45 dst_sel:WORD_1 dst_unused:UNUSED_PRESERVE src0_sel:WORD_1
	v_pk_add_f16 v37, v37, v50
	v_pk_add_f16 v36, v36, v51
	v_rcp_f16_e32 v42, v37
	v_rcp_f16_sdwa v37, v37 dst_sel:DWORD dst_unused:UNUSED_PAD src0_sel:WORD_1
	v_pk_add_f16 v35, v35, v52
	v_rcp_f16_e32 v43, v36
	v_rcp_f16_sdwa v36, v36 dst_sel:DWORD dst_unused:UNUSED_PAD src0_sel:WORD_1
	v_pk_add_f16 v34, v34, v53
	v_pk_fma_f16 v22, v62, v50, v22
	v_rcp_f16_e32 v50, v35
	v_rcp_f16_sdwa v35, v35 dst_sel:DWORD dst_unused:UNUSED_PAD src0_sel:WORD_1
	v_pk_fma_f16 v23, v63, v51, v23
	v_rcp_f16_e32 v51, v34
	v_rcp_f16_sdwa v34, v34 dst_sel:DWORD dst_unused:UNUSED_PAD src0_sel:WORD_1
	v_pack_b32_f16 v37, v42, v37
	v_pk_mul_f16 v45, v22, v37
	v_pack_b32_f16 v22, v43, v36
	v_pk_fma_f16 v24, v64, v52, v24
	v_pk_mul_f16 v44, v23, v22
	v_pack_b32_f16 v22, v50, v35
	v_pk_fma_f16 v25, v65, v53, v25
	v_pk_mul_f16 v43, v24, v22
	v_pack_b32_f16 v22, v51, v34
	v_pk_mul_f16 v42, v25, v22
	s_waitcnt vmcnt(0)
	s_mul_i32 s84, s81, s83
	s_add_i32 s84, s84, s82
	s_mul_i32 s84, s84, 0x60000
	s_mul_i32 s85, s94, 0x6000
	s_add_u32 s84, s84, s85
	s_add_u32 s88, s86, s84
	s_addc_u32 s89, s87, 0
	v_mbcnt_lo_u32_b32 v251, -1, 0
	v_mbcnt_hi_u32_b32 v251, -1, v251
	v_lshlrev_b32_e32 v251, 4, v251
	global_load_dwordx4 v[252:255], v251, s[88:89]
	global_load_dwordx4 v[252:255], v251, s[88:89] offset:1024
	global_load_dwordx4 v[252:255], v251, s[88:89] offset:2048
	global_load_dwordx4 v[252:255], v251, s[88:89] offset:3072
	s_add_u32 s88, s88, 0x1000
	s_addc_u32 s89, s89, 0
	global_load_dwordx4 v[252:255], v251, s[88:89]
	global_load_dwordx4 v[252:255], v251, s[88:89] offset:1024
	global_load_dwordx4 v[252:255], v251, s[88:89] offset:2048
	global_load_dwordx4 v[252:255], v251, s[88:89] offset:3072
	s_add_u32 s88, s88, 0x1000
	s_addc_u32 s89, s89, 0
	global_load_dwordx4 v[252:255], v251, s[88:89]
	global_load_dwordx4 v[252:255], v251, s[88:89] offset:1024
	global_load_dwordx4 v[252:255], v251, s[88:89] offset:2048
	global_load_dwordx4 v[252:255], v251, s[88:89] offset:3072
	v_pk_mul_f16 v22, v160, v146 op_sel_hi:[0,1]
	v_pk_mul_f16 v23, v160, v147 op_sel_hi:[0,1]
	v_pk_mul_f16 v24, v160, v148 op_sel_hi:[0,1]
	v_pk_mul_f16 v25, v160, v149 op_sel_hi:[0,1]
	v_pk_mul_f16 v50, v159, v146 op_sel_hi:[0,1]
	v_pk_mul_f16 v51, v159, v147 op_sel_hi:[0,1]
	v_pk_mul_f16 v52, v159, v148 op_sel_hi:[0,1]
	v_pk_mul_f16 v53, v159, v149 op_sel_hi:[0,1]
	v_pk_mul_f16 v34, v158, v146 op_sel_hi:[0,1]
	v_pk_mul_f16 v35, v158, v147 op_sel_hi:[0,1]
	v_pk_mul_f16 v36, v158, v148 op_sel_hi:[0,1]
	v_pk_mul_f16 v37, v158, v149 op_sel_hi:[0,1]
	v_pk_fma_f16 v29, v29, v149, v25
	v_pk_fma_f16 v28, v28, v148, v24
	v_pk_fma_f16 v27, v27, v147, v23
	v_pk_fma_f16 v26, v26, v146, v22
	v_pk_fma_f16 v41, v41, v149, v25
	v_pk_fma_f16 v40, v40, v148, v24
	v_pk_fma_f16 v39, v39, v147, v23
	v_pk_fma_f16 v38, v38, v146, v22
	v_pk_fma_f16 v25, v61, v149, v25
	v_pk_fma_f16 v24, v60, v148, v24
	v_pk_fma_f16 v23, v59, v147, v23
	v_pk_fma_f16 v22, v58, v146, v22
	v_pk_fma_f16 v66, v137, v149, v53
	v_pk_fma_f16 v67, v136, v148, v52
	v_pk_fma_f16 v68, v135, v147, v51
	v_pk_fma_f16 v69, v134, v146, v50
	v_pk_fma_f16 v70, v145, v149, v53
	v_pk_fma_f16 v71, v144, v148, v52
	v_pk_fma_f16 v72, v143, v147, v51
	v_pk_fma_f16 v73, v142, v146, v50
	v_pk_fma_f16 v9, v9, v149, v53
	v_pk_fma_f16 v8, v8, v148, v52
	v_pk_fma_f16 v7, v7, v147, v51
	v_pk_fma_f16 v6, v6, v146, v50
	v_pk_maximum3_f16 v50, v26, v38, v22
	v_pk_maximum3_f16 v51, v27, v39, v23
	v_pk_maximum3_f16 v52, v28, v40, v24
	v_pk_maximum3_f16 v53, v29, v41, v25
	v_pk_fma_f16 v54, v81, v149, v37
	v_pk_fma_f16 v55, v80, v148, v36
	v_pk_fma_f16 v56, v79, v147, v35
	v_pk_fma_f16 v57, v78, v146, v34
	v_pk_fma_f16 v58, v109, v149, v37
	v_pk_fma_f16 v59, v108, v148, v36
	v_pk_fma_f16 v60, v107, v147, v35
	v_pk_fma_f16 v61, v106, v146, v34
	v_pk_fma_f16 v37, v125, v149, v37
	v_pk_fma_f16 v36, v124, v148, v36
	v_pk_fma_f16 v35, v123, v147, v35
	v_pk_fma_f16 v34, v122, v146, v34
	v_pk_maximum3_f16 v75, v56, v60, v35
	v_pk_maximum3_f16 v76, v55, v59, v36
	v_pk_maximum3_f16 v77, v54, v58, v37
	v_pk_maximum3_f16 v78, v69, v73, v6
	v_pk_maximum3_f16 v79, v68, v72, v7
	v_pk_maximum3_f16 v74, v57, v61, v34
	v_pk_maximum3_f16 v80, v67, v71, v8
	v_pk_maximum3_f16 v81, v66, v70, v9
	v_pk_maximum3_f16 v50, v50, v74, v78
	v_pk_maximum3_f16 v51, v51, v75, v79
	v_pk_maximum3_f16 v52, v52, v76, v80
	v_pk_maximum3_f16 v53, v53, v77, v81
	s_nop 0
	v_pk_add_f16 v26, v26, v50 neg_lo:[0,1] neg_hi:[0,1]
	v_pk_add_f16 v27, v27, v51 neg_lo:[0,1] neg_hi:[0,1]
	v_pk_add_f16 v28, v28, v52 neg_lo:[0,1] neg_hi:[0,1]
	v_pk_add_f16 v29, v29, v53 neg_lo:[0,1] neg_hi:[0,1]
	v_pk_add_f16 v38, v38, v50 neg_lo:[0,1] neg_hi:[0,1]
	v_exp_f16_sdwa v74, v26 dst_sel:WORD_0 dst_unused:UNUSED_PAD src0_sel:WORD_0
	v_exp_f16_sdwa v75, v27 dst_sel:WORD_0 dst_unused:UNUSED_PAD src0_sel:WORD_0
	v_exp_f16_sdwa v76, v28 dst_sel:WORD_0 dst_unused:UNUSED_PAD src0_sel:WORD_0
	v_exp_f16_sdwa v77, v29 dst_sel:WORD_0 dst_unused:UNUSED_PAD src0_sel:WORD_0
	v_exp_f16_sdwa v74, v26 dst_sel:WORD_1 dst_unused:UNUSED_PRESERVE src0_sel:WORD_1
	v_exp_f16_sdwa v75, v27 dst_sel:WORD_1 dst_unused:UNUSED_PRESERVE src0_sel:WORD_1
	v_exp_f16_sdwa v76, v28 dst_sel:WORD_1 dst_unused:UNUSED_PRESERVE src0_sel:WORD_1
	v_exp_f16_sdwa v77, v29 dst_sel:WORD_1 dst_unused:UNUSED_PRESERVE src0_sel:WORD_1
	v_pk_add_f16 v39, v39, v51 neg_lo:[0,1] neg_hi:[0,1]
	v_pk_add_f16 v26, v74, 0
	v_pk_add_f16 v27, v75, 0
	v_pk_add_f16 v28, v76, 0
	v_pk_add_f16 v29, v77, 0
	v_pk_fma_f16 v10, v10, v74, 0
	v_pk_fma_f16 v11, v11, v75, 0
	v_pk_fma_f16 v12, v12, v76, 0
	v_pk_fma_f16 v13, v13, v77, 0
	v_pk_add_f16 v40, v40, v52 neg_lo:[0,1] neg_hi:[0,1]
	v_pk_add_f16 v41, v41, v53 neg_lo:[0,1] neg_hi:[0,1]
	v_pk_add_f16 v6, v6, v50 neg_lo:[0,1] neg_hi:[0,1]
	v_exp_f16_sdwa v74, v38 dst_sel:WORD_0 dst_unused:UNUSED_PAD src0_sel:WORD_0
	v_exp_f16_sdwa v75, v39 dst_sel:WORD_0 dst_unused:UNUSED_PAD src0_sel:WORD_0
	v_exp_f16_sdwa v76, v40 dst_sel:WORD_0 dst_unused:UNUSED_PAD src0_sel:WORD_0
	v_exp_f16_sdwa v77, v41 dst_sel:WORD_0 dst_unused:UNUSED_PAD src0_sel:WORD_0
	v_exp_f16_sdwa v74, v38 dst_sel:WORD_1 dst_unused:UNUSED_PRESERVE src0_sel:WORD_1
	v_exp_f16_sdwa v75, v39 dst_sel:WORD_1 dst_unused:UNUSED_PRESERVE src0_sel:WORD_1
	v_exp_f16_sdwa v76, v40 dst_sel:WORD_1 dst_unused:UNUSED_PRESERVE src0_sel:WORD_1
	v_exp_f16_sdwa v77, v41 dst_sel:WORD_1 dst_unused:UNUSED_PRESERVE src0_sel:WORD_1
	v_pk_add_f16 v7, v7, v51 neg_lo:[0,1] neg_hi:[0,1]
	v_pk_add_f16 v29, v29, v77
	v_pk_add_f16 v28, v28, v76
	v_pk_add_f16 v27, v27, v75
	v_pk_add_f16 v26, v26, v74
	v_pk_fma_f16 v13, v17, v77, v13
	v_pk_fma_f16 v12, v16, v76, v12
	v_pk_fma_f16 v11, v15, v75, v11
	v_pk_fma_f16 v10, v14, v74, v10
	v_pk_add_f16 v14, v22, v50 neg_lo:[0,1] neg_hi:[0,1]
	v_pk_add_f16 v15, v23, v51 neg_lo:[0,1] neg_hi:[0,1]
	v_pk_add_f16 v16, v24, v52 neg_lo:[0,1] neg_hi:[0,1]
	v_pk_add_f16 v17, v25, v53 neg_lo:[0,1] neg_hi:[0,1]
	v_pk_add_f16 v8, v8, v52 neg_lo:[0,1] neg_hi:[0,1]
	v_exp_f16_sdwa v22, v14 dst_sel:WORD_0 dst_unused:UNUSED_PAD src0_sel:WORD_0
	v_exp_f16_sdwa v23, v15 dst_sel:WORD_0 dst_unused:UNUSED_PAD src0_sel:WORD_0
	v_exp_f16_sdwa v24, v16 dst_sel:WORD_0 dst_unused:UNUSED_PAD src0_sel:WORD_0
	v_exp_f16_sdwa v25, v17 dst_sel:WORD_0 dst_unused:UNUSED_PAD src0_sel:WORD_0
	v_exp_f16_sdwa v22, v14 dst_sel:WORD_1 dst_unused:UNUSED_PRESERVE src0_sel:WORD_1
	v_exp_f16_sdwa v23, v15 dst_sel:WORD_1 dst_unused:UNUSED_PRESERVE src0_sel:WORD_1
	v_exp_f16_sdwa v24, v16 dst_sel:WORD_1 dst_unused:UNUSED_PRESERVE src0_sel:WORD_1
	v_exp_f16_sdwa v25, v17 dst_sel:WORD_1 dst_unused:UNUSED_PRESERVE src0_sel:WORD_1
	v_pk_add_f16 v9, v9, v53 neg_lo:[0,1] neg_hi:[0,1]
	v_pk_add_f16 v14, v26, v22
	v_pk_add_f16 v15, v27, v23
	v_pk_add_f16 v16, v28, v24
	v_pk_add_f16 v17, v29, v25
	v_pk_fma_f16 v10, v18, v22, v10
	v_pk_fma_f16 v11, v19, v23, v11
	v_pk_fma_f16 v12, v20, v24, v12
	v_pk_fma_f16 v13, v21, v25, v13
	v_pk_add_f16 v18, v57, v50 neg_lo:[0,1] neg_hi:[0,1]
	v_pk_add_f16 v19, v56, v51 neg_lo:[0,1] neg_hi:[0,1]
	v_pk_add_f16 v20, v55, v52 neg_lo:[0,1] neg_hi:[0,1]
	v_pk_add_f16 v21, v54, v53 neg_lo:[0,1] neg_hi:[0,1]
	v_exp_f16_sdwa v22, v18 dst_sel:WORD_0 dst_unused:UNUSED_PAD src0_sel:WORD_0
	v_exp_f16_sdwa v23, v19 dst_sel:WORD_0 dst_unused:UNUSED_PAD src0_sel:WORD_0
	v_exp_f16_sdwa v24, v20 dst_sel:WORD_0 dst_unused:UNUSED_PAD src0_sel:WORD_0
	v_exp_f16_sdwa v25, v21 dst_sel:WORD_0 dst_unused:UNUSED_PAD src0_sel:WORD_0
	v_exp_f16_sdwa v22, v18 dst_sel:WORD_1 dst_unused:UNUSED_PRESERVE src0_sel:WORD_1
	v_exp_f16_sdwa v23, v19 dst_sel:WORD_1 dst_unused:UNUSED_PRESERVE src0_sel:WORD_1
	v_exp_f16_sdwa v24, v20 dst_sel:WORD_1 dst_unused:UNUSED_PRESERVE src0_sel:WORD_1
	v_exp_f16_sdwa v25, v21 dst_sel:WORD_1 dst_unused:UNUSED_PRESERVE src0_sel:WORD_1
	v_pk_add_f16 v18, v61, v50 neg_lo:[0,1] neg_hi:[0,1]
	v_pk_add_f16 v17, v17, v25
	v_pk_add_f16 v16, v16, v24
	v_pk_add_f16 v15, v15, v23
	v_pk_add_f16 v14, v14, v22
	v_pk_fma_f16 v13, v33, v25, v13
	v_pk_fma_f16 v12, v32, v24, v12
	v_pk_fma_f16 v11, v31, v23, v11
	v_pk_fma_f16 v10, v30, v22, v10
	v_pk_add_f16 v19, v60, v51 neg_lo:[0,1] neg_hi:[0,1]
	v_pk_add_f16 v20, v59, v52 neg_lo:[0,1] neg_hi:[0,1]
	v_pk_add_f16 v21, v58, v53 neg_lo:[0,1] neg_hi:[0,1]
	v_exp_f16_sdwa v22, v18 dst_sel:WORD_0 dst_unused:UNUSED_PAD src0_sel:WORD_0
	v_exp_f16_sdwa v23, v19 dst_sel:WORD_0 dst_unused:UNUSED_PAD src0_sel:WORD_0
	v_exp_f16_sdwa v24, v20 dst_sel:WORD_0 dst_unused:UNUSED_PAD src0_sel:WORD_0
	v_exp_f16_sdwa v25, v21 dst_sel:WORD_0 dst_unused:UNUSED_PAD src0_sel:WORD_0
	v_exp_f16_sdwa v22, v18 dst_sel:WORD_1 dst_unused:UNUSED_PRESERVE src0_sel:WORD_1
	v_exp_f16_sdwa v23, v19 dst_sel:WORD_1 dst_unused:UNUSED_PRESERVE src0_sel:WORD_1
	v_exp_f16_sdwa v24, v20 dst_sel:WORD_1 dst_unused:UNUSED_PRESERVE src0_sel:WORD_1
	v_exp_f16_sdwa v25, v21 dst_sel:WORD_1 dst_unused:UNUSED_PRESERVE src0_sel:WORD_1
	v_pk_add_f16 v18, v34, v50 neg_lo:[0,1] neg_hi:[0,1]
	v_pk_add_f16 v14, v14, v22
	v_pk_add_f16 v15, v15, v23
	v_pk_add_f16 v16, v16, v24
	v_pk_add_f16 v17, v17, v25
	v_pk_fma_f16 v10, v46, v22, v10
	v_pk_fma_f16 v11, v47, v23, v11
	v_pk_fma_f16 v12, v48, v24, v12
	v_pk_fma_f16 v13, v49, v25, v13
	v_pk_add_f16 v19, v35, v51 neg_lo:[0,1] neg_hi:[0,1]
	v_pk_add_f16 v20, v36, v52 neg_lo:[0,1] neg_hi:[0,1]
	v_pk_add_f16 v21, v37, v53 neg_lo:[0,1] neg_hi:[0,1]
	v_exp_f16_sdwa v22, v18 dst_sel:WORD_0 dst_unused:UNUSED_PAD src0_sel:WORD_0
	v_exp_f16_sdwa v23, v19 dst_sel:WORD_0 dst_unused:UNUSED_PAD src0_sel:WORD_0
	v_exp_f16_sdwa v24, v20 dst_sel:WORD_0 dst_unused:UNUSED_PAD src0_sel:WORD_0
	v_exp_f16_sdwa v25, v21 dst_sel:WORD_0 dst_unused:UNUSED_PAD src0_sel:WORD_0
	v_exp_f16_sdwa v22, v18 dst_sel:WORD_1 dst_unused:UNUSED_PRESERVE src0_sel:WORD_1
	v_exp_f16_sdwa v23, v19 dst_sel:WORD_1 dst_unused:UNUSED_PRESERVE src0_sel:WORD_1
	v_exp_f16_sdwa v24, v20 dst_sel:WORD_1 dst_unused:UNUSED_PRESERVE src0_sel:WORD_1
	v_exp_f16_sdwa v25, v21 dst_sel:WORD_1 dst_unused:UNUSED_PRESERVE src0_sel:WORD_1
	v_pk_add_f16 v18, v69, v50 neg_lo:[0,1] neg_hi:[0,1]
	v_pk_add_f16 v17, v17, v25
	v_pk_add_f16 v16, v16, v24
	v_pk_add_f16 v15, v15, v23
	v_pk_add_f16 v14, v14, v22
	v_pk_fma_f16 v13, v65, v25, v13
	v_pk_fma_f16 v12, v64, v24, v12
	v_pk_fma_f16 v11, v63, v23, v11
	v_pk_fma_f16 v10, v62, v22, v10
	v_pk_add_f16 v19, v68, v51 neg_lo:[0,1] neg_hi:[0,1]
	v_pk_add_f16 v20, v67, v52 neg_lo:[0,1] neg_hi:[0,1]
	v_pk_add_f16 v21, v66, v53 neg_lo:[0,1] neg_hi:[0,1]
	v_exp_f16_sdwa v22, v18 dst_sel:WORD_0 dst_unused:UNUSED_PAD src0_sel:WORD_0
	v_exp_f16_sdwa v23, v19 dst_sel:WORD_0 dst_unused:UNUSED_PAD src0_sel:WORD_0
	v_exp_f16_sdwa v24, v20 dst_sel:WORD_0 dst_unused:UNUSED_PAD src0_sel:WORD_0
	v_exp_f16_sdwa v25, v21 dst_sel:WORD_0 dst_unused:UNUSED_PAD src0_sel:WORD_0
	v_exp_f16_sdwa v22, v18 dst_sel:WORD_1 dst_unused:UNUSED_PRESERVE src0_sel:WORD_1
	v_exp_f16_sdwa v23, v19 dst_sel:WORD_1 dst_unused:UNUSED_PRESERVE src0_sel:WORD_1
	v_exp_f16_sdwa v24, v20 dst_sel:WORD_1 dst_unused:UNUSED_PRESERVE src0_sel:WORD_1
	v_exp_f16_sdwa v25, v21 dst_sel:WORD_1 dst_unused:UNUSED_PRESERVE src0_sel:WORD_1
	v_pk_add_f16 v18, v73, v50 neg_lo:[0,1] neg_hi:[0,1]
	v_pk_add_f16 v14, v14, v22
	v_pk_add_f16 v15, v15, v23
	v_pk_add_f16 v16, v16, v24
	v_pk_add_f16 v17, v17, v25
	v_pk_fma_f16 v10, v82, v22, v10
	v_pk_fma_f16 v11, v83, v23, v11
	v_pk_fma_f16 v12, v84, v24, v12
	v_pk_fma_f16 v13, v85, v25, v13
	v_pk_add_f16 v19, v72, v51 neg_lo:[0,1] neg_hi:[0,1]
	v_pk_add_f16 v20, v71, v52 neg_lo:[0,1] neg_hi:[0,1]
	v_pk_add_f16 v21, v70, v53 neg_lo:[0,1] neg_hi:[0,1]
	v_exp_f16_sdwa v22, v18 dst_sel:WORD_0 dst_unused:UNUSED_PAD src0_sel:WORD_0
	v_exp_f16_sdwa v23, v19 dst_sel:WORD_0 dst_unused:UNUSED_PAD src0_sel:WORD_0
	v_exp_f16_sdwa v24, v20 dst_sel:WORD_0 dst_unused:UNUSED_PAD src0_sel:WORD_0
	v_exp_f16_sdwa v25, v21 dst_sel:WORD_0 dst_unused:UNUSED_PAD src0_sel:WORD_0
	v_exp_f16_sdwa v22, v18 dst_sel:WORD_1 dst_unused:UNUSED_PRESERVE src0_sel:WORD_1
	v_exp_f16_sdwa v23, v19 dst_sel:WORD_1 dst_unused:UNUSED_PRESERVE src0_sel:WORD_1
	v_exp_f16_sdwa v24, v20 dst_sel:WORD_1 dst_unused:UNUSED_PRESERVE src0_sel:WORD_1
	v_exp_f16_sdwa v25, v21 dst_sel:WORD_1 dst_unused:UNUSED_PRESERVE src0_sel:WORD_1
	s_nop 0
	v_pk_add_f16 v17, v17, v25
	v_pk_add_f16 v16, v16, v24
	v_pk_add_f16 v15, v15, v23
	v_pk_add_f16 v14, v14, v22
	v_pk_fma_f16 v21, v105, v25, v13
	v_pk_fma_f16 v20, v104, v24, v12
	v_pk_fma_f16 v19, v103, v23, v11
	v_pk_fma_f16 v18, v102, v22, v10
	v_mov_b32_e32 v13, v5
	v_mov_b32_e32 v12, v4
	v_mov_b32_e32 v11, v3
	v_mov_b32_e32 v10, v2
	v_exp_f16_sdwa v22, v6 dst_sel:WORD_0 dst_unused:UNUSED_PAD src0_sel:WORD_0
	v_exp_f16_sdwa v23, v7 dst_sel:WORD_0 dst_unused:UNUSED_PAD src0_sel:WORD_0
	v_exp_f16_sdwa v24, v8 dst_sel:WORD_0 dst_unused:UNUSED_PAD src0_sel:WORD_0
	v_exp_f16_sdwa v25, v9 dst_sel:WORD_0 dst_unused:UNUSED_PAD src0_sel:WORD_0
	v_exp_f16_sdwa v22, v6 dst_sel:WORD_1 dst_unused:UNUSED_PRESERVE src0_sel:WORD_1
	v_exp_f16_sdwa v23, v7 dst_sel:WORD_1 dst_unused:UNUSED_PRESERVE src0_sel:WORD_1
	v_exp_f16_sdwa v24, v8 dst_sel:WORD_1 dst_unused:UNUSED_PRESERVE src0_sel:WORD_1
	v_exp_f16_sdwa v25, v9 dst_sel:WORD_1 dst_unused:UNUSED_PRESERVE src0_sel:WORD_1
	s_nop 0

.Lmyf_C3_7:
	s_mov_b64 exec, -1
	s_waitcnt vmcnt(21)
	v_cvt_f16_f32_e32 v206, v155
	v_cvt_f16_f32_e32 v208, v154
	v_cvt_f16_f32_e32 v207, v156
	v_add_u32_e32 v251, 0x48000, v200
	buffer_load_dwordx4 v[154:157], v251, s[12:15], 0 offen
	s_mov_b64 s[4:5], 0
	s_waitcnt vmcnt(3)
	v_pk_mul_f16 v216, v208, v213 op_sel_hi:[0,1]
	v_pk_mul_f16 v220, v206, v213 op_sel_hi:[0,1]
	v_pk_mul_f16 v224, v207, v213 op_sel_hi:[0,1]
	v_pk_mul_f16 v209, v208, v210 op_sel_hi:[0,1]
	v_pk_mul_f16 v214, v208, v211 op_sel_hi:[0,1]
	v_pk_mul_f16 v215, v208, v212 op_sel_hi:[0,1]
	v_pk_mul_f16 v217, v206, v210 op_sel_hi:[0,1]
	s_mov_b64 exec, s[64:65]
	buffer_load_dwordx4 v[34:37], v245, s[12:15], 0 offen
	buffer_load_dwordx4 v[18:21], v245, s[12:15], 0 offen offset:512
	s_mov_b64 exec, -1
	v_pk_mul_f16 v218, v206, v211 op_sel_hi:[0,1]
	v_pk_mul_f16 v219, v206, v212 op_sel_hi:[0,1]
	v_pk_mul_f16 v221, v207, v210 op_sel_hi:[0,1]
	v_pk_mul_f16 v222, v207, v211 op_sel_hi:[0,1]
	v_pk_mul_f16 v223, v207, v212 op_sel_hi:[0,1]
	v_pk_fma_f16 v125, v125, v213, v216
	v_pk_fma_f16 v141, v141, v213, v220
	v_pk_fma_f16 v149, v149, v213, v224
	v_pk_fma_f16 v225, v97, v213, v216
	v_pk_fma_f16 v229, v121, v213, v220
	v_pk_fma_f16 v233, v137, v213, v224
	v_pk_fma_f16 v216, v65, v213, v216
	v_pk_fma_f16 v220, v81, v213, v220
	buffer_load_dwordx4 v[46:49], v246, s[12:15], 0 offen offset:512
	buffer_load_dwordx4 v[22:25], v246, s[12:15], 0 offen offset:1024
	v_pk_fma_f16 v213, v105, v213, v224
	v_pk_maximum3_f16 v224, v125, v141, v149
	v_pk_fma_f16 v124, v124, v212, v215
	v_pk_fma_f16 v123, v123, v211, v214
	v_pk_fma_f16 v122, v122, v210, v209
	v_pk_fma_f16 v140, v140, v212, v219
	v_pk_fma_f16 v139, v139, v211, v218
	v_pk_fma_f16 v138, v138, v210, v217
	v_pk_fma_f16 v148, v148, v212, v223
	v_pk_fma_f16 v147, v147, v211, v222
	v_pk_fma_f16 v146, v146, v210, v221
	v_pk_fma_f16 v226, v96, v212, v215
	v_pk_fma_f16 v227, v95, v211, v214
	v_pk_fma_f16 v228, v94, v210, v209
	v_pk_fma_f16 v230, v120, v212, v219
	v_pk_fma_f16 v231, v119, v211, v218
	s_mov_b64 exec, s[66:67]
	buffer_load_dwordx4 v[66:69], v246, s[12:15], 0 offen offset:2048
	buffer_load_dwordx4 v[26:29], v246, s[12:15], 0 offen offset:2560
	s_mov_b64 exec, -1
	v_pk_fma_f16 v232, v118, v210, v217
	v_pk_fma_f16 v234, v136, v212, v223
	v_pk_fma_f16 v235, v135, v211, v222
	v_pk_fma_f16 v236, v134, v210, v221
	v_pk_fma_f16 v215, v64, v212, v215
	v_pk_fma_f16 v214, v63, v211, v214
	v_pk_fma_f16 v209, v62, v210, v209
	v_pk_fma_f16 v219, v80, v212, v219
	v_pk_fma_f16 v218, v79, v211, v218
	v_pk_fma_f16 v217, v78, v210, v217
	v_pk_fma_f16 v212, v104, v212, v223
	v_pk_fma_f16 v211, v103, v211, v222
	v_pk_fma_f16 v210, v102, v210, v221
	v_pk_maximum3_f16 v221, v122, v138, v146
	v_pk_maximum3_f16 v222, v123, v139, v147
	v_pk_maximum3_f16 v223, v124, v140, v148
	v_pk_maximum3_f16 v240, v225, v229, v233
	v_pk_maximum3_f16 v244, v216, v220, v213
	v_pk_maximum3_f16 v237, v228, v232, v236
	v_pk_maximum3_f16 v238, v227, v231, v235
	v_pk_maximum3_f16 v239, v226, v230, v234
	v_pk_maximum3_f16 v241, v209, v217, v210
	v_pk_maximum3_f16 v242, v214, v218, v211
	v_pk_maximum3_f16 v224, v224, v240, v244
	v_pk_maximum3_f16 v243, v215, v219, v212
	v_pk_maximum3_f16 v221, v221, v237, v241
	v_pk_maximum3_f16 v222, v222, v238, v242
	v_pk_maximum3_f16 v223, v223, v239, v243
	v_pk_add_f16 v125, v125, v224 neg_lo:[0,1] neg_hi:[0,1]
	s_mov_b64 exec, s[64:65]
	buffer_load_dwordx4 v[86:89], v247, s[12:15], 0 offen
	buffer_load_dwordx4 v[38:41], v247, s[12:15], 0 offen offset:512
	s_mov_b64 exec, -1
	v_pk_add_f16 v122, v122, v221 neg_lo:[0,1] neg_hi:[0,1]
	v_pk_add_f16 v123, v123, v222 neg_lo:[0,1] neg_hi:[0,1]
	v_pk_add_f16 v124, v124, v223 neg_lo:[0,1] neg_hi:[0,1]
	v_pk_add_f16 v138, v138, v221 neg_lo:[0,1] neg_hi:[0,1]
	v_exp_f16_sdwa v237, v122 dst_sel:WORD_0 dst_unused:UNUSED_PAD src0_sel:WORD_0
	v_exp_f16_sdwa v238, v123 dst_sel:WORD_0 dst_unused:UNUSED_PAD src0_sel:WORD_0
	v_exp_f16_sdwa v239, v124 dst_sel:WORD_0 dst_unused:UNUSED_PAD src0_sel:WORD_0
	v_exp_f16_sdwa v240, v125 dst_sel:WORD_0 dst_unused:UNUSED_PAD src0_sel:WORD_0
	v_exp_f16_sdwa v237, v122 dst_sel:WORD_1 dst_unused:UNUSED_PRESERVE src0_sel:WORD_1
	v_exp_f16_sdwa v238, v123 dst_sel:WORD_1 dst_unused:UNUSED_PRESERVE src0_sel:WORD_1
	v_exp_f16_sdwa v239, v124 dst_sel:WORD_1 dst_unused:UNUSED_PRESERVE src0_sel:WORD_1
	v_exp_f16_sdwa v240, v125 dst_sel:WORD_1 dst_unused:UNUSED_PRESERVE src0_sel:WORD_1
	v_pk_add_f16 v139, v139, v222 neg_lo:[0,1] neg_hi:[0,1]
	v_pk_add_f16 v125, v237, 0
	v_pk_fma_f16 v85, v85, v240, 0
	v_pk_add_f16 v122, v240, 0
	v_pk_add_f16 v123, v239, 0
	v_pk_add_f16 v124, v238, 0
	v_pk_fma_f16 v84, v84, v239, 0
	v_pk_fma_f16 v83, v83, v238, 0
	v_pk_fma_f16 v82, v82, v237, 0
	v_pk_add_f16 v140, v140, v223 neg_lo:[0,1] neg_hi:[0,1]
	buffer_load_dwordx4 v[114:117], v248, s[12:15], 0 offen offset:512
	buffer_load_dwordx4 v[50:53], v248, s[12:15], 0 offen offset:1024
	v_pk_add_f16 v141, v141, v224 neg_lo:[0,1] neg_hi:[0,1]
	v_exp_f16_sdwa v237, v138 dst_sel:WORD_0 dst_unused:UNUSED_PAD src0_sel:WORD_0
	v_exp_f16_sdwa v238, v139 dst_sel:WORD_0 dst_unused:UNUSED_PAD src0_sel:WORD_0
	v_exp_f16_sdwa v239, v140 dst_sel:WORD_0 dst_unused:UNUSED_PAD src0_sel:WORD_0
	v_exp_f16_sdwa v240, v141 dst_sel:WORD_0 dst_unused:UNUSED_PAD src0_sel:WORD_0
	v_exp_f16_sdwa v237, v138 dst_sel:WORD_1 dst_unused:UNUSED_PRESERVE src0_sel:WORD_1
	v_exp_f16_sdwa v238, v139 dst_sel:WORD_1 dst_unused:UNUSED_PRESERVE src0_sel:WORD_1
	v_exp_f16_sdwa v239, v140 dst_sel:WORD_1 dst_unused:UNUSED_PRESERVE src0_sel:WORD_1
	v_exp_f16_sdwa v240, v141 dst_sel:WORD_1 dst_unused:UNUSED_PRESERVE src0_sel:WORD_1
	v_pk_add_f16 v125, v125, v237
	v_pk_fma_f16 v85, v109, v240, v85
	v_pk_add_f16 v109, v149, v224 neg_lo:[0,1] neg_hi:[0,1]
	v_pk_add_f16 v124, v124, v238
	v_pk_add_f16 v123, v123, v239
	v_pk_add_f16 v122, v122, v240
	v_pk_fma_f16 v82, v106, v237, v82
	v_pk_fma_f16 v83, v107, v238, v83
	v_pk_fma_f16 v84, v108, v239, v84
	v_pk_add_f16 v106, v146, v221 neg_lo:[0,1] neg_hi:[0,1]
	v_pk_add_f16 v107, v147, v222 neg_lo:[0,1] neg_hi:[0,1]
	v_pk_add_f16 v108, v148, v223 neg_lo:[0,1] neg_hi:[0,1]
	v_exp_f16_sdwa v138, v106 dst_sel:WORD_0 dst_unused:UNUSED_PAD src0_sel:WORD_0
	v_exp_f16_sdwa v139, v107 dst_sel:WORD_0 dst_unused:UNUSED_PAD src0_sel:WORD_0
	v_exp_f16_sdwa v140, v108 dst_sel:WORD_0 dst_unused:UNUSED_PAD src0_sel:WORD_0
	v_exp_f16_sdwa v141, v109 dst_sel:WORD_0 dst_unused:UNUSED_PAD src0_sel:WORD_0
	v_exp_f16_sdwa v138, v106 dst_sel:WORD_1 dst_unused:UNUSED_PRESERVE src0_sel:WORD_1
	v_exp_f16_sdwa v139, v107 dst_sel:WORD_1 dst_unused:UNUSED_PRESERVE src0_sel:WORD_1
	v_exp_f16_sdwa v140, v108 dst_sel:WORD_1 dst_unused:UNUSED_PRESERVE src0_sel:WORD_1
	v_exp_f16_sdwa v141, v109 dst_sel:WORD_1 dst_unused:UNUSED_PRESERVE src0_sel:WORD_1
	v_pk_add_f16 v109, v125, v138
	v_pk_add_f16 v106, v122, v141
	s_mov_b64 exec, s[66:67]
	buffer_load_dwordx4 v[130:133], v248, s[12:15], 0 offen offset:2048
	buffer_load_dwordx4 v[70:73], v248, s[12:15], 0 offen offset:2560
	s_mov_b64 exec, -1
	v_pk_add_f16 v107, v123, v140
	v_pk_add_f16 v108, v124, v139
	v_pk_fma_f16 v85, v129, v141, v85
	v_pk_fma_f16 v84, v128, v140, v84
	v_pk_fma_f16 v83, v127, v139, v83
	v_pk_fma_f16 v82, v126, v138, v82
	v_pk_add_f16 v122, v228, v221 neg_lo:[0,1] neg_hi:[0,1]
	v_pk_add_f16 v123, v227, v222 neg_lo:[0,1] neg_hi:[0,1]
	v_pk_add_f16 v124, v226, v223 neg_lo:[0,1] neg_hi:[0,1]
	v_pk_add_f16 v125, v225, v224 neg_lo:[0,1] neg_hi:[0,1]
	v_exp_f16_sdwa v126, v122 dst_sel:WORD_0 dst_unused:UNUSED_PAD src0_sel:WORD_0
	v_exp_f16_sdwa v127, v123 dst_sel:WORD_0 dst_unused:UNUSED_PAD src0_sel:WORD_0
	v_exp_f16_sdwa v128, v124 dst_sel:WORD_0 dst_unused:UNUSED_PAD src0_sel:WORD_0
	v_exp_f16_sdwa v129, v125 dst_sel:WORD_0 dst_unused:UNUSED_PAD src0_sel:WORD_0
	v_exp_f16_sdwa v126, v122 dst_sel:WORD_1 dst_unused:UNUSED_PRESERVE src0_sel:WORD_1
	v_exp_f16_sdwa v127, v123 dst_sel:WORD_1 dst_unused:UNUSED_PRESERVE src0_sel:WORD_1
	v_exp_f16_sdwa v128, v124 dst_sel:WORD_1 dst_unused:UNUSED_PRESERVE src0_sel:WORD_1
	v_exp_f16_sdwa v129, v125 dst_sel:WORD_1 dst_unused:UNUSED_PRESERVE src0_sel:WORD_1
	v_pk_add_f16 v122, v232, v221 neg_lo:[0,1] neg_hi:[0,1]
	v_pk_add_f16 v109, v109, v126
	v_pk_add_f16 v108, v108, v127
	v_pk_add_f16 v107, v107, v128
	s_mov_b64 exec, s[76:77]
	buffer_load_dwordx4 v[142:145], v249, s[12:15], 0 offen
	buffer_load_dwordx4 v[90:93], v249, s[12:15], 0 offen offset:512
	s_mov_b64 exec, -1
	v_pk_add_f16 v106, v106, v129
	v_pk_fma_f16 v82, v54, v126, v82
	v_pk_fma_f16 v83, v55, v127, v83
	v_pk_fma_f16 v84, v56, v128, v84
	v_pk_fma_f16 v85, v57, v129, v85
	v_pk_add_f16 v123, v231, v222 neg_lo:[0,1] neg_hi:[0,1]
	v_pk_add_f16 v124, v230, v223 neg_lo:[0,1] neg_hi:[0,1]
	v_pk_add_f16 v125, v229, v224 neg_lo:[0,1] neg_hi:[0,1]
	v_exp_f16_sdwa v126, v122 dst_sel:WORD_0 dst_unused:UNUSED_PAD src0_sel:WORD_0
	v_exp_f16_sdwa v127, v123 dst_sel:WORD_0 dst_unused:UNUSED_PAD src0_sel:WORD_0
	v_exp_f16_sdwa v128, v124 dst_sel:WORD_0 dst_unused:UNUSED_PAD src0_sel:WORD_0
	v_exp_f16_sdwa v129, v125 dst_sel:WORD_0 dst_unused:UNUSED_PAD src0_sel:WORD_0
	v_exp_f16_sdwa v126, v122 dst_sel:WORD_1 dst_unused:UNUSED_PRESERVE src0_sel:WORD_1
	v_exp_f16_sdwa v127, v123 dst_sel:WORD_1 dst_unused:UNUSED_PRESERVE src0_sel:WORD_1
	v_exp_f16_sdwa v128, v124 dst_sel:WORD_1 dst_unused:UNUSED_PRESERVE src0_sel:WORD_1
	v_exp_f16_sdwa v129, v125 dst_sel:WORD_1 dst_unused:UNUSED_PRESERVE src0_sel:WORD_1
	v_pk_add_f16 v122, v236, v221 neg_lo:[0,1] neg_hi:[0,1]
	v_pk_add_f16 v109, v109, v126
	v_pk_add_f16 v106, v106, v129
	v_pk_add_f16 v107, v107, v128
	v_pk_add_f16 v108, v108, v127
	v_pk_fma_f16 v85, v77, v129, v85
	v_pk_fma_f16 v84, v76, v128, v84
	s_mov_b64 exec, s[70:71]
	buffer_load_dwordx4 v[150:153], v250, s[12:15], 0 offen offset:512
	buffer_load_dwordx4 v[110:113], v250, s[12:15], 0 offen offset:1024
	s_mov_b64 exec, -1
	v_pk_fma_f16 v83, v75, v127, v83
	v_pk_fma_f16 v82, v74, v126, v82
	v_pk_add_f16 v123, v235, v222 neg_lo:[0,1] neg_hi:[0,1]
	v_pk_add_f16 v124, v234, v223 neg_lo:[0,1] neg_hi:[0,1]
	v_pk_add_f16 v125, v233, v224 neg_lo:[0,1] neg_hi:[0,1]
	v_exp_f16_sdwa v126, v122 dst_sel:WORD_0 dst_unused:UNUSED_PAD src0_sel:WORD_0
	v_exp_f16_sdwa v127, v123 dst_sel:WORD_0 dst_unused:UNUSED_PAD src0_sel:WORD_0
	v_exp_f16_sdwa v128, v124 dst_sel:WORD_0 dst_unused:UNUSED_PAD src0_sel:WORD_0
	v_exp_f16_sdwa v129, v125 dst_sel:WORD_0 dst_unused:UNUSED_PAD src0_sel:WORD_0
	v_exp_f16_sdwa v126, v122 dst_sel:WORD_1 dst_unused:UNUSED_PRESERVE src0_sel:WORD_1
	v_exp_f16_sdwa v127, v123 dst_sel:WORD_1 dst_unused:UNUSED_PRESERVE src0_sel:WORD_1
	v_exp_f16_sdwa v128, v124 dst_sel:WORD_1 dst_unused:UNUSED_PRESERVE src0_sel:WORD_1
	v_exp_f16_sdwa v129, v125 dst_sel:WORD_1 dst_unused:UNUSED_PRESERVE src0_sel:WORD_1
	v_pk_add_f16 v122, v209, v221 neg_lo:[0,1] neg_hi:[0,1]
	v_pk_add_f16 v109, v109, v126
	v_pk_add_f16 v108, v108, v127
	v_pk_add_f16 v107, v107, v128
	v_pk_add_f16 v106, v106, v129
	v_pk_fma_f16 v82, v98, v126, v82
	v_pk_fma_f16 v83, v99, v127, v83
	v_pk_fma_f16 v84, v100, v128, v84
	v_pk_fma_f16 v85, v101, v129, v85
	s_mov_b64 exec, s[78:79]
	buffer_load_dwordx4 v[14:17], v250, s[12:15], 0 offen offset:2048
	buffer_load_dwordx4 v[10:13], v250, s[12:15], 0 offen offset:2560
	s_mov_b64 exec, -1
	v_pk_add_f16 v123, v214, v222 neg_lo:[0,1] neg_hi:[0,1]
	v_pk_add_f16 v124, v215, v223 neg_lo:[0,1] neg_hi:[0,1]
	v_pk_add_f16 v125, v216, v224 neg_lo:[0,1] neg_hi:[0,1]
	v_exp_f16_sdwa v126, v122 dst_sel:WORD_0 dst_unused:UNUSED_PAD src0_sel:WORD_0
	v_exp_f16_sdwa v127, v123 dst_sel:WORD_0 dst_unused:UNUSED_PAD src0_sel:WORD_0
	v_exp_f16_sdwa v128, v124 dst_sel:WORD_0 dst_unused:UNUSED_PAD src0_sel:WORD_0
	v_exp_f16_sdwa v129, v125 dst_sel:WORD_0 dst_unused:UNUSED_PAD src0_sel:WORD_0
	v_exp_f16_sdwa v126, v122 dst_sel:WORD_1 dst_unused:UNUSED_PRESERVE src0_sel:WORD_1
	v_exp_f16_sdwa v127, v123 dst_sel:WORD_1 dst_unused:UNUSED_PRESERVE src0_sel:WORD_1
	v_exp_f16_sdwa v128, v124 dst_sel:WORD_1 dst_unused:UNUSED_PRESERVE src0_sel:WORD_1
	v_exp_f16_sdwa v129, v125 dst_sel:WORD_1 dst_unused:UNUSED_PRESERVE src0_sel:WORD_1
	v_pk_add_f16 v122, v217, v221 neg_lo:[0,1] neg_hi:[0,1]
	v_pk_add_f16 v109, v109, v126
	v_pk_add_f16 v106, v106, v129
	v_pk_add_f16 v107, v107, v128
	v_pk_add_f16 v108, v108, v127
	v_pk_fma_f16 v85, v33, v129, v85
	v_pk_fma_f16 v84, v32, v128, v84
	v_pk_fma_f16 v83, v31, v127, v83
	v_pk_fma_f16 v82, v30, v126, v82
	v_pk_add_f16 v123, v218, v222 neg_lo:[0,1] neg_hi:[0,1]
	v_pk_add_f16 v124, v219, v223 neg_lo:[0,1] neg_hi:[0,1]
	v_pk_add_f16 v125, v220, v224 neg_lo:[0,1] neg_hi:[0,1]
	v_exp_f16_sdwa v126, v122 dst_sel:WORD_0 dst_unused:UNUSED_PAD src0_sel:WORD_0
	v_exp_f16_sdwa v127, v123 dst_sel:WORD_0 dst_unused:UNUSED_PAD src0_sel:WORD_0
	v_exp_f16_sdwa v128, v124 dst_sel:WORD_0 dst_unused:UNUSED_PAD src0_sel:WORD_0
	v_exp_f16_sdwa v129, v125 dst_sel:WORD_0 dst_unused:UNUSED_PAD src0_sel:WORD_0
	v_exp_f16_sdwa v126, v122 dst_sel:WORD_1 dst_unused:UNUSED_PRESERVE src0_sel:WORD_1
	v_exp_f16_sdwa v127, v123 dst_sel:WORD_1 dst_unused:UNUSED_PRESERVE src0_sel:WORD_1
	v_exp_f16_sdwa v128, v124 dst_sel:WORD_1 dst_unused:UNUSED_PRESERVE src0_sel:WORD_1
	v_exp_f16_sdwa v129, v125 dst_sel:WORD_1 dst_unused:UNUSED_PRESERVE src0_sel:WORD_1
	v_pk_add_f16 v122, v210, v221 neg_lo:[0,1] neg_hi:[0,1]
	v_pk_add_f16 v109, v109, v126
	v_pk_add_f16 v108, v108, v127
	v_pk_add_f16 v107, v107, v128
	v_pk_add_f16 v106, v106, v129
	v_pk_fma_f16 v82, v42, v126, v82
	v_pk_fma_f16 v83, v43, v127, v83
	v_pk_fma_f16 v84, v44, v128, v84
	v_pk_fma_f16 v85, v45, v129, v85
	v_pk_add_f16 v123, v211, v222 neg_lo:[0,1] neg_hi:[0,1]
	v_pk_add_f16 v124, v212, v223 neg_lo:[0,1] neg_hi:[0,1]
	v_pk_add_f16 v125, v213, v224 neg_lo:[0,1] neg_hi:[0,1]
	v_exp_f16_sdwa v126, v122 dst_sel:WORD_0 dst_unused:UNUSED_PAD src0_sel:WORD_0
	v_exp_f16_sdwa v127, v123 dst_sel:WORD_0 dst_unused:UNUSED_PAD src0_sel:WORD_0
	v_exp_f16_sdwa v128, v124 dst_sel:WORD_0 dst_unused:UNUSED_PAD src0_sel:WORD_0
	v_exp_f16_sdwa v129, v125 dst_sel:WORD_0 dst_unused:UNUSED_PAD src0_sel:WORD_0
	v_exp_f16_sdwa v126, v122 dst_sel:WORD_1 dst_unused:UNUSED_PRESERVE src0_sel:WORD_1
	v_exp_f16_sdwa v127, v123 dst_sel:WORD_1 dst_unused:UNUSED_PRESERVE src0_sel:WORD_1
	v_exp_f16_sdwa v128, v124 dst_sel:WORD_1 dst_unused:UNUSED_PRESERVE src0_sel:WORD_1
	v_exp_f16_sdwa v129, v125 dst_sel:WORD_1 dst_unused:UNUSED_PRESERVE src0_sel:WORD_1
	v_pk_add_f16 v109, v109, v126
	v_pk_add_f16 v108, v108, v127
	v_rcp_f16_e32 v122, v109
	v_rcp_f16_sdwa v109, v109 dst_sel:DWORD dst_unused:UNUSED_PAD src0_sel:WORD_1
	v_pk_add_f16 v107, v107, v128
	v_rcp_f16_e32 v123, v108
	v_rcp_f16_sdwa v108, v108 dst_sel:DWORD dst_unused:UNUSED_PAD src0_sel:WORD_1
	v_pk_add_f16 v106, v106, v129
	v_rcp_f16_e32 v124, v107
	v_rcp_f16_sdwa v107, v107 dst_sel:DWORD dst_unused:UNUSED_PAD src0_sel:WORD_1
	v_rcp_f16_e32 v125, v106
	v_rcp_f16_sdwa v106, v106 dst_sel:DWORD dst_unused:UNUSED_PAD src0_sel:WORD_1
	v_pk_fma_f16 v82, v58, v126, v82
	v_pack_b32_f16 v109, v122, v109
	v_pk_fma_f16 v83, v59, v127, v83
	v_pk_mul_f16 v141, v82, v109
	v_pack_b32_f16 v82, v123, v108
	v_pk_fma_f16 v84, v60, v128, v84
	v_pk_mul_f16 v140, v83, v82
	v_pack_b32_f16 v82, v124, v107
	v_pk_fma_f16 v85, v61, v129, v85
	v_pk_mul_f16 v139, v84, v82
	v_pack_b32_f16 v82, v125, v106
	v_pk_mul_f16 v138, v85, v82
	s_waitcnt vmcnt(12)
	v_pk_mul_f16 v85, v208, v165 op_sel_hi:[0,1]
	v_pk_mul_f16 v109, v206, v165 op_sel_hi:[0,1]
	v_pk_mul_f16 v122, v207, v162 op_sel_hi:[0,1]
	v_pk_mul_f16 v125, v207, v165 op_sel_hi:[0,1]
	v_pk_mul_f16 v82, v208, v162 op_sel_hi:[0,1]
	v_pk_mul_f16 v83, v208, v163 op_sel_hi:[0,1]
	v_pk_mul_f16 v84, v208, v164 op_sel_hi:[0,1]
	v_pk_mul_f16 v106, v206, v162 op_sel_hi:[0,1]
	v_pk_mul_f16 v107, v206, v163 op_sel_hi:[0,1]
	v_pk_mul_f16 v108, v206, v164 op_sel_hi:[0,1]
	v_pk_mul_f16 v123, v207, v163 op_sel_hi:[0,1]
	v_pk_mul_f16 v124, v207, v164 op_sel_hi:[0,1]
	v_pk_fma_f16 v97, v97, v165, v85
	v_pk_fma_f16 v121, v121, v165, v109
	v_pk_fma_f16 v126, v137, v165, v125
	v_pk_fma_f16 v129, v134, v162, v122
	v_pk_fma_f16 v134, v65, v165, v85
	v_pk_fma_f16 v146, v81, v165, v109
	v_pk_fma_f16 v209, v105, v165, v125
	v_pk_fma_f16 v85, v37, v165, v85
	v_pk_fma_f16 v109, v49, v165, v109
	v_pk_fma_f16 v125, v69, v165, v125
	v_pk_maximum3_f16 v165, v97, v121, v126
	v_pk_fma_f16 v96, v96, v164, v84
	v_pk_fma_f16 v95, v95, v163, v83
	v_pk_fma_f16 v94, v94, v162, v82
	v_pk_fma_f16 v120, v120, v164, v108
	v_pk_fma_f16 v119, v119, v163, v107
	v_pk_fma_f16 v118, v118, v162, v106
	v_pk_fma_f16 v127, v136, v164, v124
	v_pk_fma_f16 v128, v135, v163, v123
	v_pk_fma_f16 v135, v64, v164, v84
	v_pk_fma_f16 v136, v63, v163, v83
	v_pk_fma_f16 v137, v62, v162, v82
	v_pk_fma_f16 v147, v80, v164, v108
	v_pk_fma_f16 v148, v79, v163, v107
	v_pk_fma_f16 v149, v78, v162, v106
	v_pk_fma_f16 v210, v104, v164, v124
	v_pk_fma_f16 v211, v103, v163, v123
	v_pk_fma_f16 v212, v102, v162, v122
	v_pk_fma_f16 v84, v36, v164, v84
	v_pk_fma_f16 v83, v35, v163, v83
	v_pk_fma_f16 v82, v34, v162, v82
	v_pk_fma_f16 v108, v48, v164, v108
	v_pk_fma_f16 v107, v47, v163, v107
	v_pk_fma_f16 v106, v46, v162, v106
	v_pk_fma_f16 v124, v68, v164, v124
	v_pk_fma_f16 v123, v67, v163, v123
	v_pk_fma_f16 v122, v66, v162, v122
	v_pk_maximum3_f16 v162, v94, v118, v129
	v_pk_maximum3_f16 v163, v95, v119, v128
	v_pk_maximum3_f16 v164, v96, v120, v127
	v_pk_maximum3_f16 v216, v134, v146, v209
	v_pk_maximum3_f16 v220, v85, v109, v125
	v_pk_maximum3_f16 v213, v137, v149, v212
	v_pk_maximum3_f16 v214, v136, v148, v211
	v_pk_maximum3_f16 v215, v135, v147, v210
	v_pk_maximum3_f16 v217, v82, v106, v122
	v_pk_maximum3_f16 v218, v83, v107, v123
	v_pk_maximum3_f16 v165, v165, v216, v220
	v_pk_maximum3_f16 v219, v84, v108, v124
	v_pk_maximum3_f16 v162, v162, v213, v217
	v_pk_maximum3_f16 v163, v163, v214, v218
	v_pk_maximum3_f16 v164, v164, v215, v219
	v_pk_add_f16 v97, v97, v165 neg_lo:[0,1] neg_hi:[0,1]
	v_pk_add_f16 v94, v94, v162 neg_lo:[0,1] neg_hi:[0,1]
	v_pk_add_f16 v95, v95, v163 neg_lo:[0,1] neg_hi:[0,1]
	v_pk_add_f16 v96, v96, v164 neg_lo:[0,1] neg_hi:[0,1]
	v_pk_add_f16 v118, v118, v162 neg_lo:[0,1] neg_hi:[0,1]
	v_exp_f16_sdwa v213, v94 dst_sel:WORD_0 dst_unused:UNUSED_PAD src0_sel:WORD_0
	v_exp_f16_sdwa v214, v95 dst_sel:WORD_0 dst_unused:UNUSED_PAD src0_sel:WORD_0
	v_exp_f16_sdwa v215, v96 dst_sel:WORD_0 dst_unused:UNUSED_PAD src0_sel:WORD_0
	v_exp_f16_sdwa v216, v97 dst_sel:WORD_0 dst_unused:UNUSED_PAD src0_sel:WORD_0
	v_exp_f16_sdwa v213, v94 dst_sel:WORD_1 dst_unused:UNUSED_PRESERVE src0_sel:WORD_1
	v_exp_f16_sdwa v214, v95 dst_sel:WORD_1 dst_unused:UNUSED_PRESERVE src0_sel:WORD_1
	v_exp_f16_sdwa v215, v96 dst_sel:WORD_1 dst_unused:UNUSED_PRESERVE src0_sel:WORD_1
	v_exp_f16_sdwa v216, v97 dst_sel:WORD_1 dst_unused:UNUSED_PRESERVE src0_sel:WORD_1
	v_pk_add_f16 v119, v119, v163 neg_lo:[0,1] neg_hi:[0,1]
	v_pk_add_f16 v97, v213, 0
	v_pk_fma_f16 v57, v57, v216, 0
	v_pk_add_f16 v94, v216, 0
	v_pk_add_f16 v95, v215, 0
	v_pk_add_f16 v96, v214, 0
	v_pk_fma_f16 v56, v56, v215, 0
	v_pk_fma_f16 v55, v55, v214, 0
	v_pk_fma_f16 v54, v54, v213, 0
	v_pk_add_f16 v120, v120, v164 neg_lo:[0,1] neg_hi:[0,1]
	v_pk_add_f16 v121, v121, v165 neg_lo:[0,1] neg_hi:[0,1]
	v_pk_add_f16 v82, v82, v162 neg_lo:[0,1] neg_hi:[0,1]
	v_exp_f16_sdwa v213, v118 dst_sel:WORD_0 dst_unused:UNUSED_PAD src0_sel:WORD_0
	v_exp_f16_sdwa v214, v119 dst_sel:WORD_0 dst_unused:UNUSED_PAD src0_sel:WORD_0
	v_exp_f16_sdwa v215, v120 dst_sel:WORD_0 dst_unused:UNUSED_PAD src0_sel:WORD_0
	v_exp_f16_sdwa v216, v121 dst_sel:WORD_0 dst_unused:UNUSED_PAD src0_sel:WORD_0
	v_exp_f16_sdwa v213, v118 dst_sel:WORD_1 dst_unused:UNUSED_PRESERVE src0_sel:WORD_1
	v_exp_f16_sdwa v214, v119 dst_sel:WORD_1 dst_unused:UNUSED_PRESERVE src0_sel:WORD_1
	v_exp_f16_sdwa v215, v120 dst_sel:WORD_1 dst_unused:UNUSED_PRESERVE src0_sel:WORD_1
	v_exp_f16_sdwa v216, v121 dst_sel:WORD_1 dst_unused:UNUSED_PRESERVE src0_sel:WORD_1
	v_pk_add_f16 v83, v83, v163 neg_lo:[0,1] neg_hi:[0,1]
	v_pk_add_f16 v97, v97, v213
	v_pk_fma_f16 v57, v77, v216, v57
	v_pk_add_f16 v77, v126, v165 neg_lo:[0,1] neg_hi:[0,1]
	v_pk_add_f16 v96, v96, v214
	v_pk_add_f16 v95, v95, v215
	v_pk_add_f16 v94, v94, v216
	v_pk_fma_f16 v54, v74, v213, v54
	v_pk_fma_f16 v55, v75, v214, v55
	v_pk_fma_f16 v56, v76, v215, v56
	v_pk_add_f16 v74, v129, v162 neg_lo:[0,1] neg_hi:[0,1]
	v_pk_add_f16 v75, v128, v163 neg_lo:[0,1] neg_hi:[0,1]
	v_pk_add_f16 v76, v127, v164 neg_lo:[0,1] neg_hi:[0,1]
	v_pk_add_f16 v84, v84, v164 neg_lo:[0,1] neg_hi:[0,1]
	v_exp_f16_sdwa v118, v74 dst_sel:WORD_0 dst_unused:UNUSED_PAD src0_sel:WORD_0
	v_exp_f16_sdwa v119, v75 dst_sel:WORD_0 dst_unused:UNUSED_PAD src0_sel:WORD_0
	v_exp_f16_sdwa v120, v76 dst_sel:WORD_0 dst_unused:UNUSED_PAD src0_sel:WORD_0
	v_exp_f16_sdwa v121, v77 dst_sel:WORD_0 dst_unused:UNUSED_PAD src0_sel:WORD_0
	v_exp_f16_sdwa v118, v74 dst_sel:WORD_1 dst_unused:UNUSED_PRESERVE src0_sel:WORD_1
	v_exp_f16_sdwa v119, v75 dst_sel:WORD_1 dst_unused:UNUSED_PRESERVE src0_sel:WORD_1
	v_exp_f16_sdwa v120, v76 dst_sel:WORD_1 dst_unused:UNUSED_PRESERVE src0_sel:WORD_1
	v_exp_f16_sdwa v121, v77 dst_sel:WORD_1 dst_unused:UNUSED_PRESERVE src0_sel:WORD_1
	v_pk_add_f16 v85, v85, v165 neg_lo:[0,1] neg_hi:[0,1]
	v_pk_add_f16 v77, v97, v118
	v_pk_add_f16 v74, v94, v121
	v_pk_add_f16 v75, v95, v120
	v_pk_add_f16 v76, v96, v119
	v_pk_fma_f16 v57, v101, v121, v57
	v_pk_fma_f16 v56, v100, v120, v56
	v_pk_fma_f16 v55, v99, v119, v55
	v_pk_fma_f16 v54, v98, v118, v54
	v_pk_add_f16 v94, v137, v162 neg_lo:[0,1] neg_hi:[0,1]
	v_pk_add_f16 v95, v136, v163 neg_lo:[0,1] neg_hi:[0,1]
	v_pk_add_f16 v96, v135, v164 neg_lo:[0,1] neg_hi:[0,1]
	v_pk_add_f16 v97, v134, v165 neg_lo:[0,1] neg_hi:[0,1]
	v_exp_f16_sdwa v98, v94 dst_sel:WORD_0 dst_unused:UNUSED_PAD src0_sel:WORD_0
	v_exp_f16_sdwa v99, v95 dst_sel:WORD_0 dst_unused:UNUSED_PAD src0_sel:WORD_0
	v_exp_f16_sdwa v100, v96 dst_sel:WORD_0 dst_unused:UNUSED_PAD src0_sel:WORD_0
	v_exp_f16_sdwa v101, v97 dst_sel:WORD_0 dst_unused:UNUSED_PAD src0_sel:WORD_0
	v_exp_f16_sdwa v98, v94 dst_sel:WORD_1 dst_unused:UNUSED_PRESERVE src0_sel:WORD_1
	v_exp_f16_sdwa v99, v95 dst_sel:WORD_1 dst_unused:UNUSED_PRESERVE src0_sel:WORD_1
	v_exp_f16_sdwa v100, v96 dst_sel:WORD_1 dst_unused:UNUSED_PRESERVE src0_sel:WORD_1
	v_exp_f16_sdwa v101, v97 dst_sel:WORD_1 dst_unused:UNUSED_PRESERVE src0_sel:WORD_1
	v_pk_add_f16 v94, v149, v162 neg_lo:[0,1] neg_hi:[0,1]
	v_pk_add_f16 v77, v77, v98
	v_pk_add_f16 v76, v76, v99
	v_pk_add_f16 v75, v75, v100
	v_pk_add_f16 v74, v74, v101
	v_pk_fma_f16 v54, v30, v98, v54
	v_pk_fma_f16 v55, v31, v99, v55
	v_pk_fma_f16 v56, v32, v100, v56
	v_pk_fma_f16 v57, v33, v101, v57
	v_pk_add_f16 v95, v148, v163 neg_lo:[0,1] neg_hi:[0,1]
	v_pk_add_f16 v96, v147, v164 neg_lo:[0,1] neg_hi:[0,1]
	v_pk_add_f16 v97, v146, v165 neg_lo:[0,1] neg_hi:[0,1]
	v_exp_f16_sdwa v98, v94 dst_sel:WORD_0 dst_unused:UNUSED_PAD src0_sel:WORD_0
	v_exp_f16_sdwa v99, v95 dst_sel:WORD_0 dst_unused:UNUSED_PAD src0_sel:WORD_0
	v_exp_f16_sdwa v100, v96 dst_sel:WORD_0 dst_unused:UNUSED_PAD src0_sel:WORD_0
	v_exp_f16_sdwa v101, v97 dst_sel:WORD_0 dst_unused:UNUSED_PAD src0_sel:WORD_0
	v_exp_f16_sdwa v98, v94 dst_sel:WORD_1 dst_unused:UNUSED_PRESERVE src0_sel:WORD_1
	v_exp_f16_sdwa v99, v95 dst_sel:WORD_1 dst_unused:UNUSED_PRESERVE src0_sel:WORD_1
	v_exp_f16_sdwa v100, v96 dst_sel:WORD_1 dst_unused:UNUSED_PRESERVE src0_sel:WORD_1
	v_exp_f16_sdwa v101, v97 dst_sel:WORD_1 dst_unused:UNUSED_PRESERVE src0_sel:WORD_1
	v_pk_add_f16 v94, v212, v162 neg_lo:[0,1] neg_hi:[0,1]
	v_pk_add_f16 v77, v77, v98
	v_pk_add_f16 v74, v74, v101
	v_pk_add_f16 v75, v75, v100
	v_pk_add_f16 v76, v76, v99
	v_pk_fma_f16 v57, v45, v101, v57
	v_pk_fma_f16 v56, v44, v100, v56
	v_pk_fma_f16 v55, v43, v99, v55
	v_pk_fma_f16 v54, v42, v98, v54
	v_pk_add_f16 v95, v211, v163 neg_lo:[0,1] neg_hi:[0,1]
	v_pk_add_f16 v96, v210, v164 neg_lo:[0,1] neg_hi:[0,1]
	v_pk_add_f16 v97, v209, v165 neg_lo:[0,1] neg_hi:[0,1]
	v_exp_f16_sdwa v98, v94 dst_sel:WORD_0 dst_unused:UNUSED_PAD src0_sel:WORD_0
	v_exp_f16_sdwa v99, v95 dst_sel:WORD_0 dst_unused:UNUSED_PAD src0_sel:WORD_0
	v_exp_f16_sdwa v100, v96 dst_sel:WORD_0 dst_unused:UNUSED_PAD src0_sel:WORD_0
	v_exp_f16_sdwa v101, v97 dst_sel:WORD_0 dst_unused:UNUSED_PAD src0_sel:WORD_0
	v_exp_f16_sdwa v98, v94 dst_sel:WORD_1 dst_unused:UNUSED_PRESERVE src0_sel:WORD_1
	v_exp_f16_sdwa v99, v95 dst_sel:WORD_1 dst_unused:UNUSED_PRESERVE src0_sel:WORD_1
	v_exp_f16_sdwa v100, v96 dst_sel:WORD_1 dst_unused:UNUSED_PRESERVE src0_sel:WORD_1
	v_exp_f16_sdwa v101, v97 dst_sel:WORD_1 dst_unused:UNUSED_PRESERVE src0_sel:WORD_1
	v_exp_f16_sdwa v94, v82 dst_sel:WORD_0 dst_unused:UNUSED_PAD src0_sel:WORD_0
	v_exp_f16_sdwa v95, v83 dst_sel:WORD_0 dst_unused:UNUSED_PAD src0_sel:WORD_0
	v_exp_f16_sdwa v96, v84 dst_sel:WORD_0 dst_unused:UNUSED_PAD src0_sel:WORD_0
	v_exp_f16_sdwa v97, v85 dst_sel:WORD_0 dst_unused:UNUSED_PAD src0_sel:WORD_0
	v_exp_f16_sdwa v94, v82 dst_sel:WORD_1 dst_unused:UNUSED_PRESERVE src0_sel:WORD_1
	v_exp_f16_sdwa v95, v83 dst_sel:WORD_1 dst_unused:UNUSED_PRESERVE src0_sel:WORD_1
	v_exp_f16_sdwa v96, v84 dst_sel:WORD_1 dst_unused:UNUSED_PRESERVE src0_sel:WORD_1
	v_exp_f16_sdwa v97, v85 dst_sel:WORD_1 dst_unused:UNUSED_PRESERVE src0_sel:WORD_1
	v_pk_add_f16 v82, v106, v162 neg_lo:[0,1] neg_hi:[0,1]
	v_pk_add_f16 v77, v77, v98
	v_pk_add_f16 v76, v76, v99
	v_pk_add_f16 v75, v75, v100
	v_pk_add_f16 v74, v74, v101
	v_pk_fma_f16 v54, v58, v98, v54
	v_pk_fma_f16 v55, v59, v99, v55
	v_pk_fma_f16 v56, v60, v100, v56
	v_pk_fma_f16 v57, v61, v101, v57
	v_pk_add_f16 v77, v77, v94
	v_pk_add_f16 v74, v74, v97
	v_pk_add_f16 v75, v75, v96
	v_pk_add_f16 v76, v76, v95
	v_pk_fma_f16 v57, v21, v97, v57
	v_pk_fma_f16 v56, v20, v96, v56
	v_pk_fma_f16 v55, v19, v95, v55
	v_pk_fma_f16 v54, v18, v94, v54
	v_pk_add_f16 v83, v107, v163 neg_lo:[0,1] neg_hi:[0,1]
	v_pk_add_f16 v84, v108, v164 neg_lo:[0,1] neg_hi:[0,1]
	v_pk_add_f16 v85, v109, v165 neg_lo:[0,1] neg_hi:[0,1]
	v_exp_f16_sdwa v94, v82 dst_sel:WORD_0 dst_unused:UNUSED_PAD src0_sel:WORD_0
	v_exp_f16_sdwa v95, v83 dst_sel:WORD_0 dst_unused:UNUSED_PAD src0_sel:WORD_0
	v_exp_f16_sdwa v96, v84 dst_sel:WORD_0 dst_unused:UNUSED_PAD src0_sel:WORD_0
	v_exp_f16_sdwa v97, v85 dst_sel:WORD_0 dst_unused:UNUSED_PAD src0_sel:WORD_0
	v_exp_f16_sdwa v94, v82 dst_sel:WORD_1 dst_unused:UNUSED_PRESERVE src0_sel:WORD_1
	v_exp_f16_sdwa v95, v83 dst_sel:WORD_1 dst_unused:UNUSED_PRESERVE src0_sel:WORD_1
	v_exp_f16_sdwa v96, v84 dst_sel:WORD_1 dst_unused:UNUSED_PRESERVE src0_sel:WORD_1
	v_exp_f16_sdwa v97, v85 dst_sel:WORD_1 dst_unused:UNUSED_PRESERVE src0_sel:WORD_1
	v_pk_add_f16 v82, v122, v162 neg_lo:[0,1] neg_hi:[0,1]
	v_pk_add_f16 v77, v77, v94
	v_pk_add_f16 v76, v76, v95
	v_pk_add_f16 v75, v75, v96
	v_pk_add_f16 v74, v74, v97
	v_pk_fma_f16 v54, v22, v94, v54
	v_pk_fma_f16 v55, v23, v95, v55
	v_pk_fma_f16 v56, v24, v96, v56
	v_pk_fma_f16 v57, v25, v97, v57
	v_pk_add_f16 v83, v123, v163 neg_lo:[0,1] neg_hi:[0,1]
	v_pk_add_f16 v84, v124, v164 neg_lo:[0,1] neg_hi:[0,1]
	v_pk_add_f16 v85, v125, v165 neg_lo:[0,1] neg_hi:[0,1]
	v_exp_f16_sdwa v94, v82 dst_sel:WORD_0 dst_unused:UNUSED_PAD src0_sel:WORD_0
	v_exp_f16_sdwa v95, v83 dst_sel:WORD_0 dst_unused:UNUSED_PAD src0_sel:WORD_0
	v_exp_f16_sdwa v96, v84 dst_sel:WORD_0 dst_unused:UNUSED_PAD src0_sel:WORD_0
	v_exp_f16_sdwa v97, v85 dst_sel:WORD_0 dst_unused:UNUSED_PAD src0_sel:WORD_0
	v_exp_f16_sdwa v94, v82 dst_sel:WORD_1 dst_unused:UNUSED_PRESERVE src0_sel:WORD_1
	v_exp_f16_sdwa v95, v83 dst_sel:WORD_1 dst_unused:UNUSED_PRESERVE src0_sel:WORD_1
	v_exp_f16_sdwa v96, v84 dst_sel:WORD_1 dst_unused:UNUSED_PRESERVE src0_sel:WORD_1
	v_exp_f16_sdwa v97, v85 dst_sel:WORD_1 dst_unused:UNUSED_PRESERVE src0_sel:WORD_1
	v_pk_add_f16 v77, v77, v94
	v_pk_add_f16 v76, v76, v95
	v_rcp_f16_e32 v82, v77
	v_rcp_f16_sdwa v77, v77 dst_sel:DWORD dst_unused:UNUSED_PAD src0_sel:WORD_1
	v_pk_add_f16 v75, v75, v96
	v_rcp_f16_e32 v83, v76
	v_rcp_f16_sdwa v76, v76 dst_sel:DWORD dst_unused:UNUSED_PAD src0_sel:WORD_1
	v_pk_add_f16 v74, v74, v97
	v_rcp_f16_e32 v84, v75
	v_rcp_f16_sdwa v75, v75 dst_sel:DWORD dst_unused:UNUSED_PAD src0_sel:WORD_1
	v_rcp_f16_e32 v85, v74
	v_rcp_f16_sdwa v74, v74 dst_sel:DWORD dst_unused:UNUSED_PAD src0_sel:WORD_1
	v_pk_fma_f16 v54, v26, v94, v54
	v_pack_b32_f16 v77, v82, v77
	v_pk_fma_f16 v57, v29, v97, v57
	v_pk_fma_f16 v55, v27, v95, v55
	v_pk_mul_f16 v97, v54, v77
	v_pack_b32_f16 v54, v83, v76
	v_pk_fma_f16 v56, v28, v96, v56
	v_pk_mul_f16 v96, v55, v54
	v_pack_b32_f16 v54, v84, v75
	v_pk_mul_f16 v95, v56, v54
	v_pack_b32_f16 v54, v85, v74
	v_pk_mul_f16 v94, v57, v54
	s_waitcnt vmcnt(6)
	v_pk_mul_f16 v57, v208, v161 op_sel_hi:[0,1]
	v_pk_mul_f16 v77, v206, v161 op_sel_hi:[0,1]
	v_pk_mul_f16 v85, v207, v161 op_sel_hi:[0,1]
	v_pk_mul_f16 v54, v208, v158 op_sel_hi:[0,1]
	v_pk_mul_f16 v55, v208, v159 op_sel_hi:[0,1]
	v_pk_mul_f16 v56, v208, v160 op_sel_hi:[0,1]
	v_pk_mul_f16 v74, v206, v158 op_sel_hi:[0,1]
	v_pk_mul_f16 v75, v206, v159 op_sel_hi:[0,1]
	v_pk_mul_f16 v76, v206, v160 op_sel_hi:[0,1]
	v_pk_mul_f16 v82, v207, v158 op_sel_hi:[0,1]
	v_pk_mul_f16 v83, v207, v159 op_sel_hi:[0,1]
	v_pk_mul_f16 v84, v207, v160 op_sel_hi:[0,1]
	v_pk_fma_f16 v65, v65, v161, v57
	v_pk_fma_f16 v81, v81, v161, v77
	v_pk_fma_f16 v98, v105, v161, v85
	v_pk_fma_f16 v64, v64, v160, v56
	v_pk_maximum3_f16 v125, v65, v81, v98
	v_pk_fma_f16 v63, v63, v159, v55
	v_pk_fma_f16 v62, v62, v158, v54
	v_pk_fma_f16 v80, v80, v160, v76
	v_pk_fma_f16 v79, v79, v159, v75
	v_pk_fma_f16 v78, v78, v158, v74
	v_pk_fma_f16 v99, v104, v160, v84
	v_pk_fma_f16 v100, v103, v159, v83
	v_pk_fma_f16 v101, v102, v158, v82
	v_pk_fma_f16 v102, v37, v161, v57
	v_pk_fma_f16 v106, v49, v161, v77
	v_pk_fma_f16 v118, v69, v161, v85
	v_pk_fma_f16 v57, v89, v161, v57
	v_pk_fma_f16 v77, v117, v161, v77
	v_pk_fma_f16 v85, v133, v161, v85
	v_pk_maximum3_f16 v122, v62, v78, v101
	v_pk_maximum3_f16 v123, v63, v79, v100
	v_pk_maximum3_f16 v124, v64, v80, v99
	v_pk_maximum3_f16 v129, v102, v106, v118
	v_pk_fma_f16 v103, v36, v160, v56
	v_pk_maximum3_f16 v137, v57, v77, v85
	v_pk_fma_f16 v104, v35, v159, v55
	v_pk_maximum3_f16 v125, v125, v129, v137
	v_pk_fma_f16 v105, v34, v158, v54
	v_pk_fma_f16 v107, v48, v160, v76
	v_pk_fma_f16 v108, v47, v159, v75
	v_pk_fma_f16 v109, v46, v158, v74
	v_pk_fma_f16 v119, v68, v160, v84
	v_pk_fma_f16 v120, v67, v159, v83
	v_pk_fma_f16 v121, v66, v158, v82
	v_pk_fma_f16 v56, v88, v160, v56
	v_pk_fma_f16 v55, v87, v159, v55
	v_pk_fma_f16 v54, v86, v158, v54
	v_pk_fma_f16 v76, v116, v160, v76
	v_pk_fma_f16 v75, v115, v159, v75
	v_pk_fma_f16 v74, v114, v158, v74
	v_pk_fma_f16 v84, v132, v160, v84
	v_pk_fma_f16 v83, v131, v159, v83
	v_pk_fma_f16 v82, v130, v158, v82
	v_pk_maximum3_f16 v126, v105, v109, v121
	v_pk_maximum3_f16 v127, v104, v108, v120
	v_pk_maximum3_f16 v128, v103, v107, v119
	v_pk_maximum3_f16 v135, v55, v75, v83
	v_pk_maximum3_f16 v136, v56, v76, v84
	v_pk_maximum3_f16 v134, v54, v74, v82
	v_pk_maximum3_f16 v122, v122, v126, v134
	v_pk_maximum3_f16 v123, v123, v127, v135
	v_pk_maximum3_f16 v124, v124, v128, v136
	v_pk_add_f16 v65, v65, v125 neg_lo:[0,1] neg_hi:[0,1]
	v_pk_add_f16 v62, v62, v122 neg_lo:[0,1] neg_hi:[0,1]
	v_pk_add_f16 v63, v63, v123 neg_lo:[0,1] neg_hi:[0,1]
	v_pk_add_f16 v64, v64, v124 neg_lo:[0,1] neg_hi:[0,1]
	v_pk_add_f16 v78, v78, v122 neg_lo:[0,1] neg_hi:[0,1]
	v_exp_f16_sdwa v126, v62 dst_sel:WORD_0 dst_unused:UNUSED_PAD src0_sel:WORD_0
	v_exp_f16_sdwa v127, v63 dst_sel:WORD_0 dst_unused:UNUSED_PAD src0_sel:WORD_0
	v_exp_f16_sdwa v128, v64 dst_sel:WORD_0 dst_unused:UNUSED_PAD src0_sel:WORD_0
	v_exp_f16_sdwa v129, v65 dst_sel:WORD_0 dst_unused:UNUSED_PAD src0_sel:WORD_0
	v_exp_f16_sdwa v126, v62 dst_sel:WORD_1 dst_unused:UNUSED_PRESERVE src0_sel:WORD_1
	v_exp_f16_sdwa v127, v63 dst_sel:WORD_1 dst_unused:UNUSED_PRESERVE src0_sel:WORD_1
	v_exp_f16_sdwa v128, v64 dst_sel:WORD_1 dst_unused:UNUSED_PRESERVE src0_sel:WORD_1
	v_exp_f16_sdwa v129, v65 dst_sel:WORD_1 dst_unused:UNUSED_PRESERVE src0_sel:WORD_1
	v_pk_add_f16 v79, v79, v123 neg_lo:[0,1] neg_hi:[0,1]
	v_pk_add_f16 v65, v126, 0
	v_pk_fma_f16 v33, v33, v129, 0
	v_pk_add_f16 v62, v129, 0
	v_pk_add_f16 v63, v128, 0
	v_pk_add_f16 v64, v127, 0
	v_pk_fma_f16 v32, v32, v128, 0
	v_pk_fma_f16 v31, v31, v127, 0
	v_pk_fma_f16 v30, v30, v126, 0
	v_pk_add_f16 v80, v80, v124 neg_lo:[0,1] neg_hi:[0,1]
	v_pk_add_f16 v81, v81, v125 neg_lo:[0,1] neg_hi:[0,1]
	v_pk_add_f16 v54, v54, v122 neg_lo:[0,1] neg_hi:[0,1]
	v_exp_f16_sdwa v126, v78 dst_sel:WORD_0 dst_unused:UNUSED_PAD src0_sel:WORD_0
	v_exp_f16_sdwa v127, v79 dst_sel:WORD_0 dst_unused:UNUSED_PAD src0_sel:WORD_0
	v_exp_f16_sdwa v128, v80 dst_sel:WORD_0 dst_unused:UNUSED_PAD src0_sel:WORD_0
	v_exp_f16_sdwa v129, v81 dst_sel:WORD_0 dst_unused:UNUSED_PAD src0_sel:WORD_0
	v_exp_f16_sdwa v126, v78 dst_sel:WORD_1 dst_unused:UNUSED_PRESERVE src0_sel:WORD_1
	v_exp_f16_sdwa v127, v79 dst_sel:WORD_1 dst_unused:UNUSED_PRESERVE src0_sel:WORD_1
	v_exp_f16_sdwa v128, v80 dst_sel:WORD_1 dst_unused:UNUSED_PRESERVE src0_sel:WORD_1
	v_exp_f16_sdwa v129, v81 dst_sel:WORD_1 dst_unused:UNUSED_PRESERVE src0_sel:WORD_1
	v_pk_add_f16 v55, v55, v123 neg_lo:[0,1] neg_hi:[0,1]
	v_pk_add_f16 v65, v65, v126
	v_pk_fma_f16 v33, v45, v129, v33
	v_pk_add_f16 v45, v98, v125 neg_lo:[0,1] neg_hi:[0,1]
	v_pk_add_f16 v64, v64, v127
	v_pk_add_f16 v63, v63, v128
	v_pk_add_f16 v62, v62, v129
	v_pk_fma_f16 v30, v42, v126, v30
	v_pk_fma_f16 v31, v43, v127, v31
	v_pk_fma_f16 v32, v44, v128, v32
	v_pk_add_f16 v42, v101, v122 neg_lo:[0,1] neg_hi:[0,1]
	v_pk_add_f16 v43, v100, v123 neg_lo:[0,1] neg_hi:[0,1]
	v_pk_add_f16 v44, v99, v124 neg_lo:[0,1] neg_hi:[0,1]
	v_pk_add_f16 v56, v56, v124 neg_lo:[0,1] neg_hi:[0,1]
	v_exp_f16_sdwa v78, v42 dst_sel:WORD_0 dst_unused:UNUSED_PAD src0_sel:WORD_0
	v_exp_f16_sdwa v79, v43 dst_sel:WORD_0 dst_unused:UNUSED_PAD src0_sel:WORD_0
	v_exp_f16_sdwa v80, v44 dst_sel:WORD_0 dst_unused:UNUSED_PAD src0_sel:WORD_0
	v_exp_f16_sdwa v81, v45 dst_sel:WORD_0 dst_unused:UNUSED_PAD src0_sel:WORD_0
	v_exp_f16_sdwa v78, v42 dst_sel:WORD_1 dst_unused:UNUSED_PRESERVE src0_sel:WORD_1
	v_exp_f16_sdwa v79, v43 dst_sel:WORD_1 dst_unused:UNUSED_PRESERVE src0_sel:WORD_1
	v_exp_f16_sdwa v80, v44 dst_sel:WORD_1 dst_unused:UNUSED_PRESERVE src0_sel:WORD_1
	v_exp_f16_sdwa v81, v45 dst_sel:WORD_1 dst_unused:UNUSED_PRESERVE src0_sel:WORD_1
	v_pk_add_f16 v57, v57, v125 neg_lo:[0,1] neg_hi:[0,1]
	v_pk_add_f16 v45, v65, v78
	v_pk_add_f16 v42, v62, v81
	v_pk_add_f16 v43, v63, v80
	v_pk_add_f16 v44, v64, v79
	v_pk_fma_f16 v33, v61, v81, v33
	v_pk_fma_f16 v32, v60, v80, v32
	v_pk_fma_f16 v31, v59, v79, v31
	v_pk_fma_f16 v30, v58, v78, v30
	v_pk_add_f16 v58, v105, v122 neg_lo:[0,1] neg_hi:[0,1]
	v_pk_add_f16 v59, v104, v123 neg_lo:[0,1] neg_hi:[0,1]
	v_pk_add_f16 v60, v103, v124 neg_lo:[0,1] neg_hi:[0,1]
	v_pk_add_f16 v61, v102, v125 neg_lo:[0,1] neg_hi:[0,1]
	v_exp_f16_sdwa v62, v58 dst_sel:WORD_0 dst_unused:UNUSED_PAD src0_sel:WORD_0
	v_exp_f16_sdwa v63, v59 dst_sel:WORD_0 dst_unused:UNUSED_PAD src0_sel:WORD_0
	v_exp_f16_sdwa v64, v60 dst_sel:WORD_0 dst_unused:UNUSED_PAD src0_sel:WORD_0
	v_exp_f16_sdwa v65, v61 dst_sel:WORD_0 dst_unused:UNUSED_PAD src0_sel:WORD_0
	v_exp_f16_sdwa v62, v58 dst_sel:WORD_1 dst_unused:UNUSED_PRESERVE src0_sel:WORD_1
	v_exp_f16_sdwa v63, v59 dst_sel:WORD_1 dst_unused:UNUSED_PRESERVE src0_sel:WORD_1
	v_exp_f16_sdwa v64, v60 dst_sel:WORD_1 dst_unused:UNUSED_PRESERVE src0_sel:WORD_1
	v_exp_f16_sdwa v65, v61 dst_sel:WORD_1 dst_unused:UNUSED_PRESERVE src0_sel:WORD_1
	v_pk_add_f16 v58, v109, v122 neg_lo:[0,1] neg_hi:[0,1]
	v_pk_add_f16 v45, v45, v62
	v_pk_add_f16 v44, v44, v63
	v_pk_add_f16 v43, v43, v64
	v_pk_add_f16 v42, v42, v65
	v_pk_fma_f16 v30, v18, v62, v30
	v_pk_fma_f16 v31, v19, v63, v31
	v_pk_fma_f16 v32, v20, v64, v32
	v_pk_fma_f16 v33, v21, v65, v33
	v_pk_add_f16 v59, v108, v123 neg_lo:[0,1] neg_hi:[0,1]
	v_pk_add_f16 v60, v107, v124 neg_lo:[0,1] neg_hi:[0,1]
	v_pk_add_f16 v61, v106, v125 neg_lo:[0,1] neg_hi:[0,1]
	v_exp_f16_sdwa v62, v58 dst_sel:WORD_0 dst_unused:UNUSED_PAD src0_sel:WORD_0
	v_exp_f16_sdwa v63, v59 dst_sel:WORD_0 dst_unused:UNUSED_PAD src0_sel:WORD_0
	v_exp_f16_sdwa v64, v60 dst_sel:WORD_0 dst_unused:UNUSED_PAD src0_sel:WORD_0
	v_exp_f16_sdwa v65, v61 dst_sel:WORD_0 dst_unused:UNUSED_PAD src0_sel:WORD_0
	v_exp_f16_sdwa v62, v58 dst_sel:WORD_1 dst_unused:UNUSED_PRESERVE src0_sel:WORD_1
	v_exp_f16_sdwa v63, v59 dst_sel:WORD_1 dst_unused:UNUSED_PRESERVE src0_sel:WORD_1
	v_exp_f16_sdwa v64, v60 dst_sel:WORD_1 dst_unused:UNUSED_PRESERVE src0_sel:WORD_1
	v_exp_f16_sdwa v65, v61 dst_sel:WORD_1 dst_unused:UNUSED_PRESERVE src0_sel:WORD_1
	v_pk_add_f16 v58, v121, v122 neg_lo:[0,1] neg_hi:[0,1]
	v_pk_add_f16 v45, v45, v62
	v_pk_add_f16 v42, v42, v65
	v_pk_add_f16 v43, v43, v64
	v_pk_add_f16 v44, v44, v63
	v_pk_fma_f16 v33, v25, v65, v33
	v_pk_fma_f16 v32, v24, v64, v32
	v_pk_fma_f16 v31, v23, v63, v31
	v_pk_fma_f16 v30, v22, v62, v30
	v_pk_add_f16 v59, v120, v123 neg_lo:[0,1] neg_hi:[0,1]
	v_pk_add_f16 v60, v119, v124 neg_lo:[0,1] neg_hi:[0,1]
	v_pk_add_f16 v61, v118, v125 neg_lo:[0,1] neg_hi:[0,1]
	v_exp_f16_sdwa v62, v58 dst_sel:WORD_0 dst_unused:UNUSED_PAD src0_sel:WORD_0
	v_exp_f16_sdwa v63, v59 dst_sel:WORD_0 dst_unused:UNUSED_PAD src0_sel:WORD_0
	v_exp_f16_sdwa v64, v60 dst_sel:WORD_0 dst_unused:UNUSED_PAD src0_sel:WORD_0
	v_exp_f16_sdwa v65, v61 dst_sel:WORD_0 dst_unused:UNUSED_PAD src0_sel:WORD_0
	v_exp_f16_sdwa v62, v58 dst_sel:WORD_1 dst_unused:UNUSED_PRESERVE src0_sel:WORD_1
	v_exp_f16_sdwa v63, v59 dst_sel:WORD_1 dst_unused:UNUSED_PRESERVE src0_sel:WORD_1
	v_exp_f16_sdwa v64, v60 dst_sel:WORD_1 dst_unused:UNUSED_PRESERVE src0_sel:WORD_1
	v_exp_f16_sdwa v65, v61 dst_sel:WORD_1 dst_unused:UNUSED_PRESERVE src0_sel:WORD_1
	v_exp_f16_sdwa v58, v54 dst_sel:WORD_0 dst_unused:UNUSED_PAD src0_sel:WORD_0
	v_exp_f16_sdwa v59, v55 dst_sel:WORD_0 dst_unused:UNUSED_PAD src0_sel:WORD_0
	v_exp_f16_sdwa v60, v56 dst_sel:WORD_0 dst_unused:UNUSED_PAD src0_sel:WORD_0
	v_exp_f16_sdwa v61, v57 dst_sel:WORD_0 dst_unused:UNUSED_PAD src0_sel:WORD_0
	v_exp_f16_sdwa v58, v54 dst_sel:WORD_1 dst_unused:UNUSED_PRESERVE src0_sel:WORD_1
	v_exp_f16_sdwa v59, v55 dst_sel:WORD_1 dst_unused:UNUSED_PRESERVE src0_sel:WORD_1
	v_exp_f16_sdwa v60, v56 dst_sel:WORD_1 dst_unused:UNUSED_PRESERVE src0_sel:WORD_1
	v_exp_f16_sdwa v61, v57 dst_sel:WORD_1 dst_unused:UNUSED_PRESERVE src0_sel:WORD_1
	v_pk_add_f16 v54, v74, v122 neg_lo:[0,1] neg_hi:[0,1]
	v_pk_add_f16 v45, v45, v62
	v_pk_add_f16 v44, v44, v63
	v_pk_add_f16 v43, v43, v64
	v_pk_add_f16 v42, v42, v65
	v_pk_fma_f16 v30, v26, v62, v30
	v_pk_fma_f16 v31, v27, v63, v31
	v_pk_fma_f16 v32, v28, v64, v32
	v_pk_fma_f16 v33, v29, v65, v33
	v_pk_add_f16 v45, v45, v58
	v_pk_add_f16 v42, v42, v61
	v_pk_add_f16 v43, v43, v60
	v_pk_add_f16 v44, v44, v59
	v_pk_fma_f16 v33, v41, v61, v33
	v_pk_fma_f16 v32, v40, v60, v32
	v_pk_fma_f16 v31, v39, v59, v31
	v_pk_fma_f16 v30, v38, v58, v30
	v_pk_add_f16 v55, v75, v123 neg_lo:[0,1] neg_hi:[0,1]
	v_pk_add_f16 v56, v76, v124 neg_lo:[0,1] neg_hi:[0,1]
	v_pk_add_f16 v57, v77, v125 neg_lo:[0,1] neg_hi:[0,1]
	v_exp_f16_sdwa v58, v54 dst_sel:WORD_0 dst_unused:UNUSED_PAD src0_sel:WORD_0
	v_exp_f16_sdwa v59, v55 dst_sel:WORD_0 dst_unused:UNUSED_PAD src0_sel:WORD_0
	v_exp_f16_sdwa v60, v56 dst_sel:WORD_0 dst_unused:UNUSED_PAD src0_sel:WORD_0
	v_exp_f16_sdwa v61, v57 dst_sel:WORD_0 dst_unused:UNUSED_PAD src0_sel:WORD_0
	v_exp_f16_sdwa v58, v54 dst_sel:WORD_1 dst_unused:UNUSED_PRESERVE src0_sel:WORD_1
	v_exp_f16_sdwa v59, v55 dst_sel:WORD_1 dst_unused:UNUSED_PRESERVE src0_sel:WORD_1
	v_exp_f16_sdwa v60, v56 dst_sel:WORD_1 dst_unused:UNUSED_PRESERVE src0_sel:WORD_1
	v_exp_f16_sdwa v61, v57 dst_sel:WORD_1 dst_unused:UNUSED_PRESERVE src0_sel:WORD_1
	v_pk_add_f16 v54, v82, v122 neg_lo:[0,1] neg_hi:[0,1]
	v_pk_add_f16 v45, v45, v58
	v_pk_add_f16 v44, v44, v59
	v_pk_add_f16 v43, v43, v60
	v_pk_add_f16 v42, v42, v61
	v_pk_fma_f16 v30, v50, v58, v30
	v_pk_fma_f16 v31, v51, v59, v31
	v_pk_fma_f16 v32, v52, v60, v32
	v_pk_fma_f16 v33, v53, v61, v33
	v_pk_add_f16 v55, v83, v123 neg_lo:[0,1] neg_hi:[0,1]
	v_pk_add_f16 v56, v84, v124 neg_lo:[0,1] neg_hi:[0,1]
	v_pk_add_f16 v57, v85, v125 neg_lo:[0,1] neg_hi:[0,1]
	v_exp_f16_sdwa v58, v54 dst_sel:WORD_0 dst_unused:UNUSED_PAD src0_sel:WORD_0
	v_exp_f16_sdwa v59, v55 dst_sel:WORD_0 dst_unused:UNUSED_PAD src0_sel:WORD_0
	v_exp_f16_sdwa v60, v56 dst_sel:WORD_0 dst_unused:UNUSED_PAD src0_sel:WORD_0
	v_exp_f16_sdwa v61, v57 dst_sel:WORD_0 dst_unused:UNUSED_PAD src0_sel:WORD_0
	v_exp_f16_sdwa v58, v54 dst_sel:WORD_1 dst_unused:UNUSED_PRESERVE src0_sel:WORD_1
	v_exp_f16_sdwa v59, v55 dst_sel:WORD_1 dst_unused:UNUSED_PRESERVE src0_sel:WORD_1
	v_exp_f16_sdwa v60, v56 dst_sel:WORD_1 dst_unused:UNUSED_PRESERVE src0_sel:WORD_1
	v_exp_f16_sdwa v61, v57 dst_sel:WORD_1 dst_unused:UNUSED_PRESERVE src0_sel:WORD_1
	v_pk_add_f16 v45, v45, v58
	v_pk_add_f16 v44, v44, v59
	v_rcp_f16_e32 v54, v45
	v_rcp_f16_sdwa v45, v45 dst_sel:DWORD dst_unused:UNUSED_PAD src0_sel:WORD_1
	v_pk_add_f16 v43, v43, v60
	v_rcp_f16_e32 v55, v44
	v_rcp_f16_sdwa v44, v44 dst_sel:DWORD dst_unused:UNUSED_PAD src0_sel:WORD_1
	v_pk_add_f16 v42, v42, v61
	v_rcp_f16_e32 v56, v43
	v_rcp_f16_sdwa v43, v43 dst_sel:DWORD dst_unused:UNUSED_PAD src0_sel:WORD_1
	v_rcp_f16_e32 v57, v42
	v_rcp_f16_sdwa v42, v42 dst_sel:DWORD dst_unused:UNUSED_PAD src0_sel:WORD_1
	v_pk_fma_f16 v30, v70, v58, v30
	v_pack_b32_f16 v45, v54, v45
	v_pk_fma_f16 v31, v71, v59, v31
	v_pk_mul_f16 v45, v30, v45
	v_pack_b32_f16 v30, v55, v44
	v_pk_fma_f16 v32, v72, v60, v32
	v_pk_mul_f16 v44, v31, v30
	v_pack_b32_f16 v30, v56, v43
	v_pk_fma_f16 v33, v73, v61, v33
	v_pk_mul_f16 v43, v32, v30
	v_pack_b32_f16 v30, v57, v42
	v_pk_mul_f16 v42, v33, v30
	s_waitcnt vmcnt(0)
	s_mul_i32 s84, s81, s83
	s_add_i32 s84, s84, s82
	s_mul_i32 s84, s84, 0x60000
	s_mul_i32 s85, s94, 0x6000
	s_add_u32 s84, s84, s85
	s_add_u32 s88, s86, s84
	s_addc_u32 s89, s87, 0
	v_mbcnt_lo_u32_b32 v251, -1, 0
	v_mbcnt_hi_u32_b32 v251, -1, v251
	v_lshlrev_b32_e32 v251, 4, v251
	global_load_dwordx4 v[252:255], v251, s[88:89]
	global_load_dwordx4 v[252:255], v251, s[88:89] offset:1024
	global_load_dwordx4 v[252:255], v251, s[88:89] offset:2048
	global_load_dwordx4 v[252:255], v251, s[88:89] offset:3072
	s_add_u32 s88, s88, 0x1000
	s_addc_u32 s89, s89, 0
	global_load_dwordx4 v[252:255], v251, s[88:89]
	global_load_dwordx4 v[252:255], v251, s[88:89] offset:1024
	global_load_dwordx4 v[252:255], v251, s[88:89] offset:2048
	global_load_dwordx4 v[252:255], v251, s[88:89] offset:3072
	s_add_u32 s88, s88, 0x1000
	s_addc_u32 s89, s89, 0
	global_load_dwordx4 v[252:255], v251, s[88:89]
	global_load_dwordx4 v[252:255], v251, s[88:89] offset:1024
	global_load_dwordx4 v[252:255], v251, s[88:89] offset:2048
	global_load_dwordx4 v[252:255], v251, s[88:89] offset:3072
	v_pk_mul_f16 v30, v208, v154 op_sel_hi:[0,1]
	v_pk_mul_f16 v31, v208, v155 op_sel_hi:[0,1]
	v_pk_mul_f16 v32, v208, v156 op_sel_hi:[0,1]
	v_pk_mul_f16 v33, v208, v157 op_sel_hi:[0,1]
	v_pk_mul_f16 v54, v206, v154 op_sel_hi:[0,1]
	v_pk_mul_f16 v55, v206, v155 op_sel_hi:[0,1]
	v_pk_mul_f16 v56, v206, v156 op_sel_hi:[0,1]
	v_pk_mul_f16 v57, v206, v157 op_sel_hi:[0,1]
	v_pk_mul_f16 v58, v207, v154 op_sel_hi:[0,1]
	v_pk_mul_f16 v59, v207, v155 op_sel_hi:[0,1]
	v_pk_mul_f16 v60, v207, v156 op_sel_hi:[0,1]
	v_pk_mul_f16 v61, v207, v157 op_sel_hi:[0,1]
	v_pk_fma_f16 v37, v37, v157, v33
	v_pk_fma_f16 v36, v36, v156, v32
	v_pk_fma_f16 v35, v35, v155, v31
	v_pk_fma_f16 v34, v34, v154, v30
	v_pk_fma_f16 v49, v49, v157, v57
	v_pk_fma_f16 v48, v48, v156, v56
	v_pk_fma_f16 v47, v47, v155, v55
	v_pk_fma_f16 v46, v46, v154, v54
	v_pk_fma_f16 v62, v69, v157, v61
	v_pk_fma_f16 v63, v68, v156, v60
	v_pk_fma_f16 v64, v67, v155, v59
	v_pk_fma_f16 v65, v66, v154, v58
	v_pk_fma_f16 v66, v89, v157, v33
	v_pk_fma_f16 v67, v88, v156, v32
	v_pk_fma_f16 v68, v87, v155, v31
	v_pk_fma_f16 v69, v86, v154, v30
	v_pk_fma_f16 v74, v117, v157, v57
	v_pk_fma_f16 v75, v116, v156, v56
	v_pk_fma_f16 v76, v115, v155, v55
	v_pk_fma_f16 v77, v114, v154, v54
	v_pk_fma_f16 v78, v133, v157, v61
	v_pk_fma_f16 v79, v132, v156, v60
	v_pk_fma_f16 v80, v131, v155, v59
	v_pk_fma_f16 v81, v130, v154, v58
	v_pk_fma_f16 v61, v17, v157, v61
	v_pk_fma_f16 v60, v16, v156, v60
	v_pk_fma_f16 v59, v15, v155, v59
	v_pk_fma_f16 v58, v14, v154, v58
	v_pk_maximum3_f16 v14, v34, v46, v65
	v_pk_maximum3_f16 v15, v35, v47, v64
	v_pk_maximum3_f16 v16, v36, v48, v63
	v_pk_maximum3_f16 v17, v37, v49, v62
	v_pk_maximum3_f16 v82, v69, v77, v81
	v_pk_maximum3_f16 v83, v68, v76, v80
	v_pk_maximum3_f16 v84, v67, v75, v79
	v_pk_maximum3_f16 v85, v66, v74, v78
	v_pk_fma_f16 v33, v145, v157, v33
	v_pk_fma_f16 v32, v144, v156, v32
	v_pk_fma_f16 v31, v143, v155, v31
	v_pk_fma_f16 v30, v142, v154, v30
	v_pk_fma_f16 v57, v153, v157, v57
	v_pk_fma_f16 v56, v152, v156, v56
	v_pk_fma_f16 v55, v151, v155, v55
	v_pk_fma_f16 v54, v150, v154, v54
	v_pk_maximum3_f16 v87, v31, v55, v59
	v_pk_maximum3_f16 v88, v32, v56, v60
	v_pk_maximum3_f16 v89, v33, v57, v61
	v_pk_maximum3_f16 v86, v30, v54, v58
	v_pk_maximum3_f16 v15, v15, v83, v87
	v_pk_maximum3_f16 v16, v16, v84, v88
	v_pk_maximum3_f16 v17, v17, v85, v89
	v_pk_maximum3_f16 v14, v14, v82, v86
	v_xor_b32_e32 v82, 0x80008000, v17
	v_xor_b32_e32 v83, 0x80008000, v16
	v_xor_b32_e32 v84, 0x80008000, v15
	v_xor_b32_e32 v85, 0x80008000, v14
	v_pk_add_f16 v14, v34, v85
	v_pk_add_f16 v15, v35, v84
	v_pk_add_f16 v16, v36, v83
	v_pk_add_f16 v17, v37, v82
	v_exp_f16_sdwa v34, v14 dst_sel:WORD_0 dst_unused:UNUSED_PAD src0_sel:WORD_0
	v_exp_f16_sdwa v35, v15 dst_sel:WORD_0 dst_unused:UNUSED_PAD src0_sel:WORD_0
	v_exp_f16_sdwa v36, v16 dst_sel:WORD_0 dst_unused:UNUSED_PAD src0_sel:WORD_0
	v_exp_f16_sdwa v37, v17 dst_sel:WORD_0 dst_unused:UNUSED_PAD src0_sel:WORD_0
	v_exp_f16_sdwa v34, v14 dst_sel:WORD_1 dst_unused:UNUSED_PRESERVE src0_sel:WORD_1
	v_exp_f16_sdwa v35, v15 dst_sel:WORD_1 dst_unused:UNUSED_PRESERVE src0_sel:WORD_1
	v_exp_f16_sdwa v36, v16 dst_sel:WORD_1 dst_unused:UNUSED_PRESERVE src0_sel:WORD_1
	v_exp_f16_sdwa v37, v17 dst_sel:WORD_1 dst_unused:UNUSED_PRESERVE src0_sel:WORD_1
	v_pk_add_f16 v14, v34, 0
	v_pk_add_f16 v15, v35, 0
	v_pk_add_f16 v16, v36, 0
	v_pk_add_f16 v17, v37, 0
	v_pk_fma_f16 v18, v18, v34, 0
	v_pk_fma_f16 v19, v19, v35, 0
	v_pk_fma_f16 v20, v20, v36, 0
	v_pk_fma_f16 v21, v21, v37, 0
	v_pk_add_f16 v34, v46, v85
	v_pk_add_f16 v35, v47, v84
	v_pk_add_f16 v36, v48, v83
	v_pk_add_f16 v37, v49, v82
	v_exp_f16_sdwa v46, v34 dst_sel:WORD_0 dst_unused:UNUSED_PAD src0_sel:WORD_0
	v_exp_f16_sdwa v47, v35 dst_sel:WORD_0 dst_unused:UNUSED_PAD src0_sel:WORD_0
	v_exp_f16_sdwa v48, v36 dst_sel:WORD_0 dst_unused:UNUSED_PAD src0_sel:WORD_0
	v_exp_f16_sdwa v49, v37 dst_sel:WORD_0 dst_unused:UNUSED_PAD src0_sel:WORD_0
	v_exp_f16_sdwa v46, v34 dst_sel:WORD_1 dst_unused:UNUSED_PRESERVE src0_sel:WORD_1
	v_exp_f16_sdwa v47, v35 dst_sel:WORD_1 dst_unused:UNUSED_PRESERVE src0_sel:WORD_1
	v_exp_f16_sdwa v48, v36 dst_sel:WORD_1 dst_unused:UNUSED_PRESERVE src0_sel:WORD_1
	v_exp_f16_sdwa v49, v37 dst_sel:WORD_1 dst_unused:UNUSED_PRESERVE src0_sel:WORD_1
	s_nop 0
	v_pk_add_f16 v17, v17, v49
	v_pk_add_f16 v16, v16, v48
	v_pk_add_f16 v15, v15, v47
	v_pk_add_f16 v14, v14, v46
	v_pk_fma_f16 v21, v25, v49, v21
	v_pk_fma_f16 v20, v24, v48, v20
	v_pk_fma_f16 v19, v23, v47, v19
	v_pk_fma_f16 v18, v22, v46, v18
	v_pk_add_f16 v22, v65, v85
	v_pk_add_f16 v23, v64, v84
	v_pk_add_f16 v24, v63, v83
	v_pk_add_f16 v25, v62, v82
	v_exp_f16_sdwa v34, v22 dst_sel:WORD_0 dst_unused:UNUSED_PAD src0_sel:WORD_0
	v_exp_f16_sdwa v35, v23 dst_sel:WORD_0 dst_unused:UNUSED_PAD src0_sel:WORD_0
	v_exp_f16_sdwa v36, v24 dst_sel:WORD_0 dst_unused:UNUSED_PAD src0_sel:WORD_0
	v_exp_f16_sdwa v37, v25 dst_sel:WORD_0 dst_unused:UNUSED_PAD src0_sel:WORD_0
	v_exp_f16_sdwa v34, v22 dst_sel:WORD_1 dst_unused:UNUSED_PRESERVE src0_sel:WORD_1
	v_exp_f16_sdwa v35, v23 dst_sel:WORD_1 dst_unused:UNUSED_PRESERVE src0_sel:WORD_1
	v_exp_f16_sdwa v36, v24 dst_sel:WORD_1 dst_unused:UNUSED_PRESERVE src0_sel:WORD_1
	v_exp_f16_sdwa v37, v25 dst_sel:WORD_1 dst_unused:UNUSED_PRESERVE src0_sel:WORD_1
	v_pk_add_f16 v22, v69, v85
	v_pk_add_f16 v14, v14, v34
	v_pk_add_f16 v15, v15, v35
	v_pk_add_f16 v16, v16, v36
	v_pk_add_f16 v17, v17, v37
	v_pk_fma_f16 v18, v26, v34, v18
	v_pk_fma_f16 v19, v27, v35, v19
	v_pk_fma_f16 v20, v28, v36, v20
	v_pk_fma_f16 v21, v29, v37, v21
	v_pk_add_f16 v23, v68, v84
	v_pk_add_f16 v24, v67, v83
	v_pk_add_f16 v25, v66, v82
	v_exp_f16_sdwa v26, v22 dst_sel:WORD_0 dst_unused:UNUSED_PAD src0_sel:WORD_0
	v_exp_f16_sdwa v27, v23 dst_sel:WORD_0 dst_unused:UNUSED_PAD src0_sel:WORD_0
	v_exp_f16_sdwa v28, v24 dst_sel:WORD_0 dst_unused:UNUSED_PAD src0_sel:WORD_0
	v_exp_f16_sdwa v29, v25 dst_sel:WORD_0 dst_unused:UNUSED_PAD src0_sel:WORD_0
	v_exp_f16_sdwa v26, v22 dst_sel:WORD_1 dst_unused:UNUSED_PRESERVE src0_sel:WORD_1
	v_exp_f16_sdwa v27, v23 dst_sel:WORD_1 dst_unused:UNUSED_PRESERVE src0_sel:WORD_1
	v_exp_f16_sdwa v28, v24 dst_sel:WORD_1 dst_unused:UNUSED_PRESERVE src0_sel:WORD_1
	v_exp_f16_sdwa v29, v25 dst_sel:WORD_1 dst_unused:UNUSED_PRESERVE src0_sel:WORD_1
	v_pk_add_f16 v22, v77, v85
	v_pk_add_f16 v17, v17, v29
	v_pk_add_f16 v16, v16, v28
	v_pk_add_f16 v15, v15, v27
	v_pk_add_f16 v14, v14, v26
	v_pk_fma_f16 v21, v41, v29, v21
	v_pk_fma_f16 v20, v40, v28, v20
	v_pk_fma_f16 v19, v39, v27, v19
	v_pk_fma_f16 v18, v38, v26, v18
	v_pk_add_f16 v23, v76, v84
	v_pk_add_f16 v24, v75, v83
	v_pk_add_f16 v25, v74, v82
	v_exp_f16_sdwa v26, v22 dst_sel:WORD_0 dst_unused:UNUSED_PAD src0_sel:WORD_0
	v_exp_f16_sdwa v27, v23 dst_sel:WORD_0 dst_unused:UNUSED_PAD src0_sel:WORD_0
	v_exp_f16_sdwa v28, v24 dst_sel:WORD_0 dst_unused:UNUSED_PAD src0_sel:WORD_0
	v_exp_f16_sdwa v29, v25 dst_sel:WORD_0 dst_unused:UNUSED_PAD src0_sel:WORD_0
	v_exp_f16_sdwa v26, v22 dst_sel:WORD_1 dst_unused:UNUSED_PRESERVE src0_sel:WORD_1
	v_exp_f16_sdwa v27, v23 dst_sel:WORD_1 dst_unused:UNUSED_PRESERVE src0_sel:WORD_1
	v_exp_f16_sdwa v28, v24 dst_sel:WORD_1 dst_unused:UNUSED_PRESERVE src0_sel:WORD_1
	v_exp_f16_sdwa v29, v25 dst_sel:WORD_1 dst_unused:UNUSED_PRESERVE src0_sel:WORD_1
	v_pk_add_f16 v22, v81, v85
	v_pk_add_f16 v14, v14, v26
	v_pk_add_f16 v15, v15, v27
	v_pk_add_f16 v16, v16, v28
	v_pk_add_f16 v17, v17, v29
	v_pk_fma_f16 v18, v50, v26, v18
	v_pk_fma_f16 v19, v51, v27, v19
	v_pk_fma_f16 v20, v52, v28, v20
	v_pk_fma_f16 v21, v53, v29, v21
	v_pk_add_f16 v23, v80, v84
	v_pk_add_f16 v24, v79, v83
	v_pk_add_f16 v25, v78, v82
	v_exp_f16_sdwa v26, v22 dst_sel:WORD_0 dst_unused:UNUSED_PAD src0_sel:WORD_0
	v_exp_f16_sdwa v27, v23 dst_sel:WORD_0 dst_unused:UNUSED_PAD src0_sel:WORD_0
	v_exp_f16_sdwa v28, v24 dst_sel:WORD_0 dst_unused:UNUSED_PAD src0_sel:WORD_0
	v_exp_f16_sdwa v29, v25 dst_sel:WORD_0 dst_unused:UNUSED_PAD src0_sel:WORD_0
	v_exp_f16_sdwa v26, v22 dst_sel:WORD_1 dst_unused:UNUSED_PRESERVE src0_sel:WORD_1
	v_exp_f16_sdwa v27, v23 dst_sel:WORD_1 dst_unused:UNUSED_PRESERVE src0_sel:WORD_1
	v_exp_f16_sdwa v28, v24 dst_sel:WORD_1 dst_unused:UNUSED_PRESERVE src0_sel:WORD_1
	v_exp_f16_sdwa v29, v25 dst_sel:WORD_1 dst_unused:UNUSED_PRESERVE src0_sel:WORD_1
	v_pk_add_f16 v22, v30, v85
	v_pk_add_f16 v17, v17, v29
	v_pk_add_f16 v16, v16, v28
	v_pk_add_f16 v15, v15, v27
	v_pk_add_f16 v14, v14, v26
	v_pk_fma_f16 v21, v73, v29, v21
	v_pk_fma_f16 v20, v72, v28, v20
	v_pk_fma_f16 v19, v71, v27, v19
	v_pk_fma_f16 v18, v70, v26, v18
	v_pk_add_f16 v23, v31, v84
	v_pk_add_f16 v24, v32, v83
	v_pk_add_f16 v25, v33, v82
	v_exp_f16_sdwa v26, v22 dst_sel:WORD_0 dst_unused:UNUSED_PAD src0_sel:WORD_0
	v_exp_f16_sdwa v27, v23 dst_sel:WORD_0 dst_unused:UNUSED_PAD src0_sel:WORD_0
	v_exp_f16_sdwa v28, v24 dst_sel:WORD_0 dst_unused:UNUSED_PAD src0_sel:WORD_0
	v_exp_f16_sdwa v29, v25 dst_sel:WORD_0 dst_unused:UNUSED_PAD src0_sel:WORD_0
	v_exp_f16_sdwa v26, v22 dst_sel:WORD_1 dst_unused:UNUSED_PRESERVE src0_sel:WORD_1
	v_exp_f16_sdwa v27, v23 dst_sel:WORD_1 dst_unused:UNUSED_PRESERVE src0_sel:WORD_1
	v_exp_f16_sdwa v28, v24 dst_sel:WORD_1 dst_unused:UNUSED_PRESERVE src0_sel:WORD_1
	v_exp_f16_sdwa v29, v25 dst_sel:WORD_1 dst_unused:UNUSED_PRESERVE src0_sel:WORD_1
	v_pk_add_f16 v22, v54, v85
	v_pk_add_f16 v14, v14, v26
	v_pk_add_f16 v15, v15, v27
	v_pk_add_f16 v16, v16, v28
	v_pk_add_f16 v17, v17, v29
	v_pk_fma_f16 v18, v90, v26, v18
	v_pk_fma_f16 v19, v91, v27, v19
	v_pk_fma_f16 v20, v92, v28, v20
	v_pk_fma_f16 v21, v93, v29, v21
	v_pk_add_f16 v23, v55, v84
	v_pk_add_f16 v24, v56, v83
	v_pk_add_f16 v25, v57, v82
	v_exp_f16_sdwa v26, v22 dst_sel:WORD_0 dst_unused:UNUSED_PAD src0_sel:WORD_0
	v_exp_f16_sdwa v27, v23 dst_sel:WORD_0 dst_unused:UNUSED_PAD src0_sel:WORD_0
	v_exp_f16_sdwa v28, v24 dst_sel:WORD_0 dst_unused:UNUSED_PAD src0_sel:WORD_0
	v_exp_f16_sdwa v29, v25 dst_sel:WORD_0 dst_unused:UNUSED_PAD src0_sel:WORD_0
	v_exp_f16_sdwa v26, v22 dst_sel:WORD_1 dst_unused:UNUSED_PRESERVE src0_sel:WORD_1
	v_exp_f16_sdwa v27, v23 dst_sel:WORD_1 dst_unused:UNUSED_PRESERVE src0_sel:WORD_1
	v_exp_f16_sdwa v28, v24 dst_sel:WORD_1 dst_unused:UNUSED_PRESERVE src0_sel:WORD_1
	v_exp_f16_sdwa v29, v25 dst_sel:WORD_1 dst_unused:UNUSED_PRESERVE src0_sel:WORD_1
	s_nop 0
	v_pk_add_f16 v17, v17, v29
	v_pk_add_f16 v16, v16, v28
	v_pk_add_f16 v15, v15, v27
	v_pk_add_f16 v14, v14, v26
	v_pk_fma_f16 v21, v113, v29, v21
	v_pk_fma_f16 v20, v112, v28, v20
	v_pk_fma_f16 v19, v111, v27, v19
	v_pk_fma_f16 v18, v110, v26, v18
	v_pk_add_f16 v26, v58, v85
	v_pk_add_f16 v27, v59, v84
	v_pk_add_f16 v28, v60, v83
	v_pk_add_f16 v29, v61, v82
	v_exp_f16_sdwa v22, v26 dst_sel:WORD_0 dst_unused:UNUSED_PAD src0_sel:WORD_0
	v_exp_f16_sdwa v23, v27 dst_sel:WORD_0 dst_unused:UNUSED_PAD src0_sel:WORD_0
	v_exp_f16_sdwa v24, v28 dst_sel:WORD_0 dst_unused:UNUSED_PAD src0_sel:WORD_0
	v_exp_f16_sdwa v25, v29 dst_sel:WORD_0 dst_unused:UNUSED_PAD src0_sel:WORD_0
	v_exp_f16_sdwa v22, v26 dst_sel:WORD_1 dst_unused:UNUSED_PRESERVE src0_sel:WORD_1
	v_exp_f16_sdwa v23, v27 dst_sel:WORD_1 dst_unused:UNUSED_PRESERVE src0_sel:WORD_1
	v_exp_f16_sdwa v24, v28 dst_sel:WORD_1 dst_unused:UNUSED_PRESERVE src0_sel:WORD_1
	v_exp_f16_sdwa v25, v29 dst_sel:WORD_1 dst_unused:UNUSED_PRESERVE src0_sel:WORD_1
	s_nop 0

_Z7k_stageILi0ELi4EEv8AttnArgsPKDF16_PKfPDF16_iii:
	s_load_dwordx2 s[86:87], s[0:1], 0x70
	s_load_dwordx2 s[82:83], s[0:1], 0x88
	s_mov_b32 s81, s3
	s_load_dwordx16 s[64:79], s[0:1], 0x0
	v_readfirstlane_b32 s94, v0
	s_nop 0
	s_lshr_b32 s94, s94, 6
	s_load_dwordx4 s[8:11], s[0:1], 0x70
	s_load_dwordx2 s[20:21], s[0:1], 0x80
	s_load_dwordx4 s[12:15], s[0:1], 0x88
	s_lshl_b32 s5, s2, 5
	s_waitcnt lgkmcnt(0)
	s_and_b32 s15, s5, 0xe0
	s_lshr_b32 s5, s2, 3
	s_add_i32 s15, s15, s5
	s_and_b32 s2, s2, 56
	v_readfirstlane_b32 s4, v0
	v_and_b32_e32 v1, 15, v0
	s_cmp_lt_i32 s14, 1
	v_bfe_u32 v158, v0, 4, 2
	s_cbranch_scc1 .LBB5_79
	s_bfe_u32 s5, s4, 0x10006
	s_lshl_b32 s6, s5, 4
	s_mul_i32 s16, s3, 40
	s_mul_hi_i32 s7, s3, 40
	s_add_u32 s22, s0, s16
	s_addc_u32 s23, s1, s7
	s_load_dwordx4 s[16:19], s[22:23], 0x0
	s_load_dwordx2 s[0:1], s[22:23], 0x10
	v_or_b32_e32 v159, s6, v1
	v_lshlrev_b32_e32 v18, 5, v159
	s_waitcnt lgkmcnt(0)
	global_load_dwordx4 v[230:233], v18, s[18:19]
	global_load_dwordx4 v[234:237], v18, s[0:1]
	global_load_dwordx4 v[238:241], v18, s[18:19] offset:16
	global_load_dwordx4 v[242:245], v18, s[0:1] offset:16
	v_bfe_u32 v21, v0, 7, 1
	v_lshrrev_b32_e32 v19, 4, v0
	v_lshlrev_b16_e32 v23, 2, v21
	v_lshrrev_b32_e32 v18, 5, v0
	v_lshrrev_b32_e32 v20, 6, v0
	v_and_b32_e32 v24, 3, v19
	v_bitop3_b16 v19, v23, v19, 3 bitop3:0xf8
	s_movk_i32 s0, 0x3000
	v_and_b32_e32 v18, 4, v18
	v_and_b32_e32 v22, 4, v20
	v_lshlrev_b32_e32 v20, 12, v20
	v_lshlrev_b32_e32 v21, 11, v21
	v_and_b32_e32 v19, 0xffff, v19
	s_bitcmp1_b32 s4, 6
	v_or_b32_e32 v161, v18, v158
	v_and_or_b32 v162, s15, 56, v22
	v_bitop3_b16 v23, v23, 8, v24 bitop3:0xfe
	v_lshlrev_b32_e32 v24, 3, v22
	v_lshl_or_b32 v22, v22, 12, v21
	v_or3_b32 v163, v20, v21, s0
	v_bitop3_b32 v18, v18, v159, v158 bitop3:0x36
	v_bitop3_b32 v19, s6, v19, v1 bitop3:0x36
	s_cselect_b64 s[24:25], -1, 0
	s_and_b32 s0, s15, 0x1ffc0
	s_movk_i32 s1, 0x2000
	v_lshl_or_b32 v168, v18, 4, v22
	v_lshlrev_b32_e32 v18, 4, v19
	v_or_b32_e32 v19, s0, v162
	v_add3_u32 v170, v22, v18, s1
	v_lshl_or_b32 v18, v19, 6, s2
	v_add_u32_e32 v18, v161, v18
	v_mul_u32_u24_e32 v18, 0x600, v18
	v_and_b32_e32 v20, 0xffff, v23
	v_lshl_or_b32 v18, s5, 8, v18
	v_lshlrev_b32_e32 v160, 9, v158
	v_bitop3_b32 v20, s6, v20, v1 bitop3:0x36
	v_lshl_or_b32 v18, v1, 4, v18
	v_add_u32_e32 v164, -1, v162
	v_add_u32_e32 v165, 4, v162
	v_or3_b32 v166, v161, v24, 8
	v_or_b32_e32 v167, 0x1000, v22
	v_lshl_or_b32 v169, v20, 4, v160
	s_and_b32 s17, s17, 0xffff
	s_mov_b32 s19, 0x20000
	s_mov_b32 s18, 0x1800000
	v_add_u32_e32 v171, 0xfffe7c00, v18
	s_mov_b32 s30, s2
	s_mov_b32 s93, 0
	s_branch .LBB5_4
.LBB5_2:
	s_waitcnt lgkmcnt(0)
	v_cvt_f16_f32_e32 v180, s7
	v_cvt_f16_f32_e32 v182, s6
	v_cvt_f16_f32_e32 v181, s28
	s_waitcnt vmcnt(3)
	v_pk_mul_f16 v183, v182, v184 op_sel_hi:[0,1]
	v_pk_mul_f16 v190, v182, v187 op_sel_hi:[0,1]
	v_pk_mul_f16 v194, v180, v187 op_sel_hi:[0,1]
	v_pk_mul_f16 v198, v181, v187 op_sel_hi:[0,1]
	v_pk_mul_f16 v188, v182, v185 op_sel_hi:[0,1]
	v_pk_mul_f16 v189, v182, v186 op_sel_hi:[0,1]
	v_pk_mul_f16 v191, v180, v184 op_sel_hi:[0,1]
	s_mov_b64 exec, s[64:65]
	buffer_load_dwordx4 v[18:21], v224, s[16:19], 0 offen
	buffer_load_dwordx4 v[6:9], v224, s[16:19], 0 offen offset:512
	s_mov_b64 exec, -1
	v_pk_mul_f16 v192, v180, v185 op_sel_hi:[0,1]
	v_pk_mul_f16 v193, v180, v186 op_sel_hi:[0,1]
	v_pk_mul_f16 v195, v181, v184 op_sel_hi:[0,1]
	v_pk_mul_f16 v196, v181, v185 op_sel_hi:[0,1]
	v_pk_mul_f16 v197, v181, v186 op_sel_hi:[0,1]
	v_pk_fma_f16 v113, v113, v187, v190
	v_pk_fma_f16 v110, v110, v184, v183
	v_pk_fma_f16 v129, v129, v187, v190
	v_pk_fma_f16 v126, v126, v184, v183
	v_pk_fma_f16 v137, v137, v187, v190
	v_pk_fma_f16 v134, v134, v184, v183
	v_pk_fma_f16 v183, v85, v187, v194
	v_pk_fma_f16 v199, v109, v187, v194
	buffer_load_dwordx4 v[30:33], v225, s[16:19], 0 offen offset:512
	buffer_load_dwordx4 v[10:13], v225, s[16:19], 0 offen offset:1024
	v_pk_fma_f16 v194, v125, v187, v194
	v_pk_fma_f16 v203, v53, v187, v198
	v_pk_fma_f16 v207, v69, v187, v198
	v_pk_fma_f16 v187, v97, v187, v198
	v_pk_maximum3_f16 v198, v113, v129, v137
	v_pk_fma_f16 v112, v112, v186, v189
	v_pk_fma_f16 v111, v111, v185, v188
	v_pk_fma_f16 v128, v128, v186, v189
	v_pk_fma_f16 v127, v127, v185, v188
	v_pk_fma_f16 v136, v136, v186, v189
	v_pk_fma_f16 v135, v135, v185, v188
	v_pk_fma_f16 v188, v84, v186, v193
	v_pk_fma_f16 v189, v83, v185, v192
	v_pk_fma_f16 v190, v82, v184, v191
	v_pk_fma_f16 v200, v108, v186, v193
	v_pk_fma_f16 v201, v107, v185, v192
	s_mov_b64 exec, s[66:67]
	buffer_load_dwordx4 v[54:57], v225, s[16:19], 0 offen offset:2048
	buffer_load_dwordx4 v[14:17], v225, s[16:19], 0 offen offset:2560
	s_mov_b64 exec, -1
	v_pk_fma_f16 v202, v106, v184, v191
	v_pk_fma_f16 v193, v124, v186, v193
	v_pk_fma_f16 v192, v123, v185, v192
	v_pk_fma_f16 v191, v122, v184, v191
	v_pk_fma_f16 v204, v52, v186, v197
	v_pk_fma_f16 v205, v51, v185, v196
	v_pk_fma_f16 v206, v50, v184, v195
	v_pk_fma_f16 v208, v68, v186, v197
	v_pk_fma_f16 v209, v67, v185, v196
	v_pk_fma_f16 v210, v66, v184, v195
	v_pk_fma_f16 v186, v96, v186, v197
	v_pk_fma_f16 v185, v95, v185, v196
	v_pk_fma_f16 v184, v94, v184, v195
	v_pk_maximum3_f16 v195, v110, v126, v134
	v_pk_maximum3_f16 v196, v111, v127, v135
	v_pk_maximum3_f16 v197, v112, v128, v136
	v_pk_maximum3_f16 v214, v183, v199, v194
	v_pk_maximum3_f16 v218, v203, v207, v187
	v_pk_maximum3_f16 v211, v190, v202, v191
	v_pk_maximum3_f16 v212, v189, v201, v192
	v_pk_maximum3_f16 v213, v188, v200, v193
	v_pk_maximum3_f16 v215, v206, v210, v184
	v_pk_maximum3_f16 v216, v205, v209, v185
	v_pk_maximum3_f16 v198, v198, v214, v218
	v_pk_maximum3_f16 v217, v204, v208, v186
	v_pk_maximum3_f16 v195, v195, v211, v215
	v_pk_maximum3_f16 v196, v196, v212, v216
	v_pk_maximum3_f16 v197, v197, v213, v217
	v_pk_add_f16 v113, v113, v198 neg_lo:[0,1] neg_hi:[0,1]
	s_mov_b64 exec, s[64:65]
	buffer_load_dwordx4 v[74:77], v226, s[16:19], 0 offen
	buffer_load_dwordx4 v[26:29], v226, s[16:19], 0 offen offset:512
	s_mov_b64 exec, -1
	v_pk_add_f16 v110, v110, v195 neg_lo:[0,1] neg_hi:[0,1]
	v_pk_add_f16 v111, v111, v196 neg_lo:[0,1] neg_hi:[0,1]
	v_pk_add_f16 v112, v112, v197 neg_lo:[0,1] neg_hi:[0,1]
	v_pk_add_f16 v126, v126, v195 neg_lo:[0,1] neg_hi:[0,1]
	v_exp_f16_sdwa v211, v110 dst_sel:WORD_0 dst_unused:UNUSED_PAD src0_sel:WORD_0
	v_exp_f16_sdwa v212, v111 dst_sel:WORD_0 dst_unused:UNUSED_PAD src0_sel:WORD_0
	v_exp_f16_sdwa v213, v112 dst_sel:WORD_0 dst_unused:UNUSED_PAD src0_sel:WORD_0
	v_exp_f16_sdwa v214, v113 dst_sel:WORD_0 dst_unused:UNUSED_PAD src0_sel:WORD_0
	v_exp_f16_sdwa v211, v110 dst_sel:WORD_1 dst_unused:UNUSED_PRESERVE src0_sel:WORD_1
	v_exp_f16_sdwa v212, v111 dst_sel:WORD_1 dst_unused:UNUSED_PRESERVE src0_sel:WORD_1
	v_exp_f16_sdwa v213, v112 dst_sel:WORD_1 dst_unused:UNUSED_PRESERVE src0_sel:WORD_1
	v_exp_f16_sdwa v214, v113 dst_sel:WORD_1 dst_unused:UNUSED_PRESERVE src0_sel:WORD_1
	v_pk_add_f16 v127, v127, v196 neg_lo:[0,1] neg_hi:[0,1]
	v_pk_add_f16 v113, v211, 0
	v_pk_fma_f16 v81, v81, v214, 0
	v_pk_add_f16 v110, v214, 0
	v_pk_add_f16 v111, v213, 0
	v_pk_add_f16 v112, v212, 0
	v_pk_fma_f16 v80, v80, v213, 0
	v_pk_fma_f16 v79, v79, v212, 0
	v_pk_fma_f16 v78, v78, v211, 0
	v_pk_add_f16 v128, v128, v197 neg_lo:[0,1] neg_hi:[0,1]
	buffer_load_dwordx4 v[98:101], v227, s[16:19], 0 offen offset:512
	buffer_load_dwordx4 v[38:41], v227, s[16:19], 0 offen offset:1024
	v_pk_add_f16 v129, v129, v198 neg_lo:[0,1] neg_hi:[0,1]
	v_exp_f16_sdwa v211, v126 dst_sel:WORD_0 dst_unused:UNUSED_PAD src0_sel:WORD_0
	v_exp_f16_sdwa v212, v127 dst_sel:WORD_0 dst_unused:UNUSED_PAD src0_sel:WORD_0
	v_exp_f16_sdwa v213, v128 dst_sel:WORD_0 dst_unused:UNUSED_PAD src0_sel:WORD_0
	v_exp_f16_sdwa v214, v129 dst_sel:WORD_0 dst_unused:UNUSED_PAD src0_sel:WORD_0
	v_exp_f16_sdwa v211, v126 dst_sel:WORD_1 dst_unused:UNUSED_PRESERVE src0_sel:WORD_1
	v_exp_f16_sdwa v212, v127 dst_sel:WORD_1 dst_unused:UNUSED_PRESERVE src0_sel:WORD_1
	v_exp_f16_sdwa v213, v128 dst_sel:WORD_1 dst_unused:UNUSED_PRESERVE src0_sel:WORD_1
	v_exp_f16_sdwa v214, v129 dst_sel:WORD_1 dst_unused:UNUSED_PRESERVE src0_sel:WORD_1
	v_pk_add_f16 v113, v113, v211
	v_pk_fma_f16 v81, v105, v214, v81
	v_pk_add_f16 v105, v137, v198 neg_lo:[0,1] neg_hi:[0,1]
	v_pk_add_f16 v112, v112, v212
	v_pk_add_f16 v111, v111, v213
	v_pk_add_f16 v110, v110, v214
	v_pk_fma_f16 v78, v102, v211, v78
	v_pk_fma_f16 v79, v103, v212, v79
	v_pk_fma_f16 v80, v104, v213, v80
	v_pk_add_f16 v102, v134, v195 neg_lo:[0,1] neg_hi:[0,1]
	v_pk_add_f16 v103, v135, v196 neg_lo:[0,1] neg_hi:[0,1]
	v_pk_add_f16 v104, v136, v197 neg_lo:[0,1] neg_hi:[0,1]
	v_exp_f16_sdwa v126, v102 dst_sel:WORD_0 dst_unused:UNUSED_PAD src0_sel:WORD_0
	v_exp_f16_sdwa v127, v103 dst_sel:WORD_0 dst_unused:UNUSED_PAD src0_sel:WORD_0
	v_exp_f16_sdwa v128, v104 dst_sel:WORD_0 dst_unused:UNUSED_PAD src0_sel:WORD_0
	v_exp_f16_sdwa v129, v105 dst_sel:WORD_0 dst_unused:UNUSED_PAD src0_sel:WORD_0
	v_exp_f16_sdwa v126, v102 dst_sel:WORD_1 dst_unused:UNUSED_PRESERVE src0_sel:WORD_1
	v_exp_f16_sdwa v127, v103 dst_sel:WORD_1 dst_unused:UNUSED_PRESERVE src0_sel:WORD_1
	v_exp_f16_sdwa v128, v104 dst_sel:WORD_1 dst_unused:UNUSED_PRESERVE src0_sel:WORD_1
	v_exp_f16_sdwa v129, v105 dst_sel:WORD_1 dst_unused:UNUSED_PRESERVE src0_sel:WORD_1
	v_pk_add_f16 v105, v113, v126
	v_pk_add_f16 v102, v110, v129
	s_mov_b64 exec, s[66:67]
	buffer_load_dwordx4 v[118:121], v227, s[16:19], 0 offen offset:2048
	buffer_load_dwordx4 v[58:61], v227, s[16:19], 0 offen offset:2560
	s_mov_b64 exec, -1
	v_pk_add_f16 v103, v111, v128
	v_pk_add_f16 v104, v112, v127
	v_pk_fma_f16 v81, v117, v129, v81
	v_pk_fma_f16 v80, v116, v128, v80
	v_pk_fma_f16 v79, v115, v127, v79
	v_pk_fma_f16 v78, v114, v126, v78
	v_pk_add_f16 v110, v190, v195 neg_lo:[0,1] neg_hi:[0,1]
	v_pk_add_f16 v111, v189, v196 neg_lo:[0,1] neg_hi:[0,1]
	v_pk_add_f16 v112, v188, v197 neg_lo:[0,1] neg_hi:[0,1]
	v_pk_add_f16 v113, v183, v198 neg_lo:[0,1] neg_hi:[0,1]
	v_exp_f16_sdwa v114, v110 dst_sel:WORD_0 dst_unused:UNUSED_PAD src0_sel:WORD_0
	v_exp_f16_sdwa v115, v111 dst_sel:WORD_0 dst_unused:UNUSED_PAD src0_sel:WORD_0
	v_exp_f16_sdwa v116, v112 dst_sel:WORD_0 dst_unused:UNUSED_PAD src0_sel:WORD_0
	v_exp_f16_sdwa v117, v113 dst_sel:WORD_0 dst_unused:UNUSED_PAD src0_sel:WORD_0
	v_exp_f16_sdwa v114, v110 dst_sel:WORD_1 dst_unused:UNUSED_PRESERVE src0_sel:WORD_1
	v_exp_f16_sdwa v115, v111 dst_sel:WORD_1 dst_unused:UNUSED_PRESERVE src0_sel:WORD_1
	v_exp_f16_sdwa v116, v112 dst_sel:WORD_1 dst_unused:UNUSED_PRESERVE src0_sel:WORD_1
	v_exp_f16_sdwa v117, v113 dst_sel:WORD_1 dst_unused:UNUSED_PRESERVE src0_sel:WORD_1
	v_pk_add_f16 v110, v202, v195 neg_lo:[0,1] neg_hi:[0,1]
	v_pk_add_f16 v105, v105, v114
	v_pk_add_f16 v104, v104, v115
	v_pk_add_f16 v103, v103, v116
	s_mov_b64 exec, s[76:77]
	buffer_load_dwordx4 v[130:133], v228, s[16:19], 0 offen
	buffer_load_dwordx4 v[70:73], v228, s[16:19], 0 offen offset:512
	s_mov_b64 exec, -1
	v_pk_add_f16 v102, v102, v117
	v_pk_fma_f16 v78, v42, v114, v78
	v_pk_fma_f16 v79, v43, v115, v79
	v_pk_fma_f16 v80, v44, v116, v80
	v_pk_fma_f16 v81, v45, v117, v81
	v_pk_add_f16 v111, v201, v196 neg_lo:[0,1] neg_hi:[0,1]
	v_pk_add_f16 v112, v200, v197 neg_lo:[0,1] neg_hi:[0,1]
	v_pk_add_f16 v113, v199, v198 neg_lo:[0,1] neg_hi:[0,1]
	v_exp_f16_sdwa v114, v110 dst_sel:WORD_0 dst_unused:UNUSED_PAD src0_sel:WORD_0
	v_exp_f16_sdwa v115, v111 dst_sel:WORD_0 dst_unused:UNUSED_PAD src0_sel:WORD_0
	v_exp_f16_sdwa v116, v112 dst_sel:WORD_0 dst_unused:UNUSED_PAD src0_sel:WORD_0
	v_exp_f16_sdwa v117, v113 dst_sel:WORD_0 dst_unused:UNUSED_PAD src0_sel:WORD_0
	v_exp_f16_sdwa v114, v110 dst_sel:WORD_1 dst_unused:UNUSED_PRESERVE src0_sel:WORD_1
	v_exp_f16_sdwa v115, v111 dst_sel:WORD_1 dst_unused:UNUSED_PRESERVE src0_sel:WORD_1
	v_exp_f16_sdwa v116, v112 dst_sel:WORD_1 dst_unused:UNUSED_PRESERVE src0_sel:WORD_1
	v_exp_f16_sdwa v117, v113 dst_sel:WORD_1 dst_unused:UNUSED_PRESERVE src0_sel:WORD_1
	v_pk_add_f16 v110, v191, v195 neg_lo:[0,1] neg_hi:[0,1]
	v_pk_add_f16 v105, v105, v114
	v_pk_add_f16 v102, v102, v117
	v_pk_add_f16 v103, v103, v116
	v_pk_add_f16 v104, v104, v115
	v_pk_fma_f16 v81, v65, v117, v81
	v_pk_fma_f16 v80, v64, v116, v80
	s_mov_b64 exec, s[70:71]
	buffer_load_dwordx4 v[138:141], v229, s[16:19], 0 offen offset:512
	buffer_load_dwordx4 v[90:93], v229, s[16:19], 0 offen offset:1024
	s_mov_b64 exec, -1
	v_pk_fma_f16 v79, v63, v115, v79
	v_pk_fma_f16 v78, v62, v114, v78
	v_pk_add_f16 v111, v192, v196 neg_lo:[0,1] neg_hi:[0,1]
	v_pk_add_f16 v112, v193, v197 neg_lo:[0,1] neg_hi:[0,1]
	v_pk_add_f16 v113, v194, v198 neg_lo:[0,1] neg_hi:[0,1]
	v_exp_f16_sdwa v114, v110 dst_sel:WORD_0 dst_unused:UNUSED_PAD src0_sel:WORD_0
	v_exp_f16_sdwa v115, v111 dst_sel:WORD_0 dst_unused:UNUSED_PAD src0_sel:WORD_0
	v_exp_f16_sdwa v116, v112 dst_sel:WORD_0 dst_unused:UNUSED_PAD src0_sel:WORD_0
	v_exp_f16_sdwa v117, v113 dst_sel:WORD_0 dst_unused:UNUSED_PAD src0_sel:WORD_0
	v_exp_f16_sdwa v114, v110 dst_sel:WORD_1 dst_unused:UNUSED_PRESERVE src0_sel:WORD_1
	v_exp_f16_sdwa v115, v111 dst_sel:WORD_1 dst_unused:UNUSED_PRESERVE src0_sel:WORD_1
	v_exp_f16_sdwa v116, v112 dst_sel:WORD_1 dst_unused:UNUSED_PRESERVE src0_sel:WORD_1
	v_exp_f16_sdwa v117, v113 dst_sel:WORD_1 dst_unused:UNUSED_PRESERVE src0_sel:WORD_1
	v_pk_add_f16 v110, v206, v195 neg_lo:[0,1] neg_hi:[0,1]
	v_pk_add_f16 v105, v105, v114
	v_pk_add_f16 v104, v104, v115
	v_pk_add_f16 v103, v103, v116
	v_pk_add_f16 v102, v102, v117
	v_pk_fma_f16 v78, v86, v114, v78
	v_pk_fma_f16 v79, v87, v115, v79
	v_pk_fma_f16 v80, v88, v116, v80
	v_pk_fma_f16 v81, v89, v117, v81
	s_mov_b64 exec, s[78:79]
	buffer_load_dwordx4 v[142:145], v229, s[16:19], 0 offen offset:2048
	buffer_load_dwordx4 v[2:5], v229, s[16:19], 0 offen offset:2560
	s_mov_b64 exec, -1
	v_pk_add_f16 v111, v205, v196 neg_lo:[0,1] neg_hi:[0,1]
	v_pk_add_f16 v112, v204, v197 neg_lo:[0,1] neg_hi:[0,1]
	v_pk_add_f16 v113, v203, v198 neg_lo:[0,1] neg_hi:[0,1]
	v_exp_f16_sdwa v114, v110 dst_sel:WORD_0 dst_unused:UNUSED_PAD src0_sel:WORD_0
	v_exp_f16_sdwa v115, v111 dst_sel:WORD_0 dst_unused:UNUSED_PAD src0_sel:WORD_0
	v_exp_f16_sdwa v116, v112 dst_sel:WORD_0 dst_unused:UNUSED_PAD src0_sel:WORD_0
	v_exp_f16_sdwa v117, v113 dst_sel:WORD_0 dst_unused:UNUSED_PAD src0_sel:WORD_0
	v_exp_f16_sdwa v114, v110 dst_sel:WORD_1 dst_unused:UNUSED_PRESERVE src0_sel:WORD_1
	v_exp_f16_sdwa v115, v111 dst_sel:WORD_1 dst_unused:UNUSED_PRESERVE src0_sel:WORD_1
	v_exp_f16_sdwa v116, v112 dst_sel:WORD_1 dst_unused:UNUSED_PRESERVE src0_sel:WORD_1
	v_exp_f16_sdwa v117, v113 dst_sel:WORD_1 dst_unused:UNUSED_PRESERVE src0_sel:WORD_1
	v_pk_add_f16 v110, v210, v195 neg_lo:[0,1] neg_hi:[0,1]
	v_pk_add_f16 v105, v105, v114
	v_pk_add_f16 v102, v102, v117
	v_pk_add_f16 v103, v103, v116
	v_pk_add_f16 v104, v104, v115
	v_pk_fma_f16 v81, v25, v117, v81
	v_pk_fma_f16 v80, v24, v116, v80
	v_pk_fma_f16 v79, v23, v115, v79
	v_pk_fma_f16 v78, v22, v114, v78
	v_pk_add_f16 v111, v209, v196 neg_lo:[0,1] neg_hi:[0,1]
	v_pk_add_f16 v112, v208, v197 neg_lo:[0,1] neg_hi:[0,1]
	v_pk_add_f16 v113, v207, v198 neg_lo:[0,1] neg_hi:[0,1]
	v_exp_f16_sdwa v114, v110 dst_sel:WORD_0 dst_unused:UNUSED_PAD src0_sel:WORD_0
	v_exp_f16_sdwa v115, v111 dst_sel:WORD_0 dst_unused:UNUSED_PAD src0_sel:WORD_0
	v_exp_f16_sdwa v116, v112 dst_sel:WORD_0 dst_unused:UNUSED_PAD src0_sel:WORD_0
	v_exp_f16_sdwa v117, v113 dst_sel:WORD_0 dst_unused:UNUSED_PAD src0_sel:WORD_0
	v_exp_f16_sdwa v114, v110 dst_sel:WORD_1 dst_unused:UNUSED_PRESERVE src0_sel:WORD_1
	v_exp_f16_sdwa v115, v111 dst_sel:WORD_1 dst_unused:UNUSED_PRESERVE src0_sel:WORD_1
	v_exp_f16_sdwa v116, v112 dst_sel:WORD_1 dst_unused:UNUSED_PRESERVE src0_sel:WORD_1
	v_exp_f16_sdwa v117, v113 dst_sel:WORD_1 dst_unused:UNUSED_PRESERVE src0_sel:WORD_1
	v_pk_add_f16 v110, v184, v195 neg_lo:[0,1] neg_hi:[0,1]
	v_pk_add_f16 v105, v105, v114
	v_pk_add_f16 v104, v104, v115
	v_pk_add_f16 v103, v103, v116
	v_pk_add_f16 v102, v102, v117
	v_pk_fma_f16 v78, v34, v114, v78
	v_pk_fma_f16 v79, v35, v115, v79
	v_pk_fma_f16 v80, v36, v116, v80
	v_pk_fma_f16 v81, v37, v117, v81
	v_pk_add_f16 v111, v185, v196 neg_lo:[0,1] neg_hi:[0,1]
	v_pk_add_f16 v112, v186, v197 neg_lo:[0,1] neg_hi:[0,1]
	v_pk_add_f16 v113, v187, v198 neg_lo:[0,1] neg_hi:[0,1]
	v_exp_f16_sdwa v114, v110 dst_sel:WORD_0 dst_unused:UNUSED_PAD src0_sel:WORD_0
	v_exp_f16_sdwa v115, v111 dst_sel:WORD_0 dst_unused:UNUSED_PAD src0_sel:WORD_0
	v_exp_f16_sdwa v116, v112 dst_sel:WORD_0 dst_unused:UNUSED_PAD src0_sel:WORD_0
	v_exp_f16_sdwa v117, v113 dst_sel:WORD_0 dst_unused:UNUSED_PAD src0_sel:WORD_0
	v_exp_f16_sdwa v114, v110 dst_sel:WORD_1 dst_unused:UNUSED_PRESERVE src0_sel:WORD_1
	v_exp_f16_sdwa v115, v111 dst_sel:WORD_1 dst_unused:UNUSED_PRESERVE src0_sel:WORD_1
	v_exp_f16_sdwa v116, v112 dst_sel:WORD_1 dst_unused:UNUSED_PRESERVE src0_sel:WORD_1
	v_exp_f16_sdwa v117, v113 dst_sel:WORD_1 dst_unused:UNUSED_PRESERVE src0_sel:WORD_1
	v_pk_add_f16 v105, v105, v114
	v_pk_add_f16 v104, v104, v115
	v_rcp_f16_e32 v110, v105
	v_rcp_f16_sdwa v105, v105 dst_sel:DWORD dst_unused:UNUSED_PAD src0_sel:WORD_1
	v_pk_add_f16 v103, v103, v116
	v_rcp_f16_e32 v111, v104
	v_rcp_f16_sdwa v104, v104 dst_sel:DWORD dst_unused:UNUSED_PAD src0_sel:WORD_1
	v_pk_add_f16 v102, v102, v117
	v_rcp_f16_e32 v112, v103
	v_rcp_f16_sdwa v103, v103 dst_sel:DWORD dst_unused:UNUSED_PAD src0_sel:WORD_1
	v_rcp_f16_e32 v113, v102
	v_rcp_f16_sdwa v102, v102 dst_sel:DWORD dst_unused:UNUSED_PAD src0_sel:WORD_1
	v_pk_fma_f16 v78, v46, v114, v78
	v_pack_b32_f16 v105, v110, v105
	v_pk_fma_f16 v79, v47, v115, v79
	v_pk_mul_f16 v110, v78, v105
	v_pack_b32_f16 v78, v111, v104
	v_pk_fma_f16 v80, v48, v116, v80
	v_pk_mul_f16 v111, v79, v78
	v_pack_b32_f16 v78, v112, v103
	v_pk_fma_f16 v81, v49, v117, v81
	v_pk_mul_f16 v112, v80, v78
	v_pack_b32_f16 v78, v113, v102
	v_pk_mul_f16 v113, v81, v78
	s_waitcnt vmcnt(12)
	v_pk_mul_f16 v78, v182, v154 op_sel_hi:[0,1]
	v_pk_mul_f16 v81, v182, v157 op_sel_hi:[0,1]
	v_pk_mul_f16 v102, v180, v154 op_sel_hi:[0,1]
	v_pk_mul_f16 v114, v181, v154 op_sel_hi:[0,1]
	v_pk_mul_f16 v79, v182, v155 op_sel_hi:[0,1]
	v_pk_mul_f16 v80, v182, v156 op_sel_hi:[0,1]
	v_pk_mul_f16 v103, v180, v155 op_sel_hi:[0,1]
	v_pk_mul_f16 v104, v180, v156 op_sel_hi:[0,1]
	v_pk_mul_f16 v105, v180, v157 op_sel_hi:[0,1]
	v_pk_mul_f16 v115, v181, v155 op_sel_hi:[0,1]
	v_pk_mul_f16 v116, v181, v156 op_sel_hi:[0,1]
	v_pk_mul_f16 v117, v181, v157 op_sel_hi:[0,1]
	v_pk_fma_f16 v85, v85, v157, v81
	v_pk_fma_f16 v82, v82, v154, v78
	v_pk_fma_f16 v109, v109, v157, v81
	v_pk_fma_f16 v106, v106, v154, v78
	v_pk_fma_f16 v81, v125, v157, v81
	v_pk_fma_f16 v78, v122, v154, v78
	v_pk_fma_f16 v125, v50, v154, v102
	v_pk_fma_f16 v129, v66, v154, v102
	v_pk_fma_f16 v102, v94, v154, v102
	v_pk_fma_f16 v137, v18, v154, v114
	v_pk_fma_f16 v186, v30, v154, v114
	v_pk_fma_f16 v114, v54, v154, v114
	v_pk_maximum3_f16 v154, v82, v106, v78
	v_pk_fma_f16 v84, v84, v156, v80
	v_pk_fma_f16 v83, v83, v155, v79
	v_pk_fma_f16 v108, v108, v156, v80
	v_pk_fma_f16 v107, v107, v155, v79
	v_pk_fma_f16 v80, v124, v156, v80
	v_pk_fma_f16 v79, v123, v155, v79
	v_pk_fma_f16 v122, v53, v157, v105
	v_pk_fma_f16 v123, v52, v156, v104
	v_pk_fma_f16 v124, v51, v155, v103
	v_pk_fma_f16 v126, v69, v157, v105
	v_pk_fma_f16 v127, v68, v156, v104
	v_pk_fma_f16 v128, v67, v155, v103
	v_pk_fma_f16 v105, v97, v157, v105
	v_pk_fma_f16 v104, v96, v156, v104
	v_pk_fma_f16 v103, v95, v155, v103
	v_pk_fma_f16 v134, v21, v157, v117
	v_pk_fma_f16 v135, v20, v156, v116
	v_pk_fma_f16 v136, v19, v155, v115
	v_pk_fma_f16 v183, v33, v157, v117
	v_pk_fma_f16 v184, v32, v156, v116
	v_pk_fma_f16 v185, v31, v155, v115
	v_pk_fma_f16 v117, v57, v157, v117
	v_pk_fma_f16 v116, v56, v156, v116
	v_pk_fma_f16 v115, v55, v155, v115
	v_pk_maximum3_f16 v155, v83, v107, v79
	v_pk_maximum3_f16 v156, v84, v108, v80
	v_pk_maximum3_f16 v157, v85, v109, v81
	v_pk_maximum3_f16 v187, v125, v129, v102
	v_pk_maximum3_f16 v191, v137, v186, v114
	v_pk_maximum3_f16 v188, v124, v128, v103
	v_pk_maximum3_f16 v189, v123, v127, v104
	v_pk_maximum3_f16 v190, v122, v126, v105
	v_pk_maximum3_f16 v192, v136, v185, v115
	v_pk_maximum3_f16 v193, v135, v184, v116
	v_pk_maximum3_f16 v154, v154, v187, v191
	v_pk_maximum3_f16 v194, v134, v183, v117
	v_pk_maximum3_f16 v155, v155, v188, v192
	v_pk_maximum3_f16 v156, v156, v189, v193
	v_pk_maximum3_f16 v157, v157, v190, v194
	v_pk_add_f16 v82, v82, v154 neg_lo:[0,1] neg_hi:[0,1]
	v_pk_add_f16 v83, v83, v155 neg_lo:[0,1] neg_hi:[0,1]
	v_pk_add_f16 v84, v84, v156 neg_lo:[0,1] neg_hi:[0,1]
	v_pk_add_f16 v85, v85, v157 neg_lo:[0,1] neg_hi:[0,1]
	v_pk_add_f16 v106, v106, v154 neg_lo:[0,1] neg_hi:[0,1]
	v_exp_f16_sdwa v187, v82 dst_sel:WORD_0 dst_unused:UNUSED_PAD src0_sel:WORD_0
	v_exp_f16_sdwa v188, v83 dst_sel:WORD_0 dst_unused:UNUSED_PAD src0_sel:WORD_0
	v_exp_f16_sdwa v189, v84 dst_sel:WORD_0 dst_unused:UNUSED_PAD src0_sel:WORD_0
	v_exp_f16_sdwa v190, v85 dst_sel:WORD_0 dst_unused:UNUSED_PAD src0_sel:WORD_0
	v_exp_f16_sdwa v187, v82 dst_sel:WORD_1 dst_unused:UNUSED_PRESERVE src0_sel:WORD_1
	v_exp_f16_sdwa v188, v83 dst_sel:WORD_1 dst_unused:UNUSED_PRESERVE src0_sel:WORD_1
	v_exp_f16_sdwa v189, v84 dst_sel:WORD_1 dst_unused:UNUSED_PRESERVE src0_sel:WORD_1
	v_exp_f16_sdwa v190, v85 dst_sel:WORD_1 dst_unused:UNUSED_PRESERVE src0_sel:WORD_1
	v_pk_add_f16 v107, v107, v155 neg_lo:[0,1] neg_hi:[0,1]
	v_pk_add_f16 v82, v190, 0
	v_pk_fma_f16 v42, v42, v187, 0
	v_pk_add_f16 v83, v189, 0
	v_pk_add_f16 v84, v188, 0
	v_pk_add_f16 v85, v187, 0
	v_pk_fma_f16 v45, v45, v190, 0
	v_pk_fma_f16 v44, v44, v189, 0
	v_pk_fma_f16 v43, v43, v188, 0
	v_pk_add_f16 v108, v108, v156 neg_lo:[0,1] neg_hi:[0,1]
	v_pk_add_f16 v109, v109, v157 neg_lo:[0,1] neg_hi:[0,1]
	v_exp_f16_sdwa v187, v106 dst_sel:WORD_0 dst_unused:UNUSED_PAD src0_sel:WORD_0
	v_exp_f16_sdwa v188, v107 dst_sel:WORD_0 dst_unused:UNUSED_PAD src0_sel:WORD_0
	v_exp_f16_sdwa v189, v108 dst_sel:WORD_0 dst_unused:UNUSED_PAD src0_sel:WORD_0
	v_exp_f16_sdwa v190, v109 dst_sel:WORD_0 dst_unused:UNUSED_PAD src0_sel:WORD_0
	v_exp_f16_sdwa v187, v106 dst_sel:WORD_1 dst_unused:UNUSED_PRESERVE src0_sel:WORD_1
	v_exp_f16_sdwa v188, v107 dst_sel:WORD_1 dst_unused:UNUSED_PRESERVE src0_sel:WORD_1
	v_exp_f16_sdwa v189, v108 dst_sel:WORD_1 dst_unused:UNUSED_PRESERVE src0_sel:WORD_1
	v_exp_f16_sdwa v190, v109 dst_sel:WORD_1 dst_unused:UNUSED_PRESERVE src0_sel:WORD_1
	s_nop 0
	v_pk_add_f16 v82, v82, v190
	v_pk_fma_f16 v42, v62, v187, v42
	v_pk_add_f16 v62, v78, v154 neg_lo:[0,1] neg_hi:[0,1]
	v_pk_add_f16 v85, v85, v187
	v_pk_add_f16 v84, v84, v188
	v_pk_add_f16 v83, v83, v189
	v_pk_fma_f16 v43, v63, v188, v43
	v_pk_fma_f16 v44, v64, v189, v44
	v_pk_fma_f16 v45, v65, v190, v45
	v_pk_add_f16 v63, v79, v155 neg_lo:[0,1] neg_hi:[0,1]
	v_pk_add_f16 v64, v80, v156 neg_lo:[0,1] neg_hi:[0,1]
	v_pk_add_f16 v65, v81, v157 neg_lo:[0,1] neg_hi:[0,1]
	v_exp_f16_sdwa v78, v62 dst_sel:WORD_0 dst_unused:UNUSED_PAD src0_sel:WORD_0
	v_exp_f16_sdwa v79, v63 dst_sel:WORD_0 dst_unused:UNUSED_PAD src0_sel:WORD_0
	v_exp_f16_sdwa v80, v64 dst_sel:WORD_0 dst_unused:UNUSED_PAD src0_sel:WORD_0
	v_exp_f16_sdwa v81, v65 dst_sel:WORD_0 dst_unused:UNUSED_PAD src0_sel:WORD_0
	v_exp_f16_sdwa v78, v62 dst_sel:WORD_1 dst_unused:UNUSED_PRESERVE src0_sel:WORD_1
	v_exp_f16_sdwa v79, v63 dst_sel:WORD_1 dst_unused:UNUSED_PRESERVE src0_sel:WORD_1
	v_exp_f16_sdwa v80, v64 dst_sel:WORD_1 dst_unused:UNUSED_PRESERVE src0_sel:WORD_1
	v_exp_f16_sdwa v81, v65 dst_sel:WORD_1 dst_unused:UNUSED_PRESERVE src0_sel:WORD_1
	s_nop 0
	v_pk_add_f16 v62, v82, v81
	v_pk_add_f16 v63, v83, v80
	v_pk_add_f16 v64, v84, v79
	v_pk_add_f16 v65, v85, v78
	v_pk_fma_f16 v45, v89, v81, v45
	v_pk_fma_f16 v44, v88, v80, v44
	v_pk_fma_f16 v43, v87, v79, v43
	v_pk_fma_f16 v42, v86, v78, v42
	v_pk_add_f16 v78, v125, v154 neg_lo:[0,1] neg_hi:[0,1]
	v_pk_add_f16 v79, v124, v155 neg_lo:[0,1] neg_hi:[0,1]
	v_pk_add_f16 v80, v123, v156 neg_lo:[0,1] neg_hi:[0,1]
	v_pk_add_f16 v81, v122, v157 neg_lo:[0,1] neg_hi:[0,1]
	v_exp_f16_sdwa v82, v78 dst_sel:WORD_0 dst_unused:UNUSED_PAD src0_sel:WORD_0
	v_exp_f16_sdwa v83, v79 dst_sel:WORD_0 dst_unused:UNUSED_PAD src0_sel:WORD_0
	v_exp_f16_sdwa v84, v80 dst_sel:WORD_0 dst_unused:UNUSED_PAD src0_sel:WORD_0
	v_exp_f16_sdwa v85, v81 dst_sel:WORD_0 dst_unused:UNUSED_PAD src0_sel:WORD_0
	v_exp_f16_sdwa v82, v78 dst_sel:WORD_1 dst_unused:UNUSED_PRESERVE src0_sel:WORD_1
	v_exp_f16_sdwa v83, v79 dst_sel:WORD_1 dst_unused:UNUSED_PRESERVE src0_sel:WORD_1
	v_exp_f16_sdwa v84, v80 dst_sel:WORD_1 dst_unused:UNUSED_PRESERVE src0_sel:WORD_1
	v_exp_f16_sdwa v85, v81 dst_sel:WORD_1 dst_unused:UNUSED_PRESERVE src0_sel:WORD_1
	v_pk_add_f16 v78, v129, v154 neg_lo:[0,1] neg_hi:[0,1]
	v_pk_add_f16 v62, v62, v85
	v_pk_add_f16 v65, v65, v82
	v_pk_add_f16 v64, v64, v83
	v_pk_add_f16 v63, v63, v84
	v_pk_fma_f16 v42, v22, v82, v42
	v_pk_fma_f16 v43, v23, v83, v43
	v_pk_fma_f16 v44, v24, v84, v44
	v_pk_fma_f16 v45, v25, v85, v45
	v_pk_add_f16 v79, v128, v155 neg_lo:[0,1] neg_hi:[0,1]
	v_pk_add_f16 v80, v127, v156 neg_lo:[0,1] neg_hi:[0,1]
	v_pk_add_f16 v81, v126, v157 neg_lo:[0,1] neg_hi:[0,1]
	v_exp_f16_sdwa v82, v78 dst_sel:WORD_0 dst_unused:UNUSED_PAD src0_sel:WORD_0
	v_exp_f16_sdwa v83, v79 dst_sel:WORD_0 dst_unused:UNUSED_PAD src0_sel:WORD_0
	v_exp_f16_sdwa v84, v80 dst_sel:WORD_0 dst_unused:UNUSED_PAD src0_sel:WORD_0
	v_exp_f16_sdwa v85, v81 dst_sel:WORD_0 dst_unused:UNUSED_PAD src0_sel:WORD_0
	v_exp_f16_sdwa v82, v78 dst_sel:WORD_1 dst_unused:UNUSED_PRESERVE src0_sel:WORD_1
	v_exp_f16_sdwa v83, v79 dst_sel:WORD_1 dst_unused:UNUSED_PRESERVE src0_sel:WORD_1
	v_exp_f16_sdwa v84, v80 dst_sel:WORD_1 dst_unused:UNUSED_PRESERVE src0_sel:WORD_1
	v_exp_f16_sdwa v85, v81 dst_sel:WORD_1 dst_unused:UNUSED_PRESERVE src0_sel:WORD_1
	v_pk_add_f16 v78, v102, v154 neg_lo:[0,1] neg_hi:[0,1]
	v_pk_add_f16 v62, v62, v85
	v_pk_add_f16 v63, v63, v84
	v_pk_add_f16 v64, v64, v83
	v_pk_add_f16 v65, v65, v82
	v_pk_fma_f16 v45, v37, v85, v45
	v_pk_fma_f16 v44, v36, v84, v44
	v_pk_fma_f16 v43, v35, v83, v43
	v_pk_fma_f16 v42, v34, v82, v42
	v_pk_add_f16 v79, v103, v155 neg_lo:[0,1] neg_hi:[0,1]
	v_pk_add_f16 v80, v104, v156 neg_lo:[0,1] neg_hi:[0,1]
	v_pk_add_f16 v81, v105, v157 neg_lo:[0,1] neg_hi:[0,1]
	v_exp_f16_sdwa v82, v78 dst_sel:WORD_0 dst_unused:UNUSED_PAD src0_sel:WORD_0
	v_exp_f16_sdwa v83, v79 dst_sel:WORD_0 dst_unused:UNUSED_PAD src0_sel:WORD_0
	v_exp_f16_sdwa v84, v80 dst_sel:WORD_0 dst_unused:UNUSED_PAD src0_sel:WORD_0
	v_exp_f16_sdwa v85, v81 dst_sel:WORD_0 dst_unused:UNUSED_PAD src0_sel:WORD_0
	v_exp_f16_sdwa v82, v78 dst_sel:WORD_1 dst_unused:UNUSED_PRESERVE src0_sel:WORD_1
	v_exp_f16_sdwa v83, v79 dst_sel:WORD_1 dst_unused:UNUSED_PRESERVE src0_sel:WORD_1
	v_exp_f16_sdwa v84, v80 dst_sel:WORD_1 dst_unused:UNUSED_PRESERVE src0_sel:WORD_1
	v_exp_f16_sdwa v85, v81 dst_sel:WORD_1 dst_unused:UNUSED_PRESERVE src0_sel:WORD_1
	v_pk_add_f16 v78, v137, v154 neg_lo:[0,1] neg_hi:[0,1]
	v_pk_add_f16 v62, v62, v85
	v_pk_add_f16 v65, v65, v82
	v_pk_add_f16 v64, v64, v83
	v_pk_add_f16 v63, v63, v84
	v_pk_fma_f16 v42, v46, v82, v42
	v_pk_fma_f16 v43, v47, v83, v43
	v_pk_fma_f16 v44, v48, v84, v44
	v_pk_fma_f16 v45, v49, v85, v45
	v_pk_add_f16 v79, v136, v155 neg_lo:[0,1] neg_hi:[0,1]
	v_pk_add_f16 v80, v135, v156 neg_lo:[0,1] neg_hi:[0,1]
	v_pk_add_f16 v81, v134, v157 neg_lo:[0,1] neg_hi:[0,1]
	v_exp_f16_sdwa v82, v78 dst_sel:WORD_0 dst_unused:UNUSED_PAD src0_sel:WORD_0
	v_exp_f16_sdwa v83, v79 dst_sel:WORD_0 dst_unused:UNUSED_PAD src0_sel:WORD_0
	v_exp_f16_sdwa v84, v80 dst_sel:WORD_0 dst_unused:UNUSED_PAD src0_sel:WORD_0
	v_exp_f16_sdwa v85, v81 dst_sel:WORD_0 dst_unused:UNUSED_PAD src0_sel:WORD_0
	v_exp_f16_sdwa v82, v78 dst_sel:WORD_1 dst_unused:UNUSED_PRESERVE src0_sel:WORD_1
	v_exp_f16_sdwa v83, v79 dst_sel:WORD_1 dst_unused:UNUSED_PRESERVE src0_sel:WORD_1
	v_exp_f16_sdwa v84, v80 dst_sel:WORD_1 dst_unused:UNUSED_PRESERVE src0_sel:WORD_1
	v_exp_f16_sdwa v85, v81 dst_sel:WORD_1 dst_unused:UNUSED_PRESERVE src0_sel:WORD_1
	v_pk_add_f16 v78, v186, v154 neg_lo:[0,1] neg_hi:[0,1]
	v_pk_add_f16 v62, v62, v85
	v_pk_add_f16 v63, v63, v84
	v_pk_add_f16 v64, v64, v83
	v_pk_add_f16 v65, v65, v82
	v_pk_fma_f16 v45, v9, v85, v45
	v_pk_fma_f16 v44, v8, v84, v44
	v_pk_fma_f16 v43, v7, v83, v43
	v_pk_fma_f16 v42, v6, v82, v42
	v_pk_add_f16 v79, v185, v155 neg_lo:[0,1] neg_hi:[0,1]
	v_pk_add_f16 v80, v184, v156 neg_lo:[0,1] neg_hi:[0,1]
	v_pk_add_f16 v81, v183, v157 neg_lo:[0,1] neg_hi:[0,1]
	v_exp_f16_sdwa v82, v78 dst_sel:WORD_0 dst_unused:UNUSED_PAD src0_sel:WORD_0
	v_exp_f16_sdwa v83, v79 dst_sel:WORD_0 dst_unused:UNUSED_PAD src0_sel:WORD_0
	v_exp_f16_sdwa v84, v80 dst_sel:WORD_0 dst_unused:UNUSED_PAD src0_sel:WORD_0
	v_exp_f16_sdwa v85, v81 dst_sel:WORD_0 dst_unused:UNUSED_PAD src0_sel:WORD_0
	v_exp_f16_sdwa v82, v78 dst_sel:WORD_1 dst_unused:UNUSED_PRESERVE src0_sel:WORD_1
	v_exp_f16_sdwa v83, v79 dst_sel:WORD_1 dst_unused:UNUSED_PRESERVE src0_sel:WORD_1
	v_exp_f16_sdwa v84, v80 dst_sel:WORD_1 dst_unused:UNUSED_PRESERVE src0_sel:WORD_1
	v_exp_f16_sdwa v85, v81 dst_sel:WORD_1 dst_unused:UNUSED_PRESERVE src0_sel:WORD_1
	v_pk_add_f16 v78, v114, v154 neg_lo:[0,1] neg_hi:[0,1]
	v_pk_add_f16 v62, v62, v85
	v_pk_add_f16 v65, v65, v82
	v_pk_add_f16 v64, v64, v83
	v_pk_add_f16 v63, v63, v84
	v_pk_fma_f16 v42, v10, v82, v42
	v_pk_fma_f16 v43, v11, v83, v43
	v_pk_fma_f16 v44, v12, v84, v44
	v_pk_fma_f16 v45, v13, v85, v45
	v_pk_add_f16 v79, v115, v155 neg_lo:[0,1] neg_hi:[0,1]
	v_pk_add_f16 v80, v116, v156 neg_lo:[0,1] neg_hi:[0,1]
	v_pk_add_f16 v81, v117, v157 neg_lo:[0,1] neg_hi:[0,1]
	v_exp_f16_sdwa v82, v78 dst_sel:WORD_0 dst_unused:UNUSED_PAD src0_sel:WORD_0
	v_exp_f16_sdwa v83, v79 dst_sel:WORD_0 dst_unused:UNUSED_PAD src0_sel:WORD_0
	v_exp_f16_sdwa v84, v80 dst_sel:WORD_0 dst_unused:UNUSED_PAD src0_sel:WORD_0
	v_exp_f16_sdwa v85, v81 dst_sel:WORD_0 dst_unused:UNUSED_PAD src0_sel:WORD_0
	v_exp_f16_sdwa v82, v78 dst_sel:WORD_1 dst_unused:UNUSED_PRESERVE src0_sel:WORD_1
	v_exp_f16_sdwa v83, v79 dst_sel:WORD_1 dst_unused:UNUSED_PRESERVE src0_sel:WORD_1
	v_exp_f16_sdwa v84, v80 dst_sel:WORD_1 dst_unused:UNUSED_PRESERVE src0_sel:WORD_1
	v_exp_f16_sdwa v85, v81 dst_sel:WORD_1 dst_unused:UNUSED_PRESERVE src0_sel:WORD_1
	s_nop 0
	v_pk_add_f16 v62, v62, v85
	v_pk_add_f16 v63, v63, v84
	v_pk_add_f16 v64, v64, v83
	v_pk_add_f16 v65, v65, v82
	v_rcp_f16_e32 v81, v62
	v_rcp_f16_sdwa v62, v62 dst_sel:DWORD dst_unused:UNUSED_PAD src0_sel:WORD_1
	v_rcp_f16_e32 v78, v65
	v_rcp_f16_sdwa v65, v65 dst_sel:DWORD dst_unused:UNUSED_PAD src0_sel:WORD_1
	v_rcp_f16_e32 v79, v64
	v_rcp_f16_sdwa v64, v64 dst_sel:DWORD dst_unused:UNUSED_PAD src0_sel:WORD_1
	v_rcp_f16_e32 v80, v63
	v_rcp_f16_sdwa v63, v63 dst_sel:DWORD dst_unused:UNUSED_PAD src0_sel:WORD_1
	v_pk_fma_f16 v45, v17, v85, v45
	v_pack_b32_f16 v62, v81, v62
	v_pk_fma_f16 v44, v16, v84, v44
	v_pk_fma_f16 v43, v15, v83, v43
	v_pk_fma_f16 v42, v14, v82, v42
	v_pack_b32_f16 v65, v78, v65
	v_pack_b32_f16 v64, v79, v64
	v_pack_b32_f16 v63, v80, v63
	v_pk_mul_f16 v45, v45, v62
	s_waitcnt vmcnt(6)
	v_pk_mul_f16 v62, v182, v150 op_sel_hi:[0,1]
	v_pk_mul_f16 v42, v42, v65
	v_pk_mul_f16 v43, v43, v64
	v_pk_mul_f16 v44, v44, v63
	v_pk_mul_f16 v63, v182, v151 op_sel_hi:[0,1]
	v_pk_mul_f16 v64, v182, v152 op_sel_hi:[0,1]
	v_pk_mul_f16 v65, v182, v153 op_sel_hi:[0,1]
	v_pk_mul_f16 v78, v180, v150 op_sel_hi:[0,1]
	v_pk_mul_f16 v82, v181, v150 op_sel_hi:[0,1]
	v_pk_fma_f16 v50, v50, v150, v62
	v_pk_fma_f16 v66, v66, v150, v62
	v_pk_fma_f16 v62, v94, v150, v62
	v_pk_mul_f16 v79, v180, v151 op_sel_hi:[0,1]
	v_pk_maximum3_f16 v114, v50, v66, v62
	v_pk_mul_f16 v80, v180, v152 op_sel_hi:[0,1]
	v_pk_mul_f16 v81, v180, v153 op_sel_hi:[0,1]
	v_pk_mul_f16 v83, v181, v151 op_sel_hi:[0,1]
	v_pk_mul_f16 v84, v181, v152 op_sel_hi:[0,1]
	v_pk_mul_f16 v85, v181, v153 op_sel_hi:[0,1]
	v_pk_fma_f16 v53, v53, v153, v65
	v_pk_fma_f16 v52, v52, v152, v64
	v_pk_fma_f16 v51, v51, v151, v63
	v_pk_fma_f16 v69, v69, v153, v65
	v_pk_fma_f16 v68, v68, v152, v64
	v_pk_fma_f16 v67, v67, v151, v63
	v_pk_fma_f16 v65, v97, v153, v65
	v_pk_fma_f16 v64, v96, v152, v64
	v_pk_fma_f16 v63, v95, v151, v63
	v_pk_fma_f16 v89, v18, v150, v78
	v_pk_fma_f16 v97, v30, v150, v78
	v_pk_fma_f16 v78, v54, v150, v78
	v_pk_fma_f16 v105, v74, v150, v82
	v_pk_fma_f16 v109, v98, v150, v82
	v_pk_fma_f16 v82, v118, v150, v82
	v_pk_maximum3_f16 v115, v51, v67, v63
	v_pk_maximum3_f16 v116, v52, v68, v64
	v_pk_maximum3_f16 v117, v53, v69, v65
	v_pk_maximum3_f16 v122, v89, v97, v78
	v_pk_fma_f16 v86, v21, v153, v81
	v_pk_maximum3_f16 v126, v105, v109, v82
	v_pk_fma_f16 v87, v20, v152, v80
	v_pk_maximum3_f16 v114, v114, v122, v126
	v_pk_fma_f16 v88, v19, v151, v79
	v_pk_fma_f16 v94, v33, v153, v81
	v_pk_fma_f16 v95, v32, v152, v80
	v_pk_fma_f16 v96, v31, v151, v79
	v_pk_fma_f16 v81, v57, v153, v81
	v_pk_fma_f16 v80, v56, v152, v80
	v_pk_fma_f16 v79, v55, v151, v79
	v_pk_fma_f16 v102, v77, v153, v85
	v_pk_fma_f16 v103, v76, v152, v84
	v_pk_fma_f16 v104, v75, v151, v83
	v_pk_fma_f16 v106, v101, v153, v85
	v_pk_fma_f16 v107, v100, v152, v84
	v_pk_fma_f16 v108, v99, v151, v83
	v_pk_fma_f16 v85, v121, v153, v85
	v_pk_fma_f16 v84, v120, v152, v84
	v_pk_fma_f16 v83, v119, v151, v83
	v_pk_maximum3_f16 v123, v88, v96, v79
	v_pk_maximum3_f16 v124, v87, v95, v80
	v_pk_maximum3_f16 v125, v86, v94, v81
	v_pk_maximum3_f16 v128, v103, v107, v84
	v_pk_maximum3_f16 v129, v102, v106, v85
	v_pk_maximum3_f16 v127, v104, v108, v83
	v_pk_maximum3_f16 v115, v115, v123, v127
	v_pk_maximum3_f16 v116, v116, v124, v128
	v_pk_maximum3_f16 v117, v117, v125, v129
	v_pk_add_f16 v50, v50, v114 neg_lo:[0,1] neg_hi:[0,1]
	v_pk_add_f16 v51, v51, v115 neg_lo:[0,1] neg_hi:[0,1]
	v_pk_add_f16 v52, v52, v116 neg_lo:[0,1] neg_hi:[0,1]
	v_pk_add_f16 v53, v53, v117 neg_lo:[0,1] neg_hi:[0,1]
	v_pk_add_f16 v66, v66, v114 neg_lo:[0,1] neg_hi:[0,1]
	v_exp_f16_sdwa v122, v50 dst_sel:WORD_0 dst_unused:UNUSED_PAD src0_sel:WORD_0
	v_exp_f16_sdwa v123, v51 dst_sel:WORD_0 dst_unused:UNUSED_PAD src0_sel:WORD_0
	v_exp_f16_sdwa v124, v52 dst_sel:WORD_0 dst_unused:UNUSED_PAD src0_sel:WORD_0
	v_exp_f16_sdwa v125, v53 dst_sel:WORD_0 dst_unused:UNUSED_PAD src0_sel:WORD_0
	v_exp_f16_sdwa v122, v50 dst_sel:WORD_1 dst_unused:UNUSED_PRESERVE src0_sel:WORD_1
	v_exp_f16_sdwa v123, v51 dst_sel:WORD_1 dst_unused:UNUSED_PRESERVE src0_sel:WORD_1
	v_exp_f16_sdwa v124, v52 dst_sel:WORD_1 dst_unused:UNUSED_PRESERVE src0_sel:WORD_1
	v_exp_f16_sdwa v125, v53 dst_sel:WORD_1 dst_unused:UNUSED_PRESERVE src0_sel:WORD_1
	v_pk_add_f16 v67, v67, v115 neg_lo:[0,1] neg_hi:[0,1]
	v_pk_add_f16 v50, v125, 0
	v_pk_fma_f16 v22, v22, v122, 0
	v_pk_add_f16 v51, v124, 0
	v_pk_add_f16 v52, v123, 0
	v_pk_add_f16 v53, v122, 0
	v_pk_fma_f16 v23, v23, v123, 0
	v_pk_fma_f16 v24, v24, v124, 0
	v_pk_fma_f16 v25, v25, v125, 0
	v_pk_add_f16 v68, v68, v116 neg_lo:[0,1] neg_hi:[0,1]
	v_pk_add_f16 v69, v69, v117 neg_lo:[0,1] neg_hi:[0,1]
	v_exp_f16_sdwa v122, v66 dst_sel:WORD_0 dst_unused:UNUSED_PAD src0_sel:WORD_0
	v_exp_f16_sdwa v123, v67 dst_sel:WORD_0 dst_unused:UNUSED_PAD src0_sel:WORD_0
	v_exp_f16_sdwa v124, v68 dst_sel:WORD_0 dst_unused:UNUSED_PAD src0_sel:WORD_0
	v_exp_f16_sdwa v125, v69 dst_sel:WORD_0 dst_unused:UNUSED_PAD src0_sel:WORD_0
	v_exp_f16_sdwa v122, v66 dst_sel:WORD_1 dst_unused:UNUSED_PRESERVE src0_sel:WORD_1
	v_exp_f16_sdwa v123, v67 dst_sel:WORD_1 dst_unused:UNUSED_PRESERVE src0_sel:WORD_1
	v_exp_f16_sdwa v124, v68 dst_sel:WORD_1 dst_unused:UNUSED_PRESERVE src0_sel:WORD_1
	v_exp_f16_sdwa v125, v69 dst_sel:WORD_1 dst_unused:UNUSED_PRESERVE src0_sel:WORD_1
	s_nop 0
	v_pk_add_f16 v50, v50, v125
	v_pk_fma_f16 v22, v34, v122, v22
	v_pk_add_f16 v34, v62, v114 neg_lo:[0,1] neg_hi:[0,1]
	v_pk_add_f16 v53, v53, v122
	v_pk_add_f16 v52, v52, v123
	v_pk_add_f16 v51, v51, v124
	v_pk_fma_f16 v25, v37, v125, v25
	v_pk_fma_f16 v24, v36, v124, v24
	v_pk_fma_f16 v23, v35, v123, v23
	v_pk_add_f16 v35, v63, v115 neg_lo:[0,1] neg_hi:[0,1]
	v_pk_add_f16 v36, v64, v116 neg_lo:[0,1] neg_hi:[0,1]
	v_pk_add_f16 v37, v65, v117 neg_lo:[0,1] neg_hi:[0,1]
	v_exp_f16_sdwa v62, v34 dst_sel:WORD_0 dst_unused:UNUSED_PAD src0_sel:WORD_0
	v_exp_f16_sdwa v63, v35 dst_sel:WORD_0 dst_unused:UNUSED_PAD src0_sel:WORD_0
	v_exp_f16_sdwa v64, v36 dst_sel:WORD_0 dst_unused:UNUSED_PAD src0_sel:WORD_0
	v_exp_f16_sdwa v65, v37 dst_sel:WORD_0 dst_unused:UNUSED_PAD src0_sel:WORD_0
	v_exp_f16_sdwa v62, v34 dst_sel:WORD_1 dst_unused:UNUSED_PRESERVE src0_sel:WORD_1
	v_exp_f16_sdwa v63, v35 dst_sel:WORD_1 dst_unused:UNUSED_PRESERVE src0_sel:WORD_1
	v_exp_f16_sdwa v64, v36 dst_sel:WORD_1 dst_unused:UNUSED_PRESERVE src0_sel:WORD_1
	v_exp_f16_sdwa v65, v37 dst_sel:WORD_1 dst_unused:UNUSED_PRESERVE src0_sel:WORD_1
	s_nop 0
	v_pk_add_f16 v34, v50, v65
	v_pk_add_f16 v35, v51, v64
	v_pk_add_f16 v36, v52, v63
	v_pk_add_f16 v37, v53, v62
	v_pk_fma_f16 v22, v46, v62, v22
	v_pk_fma_f16 v23, v47, v63, v23
	v_pk_fma_f16 v24, v48, v64, v24
	v_pk_fma_f16 v25, v49, v65, v25
	v_pk_add_f16 v46, v89, v114 neg_lo:[0,1] neg_hi:[0,1]
	v_pk_add_f16 v47, v88, v115 neg_lo:[0,1] neg_hi:[0,1]
	v_pk_add_f16 v48, v87, v116 neg_lo:[0,1] neg_hi:[0,1]
	v_pk_add_f16 v49, v86, v117 neg_lo:[0,1] neg_hi:[0,1]
	v_exp_f16_sdwa v50, v46 dst_sel:WORD_0 dst_unused:UNUSED_PAD src0_sel:WORD_0
	v_exp_f16_sdwa v51, v47 dst_sel:WORD_0 dst_unused:UNUSED_PAD src0_sel:WORD_0
	v_exp_f16_sdwa v52, v48 dst_sel:WORD_0 dst_unused:UNUSED_PAD src0_sel:WORD_0
	v_exp_f16_sdwa v53, v49 dst_sel:WORD_0 dst_unused:UNUSED_PAD src0_sel:WORD_0
	v_exp_f16_sdwa v50, v46 dst_sel:WORD_1 dst_unused:UNUSED_PRESERVE src0_sel:WORD_1
	v_exp_f16_sdwa v51, v47 dst_sel:WORD_1 dst_unused:UNUSED_PRESERVE src0_sel:WORD_1
	v_exp_f16_sdwa v52, v48 dst_sel:WORD_1 dst_unused:UNUSED_PRESERVE src0_sel:WORD_1
	v_exp_f16_sdwa v53, v49 dst_sel:WORD_1 dst_unused:UNUSED_PRESERVE src0_sel:WORD_1
	v_pk_add_f16 v46, v97, v114 neg_lo:[0,1] neg_hi:[0,1]
	v_pk_add_f16 v34, v34, v53
	v_pk_add_f16 v37, v37, v50
	v_pk_add_f16 v36, v36, v51
	v_pk_add_f16 v35, v35, v52
	v_pk_fma_f16 v25, v9, v53, v25
	v_pk_fma_f16 v24, v8, v52, v24
	v_pk_fma_f16 v23, v7, v51, v23
	v_pk_fma_f16 v22, v6, v50, v22
	v_pk_add_f16 v47, v96, v115 neg_lo:[0,1] neg_hi:[0,1]
	v_pk_add_f16 v48, v95, v116 neg_lo:[0,1] neg_hi:[0,1]
	v_pk_add_f16 v49, v94, v117 neg_lo:[0,1] neg_hi:[0,1]
	v_exp_f16_sdwa v50, v46 dst_sel:WORD_0 dst_unused:UNUSED_PAD src0_sel:WORD_0
	v_exp_f16_sdwa v51, v47 dst_sel:WORD_0 dst_unused:UNUSED_PAD src0_sel:WORD_0
	v_exp_f16_sdwa v52, v48 dst_sel:WORD_0 dst_unused:UNUSED_PAD src0_sel:WORD_0
	v_exp_f16_sdwa v53, v49 dst_sel:WORD_0 dst_unused:UNUSED_PAD src0_sel:WORD_0
	v_exp_f16_sdwa v50, v46 dst_sel:WORD_1 dst_unused:UNUSED_PRESERVE src0_sel:WORD_1
	v_exp_f16_sdwa v51, v47 dst_sel:WORD_1 dst_unused:UNUSED_PRESERVE src0_sel:WORD_1
	v_exp_f16_sdwa v52, v48 dst_sel:WORD_1 dst_unused:UNUSED_PRESERVE src0_sel:WORD_1
	v_exp_f16_sdwa v53, v49 dst_sel:WORD_1 dst_unused:UNUSED_PRESERVE src0_sel:WORD_1
	v_pk_add_f16 v46, v78, v114 neg_lo:[0,1] neg_hi:[0,1]
	v_pk_add_f16 v34, v34, v53
	v_pk_add_f16 v35, v35, v52
	v_pk_add_f16 v36, v36, v51
	v_pk_add_f16 v37, v37, v50
	v_pk_fma_f16 v22, v10, v50, v22
	v_pk_fma_f16 v23, v11, v51, v23
	v_pk_fma_f16 v24, v12, v52, v24
	v_pk_fma_f16 v25, v13, v53, v25
	v_pk_add_f16 v47, v79, v115 neg_lo:[0,1] neg_hi:[0,1]
	v_pk_add_f16 v48, v80, v116 neg_lo:[0,1] neg_hi:[0,1]
	v_pk_add_f16 v49, v81, v117 neg_lo:[0,1] neg_hi:[0,1]
	v_exp_f16_sdwa v50, v46 dst_sel:WORD_0 dst_unused:UNUSED_PAD src0_sel:WORD_0
	v_exp_f16_sdwa v51, v47 dst_sel:WORD_0 dst_unused:UNUSED_PAD src0_sel:WORD_0
	v_exp_f16_sdwa v52, v48 dst_sel:WORD_0 dst_unused:UNUSED_PAD src0_sel:WORD_0
	v_exp_f16_sdwa v53, v49 dst_sel:WORD_0 dst_unused:UNUSED_PAD src0_sel:WORD_0
	v_exp_f16_sdwa v50, v46 dst_sel:WORD_1 dst_unused:UNUSED_PRESERVE src0_sel:WORD_1
	v_exp_f16_sdwa v51, v47 dst_sel:WORD_1 dst_unused:UNUSED_PRESERVE src0_sel:WORD_1
	v_exp_f16_sdwa v52, v48 dst_sel:WORD_1 dst_unused:UNUSED_PRESERVE src0_sel:WORD_1
	v_exp_f16_sdwa v53, v49 dst_sel:WORD_1 dst_unused:UNUSED_PRESERVE src0_sel:WORD_1
	v_pk_add_f16 v46, v105, v114 neg_lo:[0,1] neg_hi:[0,1]
	v_pk_add_f16 v34, v34, v53
	v_pk_add_f16 v37, v37, v50
	v_pk_add_f16 v36, v36, v51
	v_pk_add_f16 v35, v35, v52
	v_pk_fma_f16 v25, v17, v53, v25
	v_pk_fma_f16 v24, v16, v52, v24
	v_pk_fma_f16 v23, v15, v51, v23
	v_pk_fma_f16 v22, v14, v50, v22
	v_pk_add_f16 v47, v104, v115 neg_lo:[0,1] neg_hi:[0,1]
	v_pk_add_f16 v48, v103, v116 neg_lo:[0,1] neg_hi:[0,1]
	v_pk_add_f16 v49, v102, v117 neg_lo:[0,1] neg_hi:[0,1]
	v_exp_f16_sdwa v50, v46 dst_sel:WORD_0 dst_unused:UNUSED_PAD src0_sel:WORD_0
	v_exp_f16_sdwa v51, v47 dst_sel:WORD_0 dst_unused:UNUSED_PAD src0_sel:WORD_0
	v_exp_f16_sdwa v52, v48 dst_sel:WORD_0 dst_unused:UNUSED_PAD src0_sel:WORD_0
	v_exp_f16_sdwa v53, v49 dst_sel:WORD_0 dst_unused:UNUSED_PAD src0_sel:WORD_0
	v_exp_f16_sdwa v50, v46 dst_sel:WORD_1 dst_unused:UNUSED_PRESERVE src0_sel:WORD_1
	v_exp_f16_sdwa v51, v47 dst_sel:WORD_1 dst_unused:UNUSED_PRESERVE src0_sel:WORD_1
	v_exp_f16_sdwa v52, v48 dst_sel:WORD_1 dst_unused:UNUSED_PRESERVE src0_sel:WORD_1
	v_exp_f16_sdwa v53, v49 dst_sel:WORD_1 dst_unused:UNUSED_PRESERVE src0_sel:WORD_1
	v_pk_add_f16 v46, v109, v114 neg_lo:[0,1] neg_hi:[0,1]
	v_pk_add_f16 v34, v34, v53
	v_pk_add_f16 v35, v35, v52
	v_pk_add_f16 v36, v36, v51
	v_pk_add_f16 v37, v37, v50
	v_pk_fma_f16 v22, v26, v50, v22
	v_pk_fma_f16 v23, v27, v51, v23
	v_pk_fma_f16 v24, v28, v52, v24
	v_pk_fma_f16 v25, v29, v53, v25
	v_pk_add_f16 v47, v108, v115 neg_lo:[0,1] neg_hi:[0,1]
	v_pk_add_f16 v48, v107, v116 neg_lo:[0,1] neg_hi:[0,1]
	v_pk_add_f16 v49, v106, v117 neg_lo:[0,1] neg_hi:[0,1]
	v_exp_f16_sdwa v50, v46 dst_sel:WORD_0 dst_unused:UNUSED_PAD src0_sel:WORD_0
	v_exp_f16_sdwa v51, v47 dst_sel:WORD_0 dst_unused:UNUSED_PAD src0_sel:WORD_0
	v_exp_f16_sdwa v52, v48 dst_sel:WORD_0 dst_unused:UNUSED_PAD src0_sel:WORD_0
	v_exp_f16_sdwa v53, v49 dst_sel:WORD_0 dst_unused:UNUSED_PAD src0_sel:WORD_0
	v_exp_f16_sdwa v50, v46 dst_sel:WORD_1 dst_unused:UNUSED_PRESERVE src0_sel:WORD_1
	v_exp_f16_sdwa v51, v47 dst_sel:WORD_1 dst_unused:UNUSED_PRESERVE src0_sel:WORD_1
	v_exp_f16_sdwa v52, v48 dst_sel:WORD_1 dst_unused:UNUSED_PRESERVE src0_sel:WORD_1
	v_exp_f16_sdwa v53, v49 dst_sel:WORD_1 dst_unused:UNUSED_PRESERVE src0_sel:WORD_1
	v_pk_add_f16 v46, v82, v114 neg_lo:[0,1] neg_hi:[0,1]
	v_pk_add_f16 v34, v34, v53
	v_pk_add_f16 v37, v37, v50
	v_pk_add_f16 v36, v36, v51
	v_pk_add_f16 v35, v35, v52
	v_pk_fma_f16 v25, v41, v53, v25
	v_pk_fma_f16 v24, v40, v52, v24
	v_pk_fma_f16 v23, v39, v51, v23
	v_pk_fma_f16 v22, v38, v50, v22
	v_pk_add_f16 v47, v83, v115 neg_lo:[0,1] neg_hi:[0,1]
	v_pk_add_f16 v48, v84, v116 neg_lo:[0,1] neg_hi:[0,1]
	v_pk_add_f16 v49, v85, v117 neg_lo:[0,1] neg_hi:[0,1]
	v_exp_f16_sdwa v50, v46 dst_sel:WORD_0 dst_unused:UNUSED_PAD src0_sel:WORD_0
	v_exp_f16_sdwa v51, v47 dst_sel:WORD_0 dst_unused:UNUSED_PAD src0_sel:WORD_0
	v_exp_f16_sdwa v52, v48 dst_sel:WORD_0 dst_unused:UNUSED_PAD src0_sel:WORD_0
	v_exp_f16_sdwa v53, v49 dst_sel:WORD_0 dst_unused:UNUSED_PAD src0_sel:WORD_0
	v_exp_f16_sdwa v50, v46 dst_sel:WORD_1 dst_unused:UNUSED_PRESERVE src0_sel:WORD_1
	v_exp_f16_sdwa v51, v47 dst_sel:WORD_1 dst_unused:UNUSED_PRESERVE src0_sel:WORD_1
	v_exp_f16_sdwa v52, v48 dst_sel:WORD_1 dst_unused:UNUSED_PRESERVE src0_sel:WORD_1
	v_exp_f16_sdwa v53, v49 dst_sel:WORD_1 dst_unused:UNUSED_PRESERVE src0_sel:WORD_1
	s_nop 0
	v_pk_add_f16 v34, v34, v53
	v_pk_add_f16 v35, v35, v52
	v_rcp_f16_e32 v48, v34
	v_rcp_f16_sdwa v34, v34 dst_sel:DWORD dst_unused:UNUSED_PAD src0_sel:WORD_1
	v_pk_add_f16 v36, v36, v51
	v_rcp_f16_e32 v49, v35
	v_rcp_f16_sdwa v35, v35 dst_sel:DWORD dst_unused:UNUSED_PAD src0_sel:WORD_1
	v_pk_add_f16 v37, v37, v50
	v_rcp_f16_e32 v47, v36
	v_rcp_f16_sdwa v36, v36 dst_sel:DWORD dst_unused:UNUSED_PAD src0_sel:WORD_1
	v_rcp_f16_e32 v46, v37
	v_rcp_f16_sdwa v37, v37 dst_sel:DWORD dst_unused:UNUSED_PAD src0_sel:WORD_1
	v_pk_fma_f16 v25, v61, v53, v25
	v_pack_b32_f16 v34, v48, v34
	v_pk_fma_f16 v24, v60, v52, v24
	v_pk_mul_f16 v25, v25, v34
	v_pack_b32_f16 v34, v49, v35
	v_pk_fma_f16 v23, v59, v51, v23
	v_pk_mul_f16 v24, v24, v34
	v_pack_b32_f16 v34, v47, v36
	v_pk_fma_f16 v22, v58, v50, v22
	v_pk_mul_f16 v23, v23, v34
	v_pack_b32_f16 v34, v46, v37
	v_pk_mul_f16 v22, v22, v34
	s_waitcnt vmcnt(0)
	s_cmp_lg_u32 s14, 1
	s_cbranch_scc1 .Lmywd5_1
	s_mul_i32 s84, s81, s83
	s_add_i32 s84, s84, s82
	s_mul_i32 s84, s84, 0x60000
	s_mul_i32 s85, s94, 0x6000
	s_add_u32 s84, s84, s85
	s_add_u32 s88, s86, s84
	s_addc_u32 s89, s87, 0
	v_mbcnt_lo_u32_b32 v251, -1, 0
	v_mbcnt_hi_u32_b32 v251, -1, v251
	v_lshlrev_b32_e32 v251, 4, v251
	global_load_dwordx4 v[252:255], v251, s[88:89]
	global_load_dwordx4 v[252:255], v251, s[88:89] offset:1024
	global_load_dwordx4 v[252:255], v251, s[88:89] offset:2048
	global_load_dwordx4 v[252:255], v251, s[88:89] offset:3072
	s_add_u32 s88, s88, 0x1000
	s_addc_u32 s89, s89, 0
	global_load_dwordx4 v[252:255], v251, s[88:89]
	global_load_dwordx4 v[252:255], v251, s[88:89] offset:1024
	global_load_dwordx4 v[252:255], v251, s[88:89] offset:2048
	global_load_dwordx4 v[252:255], v251, s[88:89] offset:3072
	s_add_u32 s88, s88, 0x1000
	s_addc_u32 s89, s89, 0
	global_load_dwordx4 v[252:255], v251, s[88:89]
	global_load_dwordx4 v[252:255], v251, s[88:89] offset:1024
	global_load_dwordx4 v[252:255], v251, s[88:89] offset:2048
	global_load_dwordx4 v[252:255], v251, s[88:89] offset:3072
.Lmywd5_1:
	v_pk_mul_f16 v34, v182, v146 op_sel_hi:[0,1]
	v_pk_mul_f16 v35, v182, v147 op_sel_hi:[0,1]
	v_pk_mul_f16 v36, v182, v148 op_sel_hi:[0,1]
	v_pk_mul_f16 v37, v182, v149 op_sel_hi:[0,1]
	v_pk_mul_f16 v46, v180, v146 op_sel_hi:[0,1]
	v_pk_mul_f16 v47, v180, v147 op_sel_hi:[0,1]
	v_pk_mul_f16 v48, v180, v148 op_sel_hi:[0,1]
	v_pk_mul_f16 v49, v180, v149 op_sel_hi:[0,1]
	v_pk_mul_f16 v50, v181, v146 op_sel_hi:[0,1]
	v_pk_mul_f16 v51, v181, v147 op_sel_hi:[0,1]
	v_pk_mul_f16 v52, v181, v148 op_sel_hi:[0,1]
	v_pk_mul_f16 v53, v181, v149 op_sel_hi:[0,1]
	v_pk_fma_f16 v21, v21, v149, v37
	v_pk_fma_f16 v20, v20, v148, v36
	v_pk_fma_f16 v19, v19, v147, v35
	v_pk_fma_f16 v18, v18, v146, v34
	v_pk_fma_f16 v33, v33, v149, v37
	v_pk_fma_f16 v32, v32, v148, v36
	v_pk_fma_f16 v31, v31, v147, v35
	v_pk_fma_f16 v30, v30, v146, v34
	v_pk_fma_f16 v37, v57, v149, v37
	v_pk_fma_f16 v36, v56, v148, v36
	v_pk_fma_f16 v35, v55, v147, v35
	v_pk_fma_f16 v34, v54, v146, v34
	v_pk_maximum3_f16 v79, v19, v31, v35
	v_pk_maximum3_f16 v80, v20, v32, v36
	v_pk_maximum3_f16 v81, v21, v33, v37
	v_pk_fma_f16 v54, v77, v149, v49
	v_pk_maximum3_f16 v78, v18, v30, v34
	v_pk_fma_f16 v55, v76, v148, v48
	v_pk_fma_f16 v56, v75, v147, v47
	v_pk_fma_f16 v57, v74, v146, v46
	v_pk_fma_f16 v62, v101, v149, v49
	v_pk_fma_f16 v63, v100, v148, v48
	v_pk_fma_f16 v64, v99, v147, v47
	v_pk_fma_f16 v65, v98, v146, v46
	v_pk_fma_f16 v49, v121, v149, v49
	v_pk_fma_f16 v48, v120, v148, v48
	v_pk_fma_f16 v47, v119, v147, v47
	v_pk_fma_f16 v46, v118, v146, v46
	v_pk_fma_f16 v66, v133, v149, v53
	v_pk_fma_f16 v67, v132, v148, v52
	v_pk_fma_f16 v68, v131, v147, v51
	v_pk_fma_f16 v69, v130, v146, v50
	v_pk_fma_f16 v74, v141, v149, v53
	v_pk_fma_f16 v75, v140, v148, v52
	v_pk_fma_f16 v76, v139, v147, v51
	v_pk_fma_f16 v77, v138, v146, v50
	v_pk_fma_f16 v53, v145, v149, v53
	v_pk_fma_f16 v52, v144, v148, v52
	v_pk_fma_f16 v51, v143, v147, v51
	v_pk_fma_f16 v50, v142, v146, v50
	v_pk_maximum3_f16 v82, v57, v65, v46
	v_pk_maximum3_f16 v83, v56, v64, v47
	v_pk_maximum3_f16 v84, v55, v63, v48
	v_pk_maximum3_f16 v85, v54, v62, v49
	v_pk_maximum3_f16 v87, v68, v76, v51
	v_pk_maximum3_f16 v86, v69, v77, v50
	v_pk_maximum3_f16 v88, v67, v75, v52
	v_pk_maximum3_f16 v89, v66, v74, v53
	v_pk_maximum3_f16 v78, v78, v82, v86
	v_pk_maximum3_f16 v79, v79, v83, v87
	v_pk_maximum3_f16 v80, v80, v84, v88
	v_pk_maximum3_f16 v81, v81, v85, v89
	s_nop 0
	v_pk_add_f16 v18, v18, v78 neg_lo:[0,1] neg_hi:[0,1]
	v_pk_add_f16 v19, v19, v79 neg_lo:[0,1] neg_hi:[0,1]
	v_pk_add_f16 v20, v20, v80 neg_lo:[0,1] neg_hi:[0,1]
	v_pk_add_f16 v21, v21, v81 neg_lo:[0,1] neg_hi:[0,1]
	v_pk_add_f16 v30, v30, v78 neg_lo:[0,1] neg_hi:[0,1]
	v_exp_f16_sdwa v82, v18 dst_sel:WORD_0 dst_unused:UNUSED_PAD src0_sel:WORD_0
	v_exp_f16_sdwa v83, v19 dst_sel:WORD_0 dst_unused:UNUSED_PAD src0_sel:WORD_0
	v_exp_f16_sdwa v84, v20 dst_sel:WORD_0 dst_unused:UNUSED_PAD src0_sel:WORD_0
	v_exp_f16_sdwa v85, v21 dst_sel:WORD_0 dst_unused:UNUSED_PAD src0_sel:WORD_0
	v_exp_f16_sdwa v82, v18 dst_sel:WORD_1 dst_unused:UNUSED_PRESERVE src0_sel:WORD_1
	v_exp_f16_sdwa v83, v19 dst_sel:WORD_1 dst_unused:UNUSED_PRESERVE src0_sel:WORD_1
	v_exp_f16_sdwa v84, v20 dst_sel:WORD_1 dst_unused:UNUSED_PRESERVE src0_sel:WORD_1
	v_exp_f16_sdwa v85, v21 dst_sel:WORD_1 dst_unused:UNUSED_PRESERVE src0_sel:WORD_1
	v_pk_add_f16 v31, v31, v79 neg_lo:[0,1] neg_hi:[0,1]
	v_pk_add_f16 v18, v82, 0
	v_pk_add_f16 v19, v83, 0
	v_pk_add_f16 v20, v84, 0
	v_pk_add_f16 v21, v85, 0
	v_pk_fma_f16 v6, v6, v82, 0
	v_pk_fma_f16 v7, v7, v83, 0
	v_pk_fma_f16 v8, v8, v84, 0
	v_pk_fma_f16 v9, v9, v85, 0
	v_pk_add_f16 v32, v32, v80 neg_lo:[0,1] neg_hi:[0,1]
	v_pk_add_f16 v33, v33, v81 neg_lo:[0,1] neg_hi:[0,1]
	v_exp_f16_sdwa v82, v30 dst_sel:WORD_0 dst_unused:UNUSED_PAD src0_sel:WORD_0
	v_exp_f16_sdwa v83, v31 dst_sel:WORD_0 dst_unused:UNUSED_PAD src0_sel:WORD_0
	v_exp_f16_sdwa v84, v32 dst_sel:WORD_0 dst_unused:UNUSED_PAD src0_sel:WORD_0
	v_exp_f16_sdwa v85, v33 dst_sel:WORD_0 dst_unused:UNUSED_PAD src0_sel:WORD_0
	v_exp_f16_sdwa v82, v30 dst_sel:WORD_1 dst_unused:UNUSED_PRESERVE src0_sel:WORD_1
	v_exp_f16_sdwa v83, v31 dst_sel:WORD_1 dst_unused:UNUSED_PRESERVE src0_sel:WORD_1
	v_exp_f16_sdwa v84, v32 dst_sel:WORD_1 dst_unused:UNUSED_PRESERVE src0_sel:WORD_1
	v_exp_f16_sdwa v85, v33 dst_sel:WORD_1 dst_unused:UNUSED_PRESERVE src0_sel:WORD_1
	s_nop 0
	v_pk_add_f16 v21, v21, v85
	v_pk_add_f16 v20, v20, v84
	v_pk_add_f16 v19, v19, v83
	v_pk_add_f16 v18, v18, v82
	v_pk_fma_f16 v9, v13, v85, v9
	v_pk_fma_f16 v8, v12, v84, v8
	v_pk_fma_f16 v7, v11, v83, v7
	v_pk_fma_f16 v6, v10, v82, v6
	v_pk_add_f16 v10, v34, v78 neg_lo:[0,1] neg_hi:[0,1]
	v_pk_add_f16 v11, v35, v79 neg_lo:[0,1] neg_hi:[0,1]
	v_pk_add_f16 v12, v36, v80 neg_lo:[0,1] neg_hi:[0,1]
	v_pk_add_f16 v13, v37, v81 neg_lo:[0,1] neg_hi:[0,1]
	v_exp_f16_sdwa v30, v10 dst_sel:WORD_0 dst_unused:UNUSED_PAD src0_sel:WORD_0
	v_exp_f16_sdwa v31, v11 dst_sel:WORD_0 dst_unused:UNUSED_PAD src0_sel:WORD_0
	v_exp_f16_sdwa v32, v12 dst_sel:WORD_0 dst_unused:UNUSED_PAD src0_sel:WORD_0
	v_exp_f16_sdwa v33, v13 dst_sel:WORD_0 dst_unused:UNUSED_PAD src0_sel:WORD_0
	v_exp_f16_sdwa v30, v10 dst_sel:WORD_1 dst_unused:UNUSED_PRESERVE src0_sel:WORD_1
	v_exp_f16_sdwa v31, v11 dst_sel:WORD_1 dst_unused:UNUSED_PRESERVE src0_sel:WORD_1
	v_exp_f16_sdwa v32, v12 dst_sel:WORD_1 dst_unused:UNUSED_PRESERVE src0_sel:WORD_1
	v_exp_f16_sdwa v33, v13 dst_sel:WORD_1 dst_unused:UNUSED_PRESERVE src0_sel:WORD_1
	v_pk_add_f16 v10, v18, v30
	v_pk_add_f16 v11, v19, v31
	v_pk_add_f16 v12, v20, v32
	v_pk_add_f16 v13, v21, v33
	v_pk_fma_f16 v6, v14, v30, v6
	v_pk_fma_f16 v7, v15, v31, v7
	v_pk_fma_f16 v8, v16, v32, v8
	v_pk_fma_f16 v9, v17, v33, v9
	v_pk_add_f16 v14, v57, v78 neg_lo:[0,1] neg_hi:[0,1]
	v_pk_add_f16 v15, v56, v79 neg_lo:[0,1] neg_hi:[0,1]
	v_pk_add_f16 v16, v55, v80 neg_lo:[0,1] neg_hi:[0,1]
	v_pk_add_f16 v17, v54, v81 neg_lo:[0,1] neg_hi:[0,1]
	v_exp_f16_sdwa v18, v14 dst_sel:WORD_0 dst_unused:UNUSED_PAD src0_sel:WORD_0
	v_exp_f16_sdwa v19, v15 dst_sel:WORD_0 dst_unused:UNUSED_PAD src0_sel:WORD_0
	v_exp_f16_sdwa v20, v16 dst_sel:WORD_0 dst_unused:UNUSED_PAD src0_sel:WORD_0
	v_exp_f16_sdwa v21, v17 dst_sel:WORD_0 dst_unused:UNUSED_PAD src0_sel:WORD_0
	v_exp_f16_sdwa v18, v14 dst_sel:WORD_1 dst_unused:UNUSED_PRESERVE src0_sel:WORD_1
	v_exp_f16_sdwa v19, v15 dst_sel:WORD_1 dst_unused:UNUSED_PRESERVE src0_sel:WORD_1
	v_exp_f16_sdwa v20, v16 dst_sel:WORD_1 dst_unused:UNUSED_PRESERVE src0_sel:WORD_1
	v_exp_f16_sdwa v21, v17 dst_sel:WORD_1 dst_unused:UNUSED_PRESERVE src0_sel:WORD_1
	v_pk_add_f16 v14, v65, v78 neg_lo:[0,1] neg_hi:[0,1]
	v_pk_add_f16 v13, v13, v21
	v_pk_add_f16 v12, v12, v20
	v_pk_add_f16 v11, v11, v19
	v_pk_add_f16 v10, v10, v18
	v_pk_fma_f16 v9, v29, v21, v9
	v_pk_fma_f16 v8, v28, v20, v8
	v_pk_fma_f16 v7, v27, v19, v7
	v_pk_fma_f16 v6, v26, v18, v6
	v_pk_add_f16 v15, v64, v79 neg_lo:[0,1] neg_hi:[0,1]
	v_pk_add_f16 v16, v63, v80 neg_lo:[0,1] neg_hi:[0,1]
	v_pk_add_f16 v17, v62, v81 neg_lo:[0,1] neg_hi:[0,1]
	v_exp_f16_sdwa v18, v14 dst_sel:WORD_0 dst_unused:UNUSED_PAD src0_sel:WORD_0
	v_exp_f16_sdwa v19, v15 dst_sel:WORD_0 dst_unused:UNUSED_PAD src0_sel:WORD_0
	v_exp_f16_sdwa v20, v16 dst_sel:WORD_0 dst_unused:UNUSED_PAD src0_sel:WORD_0
	v_exp_f16_sdwa v21, v17 dst_sel:WORD_0 dst_unused:UNUSED_PAD src0_sel:WORD_0
	v_exp_f16_sdwa v18, v14 dst_sel:WORD_1 dst_unused:UNUSED_PRESERVE src0_sel:WORD_1
	v_exp_f16_sdwa v19, v15 dst_sel:WORD_1 dst_unused:UNUSED_PRESERVE src0_sel:WORD_1
	v_exp_f16_sdwa v20, v16 dst_sel:WORD_1 dst_unused:UNUSED_PRESERVE src0_sel:WORD_1
	v_exp_f16_sdwa v21, v17 dst_sel:WORD_1 dst_unused:UNUSED_PRESERVE src0_sel:WORD_1
	v_pk_add_f16 v14, v46, v78 neg_lo:[0,1] neg_hi:[0,1]
	v_pk_add_f16 v10, v10, v18
	v_pk_add_f16 v11, v11, v19
	v_pk_add_f16 v12, v12, v20
	v_pk_add_f16 v13, v13, v21
	v_pk_fma_f16 v6, v38, v18, v6
	v_pk_fma_f16 v7, v39, v19, v7
	v_pk_fma_f16 v8, v40, v20, v8
	v_pk_fma_f16 v9, v41, v21, v9
	v_pk_add_f16 v15, v47, v79 neg_lo:[0,1] neg_hi:[0,1]
	v_pk_add_f16 v16, v48, v80 neg_lo:[0,1] neg_hi:[0,1]
	v_pk_add_f16 v17, v49, v81 neg_lo:[0,1] neg_hi:[0,1]
	v_exp_f16_sdwa v18, v14 dst_sel:WORD_0 dst_unused:UNUSED_PAD src0_sel:WORD_0
	v_exp_f16_sdwa v19, v15 dst_sel:WORD_0 dst_unused:UNUSED_PAD src0_sel:WORD_0
	v_exp_f16_sdwa v20, v16 dst_sel:WORD_0 dst_unused:UNUSED_PAD src0_sel:WORD_0
	v_exp_f16_sdwa v21, v17 dst_sel:WORD_0 dst_unused:UNUSED_PAD src0_sel:WORD_0
	v_exp_f16_sdwa v18, v14 dst_sel:WORD_1 dst_unused:UNUSED_PRESERVE src0_sel:WORD_1
	v_exp_f16_sdwa v19, v15 dst_sel:WORD_1 dst_unused:UNUSED_PRESERVE src0_sel:WORD_1
	v_exp_f16_sdwa v20, v16 dst_sel:WORD_1 dst_unused:UNUSED_PRESERVE src0_sel:WORD_1
	v_exp_f16_sdwa v21, v17 dst_sel:WORD_1 dst_unused:UNUSED_PRESERVE src0_sel:WORD_1
	v_pk_add_f16 v14, v69, v78 neg_lo:[0,1] neg_hi:[0,1]
	v_pk_add_f16 v13, v13, v21
	v_pk_add_f16 v12, v12, v20
	v_pk_add_f16 v11, v11, v19
	v_pk_add_f16 v10, v10, v18
	v_pk_fma_f16 v9, v61, v21, v9
	v_pk_fma_f16 v8, v60, v20, v8
	v_pk_fma_f16 v7, v59, v19, v7
	v_pk_fma_f16 v6, v58, v18, v6
	v_pk_add_f16 v15, v68, v79 neg_lo:[0,1] neg_hi:[0,1]
	v_pk_add_f16 v16, v67, v80 neg_lo:[0,1] neg_hi:[0,1]
	v_pk_add_f16 v17, v66, v81 neg_lo:[0,1] neg_hi:[0,1]
	v_exp_f16_sdwa v18, v14 dst_sel:WORD_0 dst_unused:UNUSED_PAD src0_sel:WORD_0
	v_exp_f16_sdwa v19, v15 dst_sel:WORD_0 dst_unused:UNUSED_PAD src0_sel:WORD_0
	v_exp_f16_sdwa v20, v16 dst_sel:WORD_0 dst_unused:UNUSED_PAD src0_sel:WORD_0
	v_exp_f16_sdwa v21, v17 dst_sel:WORD_0 dst_unused:UNUSED_PAD src0_sel:WORD_0
	v_exp_f16_sdwa v18, v14 dst_sel:WORD_1 dst_unused:UNUSED_PRESERVE src0_sel:WORD_1
	v_exp_f16_sdwa v19, v15 dst_sel:WORD_1 dst_unused:UNUSED_PRESERVE src0_sel:WORD_1
	v_exp_f16_sdwa v20, v16 dst_sel:WORD_1 dst_unused:UNUSED_PRESERVE src0_sel:WORD_1
	v_exp_f16_sdwa v21, v17 dst_sel:WORD_1 dst_unused:UNUSED_PRESERVE src0_sel:WORD_1
	v_pk_add_f16 v10, v10, v18
	v_pk_add_f16 v11, v11, v19
	v_pk_add_f16 v12, v12, v20
	v_pk_add_f16 v13, v13, v21
	v_pk_fma_f16 v14, v70, v18, v6
	v_pk_fma_f16 v15, v71, v19, v7
	v_pk_fma_f16 v16, v72, v20, v8
	v_pk_fma_f16 v17, v73, v21, v9
	v_pk_add_f16 v6, v77, v78 neg_lo:[0,1] neg_hi:[0,1]
	v_pk_add_f16 v7, v76, v79 neg_lo:[0,1] neg_hi:[0,1]
	v_pk_add_f16 v8, v75, v80 neg_lo:[0,1] neg_hi:[0,1]
	v_pk_add_f16 v9, v74, v81 neg_lo:[0,1] neg_hi:[0,1]
	v_exp_f16_sdwa v18, v6 dst_sel:WORD_0 dst_unused:UNUSED_PAD src0_sel:WORD_0
	v_exp_f16_sdwa v19, v7 dst_sel:WORD_0 dst_unused:UNUSED_PAD src0_sel:WORD_0
	v_exp_f16_sdwa v20, v8 dst_sel:WORD_0 dst_unused:UNUSED_PAD src0_sel:WORD_0
	v_exp_f16_sdwa v21, v9 dst_sel:WORD_0 dst_unused:UNUSED_PAD src0_sel:WORD_0
	v_exp_f16_sdwa v18, v6 dst_sel:WORD_1 dst_unused:UNUSED_PRESERVE src0_sel:WORD_1
	v_exp_f16_sdwa v19, v7 dst_sel:WORD_1 dst_unused:UNUSED_PRESERVE src0_sel:WORD_1
	v_exp_f16_sdwa v20, v8 dst_sel:WORD_1 dst_unused:UNUSED_PRESERVE src0_sel:WORD_1
	v_exp_f16_sdwa v21, v9 dst_sel:WORD_1 dst_unused:UNUSED_PRESERVE src0_sel:WORD_1
	s_nop 0
	v_pk_add_f16 v9, v13, v21
	v_pk_add_f16 v8, v12, v20
	v_pk_add_f16 v7, v11, v19
	v_pk_add_f16 v6, v10, v18
	v_pk_fma_f16 v13, v93, v21, v17
	v_pk_fma_f16 v12, v92, v20, v16
	v_pk_fma_f16 v11, v91, v19, v15
	v_pk_fma_f16 v10, v90, v18, v14
	v_pk_add_f16 v18, v50, v78 neg_lo:[0,1] neg_hi:[0,1]
	v_pk_add_f16 v19, v51, v79 neg_lo:[0,1] neg_hi:[0,1]
	v_pk_add_f16 v20, v52, v80 neg_lo:[0,1] neg_hi:[0,1]
	v_pk_add_f16 v21, v53, v81 neg_lo:[0,1] neg_hi:[0,1]
	v_exp_f16_sdwa v14, v18 dst_sel:WORD_0 dst_unused:UNUSED_PAD src0_sel:WORD_0
	v_exp_f16_sdwa v17, v19 dst_sel:WORD_0 dst_unused:UNUSED_PAD src0_sel:WORD_0
	v_exp_f16_sdwa v15, v20 dst_sel:WORD_0 dst_unused:UNUSED_PAD src0_sel:WORD_0
	v_exp_f16_sdwa v16, v21 dst_sel:WORD_0 dst_unused:UNUSED_PAD src0_sel:WORD_0
	v_exp_f16_sdwa v14, v18 dst_sel:WORD_1 dst_unused:UNUSED_PRESERVE src0_sel:WORD_1
	v_exp_f16_sdwa v17, v19 dst_sel:WORD_1 dst_unused:UNUSED_PRESERVE src0_sel:WORD_1
	v_exp_f16_sdwa v15, v20 dst_sel:WORD_1 dst_unused:UNUSED_PRESERVE src0_sel:WORD_1
	v_exp_f16_sdwa v16, v21 dst_sel:WORD_1 dst_unused:UNUSED_PRESERVE src0_sel:WORD_1
	s_nop 0

.Lmyf_D1_7:
	s_mov_b64 exec, -1
	s_waitcnt lgkmcnt(0)
	v_cvt_f16_f32_e32 v183, s27
	v_cvt_f16_f32_e32 v185, s26
	v_cvt_f16_f32_e32 v184, s31
	s_mov_b64 s[4:5], 0
	s_waitcnt vmcnt(3)
	v_pk_mul_f16 v193, v185, v189 op_sel_hi:[0,1]
	v_pk_mul_f16 v197, v183, v189 op_sel_hi:[0,1]
	v_pk_mul_f16 v201, v184, v189 op_sel_hi:[0,1]
	v_pk_mul_f16 v190, v185, v186 op_sel_hi:[0,1]
	v_pk_mul_f16 v191, v185, v187 op_sel_hi:[0,1]
	v_pk_mul_f16 v192, v185, v188 op_sel_hi:[0,1]
	v_pk_mul_f16 v194, v183, v186 op_sel_hi:[0,1]
	s_mov_b64 exec, s[64:65]
	buffer_load_dwordx4 v[18:21], v224, s[16:19], 0 offen
	buffer_load_dwordx4 v[6:9], v224, s[16:19], 0 offen offset:512
	s_mov_b64 exec, -1
	v_pk_mul_f16 v195, v183, v187 op_sel_hi:[0,1]
	v_pk_mul_f16 v196, v183, v188 op_sel_hi:[0,1]
	v_pk_mul_f16 v198, v184, v186 op_sel_hi:[0,1]
	v_pk_mul_f16 v199, v184, v187 op_sel_hi:[0,1]
	v_pk_mul_f16 v200, v184, v188 op_sel_hi:[0,1]
	v_pk_fma_f16 v113, v113, v189, v193
	v_pk_fma_f16 v129, v129, v189, v197
	v_pk_fma_f16 v137, v137, v189, v201
	v_pk_fma_f16 v202, v85, v189, v193
	v_pk_fma_f16 v206, v109, v189, v197
	v_pk_fma_f16 v210, v125, v189, v201
	v_pk_fma_f16 v193, v53, v189, v193
	v_pk_fma_f16 v197, v69, v189, v197
	buffer_load_dwordx4 v[34:37], v225, s[16:19], 0 offen offset:512
	buffer_load_dwordx4 v[10:13], v225, s[16:19], 0 offen offset:1024
	v_pk_fma_f16 v189, v97, v189, v201
	v_pk_maximum3_f16 v201, v113, v129, v137
	v_pk_fma_f16 v112, v112, v188, v192
	v_pk_fma_f16 v111, v111, v187, v191
	v_pk_fma_f16 v110, v110, v186, v190
	v_pk_fma_f16 v128, v128, v188, v196
	v_pk_fma_f16 v127, v127, v187, v195
	v_pk_fma_f16 v126, v126, v186, v194
	v_pk_fma_f16 v136, v136, v188, v200
	v_pk_fma_f16 v135, v135, v187, v199
	v_pk_fma_f16 v134, v134, v186, v198
	v_pk_fma_f16 v203, v84, v188, v192
	v_pk_fma_f16 v204, v83, v187, v191
	v_pk_fma_f16 v205, v82, v186, v190
	v_pk_fma_f16 v207, v108, v188, v196
	v_pk_fma_f16 v208, v107, v187, v195
	s_mov_b64 exec, s[66:67]
	buffer_load_dwordx4 v[54:57], v225, s[16:19], 0 offen offset:2048
	buffer_load_dwordx4 v[14:17], v225, s[16:19], 0 offen offset:2560
	s_mov_b64 exec, -1
	v_pk_fma_f16 v209, v106, v186, v194
	v_pk_fma_f16 v211, v124, v188, v200
	v_pk_fma_f16 v212, v123, v187, v199
	v_pk_fma_f16 v213, v122, v186, v198
	v_pk_fma_f16 v192, v52, v188, v192
	v_pk_fma_f16 v191, v51, v187, v191
	v_pk_fma_f16 v190, v50, v186, v190
	v_pk_fma_f16 v196, v68, v188, v196
	v_pk_fma_f16 v195, v67, v187, v195
	v_pk_fma_f16 v194, v66, v186, v194
	v_pk_fma_f16 v188, v96, v188, v200
	v_pk_fma_f16 v187, v95, v187, v199
	v_pk_fma_f16 v186, v94, v186, v198
	v_pk_maximum3_f16 v198, v110, v126, v134
	v_pk_maximum3_f16 v199, v111, v127, v135
	v_pk_maximum3_f16 v200, v112, v128, v136
	v_pk_maximum3_f16 v217, v202, v206, v210
	v_pk_maximum3_f16 v221, v193, v197, v189
	v_pk_maximum3_f16 v214, v205, v209, v213
	v_pk_maximum3_f16 v215, v204, v208, v212
	v_pk_maximum3_f16 v216, v203, v207, v211
	v_pk_maximum3_f16 v218, v190, v194, v186
	v_pk_maximum3_f16 v219, v191, v195, v187
	v_pk_maximum3_f16 v201, v201, v217, v221
	v_pk_maximum3_f16 v220, v192, v196, v188
	v_pk_maximum3_f16 v198, v198, v214, v218
	v_pk_maximum3_f16 v199, v199, v215, v219
	v_pk_maximum3_f16 v200, v200, v216, v220
	v_pk_add_f16 v113, v113, v201 neg_lo:[0,1] neg_hi:[0,1]
	s_mov_b64 exec, s[64:65]
	buffer_load_dwordx4 v[74:77], v226, s[16:19], 0 offen
	buffer_load_dwordx4 v[26:29], v226, s[16:19], 0 offen offset:512
	s_mov_b64 exec, -1
	v_pk_add_f16 v110, v110, v198 neg_lo:[0,1] neg_hi:[0,1]
	v_pk_add_f16 v111, v111, v199 neg_lo:[0,1] neg_hi:[0,1]
	v_pk_add_f16 v112, v112, v200 neg_lo:[0,1] neg_hi:[0,1]
	v_pk_add_f16 v126, v126, v198 neg_lo:[0,1] neg_hi:[0,1]
	v_exp_f16_sdwa v214, v110 dst_sel:WORD_0 dst_unused:UNUSED_PAD src0_sel:WORD_0
	v_exp_f16_sdwa v215, v111 dst_sel:WORD_0 dst_unused:UNUSED_PAD src0_sel:WORD_0
	v_exp_f16_sdwa v216, v112 dst_sel:WORD_0 dst_unused:UNUSED_PAD src0_sel:WORD_0
	v_exp_f16_sdwa v217, v113 dst_sel:WORD_0 dst_unused:UNUSED_PAD src0_sel:WORD_0
	v_exp_f16_sdwa v214, v110 dst_sel:WORD_1 dst_unused:UNUSED_PRESERVE src0_sel:WORD_1
	v_exp_f16_sdwa v215, v111 dst_sel:WORD_1 dst_unused:UNUSED_PRESERVE src0_sel:WORD_1
	v_exp_f16_sdwa v216, v112 dst_sel:WORD_1 dst_unused:UNUSED_PRESERVE src0_sel:WORD_1
	v_exp_f16_sdwa v217, v113 dst_sel:WORD_1 dst_unused:UNUSED_PRESERVE src0_sel:WORD_1
	v_pk_add_f16 v127, v127, v199 neg_lo:[0,1] neg_hi:[0,1]
	v_pk_add_f16 v113, v214, 0
	v_pk_fma_f16 v73, v73, v217, 0
	v_pk_add_f16 v110, v217, 0
	v_pk_add_f16 v111, v216, 0
	v_pk_add_f16 v112, v215, 0
	v_pk_fma_f16 v72, v72, v216, 0
	v_pk_fma_f16 v71, v71, v215, 0
	v_pk_fma_f16 v70, v70, v214, 0
	v_pk_add_f16 v128, v128, v200 neg_lo:[0,1] neg_hi:[0,1]
	buffer_load_dwordx4 v[102:105], v227, s[16:19], 0 offen offset:512
	buffer_load_dwordx4 v[38:41], v227, s[16:19], 0 offen offset:1024
	v_pk_add_f16 v129, v129, v201 neg_lo:[0,1] neg_hi:[0,1]
	v_exp_f16_sdwa v214, v126 dst_sel:WORD_0 dst_unused:UNUSED_PAD src0_sel:WORD_0
	v_exp_f16_sdwa v215, v127 dst_sel:WORD_0 dst_unused:UNUSED_PAD src0_sel:WORD_0
	v_exp_f16_sdwa v216, v128 dst_sel:WORD_0 dst_unused:UNUSED_PAD src0_sel:WORD_0
	v_exp_f16_sdwa v217, v129 dst_sel:WORD_0 dst_unused:UNUSED_PAD src0_sel:WORD_0
	v_exp_f16_sdwa v214, v126 dst_sel:WORD_1 dst_unused:UNUSED_PRESERVE src0_sel:WORD_1
	v_exp_f16_sdwa v215, v127 dst_sel:WORD_1 dst_unused:UNUSED_PRESERVE src0_sel:WORD_1
	v_exp_f16_sdwa v216, v128 dst_sel:WORD_1 dst_unused:UNUSED_PRESERVE src0_sel:WORD_1
	v_exp_f16_sdwa v217, v129 dst_sel:WORD_1 dst_unused:UNUSED_PRESERVE src0_sel:WORD_1
	v_pk_add_f16 v113, v113, v214
	v_pk_fma_f16 v73, v101, v217, v73
	v_pk_add_f16 v101, v137, v201 neg_lo:[0,1] neg_hi:[0,1]
	v_pk_add_f16 v112, v112, v215
	v_pk_add_f16 v111, v111, v216
	v_pk_add_f16 v110, v110, v217
	v_pk_fma_f16 v70, v98, v214, v70
	v_pk_fma_f16 v71, v99, v215, v71
	v_pk_fma_f16 v72, v100, v216, v72
	v_pk_add_f16 v98, v134, v198 neg_lo:[0,1] neg_hi:[0,1]
	v_pk_add_f16 v99, v135, v199 neg_lo:[0,1] neg_hi:[0,1]
	v_pk_add_f16 v100, v136, v200 neg_lo:[0,1] neg_hi:[0,1]
	v_exp_f16_sdwa v126, v98 dst_sel:WORD_0 dst_unused:UNUSED_PAD src0_sel:WORD_0
	v_exp_f16_sdwa v127, v99 dst_sel:WORD_0 dst_unused:UNUSED_PAD src0_sel:WORD_0
	v_exp_f16_sdwa v128, v100 dst_sel:WORD_0 dst_unused:UNUSED_PAD src0_sel:WORD_0
	v_exp_f16_sdwa v129, v101 dst_sel:WORD_0 dst_unused:UNUSED_PAD src0_sel:WORD_0
	v_exp_f16_sdwa v126, v98 dst_sel:WORD_1 dst_unused:UNUSED_PRESERVE src0_sel:WORD_1
	v_exp_f16_sdwa v127, v99 dst_sel:WORD_1 dst_unused:UNUSED_PRESERVE src0_sel:WORD_1
	v_exp_f16_sdwa v128, v100 dst_sel:WORD_1 dst_unused:UNUSED_PRESERVE src0_sel:WORD_1
	v_exp_f16_sdwa v129, v101 dst_sel:WORD_1 dst_unused:UNUSED_PRESERVE src0_sel:WORD_1
	v_pk_add_f16 v101, v113, v126
	v_pk_add_f16 v98, v110, v129
	s_mov_b64 exec, s[66:67]
	buffer_load_dwordx4 v[118:121], v227, s[16:19], 0 offen offset:2048
	buffer_load_dwordx4 v[58:61], v227, s[16:19], 0 offen offset:2560
	s_mov_b64 exec, -1
	v_pk_add_f16 v99, v111, v128
	v_pk_add_f16 v100, v112, v127
	v_pk_fma_f16 v73, v117, v129, v73
	v_pk_fma_f16 v72, v116, v128, v72
	v_pk_fma_f16 v71, v115, v127, v71
	v_pk_fma_f16 v70, v114, v126, v70
	v_pk_add_f16 v110, v205, v198 neg_lo:[0,1] neg_hi:[0,1]
	v_pk_add_f16 v111, v204, v199 neg_lo:[0,1] neg_hi:[0,1]
	v_pk_add_f16 v112, v203, v200 neg_lo:[0,1] neg_hi:[0,1]
	v_pk_add_f16 v113, v202, v201 neg_lo:[0,1] neg_hi:[0,1]
	v_exp_f16_sdwa v114, v110 dst_sel:WORD_0 dst_unused:UNUSED_PAD src0_sel:WORD_0
	v_exp_f16_sdwa v115, v111 dst_sel:WORD_0 dst_unused:UNUSED_PAD src0_sel:WORD_0
	v_exp_f16_sdwa v116, v112 dst_sel:WORD_0 dst_unused:UNUSED_PAD src0_sel:WORD_0
	v_exp_f16_sdwa v117, v113 dst_sel:WORD_0 dst_unused:UNUSED_PAD src0_sel:WORD_0
	v_exp_f16_sdwa v114, v110 dst_sel:WORD_1 dst_unused:UNUSED_PRESERVE src0_sel:WORD_1
	v_exp_f16_sdwa v115, v111 dst_sel:WORD_1 dst_unused:UNUSED_PRESERVE src0_sel:WORD_1
	v_exp_f16_sdwa v116, v112 dst_sel:WORD_1 dst_unused:UNUSED_PRESERVE src0_sel:WORD_1
	v_exp_f16_sdwa v117, v113 dst_sel:WORD_1 dst_unused:UNUSED_PRESERVE src0_sel:WORD_1
	v_pk_add_f16 v110, v209, v198 neg_lo:[0,1] neg_hi:[0,1]
	v_pk_add_f16 v101, v101, v114
	v_pk_add_f16 v100, v100, v115
	v_pk_add_f16 v99, v99, v116
	s_mov_b64 exec, s[76:77]
	buffer_load_dwordx4 v[130:133], v228, s[16:19], 0 offen
	buffer_load_dwordx4 v[78:81], v228, s[16:19], 0 offen offset:512
	s_mov_b64 exec, -1
	v_pk_add_f16 v98, v98, v117
	v_pk_fma_f16 v70, v42, v114, v70
	v_pk_fma_f16 v71, v43, v115, v71
	v_pk_fma_f16 v72, v44, v116, v72
	v_pk_fma_f16 v73, v45, v117, v73
	v_pk_add_f16 v111, v208, v199 neg_lo:[0,1] neg_hi:[0,1]
	v_pk_add_f16 v112, v207, v200 neg_lo:[0,1] neg_hi:[0,1]
	v_pk_add_f16 v113, v206, v201 neg_lo:[0,1] neg_hi:[0,1]
	v_exp_f16_sdwa v114, v110 dst_sel:WORD_0 dst_unused:UNUSED_PAD src0_sel:WORD_0
	v_exp_f16_sdwa v115, v111 dst_sel:WORD_0 dst_unused:UNUSED_PAD src0_sel:WORD_0
	v_exp_f16_sdwa v116, v112 dst_sel:WORD_0 dst_unused:UNUSED_PAD src0_sel:WORD_0
	v_exp_f16_sdwa v117, v113 dst_sel:WORD_0 dst_unused:UNUSED_PAD src0_sel:WORD_0
	v_exp_f16_sdwa v114, v110 dst_sel:WORD_1 dst_unused:UNUSED_PRESERVE src0_sel:WORD_1
	v_exp_f16_sdwa v115, v111 dst_sel:WORD_1 dst_unused:UNUSED_PRESERVE src0_sel:WORD_1
	v_exp_f16_sdwa v116, v112 dst_sel:WORD_1 dst_unused:UNUSED_PRESERVE src0_sel:WORD_1
	v_exp_f16_sdwa v117, v113 dst_sel:WORD_1 dst_unused:UNUSED_PRESERVE src0_sel:WORD_1
	v_pk_add_f16 v110, v213, v198 neg_lo:[0,1] neg_hi:[0,1]
	v_pk_add_f16 v101, v101, v114
	v_pk_add_f16 v98, v98, v117
	v_pk_add_f16 v99, v99, v116
	v_pk_add_f16 v100, v100, v115
	v_pk_fma_f16 v73, v65, v117, v73
	v_pk_fma_f16 v72, v64, v116, v72
	s_mov_b64 exec, s[70:71]
	buffer_load_dwordx4 v[138:141], v229, s[16:19], 0 offen offset:512
	buffer_load_dwordx4 v[90:93], v229, s[16:19], 0 offen offset:1024
	s_mov_b64 exec, -1
	v_pk_fma_f16 v71, v63, v115, v71
	v_pk_fma_f16 v70, v62, v114, v70
	v_pk_add_f16 v111, v212, v199 neg_lo:[0,1] neg_hi:[0,1]
	v_pk_add_f16 v112, v211, v200 neg_lo:[0,1] neg_hi:[0,1]
	v_pk_add_f16 v113, v210, v201 neg_lo:[0,1] neg_hi:[0,1]
	v_exp_f16_sdwa v114, v110 dst_sel:WORD_0 dst_unused:UNUSED_PAD src0_sel:WORD_0
	v_exp_f16_sdwa v115, v111 dst_sel:WORD_0 dst_unused:UNUSED_PAD src0_sel:WORD_0
	v_exp_f16_sdwa v116, v112 dst_sel:WORD_0 dst_unused:UNUSED_PAD src0_sel:WORD_0
	v_exp_f16_sdwa v117, v113 dst_sel:WORD_0 dst_unused:UNUSED_PAD src0_sel:WORD_0
	v_exp_f16_sdwa v114, v110 dst_sel:WORD_1 dst_unused:UNUSED_PRESERVE src0_sel:WORD_1
	v_exp_f16_sdwa v115, v111 dst_sel:WORD_1 dst_unused:UNUSED_PRESERVE src0_sel:WORD_1
	v_exp_f16_sdwa v116, v112 dst_sel:WORD_1 dst_unused:UNUSED_PRESERVE src0_sel:WORD_1
	v_exp_f16_sdwa v117, v113 dst_sel:WORD_1 dst_unused:UNUSED_PRESERVE src0_sel:WORD_1
	v_pk_add_f16 v110, v190, v198 neg_lo:[0,1] neg_hi:[0,1]
	v_pk_add_f16 v101, v101, v114
	v_pk_add_f16 v100, v100, v115
	v_pk_add_f16 v99, v99, v116
	v_pk_add_f16 v98, v98, v117
	v_pk_fma_f16 v70, v86, v114, v70
	v_pk_fma_f16 v71, v87, v115, v71
	v_pk_fma_f16 v72, v88, v116, v72
	v_pk_fma_f16 v73, v89, v117, v73
	s_mov_b64 exec, s[78:79]
	buffer_load_dwordx4 v[142:145], v229, s[16:19], 0 offen offset:2048
	buffer_load_dwordx4 v[2:5], v229, s[16:19], 0 offen offset:2560
	s_mov_b64 exec, -1
	v_pk_add_f16 v111, v191, v199 neg_lo:[0,1] neg_hi:[0,1]
	v_pk_add_f16 v112, v192, v200 neg_lo:[0,1] neg_hi:[0,1]
	v_pk_add_f16 v113, v193, v201 neg_lo:[0,1] neg_hi:[0,1]
	v_exp_f16_sdwa v114, v110 dst_sel:WORD_0 dst_unused:UNUSED_PAD src0_sel:WORD_0
	v_exp_f16_sdwa v115, v111 dst_sel:WORD_0 dst_unused:UNUSED_PAD src0_sel:WORD_0
	v_exp_f16_sdwa v116, v112 dst_sel:WORD_0 dst_unused:UNUSED_PAD src0_sel:WORD_0
	v_exp_f16_sdwa v117, v113 dst_sel:WORD_0 dst_unused:UNUSED_PAD src0_sel:WORD_0
	v_exp_f16_sdwa v114, v110 dst_sel:WORD_1 dst_unused:UNUSED_PRESERVE src0_sel:WORD_1
	v_exp_f16_sdwa v115, v111 dst_sel:WORD_1 dst_unused:UNUSED_PRESERVE src0_sel:WORD_1
	v_exp_f16_sdwa v116, v112 dst_sel:WORD_1 dst_unused:UNUSED_PRESERVE src0_sel:WORD_1
	v_exp_f16_sdwa v117, v113 dst_sel:WORD_1 dst_unused:UNUSED_PRESERVE src0_sel:WORD_1
	v_pk_add_f16 v110, v194, v198 neg_lo:[0,1] neg_hi:[0,1]
	v_pk_add_f16 v101, v101, v114
	v_pk_add_f16 v98, v98, v117
	v_pk_add_f16 v99, v99, v116
	v_pk_add_f16 v100, v100, v115
	v_pk_fma_f16 v73, v25, v117, v73
	v_pk_fma_f16 v72, v24, v116, v72
	v_pk_fma_f16 v71, v23, v115, v71
	v_pk_fma_f16 v70, v22, v114, v70
	v_pk_add_f16 v111, v195, v199 neg_lo:[0,1] neg_hi:[0,1]
	v_pk_add_f16 v112, v196, v200 neg_lo:[0,1] neg_hi:[0,1]
	v_pk_add_f16 v113, v197, v201 neg_lo:[0,1] neg_hi:[0,1]
	v_exp_f16_sdwa v114, v110 dst_sel:WORD_0 dst_unused:UNUSED_PAD src0_sel:WORD_0
	v_exp_f16_sdwa v115, v111 dst_sel:WORD_0 dst_unused:UNUSED_PAD src0_sel:WORD_0
	v_exp_f16_sdwa v116, v112 dst_sel:WORD_0 dst_unused:UNUSED_PAD src0_sel:WORD_0
	v_exp_f16_sdwa v117, v113 dst_sel:WORD_0 dst_unused:UNUSED_PAD src0_sel:WORD_0
	v_exp_f16_sdwa v114, v110 dst_sel:WORD_1 dst_unused:UNUSED_PRESERVE src0_sel:WORD_1
	v_exp_f16_sdwa v115, v111 dst_sel:WORD_1 dst_unused:UNUSED_PRESERVE src0_sel:WORD_1
	v_exp_f16_sdwa v116, v112 dst_sel:WORD_1 dst_unused:UNUSED_PRESERVE src0_sel:WORD_1
	v_exp_f16_sdwa v117, v113 dst_sel:WORD_1 dst_unused:UNUSED_PRESERVE src0_sel:WORD_1
	v_pk_add_f16 v110, v186, v198 neg_lo:[0,1] neg_hi:[0,1]
	v_pk_add_f16 v101, v101, v114
	v_pk_add_f16 v100, v100, v115
	v_pk_add_f16 v99, v99, v116
	v_pk_add_f16 v98, v98, v117
	v_pk_fma_f16 v70, v30, v114, v70
	v_pk_fma_f16 v71, v31, v115, v71
	v_pk_fma_f16 v72, v32, v116, v72
	v_pk_fma_f16 v73, v33, v117, v73
	v_pk_add_f16 v111, v187, v199 neg_lo:[0,1] neg_hi:[0,1]
	v_pk_add_f16 v112, v188, v200 neg_lo:[0,1] neg_hi:[0,1]
	v_pk_add_f16 v113, v189, v201 neg_lo:[0,1] neg_hi:[0,1]
	v_exp_f16_sdwa v114, v110 dst_sel:WORD_0 dst_unused:UNUSED_PAD src0_sel:WORD_0
	v_exp_f16_sdwa v115, v111 dst_sel:WORD_0 dst_unused:UNUSED_PAD src0_sel:WORD_0
	v_exp_f16_sdwa v116, v112 dst_sel:WORD_0 dst_unused:UNUSED_PAD src0_sel:WORD_0
	v_exp_f16_sdwa v117, v113 dst_sel:WORD_0 dst_unused:UNUSED_PAD src0_sel:WORD_0
	v_exp_f16_sdwa v114, v110 dst_sel:WORD_1 dst_unused:UNUSED_PRESERVE src0_sel:WORD_1
	v_exp_f16_sdwa v115, v111 dst_sel:WORD_1 dst_unused:UNUSED_PRESERVE src0_sel:WORD_1
	v_exp_f16_sdwa v116, v112 dst_sel:WORD_1 dst_unused:UNUSED_PRESERVE src0_sel:WORD_1
	v_exp_f16_sdwa v117, v113 dst_sel:WORD_1 dst_unused:UNUSED_PRESERVE src0_sel:WORD_1
	v_pk_add_f16 v101, v101, v114
	v_pk_add_f16 v100, v100, v115
	v_rcp_f16_e32 v110, v101
	v_rcp_f16_sdwa v101, v101 dst_sel:DWORD dst_unused:UNUSED_PAD src0_sel:WORD_1
	v_pk_add_f16 v99, v99, v116
	v_rcp_f16_e32 v111, v100
	v_rcp_f16_sdwa v100, v100 dst_sel:DWORD dst_unused:UNUSED_PAD src0_sel:WORD_1
	v_pk_add_f16 v98, v98, v117
	v_rcp_f16_e32 v112, v99
	v_rcp_f16_sdwa v99, v99 dst_sel:DWORD dst_unused:UNUSED_PAD src0_sel:WORD_1
	v_rcp_f16_e32 v113, v98
	v_rcp_f16_sdwa v98, v98 dst_sel:DWORD dst_unused:UNUSED_PAD src0_sel:WORD_1
	v_pk_fma_f16 v70, v46, v114, v70
	v_pack_b32_f16 v101, v110, v101
	v_pk_fma_f16 v71, v47, v115, v71
	v_pk_mul_f16 v110, v70, v101
	v_pack_b32_f16 v70, v111, v100
	v_pk_fma_f16 v72, v48, v116, v72
	v_pk_mul_f16 v111, v71, v70
	v_pack_b32_f16 v70, v112, v99
	v_pk_fma_f16 v73, v49, v117, v73
	v_pk_mul_f16 v112, v72, v70
	v_pack_b32_f16 v70, v113, v98
	v_pk_mul_f16 v113, v73, v70
	s_waitcnt vmcnt(12)
	v_pk_mul_f16 v70, v185, v154 op_sel_hi:[0,1]
	v_pk_mul_f16 v98, v183, v154 op_sel_hi:[0,1]
	v_pk_mul_f16 v114, v184, v154 op_sel_hi:[0,1]
	v_pk_mul_f16 v71, v185, v155 op_sel_hi:[0,1]
	v_pk_mul_f16 v72, v185, v156 op_sel_hi:[0,1]
	v_pk_mul_f16 v73, v185, v157 op_sel_hi:[0,1]
	v_pk_mul_f16 v99, v183, v155 op_sel_hi:[0,1]
	v_pk_mul_f16 v100, v183, v156 op_sel_hi:[0,1]
	v_pk_mul_f16 v101, v183, v157 op_sel_hi:[0,1]
	v_pk_mul_f16 v115, v184, v155 op_sel_hi:[0,1]
	v_pk_mul_f16 v116, v184, v156 op_sel_hi:[0,1]
	v_pk_mul_f16 v117, v184, v157 op_sel_hi:[0,1]
	v_pk_fma_f16 v82, v82, v154, v70
	v_pk_fma_f16 v106, v106, v154, v98
	v_pk_fma_f16 v122, v122, v154, v114
	v_pk_fma_f16 v129, v50, v154, v70
	v_pk_fma_f16 v137, v66, v154, v98
	v_pk_fma_f16 v189, v94, v154, v114
	v_pk_fma_f16 v70, v18, v154, v70
	v_pk_fma_f16 v98, v34, v154, v98
	v_pk_fma_f16 v114, v54, v154, v114
	v_pk_maximum3_f16 v154, v82, v106, v122
	v_pk_fma_f16 v85, v85, v157, v73
	v_pk_fma_f16 v84, v84, v156, v72
	v_pk_fma_f16 v83, v83, v155, v71
	v_pk_fma_f16 v109, v109, v157, v101
	v_pk_fma_f16 v108, v108, v156, v100
	v_pk_fma_f16 v107, v107, v155, v99
	v_pk_fma_f16 v125, v125, v157, v117
	v_pk_fma_f16 v124, v124, v156, v116
	v_pk_fma_f16 v123, v123, v155, v115
	v_pk_fma_f16 v126, v53, v157, v73
	v_pk_fma_f16 v127, v52, v156, v72
	v_pk_fma_f16 v128, v51, v155, v71
	v_pk_fma_f16 v134, v69, v157, v101
	v_pk_fma_f16 v135, v68, v156, v100
	v_pk_fma_f16 v136, v67, v155, v99
	v_pk_fma_f16 v186, v97, v157, v117
	v_pk_fma_f16 v187, v96, v156, v116
	v_pk_fma_f16 v188, v95, v155, v115
	v_pk_fma_f16 v73, v21, v157, v73
	v_pk_fma_f16 v72, v20, v156, v72
	v_pk_fma_f16 v71, v19, v155, v71
	v_pk_fma_f16 v101, v37, v157, v101
	v_pk_fma_f16 v100, v36, v156, v100
	v_pk_fma_f16 v99, v35, v155, v99
	v_pk_fma_f16 v117, v57, v157, v117
	v_pk_fma_f16 v116, v56, v156, v116
	v_pk_fma_f16 v115, v55, v155, v115
	v_pk_maximum3_f16 v155, v83, v107, v123
	v_pk_maximum3_f16 v156, v84, v108, v124
	v_pk_maximum3_f16 v157, v85, v109, v125
	v_pk_maximum3_f16 v190, v129, v137, v189
	v_pk_maximum3_f16 v194, v70, v98, v114
	v_pk_maximum3_f16 v191, v128, v136, v188
	v_pk_maximum3_f16 v192, v127, v135, v187
	v_pk_maximum3_f16 v193, v126, v134, v186
	v_pk_maximum3_f16 v195, v71, v99, v115
	v_pk_maximum3_f16 v196, v72, v100, v116
	v_pk_maximum3_f16 v154, v154, v190, v194
	v_pk_maximum3_f16 v197, v73, v101, v117
	v_pk_maximum3_f16 v155, v155, v191, v195
	v_pk_maximum3_f16 v156, v156, v192, v196
	v_pk_maximum3_f16 v157, v157, v193, v197
	v_pk_add_f16 v82, v82, v154 neg_lo:[0,1] neg_hi:[0,1]
	v_pk_add_f16 v83, v83, v155 neg_lo:[0,1] neg_hi:[0,1]
	v_pk_add_f16 v84, v84, v156 neg_lo:[0,1] neg_hi:[0,1]
	v_pk_add_f16 v85, v85, v157 neg_lo:[0,1] neg_hi:[0,1]
	v_pk_add_f16 v106, v106, v154 neg_lo:[0,1] neg_hi:[0,1]
	v_exp_f16_sdwa v190, v82 dst_sel:WORD_0 dst_unused:UNUSED_PAD src0_sel:WORD_0
	v_exp_f16_sdwa v191, v83 dst_sel:WORD_0 dst_unused:UNUSED_PAD src0_sel:WORD_0
	v_exp_f16_sdwa v192, v84 dst_sel:WORD_0 dst_unused:UNUSED_PAD src0_sel:WORD_0
	v_exp_f16_sdwa v193, v85 dst_sel:WORD_0 dst_unused:UNUSED_PAD src0_sel:WORD_0
	v_exp_f16_sdwa v190, v82 dst_sel:WORD_1 dst_unused:UNUSED_PRESERVE src0_sel:WORD_1
	v_exp_f16_sdwa v191, v83 dst_sel:WORD_1 dst_unused:UNUSED_PRESERVE src0_sel:WORD_1
	v_exp_f16_sdwa v192, v84 dst_sel:WORD_1 dst_unused:UNUSED_PRESERVE src0_sel:WORD_1
	v_exp_f16_sdwa v193, v85 dst_sel:WORD_1 dst_unused:UNUSED_PRESERVE src0_sel:WORD_1
	v_pk_add_f16 v107, v107, v155 neg_lo:[0,1] neg_hi:[0,1]
	v_pk_add_f16 v82, v193, 0
	v_pk_fma_f16 v42, v42, v190, 0
	v_pk_add_f16 v83, v192, 0
	v_pk_add_f16 v84, v191, 0
	v_pk_add_f16 v85, v190, 0
	v_pk_fma_f16 v45, v45, v193, 0
	v_pk_fma_f16 v44, v44, v192, 0
	v_pk_fma_f16 v43, v43, v191, 0
	v_pk_add_f16 v108, v108, v156 neg_lo:[0,1] neg_hi:[0,1]
	v_pk_add_f16 v109, v109, v157 neg_lo:[0,1] neg_hi:[0,1]
	v_pk_add_f16 v70, v70, v154 neg_lo:[0,1] neg_hi:[0,1]
	v_exp_f16_sdwa v190, v106 dst_sel:WORD_0 dst_unused:UNUSED_PAD src0_sel:WORD_0
	v_exp_f16_sdwa v191, v107 dst_sel:WORD_0 dst_unused:UNUSED_PAD src0_sel:WORD_0
	v_exp_f16_sdwa v192, v108 dst_sel:WORD_0 dst_unused:UNUSED_PAD src0_sel:WORD_0
	v_exp_f16_sdwa v193, v109 dst_sel:WORD_0 dst_unused:UNUSED_PAD src0_sel:WORD_0
	v_exp_f16_sdwa v190, v106 dst_sel:WORD_1 dst_unused:UNUSED_PRESERVE src0_sel:WORD_1
	v_exp_f16_sdwa v191, v107 dst_sel:WORD_1 dst_unused:UNUSED_PRESERVE src0_sel:WORD_1
	v_exp_f16_sdwa v192, v108 dst_sel:WORD_1 dst_unused:UNUSED_PRESERVE src0_sel:WORD_1
	v_exp_f16_sdwa v193, v109 dst_sel:WORD_1 dst_unused:UNUSED_PRESERVE src0_sel:WORD_1
	v_pk_add_f16 v71, v71, v155 neg_lo:[0,1] neg_hi:[0,1]
	v_pk_add_f16 v82, v82, v193
	v_pk_fma_f16 v42, v62, v190, v42
	v_pk_add_f16 v62, v122, v154 neg_lo:[0,1] neg_hi:[0,1]
	v_pk_add_f16 v85, v85, v190
	v_pk_add_f16 v84, v84, v191
	v_pk_add_f16 v83, v83, v192
	v_pk_fma_f16 v43, v63, v191, v43
	v_pk_fma_f16 v44, v64, v192, v44
	v_pk_fma_f16 v45, v65, v193, v45
	v_pk_add_f16 v63, v123, v155 neg_lo:[0,1] neg_hi:[0,1]
	v_pk_add_f16 v64, v124, v156 neg_lo:[0,1] neg_hi:[0,1]
	v_pk_add_f16 v65, v125, v157 neg_lo:[0,1] neg_hi:[0,1]
	v_pk_add_f16 v72, v72, v156 neg_lo:[0,1] neg_hi:[0,1]
	v_exp_f16_sdwa v106, v62 dst_sel:WORD_0 dst_unused:UNUSED_PAD src0_sel:WORD_0
	v_exp_f16_sdwa v107, v63 dst_sel:WORD_0 dst_unused:UNUSED_PAD src0_sel:WORD_0
	v_exp_f16_sdwa v108, v64 dst_sel:WORD_0 dst_unused:UNUSED_PAD src0_sel:WORD_0
	v_exp_f16_sdwa v109, v65 dst_sel:WORD_0 dst_unused:UNUSED_PAD src0_sel:WORD_0
	v_exp_f16_sdwa v106, v62 dst_sel:WORD_1 dst_unused:UNUSED_PRESERVE src0_sel:WORD_1
	v_exp_f16_sdwa v107, v63 dst_sel:WORD_1 dst_unused:UNUSED_PRESERVE src0_sel:WORD_1
	v_exp_f16_sdwa v108, v64 dst_sel:WORD_1 dst_unused:UNUSED_PRESERVE src0_sel:WORD_1
	v_exp_f16_sdwa v109, v65 dst_sel:WORD_1 dst_unused:UNUSED_PRESERVE src0_sel:WORD_1
	v_pk_add_f16 v73, v73, v157 neg_lo:[0,1] neg_hi:[0,1]
	v_pk_add_f16 v62, v82, v109
	v_pk_add_f16 v63, v83, v108
	v_pk_add_f16 v64, v84, v107
	v_pk_add_f16 v65, v85, v106
	v_pk_fma_f16 v45, v89, v109, v45
	v_pk_fma_f16 v44, v88, v108, v44
	v_pk_fma_f16 v43, v87, v107, v43
	v_pk_fma_f16 v42, v86, v106, v42
	v_pk_add_f16 v82, v129, v154 neg_lo:[0,1] neg_hi:[0,1]
	v_pk_add_f16 v83, v128, v155 neg_lo:[0,1] neg_hi:[0,1]
	v_pk_add_f16 v84, v127, v156 neg_lo:[0,1] neg_hi:[0,1]
	v_pk_add_f16 v85, v126, v157 neg_lo:[0,1] neg_hi:[0,1]
	v_exp_f16_sdwa v86, v82 dst_sel:WORD_0 dst_unused:UNUSED_PAD src0_sel:WORD_0
	v_exp_f16_sdwa v87, v83 dst_sel:WORD_0 dst_unused:UNUSED_PAD src0_sel:WORD_0
	v_exp_f16_sdwa v88, v84 dst_sel:WORD_0 dst_unused:UNUSED_PAD src0_sel:WORD_0
	v_exp_f16_sdwa v89, v85 dst_sel:WORD_0 dst_unused:UNUSED_PAD src0_sel:WORD_0
	v_exp_f16_sdwa v86, v82 dst_sel:WORD_1 dst_unused:UNUSED_PRESERVE src0_sel:WORD_1
	v_exp_f16_sdwa v87, v83 dst_sel:WORD_1 dst_unused:UNUSED_PRESERVE src0_sel:WORD_1
	v_exp_f16_sdwa v88, v84 dst_sel:WORD_1 dst_unused:UNUSED_PRESERVE src0_sel:WORD_1
	v_exp_f16_sdwa v89, v85 dst_sel:WORD_1 dst_unused:UNUSED_PRESERVE src0_sel:WORD_1
	v_pk_add_f16 v82, v137, v154 neg_lo:[0,1] neg_hi:[0,1]
	v_pk_add_f16 v62, v62, v89
	v_pk_add_f16 v65, v65, v86
	v_pk_add_f16 v64, v64, v87
	v_pk_add_f16 v63, v63, v88
	v_pk_fma_f16 v42, v22, v86, v42
	v_pk_fma_f16 v43, v23, v87, v43
	v_pk_fma_f16 v44, v24, v88, v44
	v_pk_fma_f16 v45, v25, v89, v45
	v_pk_add_f16 v83, v136, v155 neg_lo:[0,1] neg_hi:[0,1]
	v_pk_add_f16 v84, v135, v156 neg_lo:[0,1] neg_hi:[0,1]
	v_pk_add_f16 v85, v134, v157 neg_lo:[0,1] neg_hi:[0,1]
	v_exp_f16_sdwa v86, v82 dst_sel:WORD_0 dst_unused:UNUSED_PAD src0_sel:WORD_0
	v_exp_f16_sdwa v87, v83 dst_sel:WORD_0 dst_unused:UNUSED_PAD src0_sel:WORD_0
	v_exp_f16_sdwa v88, v84 dst_sel:WORD_0 dst_unused:UNUSED_PAD src0_sel:WORD_0
	v_exp_f16_sdwa v89, v85 dst_sel:WORD_0 dst_unused:UNUSED_PAD src0_sel:WORD_0
	v_exp_f16_sdwa v86, v82 dst_sel:WORD_1 dst_unused:UNUSED_PRESERVE src0_sel:WORD_1
	v_exp_f16_sdwa v87, v83 dst_sel:WORD_1 dst_unused:UNUSED_PRESERVE src0_sel:WORD_1
	v_exp_f16_sdwa v88, v84 dst_sel:WORD_1 dst_unused:UNUSED_PRESERVE src0_sel:WORD_1
	v_exp_f16_sdwa v89, v85 dst_sel:WORD_1 dst_unused:UNUSED_PRESERVE src0_sel:WORD_1
	v_pk_add_f16 v82, v189, v154 neg_lo:[0,1] neg_hi:[0,1]
	v_pk_add_f16 v62, v62, v89
	v_pk_add_f16 v63, v63, v88
	v_pk_add_f16 v64, v64, v87
	v_pk_add_f16 v65, v65, v86
	v_pk_fma_f16 v45, v33, v89, v45
	v_pk_fma_f16 v44, v32, v88, v44
	v_pk_fma_f16 v43, v31, v87, v43
	v_pk_fma_f16 v42, v30, v86, v42
	v_pk_add_f16 v83, v188, v155 neg_lo:[0,1] neg_hi:[0,1]
	v_pk_add_f16 v84, v187, v156 neg_lo:[0,1] neg_hi:[0,1]
	v_pk_add_f16 v85, v186, v157 neg_lo:[0,1] neg_hi:[0,1]
	v_exp_f16_sdwa v86, v82 dst_sel:WORD_0 dst_unused:UNUSED_PAD src0_sel:WORD_0
	v_exp_f16_sdwa v87, v83 dst_sel:WORD_0 dst_unused:UNUSED_PAD src0_sel:WORD_0
	v_exp_f16_sdwa v88, v84 dst_sel:WORD_0 dst_unused:UNUSED_PAD src0_sel:WORD_0
	v_exp_f16_sdwa v89, v85 dst_sel:WORD_0 dst_unused:UNUSED_PAD src0_sel:WORD_0
	v_exp_f16_sdwa v86, v82 dst_sel:WORD_1 dst_unused:UNUSED_PRESERVE src0_sel:WORD_1
	v_exp_f16_sdwa v87, v83 dst_sel:WORD_1 dst_unused:UNUSED_PRESERVE src0_sel:WORD_1
	v_exp_f16_sdwa v88, v84 dst_sel:WORD_1 dst_unused:UNUSED_PRESERVE src0_sel:WORD_1
	v_exp_f16_sdwa v89, v85 dst_sel:WORD_1 dst_unused:UNUSED_PRESERVE src0_sel:WORD_1
	v_exp_f16_sdwa v82, v70 dst_sel:WORD_0 dst_unused:UNUSED_PAD src0_sel:WORD_0
	v_exp_f16_sdwa v83, v71 dst_sel:WORD_0 dst_unused:UNUSED_PAD src0_sel:WORD_0
	v_exp_f16_sdwa v84, v72 dst_sel:WORD_0 dst_unused:UNUSED_PAD src0_sel:WORD_0
	v_exp_f16_sdwa v85, v73 dst_sel:WORD_0 dst_unused:UNUSED_PAD src0_sel:WORD_0
	v_exp_f16_sdwa v82, v70 dst_sel:WORD_1 dst_unused:UNUSED_PRESERVE src0_sel:WORD_1
	v_exp_f16_sdwa v83, v71 dst_sel:WORD_1 dst_unused:UNUSED_PRESERVE src0_sel:WORD_1
	v_exp_f16_sdwa v84, v72 dst_sel:WORD_1 dst_unused:UNUSED_PRESERVE src0_sel:WORD_1
	v_exp_f16_sdwa v85, v73 dst_sel:WORD_1 dst_unused:UNUSED_PRESERVE src0_sel:WORD_1
	v_pk_add_f16 v70, v98, v154 neg_lo:[0,1] neg_hi:[0,1]
	v_pk_add_f16 v62, v62, v89
	v_pk_add_f16 v65, v65, v86
	v_pk_add_f16 v64, v64, v87
	v_pk_add_f16 v63, v63, v88
	v_pk_fma_f16 v42, v46, v86, v42
	v_pk_fma_f16 v43, v47, v87, v43
	v_pk_fma_f16 v44, v48, v88, v44
	v_pk_fma_f16 v45, v49, v89, v45
	v_pk_add_f16 v62, v62, v85
	v_pk_add_f16 v63, v63, v84
	v_pk_add_f16 v64, v64, v83
	v_pk_add_f16 v65, v65, v82
	v_pk_fma_f16 v45, v9, v85, v45
	v_pk_fma_f16 v44, v8, v84, v44
	v_pk_fma_f16 v43, v7, v83, v43
	v_pk_fma_f16 v42, v6, v82, v42
	v_pk_add_f16 v71, v99, v155 neg_lo:[0,1] neg_hi:[0,1]
	v_pk_add_f16 v72, v100, v156 neg_lo:[0,1] neg_hi:[0,1]
	v_pk_add_f16 v73, v101, v157 neg_lo:[0,1] neg_hi:[0,1]
	v_exp_f16_sdwa v82, v70 dst_sel:WORD_0 dst_unused:UNUSED_PAD src0_sel:WORD_0
	v_exp_f16_sdwa v83, v71 dst_sel:WORD_0 dst_unused:UNUSED_PAD src0_sel:WORD_0
	v_exp_f16_sdwa v84, v72 dst_sel:WORD_0 dst_unused:UNUSED_PAD src0_sel:WORD_0
	v_exp_f16_sdwa v85, v73 dst_sel:WORD_0 dst_unused:UNUSED_PAD src0_sel:WORD_0
	v_exp_f16_sdwa v82, v70 dst_sel:WORD_1 dst_unused:UNUSED_PRESERVE src0_sel:WORD_1
	v_exp_f16_sdwa v83, v71 dst_sel:WORD_1 dst_unused:UNUSED_PRESERVE src0_sel:WORD_1
	v_exp_f16_sdwa v84, v72 dst_sel:WORD_1 dst_unused:UNUSED_PRESERVE src0_sel:WORD_1
	v_exp_f16_sdwa v85, v73 dst_sel:WORD_1 dst_unused:UNUSED_PRESERVE src0_sel:WORD_1
	v_pk_add_f16 v70, v114, v154 neg_lo:[0,1] neg_hi:[0,1]
	v_pk_add_f16 v62, v62, v85
	v_pk_add_f16 v65, v65, v82
	v_pk_add_f16 v64, v64, v83
	v_pk_add_f16 v63, v63, v84
	v_pk_fma_f16 v42, v10, v82, v42
	v_pk_fma_f16 v43, v11, v83, v43
	v_pk_fma_f16 v44, v12, v84, v44
	v_pk_fma_f16 v45, v13, v85, v45
	v_pk_add_f16 v71, v115, v155 neg_lo:[0,1] neg_hi:[0,1]
	v_pk_add_f16 v72, v116, v156 neg_lo:[0,1] neg_hi:[0,1]
	v_pk_add_f16 v73, v117, v157 neg_lo:[0,1] neg_hi:[0,1]
	v_exp_f16_sdwa v82, v70 dst_sel:WORD_0 dst_unused:UNUSED_PAD src0_sel:WORD_0
	v_exp_f16_sdwa v83, v71 dst_sel:WORD_0 dst_unused:UNUSED_PAD src0_sel:WORD_0
	v_exp_f16_sdwa v84, v72 dst_sel:WORD_0 dst_unused:UNUSED_PAD src0_sel:WORD_0
	v_exp_f16_sdwa v85, v73 dst_sel:WORD_0 dst_unused:UNUSED_PAD src0_sel:WORD_0
	v_exp_f16_sdwa v82, v70 dst_sel:WORD_1 dst_unused:UNUSED_PRESERVE src0_sel:WORD_1
	v_exp_f16_sdwa v83, v71 dst_sel:WORD_1 dst_unused:UNUSED_PRESERVE src0_sel:WORD_1
	v_exp_f16_sdwa v84, v72 dst_sel:WORD_1 dst_unused:UNUSED_PRESERVE src0_sel:WORD_1
	v_exp_f16_sdwa v85, v73 dst_sel:WORD_1 dst_unused:UNUSED_PRESERVE src0_sel:WORD_1
	s_nop 0
	v_pk_add_f16 v62, v62, v85
	v_pk_add_f16 v63, v63, v84
	v_pk_add_f16 v64, v64, v83
	v_pk_add_f16 v65, v65, v82
	v_rcp_f16_e32 v73, v62
	v_rcp_f16_sdwa v62, v62 dst_sel:DWORD dst_unused:UNUSED_PAD src0_sel:WORD_1
	v_rcp_f16_e32 v70, v65
	v_rcp_f16_sdwa v65, v65 dst_sel:DWORD dst_unused:UNUSED_PAD src0_sel:WORD_1
	v_rcp_f16_e32 v71, v64
	v_rcp_f16_sdwa v64, v64 dst_sel:DWORD dst_unused:UNUSED_PAD src0_sel:WORD_1
	v_rcp_f16_e32 v72, v63
	v_rcp_f16_sdwa v63, v63 dst_sel:DWORD dst_unused:UNUSED_PAD src0_sel:WORD_1
	v_pk_fma_f16 v45, v17, v85, v45
	v_pack_b32_f16 v62, v73, v62
	v_pk_fma_f16 v44, v16, v84, v44
	v_pk_fma_f16 v43, v15, v83, v43
	v_pk_fma_f16 v42, v14, v82, v42
	v_pack_b32_f16 v65, v70, v65
	v_pack_b32_f16 v64, v71, v64
	v_pack_b32_f16 v63, v72, v63
	v_pk_mul_f16 v45, v45, v62
	s_waitcnt vmcnt(6)
	v_pk_mul_f16 v62, v185, v150 op_sel_hi:[0,1]
	v_pk_mul_f16 v70, v183, v150 op_sel_hi:[0,1]
	v_pk_mul_f16 v82, v184, v150 op_sel_hi:[0,1]
	v_pk_mul_f16 v42, v42, v65
	v_pk_mul_f16 v43, v43, v64
	v_pk_mul_f16 v44, v44, v63
	v_pk_mul_f16 v63, v185, v151 op_sel_hi:[0,1]
	v_pk_mul_f16 v64, v185, v152 op_sel_hi:[0,1]
	v_pk_mul_f16 v65, v185, v153 op_sel_hi:[0,1]
	v_pk_mul_f16 v71, v183, v151 op_sel_hi:[0,1]
	v_pk_mul_f16 v72, v183, v152 op_sel_hi:[0,1]
	v_pk_mul_f16 v73, v183, v153 op_sel_hi:[0,1]
	v_pk_mul_f16 v83, v184, v151 op_sel_hi:[0,1]
	v_pk_mul_f16 v84, v184, v152 op_sel_hi:[0,1]
	v_pk_mul_f16 v85, v184, v153 op_sel_hi:[0,1]
	v_pk_fma_f16 v50, v50, v150, v62
	v_pk_fma_f16 v66, v66, v150, v70
	v_pk_fma_f16 v89, v94, v150, v82
	v_pk_fma_f16 v53, v53, v153, v65
	v_pk_maximum3_f16 v114, v50, v66, v89
	v_pk_fma_f16 v52, v52, v152, v64
	v_pk_fma_f16 v51, v51, v151, v63
	v_pk_fma_f16 v69, v69, v153, v73
	v_pk_fma_f16 v68, v68, v152, v72
	v_pk_fma_f16 v67, v67, v151, v71
	v_pk_fma_f16 v86, v97, v153, v85
	v_pk_fma_f16 v87, v96, v152, v84
	v_pk_fma_f16 v88, v95, v151, v83
	v_pk_fma_f16 v97, v18, v150, v62
	v_pk_fma_f16 v101, v34, v150, v70
	v_pk_fma_f16 v109, v54, v150, v82
	v_pk_fma_f16 v62, v74, v150, v62
	v_pk_fma_f16 v70, v102, v150, v70
	v_pk_fma_f16 v82, v118, v150, v82
	v_pk_maximum3_f16 v115, v51, v67, v88
	v_pk_maximum3_f16 v116, v52, v68, v87
	v_pk_maximum3_f16 v117, v53, v69, v86
	v_pk_maximum3_f16 v122, v97, v101, v109
	v_pk_fma_f16 v94, v21, v153, v65
	v_pk_maximum3_f16 v126, v62, v70, v82
	v_pk_fma_f16 v95, v20, v152, v64
	v_pk_maximum3_f16 v114, v114, v122, v126
	v_pk_fma_f16 v96, v19, v151, v63
	v_pk_fma_f16 v98, v37, v153, v73
	v_pk_fma_f16 v99, v36, v152, v72
	v_pk_fma_f16 v100, v35, v151, v71
	v_pk_fma_f16 v106, v57, v153, v85
	v_pk_fma_f16 v107, v56, v152, v84
	v_pk_fma_f16 v108, v55, v151, v83
	v_pk_fma_f16 v65, v77, v153, v65
	v_pk_fma_f16 v64, v76, v152, v64
	v_pk_fma_f16 v63, v75, v151, v63
	v_pk_fma_f16 v73, v105, v153, v73
	v_pk_fma_f16 v72, v104, v152, v72
	v_pk_fma_f16 v71, v103, v151, v71
	v_pk_fma_f16 v85, v121, v153, v85
	v_pk_fma_f16 v84, v120, v152, v84
	v_pk_fma_f16 v83, v119, v151, v83
	v_pk_maximum3_f16 v123, v96, v100, v108
	v_pk_maximum3_f16 v124, v95, v99, v107
	v_pk_maximum3_f16 v125, v94, v98, v106
	v_pk_maximum3_f16 v128, v64, v72, v84
	v_pk_maximum3_f16 v129, v65, v73, v85
	v_pk_maximum3_f16 v127, v63, v71, v83
	v_pk_maximum3_f16 v115, v115, v123, v127
	v_pk_maximum3_f16 v116, v116, v124, v128
	v_pk_maximum3_f16 v117, v117, v125, v129
	v_pk_add_f16 v50, v50, v114 neg_lo:[0,1] neg_hi:[0,1]
	v_pk_add_f16 v51, v51, v115 neg_lo:[0,1] neg_hi:[0,1]
	v_pk_add_f16 v52, v52, v116 neg_lo:[0,1] neg_hi:[0,1]
	v_pk_add_f16 v53, v53, v117 neg_lo:[0,1] neg_hi:[0,1]
	v_pk_add_f16 v66, v66, v114 neg_lo:[0,1] neg_hi:[0,1]
	v_exp_f16_sdwa v122, v50 dst_sel:WORD_0 dst_unused:UNUSED_PAD src0_sel:WORD_0
	v_exp_f16_sdwa v123, v51 dst_sel:WORD_0 dst_unused:UNUSED_PAD src0_sel:WORD_0
	v_exp_f16_sdwa v124, v52 dst_sel:WORD_0 dst_unused:UNUSED_PAD src0_sel:WORD_0
	v_exp_f16_sdwa v125, v53 dst_sel:WORD_0 dst_unused:UNUSED_PAD src0_sel:WORD_0
	v_exp_f16_sdwa v122, v50 dst_sel:WORD_1 dst_unused:UNUSED_PRESERVE src0_sel:WORD_1
	v_exp_f16_sdwa v123, v51 dst_sel:WORD_1 dst_unused:UNUSED_PRESERVE src0_sel:WORD_1
	v_exp_f16_sdwa v124, v52 dst_sel:WORD_1 dst_unused:UNUSED_PRESERVE src0_sel:WORD_1
	v_exp_f16_sdwa v125, v53 dst_sel:WORD_1 dst_unused:UNUSED_PRESERVE src0_sel:WORD_1
	v_pk_add_f16 v67, v67, v115 neg_lo:[0,1] neg_hi:[0,1]
	v_pk_add_f16 v50, v125, 0
	v_pk_fma_f16 v22, v22, v122, 0
	v_pk_add_f16 v51, v124, 0
	v_pk_add_f16 v52, v123, 0
	v_pk_add_f16 v53, v122, 0
	v_pk_fma_f16 v23, v23, v123, 0
	v_pk_fma_f16 v24, v24, v124, 0
	v_pk_fma_f16 v25, v25, v125, 0
	v_pk_add_f16 v68, v68, v116 neg_lo:[0,1] neg_hi:[0,1]
	v_pk_add_f16 v69, v69, v117 neg_lo:[0,1] neg_hi:[0,1]
	v_exp_f16_sdwa v122, v66 dst_sel:WORD_0 dst_unused:UNUSED_PAD src0_sel:WORD_0
	v_exp_f16_sdwa v123, v67 dst_sel:WORD_0 dst_unused:UNUSED_PAD src0_sel:WORD_0
	v_exp_f16_sdwa v124, v68 dst_sel:WORD_0 dst_unused:UNUSED_PAD src0_sel:WORD_0
	v_exp_f16_sdwa v125, v69 dst_sel:WORD_0 dst_unused:UNUSED_PAD src0_sel:WORD_0
	v_exp_f16_sdwa v122, v66 dst_sel:WORD_1 dst_unused:UNUSED_PRESERVE src0_sel:WORD_1
	v_exp_f16_sdwa v123, v67 dst_sel:WORD_1 dst_unused:UNUSED_PRESERVE src0_sel:WORD_1
	v_exp_f16_sdwa v124, v68 dst_sel:WORD_1 dst_unused:UNUSED_PRESERVE src0_sel:WORD_1
	v_exp_f16_sdwa v125, v69 dst_sel:WORD_1 dst_unused:UNUSED_PRESERVE src0_sel:WORD_1
	s_nop 0
	v_pk_add_f16 v50, v50, v125
	v_pk_fma_f16 v22, v30, v122, v22
	v_pk_add_f16 v30, v89, v114 neg_lo:[0,1] neg_hi:[0,1]
	v_pk_add_f16 v53, v53, v122
	v_pk_add_f16 v52, v52, v123
	v_pk_add_f16 v51, v51, v124
	v_pk_fma_f16 v25, v33, v125, v25
	v_pk_fma_f16 v24, v32, v124, v24
	v_pk_fma_f16 v23, v31, v123, v23
	v_pk_add_f16 v31, v88, v115 neg_lo:[0,1] neg_hi:[0,1]
	v_pk_add_f16 v32, v87, v116 neg_lo:[0,1] neg_hi:[0,1]
	v_pk_add_f16 v33, v86, v117 neg_lo:[0,1] neg_hi:[0,1]
	v_exp_f16_sdwa v66, v30 dst_sel:WORD_0 dst_unused:UNUSED_PAD src0_sel:WORD_0
	v_exp_f16_sdwa v67, v31 dst_sel:WORD_0 dst_unused:UNUSED_PAD src0_sel:WORD_0
	v_exp_f16_sdwa v68, v32 dst_sel:WORD_0 dst_unused:UNUSED_PAD src0_sel:WORD_0
	v_exp_f16_sdwa v69, v33 dst_sel:WORD_0 dst_unused:UNUSED_PAD src0_sel:WORD_0
	v_exp_f16_sdwa v66, v30 dst_sel:WORD_1 dst_unused:UNUSED_PRESERVE src0_sel:WORD_1
	v_exp_f16_sdwa v67, v31 dst_sel:WORD_1 dst_unused:UNUSED_PRESERVE src0_sel:WORD_1
	v_exp_f16_sdwa v68, v32 dst_sel:WORD_1 dst_unused:UNUSED_PRESERVE src0_sel:WORD_1
	v_exp_f16_sdwa v69, v33 dst_sel:WORD_1 dst_unused:UNUSED_PRESERVE src0_sel:WORD_1
	s_nop 0
	v_pk_add_f16 v30, v50, v69
	v_pk_add_f16 v31, v51, v68
	v_pk_add_f16 v32, v52, v67
	v_pk_add_f16 v33, v53, v66
	v_pk_fma_f16 v22, v46, v66, v22
	v_pk_fma_f16 v23, v47, v67, v23
	v_pk_fma_f16 v24, v48, v68, v24
	v_pk_fma_f16 v25, v49, v69, v25
	v_pk_add_f16 v46, v97, v114 neg_lo:[0,1] neg_hi:[0,1]
	v_pk_add_f16 v47, v96, v115 neg_lo:[0,1] neg_hi:[0,1]
	v_pk_add_f16 v48, v95, v116 neg_lo:[0,1] neg_hi:[0,1]
	v_pk_add_f16 v49, v94, v117 neg_lo:[0,1] neg_hi:[0,1]
	v_exp_f16_sdwa v50, v46 dst_sel:WORD_0 dst_unused:UNUSED_PAD src0_sel:WORD_0
	v_exp_f16_sdwa v51, v47 dst_sel:WORD_0 dst_unused:UNUSED_PAD src0_sel:WORD_0
	v_exp_f16_sdwa v52, v48 dst_sel:WORD_0 dst_unused:UNUSED_PAD src0_sel:WORD_0
	v_exp_f16_sdwa v53, v49 dst_sel:WORD_0 dst_unused:UNUSED_PAD src0_sel:WORD_0
	v_exp_f16_sdwa v50, v46 dst_sel:WORD_1 dst_unused:UNUSED_PRESERVE src0_sel:WORD_1
	v_exp_f16_sdwa v51, v47 dst_sel:WORD_1 dst_unused:UNUSED_PRESERVE src0_sel:WORD_1
	v_exp_f16_sdwa v52, v48 dst_sel:WORD_1 dst_unused:UNUSED_PRESERVE src0_sel:WORD_1
	v_exp_f16_sdwa v53, v49 dst_sel:WORD_1 dst_unused:UNUSED_PRESERVE src0_sel:WORD_1
	v_pk_add_f16 v46, v101, v114 neg_lo:[0,1] neg_hi:[0,1]
	v_pk_add_f16 v30, v30, v53
	v_pk_add_f16 v33, v33, v50
	v_pk_add_f16 v32, v32, v51
	v_pk_add_f16 v31, v31, v52
	v_pk_fma_f16 v25, v9, v53, v25
	v_pk_fma_f16 v24, v8, v52, v24
	v_pk_fma_f16 v23, v7, v51, v23
	v_pk_fma_f16 v22, v6, v50, v22
	v_pk_add_f16 v47, v100, v115 neg_lo:[0,1] neg_hi:[0,1]
	v_pk_add_f16 v48, v99, v116 neg_lo:[0,1] neg_hi:[0,1]
	v_pk_add_f16 v49, v98, v117 neg_lo:[0,1] neg_hi:[0,1]
	v_exp_f16_sdwa v50, v46 dst_sel:WORD_0 dst_unused:UNUSED_PAD src0_sel:WORD_0
	v_exp_f16_sdwa v51, v47 dst_sel:WORD_0 dst_unused:UNUSED_PAD src0_sel:WORD_0
	v_exp_f16_sdwa v52, v48 dst_sel:WORD_0 dst_unused:UNUSED_PAD src0_sel:WORD_0
	v_exp_f16_sdwa v53, v49 dst_sel:WORD_0 dst_unused:UNUSED_PAD src0_sel:WORD_0
	v_exp_f16_sdwa v50, v46 dst_sel:WORD_1 dst_unused:UNUSED_PRESERVE src0_sel:WORD_1
	v_exp_f16_sdwa v51, v47 dst_sel:WORD_1 dst_unused:UNUSED_PRESERVE src0_sel:WORD_1
	v_exp_f16_sdwa v52, v48 dst_sel:WORD_1 dst_unused:UNUSED_PRESERVE src0_sel:WORD_1
	v_exp_f16_sdwa v53, v49 dst_sel:WORD_1 dst_unused:UNUSED_PRESERVE src0_sel:WORD_1
	v_pk_add_f16 v46, v109, v114 neg_lo:[0,1] neg_hi:[0,1]
	v_pk_add_f16 v30, v30, v53
	v_pk_add_f16 v31, v31, v52
	v_pk_add_f16 v32, v32, v51
	v_pk_add_f16 v33, v33, v50
	v_pk_fma_f16 v22, v10, v50, v22
	v_pk_fma_f16 v23, v11, v51, v23
	v_pk_fma_f16 v24, v12, v52, v24
	v_pk_fma_f16 v25, v13, v53, v25
	v_pk_add_f16 v47, v108, v115 neg_lo:[0,1] neg_hi:[0,1]
	v_pk_add_f16 v48, v107, v116 neg_lo:[0,1] neg_hi:[0,1]
	v_pk_add_f16 v49, v106, v117 neg_lo:[0,1] neg_hi:[0,1]
	v_exp_f16_sdwa v50, v46 dst_sel:WORD_0 dst_unused:UNUSED_PAD src0_sel:WORD_0
	v_exp_f16_sdwa v51, v47 dst_sel:WORD_0 dst_unused:UNUSED_PAD src0_sel:WORD_0
	v_exp_f16_sdwa v52, v48 dst_sel:WORD_0 dst_unused:UNUSED_PAD src0_sel:WORD_0
	v_exp_f16_sdwa v53, v49 dst_sel:WORD_0 dst_unused:UNUSED_PAD src0_sel:WORD_0
	v_exp_f16_sdwa v50, v46 dst_sel:WORD_1 dst_unused:UNUSED_PRESERVE src0_sel:WORD_1
	v_exp_f16_sdwa v51, v47 dst_sel:WORD_1 dst_unused:UNUSED_PRESERVE src0_sel:WORD_1
	v_exp_f16_sdwa v52, v48 dst_sel:WORD_1 dst_unused:UNUSED_PRESERVE src0_sel:WORD_1
	v_exp_f16_sdwa v53, v49 dst_sel:WORD_1 dst_unused:UNUSED_PRESERVE src0_sel:WORD_1
	v_pk_add_f16 v46, v62, v114 neg_lo:[0,1] neg_hi:[0,1]
	v_pk_add_f16 v30, v30, v53
	v_pk_add_f16 v33, v33, v50
	v_pk_add_f16 v32, v32, v51
	v_pk_add_f16 v31, v31, v52
	v_pk_fma_f16 v25, v17, v53, v25
	v_pk_fma_f16 v24, v16, v52, v24
	v_pk_fma_f16 v23, v15, v51, v23
	v_pk_fma_f16 v22, v14, v50, v22
	v_pk_add_f16 v47, v63, v115 neg_lo:[0,1] neg_hi:[0,1]
	v_pk_add_f16 v48, v64, v116 neg_lo:[0,1] neg_hi:[0,1]
	v_pk_add_f16 v49, v65, v117 neg_lo:[0,1] neg_hi:[0,1]
	v_exp_f16_sdwa v50, v46 dst_sel:WORD_0 dst_unused:UNUSED_PAD src0_sel:WORD_0
	v_exp_f16_sdwa v51, v47 dst_sel:WORD_0 dst_unused:UNUSED_PAD src0_sel:WORD_0
	v_exp_f16_sdwa v52, v48 dst_sel:WORD_0 dst_unused:UNUSED_PAD src0_sel:WORD_0
	v_exp_f16_sdwa v53, v49 dst_sel:WORD_0 dst_unused:UNUSED_PAD src0_sel:WORD_0
	v_exp_f16_sdwa v50, v46 dst_sel:WORD_1 dst_unused:UNUSED_PRESERVE src0_sel:WORD_1
	v_exp_f16_sdwa v51, v47 dst_sel:WORD_1 dst_unused:UNUSED_PRESERVE src0_sel:WORD_1
	v_exp_f16_sdwa v52, v48 dst_sel:WORD_1 dst_unused:UNUSED_PRESERVE src0_sel:WORD_1
	v_exp_f16_sdwa v53, v49 dst_sel:WORD_1 dst_unused:UNUSED_PRESERVE src0_sel:WORD_1
	v_pk_add_f16 v46, v70, v114 neg_lo:[0,1] neg_hi:[0,1]
	v_pk_add_f16 v30, v30, v53
	v_pk_add_f16 v31, v31, v52
	v_pk_add_f16 v32, v32, v51
	v_pk_add_f16 v33, v33, v50
	v_pk_fma_f16 v22, v26, v50, v22
	v_pk_fma_f16 v23, v27, v51, v23
	v_pk_fma_f16 v24, v28, v52, v24
	v_pk_fma_f16 v25, v29, v53, v25
	v_pk_add_f16 v47, v71, v115 neg_lo:[0,1] neg_hi:[0,1]
	v_pk_add_f16 v48, v72, v116 neg_lo:[0,1] neg_hi:[0,1]
	v_pk_add_f16 v49, v73, v117 neg_lo:[0,1] neg_hi:[0,1]
	v_exp_f16_sdwa v50, v46 dst_sel:WORD_0 dst_unused:UNUSED_PAD src0_sel:WORD_0
	v_exp_f16_sdwa v51, v47 dst_sel:WORD_0 dst_unused:UNUSED_PAD src0_sel:WORD_0
	v_exp_f16_sdwa v52, v48 dst_sel:WORD_0 dst_unused:UNUSED_PAD src0_sel:WORD_0
	v_exp_f16_sdwa v53, v49 dst_sel:WORD_0 dst_unused:UNUSED_PAD src0_sel:WORD_0
	v_exp_f16_sdwa v50, v46 dst_sel:WORD_1 dst_unused:UNUSED_PRESERVE src0_sel:WORD_1
	v_exp_f16_sdwa v51, v47 dst_sel:WORD_1 dst_unused:UNUSED_PRESERVE src0_sel:WORD_1
	v_exp_f16_sdwa v52, v48 dst_sel:WORD_1 dst_unused:UNUSED_PRESERVE src0_sel:WORD_1
	v_exp_f16_sdwa v53, v49 dst_sel:WORD_1 dst_unused:UNUSED_PRESERVE src0_sel:WORD_1
	v_pk_add_f16 v46, v82, v114 neg_lo:[0,1] neg_hi:[0,1]
	v_pk_add_f16 v30, v30, v53
	v_pk_add_f16 v33, v33, v50
	v_pk_add_f16 v32, v32, v51
	v_pk_add_f16 v31, v31, v52
	v_pk_fma_f16 v25, v41, v53, v25
	v_pk_fma_f16 v24, v40, v52, v24
	v_pk_fma_f16 v23, v39, v51, v23
	v_pk_fma_f16 v22, v38, v50, v22
	v_pk_add_f16 v47, v83, v115 neg_lo:[0,1] neg_hi:[0,1]
	v_pk_add_f16 v48, v84, v116 neg_lo:[0,1] neg_hi:[0,1]
	v_pk_add_f16 v49, v85, v117 neg_lo:[0,1] neg_hi:[0,1]
	v_exp_f16_sdwa v50, v46 dst_sel:WORD_0 dst_unused:UNUSED_PAD src0_sel:WORD_0
	v_exp_f16_sdwa v51, v47 dst_sel:WORD_0 dst_unused:UNUSED_PAD src0_sel:WORD_0
	v_exp_f16_sdwa v52, v48 dst_sel:WORD_0 dst_unused:UNUSED_PAD src0_sel:WORD_0
	v_exp_f16_sdwa v53, v49 dst_sel:WORD_0 dst_unused:UNUSED_PAD src0_sel:WORD_0
	v_exp_f16_sdwa v50, v46 dst_sel:WORD_1 dst_unused:UNUSED_PRESERVE src0_sel:WORD_1
	v_exp_f16_sdwa v51, v47 dst_sel:WORD_1 dst_unused:UNUSED_PRESERVE src0_sel:WORD_1
	v_exp_f16_sdwa v52, v48 dst_sel:WORD_1 dst_unused:UNUSED_PRESERVE src0_sel:WORD_1
	v_exp_f16_sdwa v53, v49 dst_sel:WORD_1 dst_unused:UNUSED_PRESERVE src0_sel:WORD_1
	s_nop 0
	v_pk_add_f16 v30, v30, v53
	v_pk_add_f16 v31, v31, v52
	v_rcp_f16_e32 v48, v30
	v_rcp_f16_sdwa v30, v30 dst_sel:DWORD dst_unused:UNUSED_PAD src0_sel:WORD_1
	v_pk_add_f16 v32, v32, v51
	v_rcp_f16_e32 v49, v31
	v_rcp_f16_sdwa v31, v31 dst_sel:DWORD dst_unused:UNUSED_PAD src0_sel:WORD_1
	v_pk_add_f16 v33, v33, v50
	v_rcp_f16_e32 v47, v32
	v_rcp_f16_sdwa v32, v32 dst_sel:DWORD dst_unused:UNUSED_PAD src0_sel:WORD_1
	v_rcp_f16_e32 v46, v33
	v_rcp_f16_sdwa v33, v33 dst_sel:DWORD dst_unused:UNUSED_PAD src0_sel:WORD_1
	v_pk_fma_f16 v25, v61, v53, v25
	v_pack_b32_f16 v30, v48, v30
	v_pk_fma_f16 v24, v60, v52, v24
	v_pk_mul_f16 v25, v25, v30
	v_pack_b32_f16 v30, v49, v31
	v_pk_fma_f16 v23, v59, v51, v23
	v_pk_mul_f16 v24, v24, v30
	v_pack_b32_f16 v30, v47, v32
	v_pk_fma_f16 v22, v58, v50, v22
	v_pk_mul_f16 v23, v23, v30
	v_pack_b32_f16 v30, v46, v33
	v_pk_mul_f16 v22, v22, v30
	s_waitcnt vmcnt(0)
	s_cmp_lg_u32 s14, 1
	s_cbranch_scc1 .Lmywd5_0
	s_mul_i32 s84, s81, s83
	s_add_i32 s84, s84, s82
	s_mul_i32 s84, s84, 0x60000
	s_mul_i32 s85, s94, 0x6000
	s_add_u32 s84, s84, s85
	s_add_u32 s88, s86, s84
	s_addc_u32 s89, s87, 0
	v_mbcnt_lo_u32_b32 v251, -1, 0
	v_mbcnt_hi_u32_b32 v251, -1, v251
	v_lshlrev_b32_e32 v251, 4, v251
	global_load_dwordx4 v[252:255], v251, s[88:89]
	global_load_dwordx4 v[252:255], v251, s[88:89] offset:1024
	global_load_dwordx4 v[252:255], v251, s[88:89] offset:2048
	global_load_dwordx4 v[252:255], v251, s[88:89] offset:3072
	s_add_u32 s88, s88, 0x1000
	s_addc_u32 s89, s89, 0
	global_load_dwordx4 v[252:255], v251, s[88:89]
	global_load_dwordx4 v[252:255], v251, s[88:89] offset:1024
	global_load_dwordx4 v[252:255], v251, s[88:89] offset:2048
	global_load_dwordx4 v[252:255], v251, s[88:89] offset:3072
	s_add_u32 s88, s88, 0x1000
	s_addc_u32 s89, s89, 0
	global_load_dwordx4 v[252:255], v251, s[88:89]
	global_load_dwordx4 v[252:255], v251, s[88:89] offset:1024
	global_load_dwordx4 v[252:255], v251, s[88:89] offset:2048
	global_load_dwordx4 v[252:255], v251, s[88:89] offset:3072
.Lmywd5_0:
	v_pk_mul_f16 v30, v185, v146 op_sel_hi:[0,1]
	v_pk_mul_f16 v31, v185, v147 op_sel_hi:[0,1]
	v_pk_mul_f16 v32, v185, v148 op_sel_hi:[0,1]
	v_pk_mul_f16 v33, v185, v149 op_sel_hi:[0,1]
	v_pk_mul_f16 v46, v183, v146 op_sel_hi:[0,1]
	v_pk_mul_f16 v47, v183, v147 op_sel_hi:[0,1]
	v_pk_mul_f16 v48, v183, v148 op_sel_hi:[0,1]
	v_pk_mul_f16 v49, v183, v149 op_sel_hi:[0,1]
	v_pk_mul_f16 v50, v184, v146 op_sel_hi:[0,1]
	v_pk_mul_f16 v51, v184, v147 op_sel_hi:[0,1]
	v_pk_mul_f16 v52, v184, v148 op_sel_hi:[0,1]
	v_pk_mul_f16 v53, v184, v149 op_sel_hi:[0,1]
	v_pk_fma_f16 v21, v21, v149, v33
	v_pk_fma_f16 v20, v20, v148, v32
	v_pk_fma_f16 v19, v19, v147, v31
	v_pk_fma_f16 v18, v18, v146, v30
	v_pk_fma_f16 v37, v37, v149, v49
	v_pk_fma_f16 v36, v36, v148, v48
	v_pk_fma_f16 v35, v35, v147, v47
	v_pk_fma_f16 v34, v34, v146, v46
	v_pk_fma_f16 v57, v57, v149, v53
	v_pk_fma_f16 v56, v56, v148, v52
	v_pk_fma_f16 v55, v55, v147, v51
	v_pk_fma_f16 v54, v54, v146, v50
	v_pk_fma_f16 v62, v77, v149, v33
	v_pk_fma_f16 v63, v76, v148, v32
	v_pk_fma_f16 v64, v75, v147, v31
	v_pk_fma_f16 v65, v74, v146, v30
	v_pk_maximum3_f16 v74, v18, v34, v54
	v_pk_maximum3_f16 v75, v19, v35, v55
	v_pk_maximum3_f16 v76, v20, v36, v56
	v_pk_maximum3_f16 v77, v21, v37, v57
	v_pk_fma_f16 v66, v105, v149, v49
	v_pk_fma_f16 v67, v104, v148, v48
	v_pk_fma_f16 v68, v103, v147, v47
	v_pk_fma_f16 v69, v102, v146, v46
	v_pk_fma_f16 v70, v121, v149, v53
	v_pk_fma_f16 v71, v120, v148, v52
	v_pk_fma_f16 v72, v119, v147, v51
	v_pk_fma_f16 v73, v118, v146, v50
	v_pk_fma_f16 v33, v133, v149, v33
	v_pk_fma_f16 v32, v132, v148, v32
	v_pk_fma_f16 v31, v131, v147, v31
	v_pk_fma_f16 v30, v130, v146, v30
	v_pk_fma_f16 v49, v141, v149, v49
	v_pk_fma_f16 v48, v140, v148, v48
	v_pk_fma_f16 v47, v139, v147, v47
	v_pk_fma_f16 v46, v138, v146, v46
	v_pk_fma_f16 v53, v145, v149, v53
	v_pk_fma_f16 v52, v144, v148, v52
	v_pk_fma_f16 v51, v143, v147, v51
	v_pk_fma_f16 v50, v142, v146, v50
	v_pk_maximum3_f16 v82, v65, v69, v73
	v_pk_maximum3_f16 v83, v64, v68, v72
	v_pk_maximum3_f16 v84, v63, v67, v71
	v_pk_maximum3_f16 v85, v62, v66, v70
	v_pk_maximum3_f16 v87, v31, v47, v51
	v_pk_maximum3_f16 v86, v30, v46, v50
	v_pk_maximum3_f16 v88, v32, v48, v52
	v_pk_maximum3_f16 v89, v33, v49, v53
	v_pk_maximum3_f16 v74, v74, v82, v86
	v_pk_maximum3_f16 v75, v75, v83, v87
	v_pk_maximum3_f16 v76, v76, v84, v88
	v_pk_maximum3_f16 v77, v77, v85, v89
	s_nop 0
	v_pk_add_f16 v18, v18, v74 neg_lo:[0,1] neg_hi:[0,1]
	v_pk_add_f16 v19, v19, v75 neg_lo:[0,1] neg_hi:[0,1]
	v_pk_add_f16 v20, v20, v76 neg_lo:[0,1] neg_hi:[0,1]
	v_pk_add_f16 v21, v21, v77 neg_lo:[0,1] neg_hi:[0,1]
	v_pk_add_f16 v34, v34, v74 neg_lo:[0,1] neg_hi:[0,1]
	v_exp_f16_sdwa v82, v18 dst_sel:WORD_0 dst_unused:UNUSED_PAD src0_sel:WORD_0
	v_exp_f16_sdwa v83, v19 dst_sel:WORD_0 dst_unused:UNUSED_PAD src0_sel:WORD_0
	v_exp_f16_sdwa v84, v20 dst_sel:WORD_0 dst_unused:UNUSED_PAD src0_sel:WORD_0
	v_exp_f16_sdwa v85, v21 dst_sel:WORD_0 dst_unused:UNUSED_PAD src0_sel:WORD_0
	v_exp_f16_sdwa v82, v18 dst_sel:WORD_1 dst_unused:UNUSED_PRESERVE src0_sel:WORD_1
	v_exp_f16_sdwa v83, v19 dst_sel:WORD_1 dst_unused:UNUSED_PRESERVE src0_sel:WORD_1
	v_exp_f16_sdwa v84, v20 dst_sel:WORD_1 dst_unused:UNUSED_PRESERVE src0_sel:WORD_1
	v_exp_f16_sdwa v85, v21 dst_sel:WORD_1 dst_unused:UNUSED_PRESERVE src0_sel:WORD_1
	v_pk_add_f16 v35, v35, v75 neg_lo:[0,1] neg_hi:[0,1]
	v_pk_add_f16 v18, v82, 0
	v_pk_add_f16 v19, v83, 0
	v_pk_add_f16 v20, v84, 0
	v_pk_add_f16 v21, v85, 0
	v_pk_fma_f16 v6, v6, v82, 0
	v_pk_fma_f16 v7, v7, v83, 0
	v_pk_fma_f16 v8, v8, v84, 0
	v_pk_fma_f16 v9, v9, v85, 0
	v_pk_add_f16 v36, v36, v76 neg_lo:[0,1] neg_hi:[0,1]
	v_pk_add_f16 v37, v37, v77 neg_lo:[0,1] neg_hi:[0,1]
	v_exp_f16_sdwa v82, v34 dst_sel:WORD_0 dst_unused:UNUSED_PAD src0_sel:WORD_0
	v_exp_f16_sdwa v83, v35 dst_sel:WORD_0 dst_unused:UNUSED_PAD src0_sel:WORD_0
	v_exp_f16_sdwa v84, v36 dst_sel:WORD_0 dst_unused:UNUSED_PAD src0_sel:WORD_0
	v_exp_f16_sdwa v85, v37 dst_sel:WORD_0 dst_unused:UNUSED_PAD src0_sel:WORD_0
	v_exp_f16_sdwa v82, v34 dst_sel:WORD_1 dst_unused:UNUSED_PRESERVE src0_sel:WORD_1
	v_exp_f16_sdwa v83, v35 dst_sel:WORD_1 dst_unused:UNUSED_PRESERVE src0_sel:WORD_1
	v_exp_f16_sdwa v84, v36 dst_sel:WORD_1 dst_unused:UNUSED_PRESERVE src0_sel:WORD_1
	v_exp_f16_sdwa v85, v37 dst_sel:WORD_1 dst_unused:UNUSED_PRESERVE src0_sel:WORD_1
	s_nop 0
	v_pk_add_f16 v21, v21, v85
	v_pk_add_f16 v20, v20, v84
	v_pk_add_f16 v19, v19, v83
	v_pk_add_f16 v18, v18, v82
	v_pk_fma_f16 v9, v13, v85, v9
	v_pk_fma_f16 v8, v12, v84, v8
	v_pk_fma_f16 v7, v11, v83, v7
	v_pk_fma_f16 v6, v10, v82, v6
	v_pk_add_f16 v10, v54, v74 neg_lo:[0,1] neg_hi:[0,1]
	v_pk_add_f16 v11, v55, v75 neg_lo:[0,1] neg_hi:[0,1]
	v_pk_add_f16 v12, v56, v76 neg_lo:[0,1] neg_hi:[0,1]
	v_pk_add_f16 v13, v57, v77 neg_lo:[0,1] neg_hi:[0,1]
	v_exp_f16_sdwa v34, v10 dst_sel:WORD_0 dst_unused:UNUSED_PAD src0_sel:WORD_0
	v_exp_f16_sdwa v35, v11 dst_sel:WORD_0 dst_unused:UNUSED_PAD src0_sel:WORD_0
	v_exp_f16_sdwa v36, v12 dst_sel:WORD_0 dst_unused:UNUSED_PAD src0_sel:WORD_0
	v_exp_f16_sdwa v37, v13 dst_sel:WORD_0 dst_unused:UNUSED_PAD src0_sel:WORD_0
	v_exp_f16_sdwa v34, v10 dst_sel:WORD_1 dst_unused:UNUSED_PRESERVE src0_sel:WORD_1
	v_exp_f16_sdwa v35, v11 dst_sel:WORD_1 dst_unused:UNUSED_PRESERVE src0_sel:WORD_1
	v_exp_f16_sdwa v36, v12 dst_sel:WORD_1 dst_unused:UNUSED_PRESERVE src0_sel:WORD_1
	v_exp_f16_sdwa v37, v13 dst_sel:WORD_1 dst_unused:UNUSED_PRESERVE src0_sel:WORD_1
	v_pk_add_f16 v10, v18, v34
	v_pk_add_f16 v11, v19, v35
	v_pk_add_f16 v12, v20, v36
	v_pk_add_f16 v13, v21, v37
	v_pk_fma_f16 v6, v14, v34, v6
	v_pk_fma_f16 v7, v15, v35, v7
	v_pk_fma_f16 v8, v16, v36, v8
	v_pk_fma_f16 v9, v17, v37, v9
	v_pk_add_f16 v14, v65, v74 neg_lo:[0,1] neg_hi:[0,1]
	v_pk_add_f16 v15, v64, v75 neg_lo:[0,1] neg_hi:[0,1]
	v_pk_add_f16 v16, v63, v76 neg_lo:[0,1] neg_hi:[0,1]
	v_pk_add_f16 v17, v62, v77 neg_lo:[0,1] neg_hi:[0,1]
	v_exp_f16_sdwa v18, v14 dst_sel:WORD_0 dst_unused:UNUSED_PAD src0_sel:WORD_0
	v_exp_f16_sdwa v19, v15 dst_sel:WORD_0 dst_unused:UNUSED_PAD src0_sel:WORD_0
	v_exp_f16_sdwa v20, v16 dst_sel:WORD_0 dst_unused:UNUSED_PAD src0_sel:WORD_0
	v_exp_f16_sdwa v21, v17 dst_sel:WORD_0 dst_unused:UNUSED_PAD src0_sel:WORD_0
	v_exp_f16_sdwa v18, v14 dst_sel:WORD_1 dst_unused:UNUSED_PRESERVE src0_sel:WORD_1
	v_exp_f16_sdwa v19, v15 dst_sel:WORD_1 dst_unused:UNUSED_PRESERVE src0_sel:WORD_1
	v_exp_f16_sdwa v20, v16 dst_sel:WORD_1 dst_unused:UNUSED_PRESERVE src0_sel:WORD_1
	v_exp_f16_sdwa v21, v17 dst_sel:WORD_1 dst_unused:UNUSED_PRESERVE src0_sel:WORD_1
	v_pk_add_f16 v14, v69, v74 neg_lo:[0,1] neg_hi:[0,1]
	v_pk_add_f16 v13, v13, v21
	v_pk_add_f16 v12, v12, v20
	v_pk_add_f16 v11, v11, v19
	v_pk_add_f16 v10, v10, v18
	v_pk_fma_f16 v9, v29, v21, v9
	v_pk_fma_f16 v8, v28, v20, v8
	v_pk_fma_f16 v7, v27, v19, v7
	v_pk_fma_f16 v6, v26, v18, v6
	v_pk_add_f16 v15, v68, v75 neg_lo:[0,1] neg_hi:[0,1]
	v_pk_add_f16 v16, v67, v76 neg_lo:[0,1] neg_hi:[0,1]
	v_pk_add_f16 v17, v66, v77 neg_lo:[0,1] neg_hi:[0,1]
	v_exp_f16_sdwa v18, v14 dst_sel:WORD_0 dst_unused:UNUSED_PAD src0_sel:WORD_0
	v_exp_f16_sdwa v19, v15 dst_sel:WORD_0 dst_unused:UNUSED_PAD src0_sel:WORD_0
	v_exp_f16_sdwa v20, v16 dst_sel:WORD_0 dst_unused:UNUSED_PAD src0_sel:WORD_0
	v_exp_f16_sdwa v21, v17 dst_sel:WORD_0 dst_unused:UNUSED_PAD src0_sel:WORD_0
	v_exp_f16_sdwa v18, v14 dst_sel:WORD_1 dst_unused:UNUSED_PRESERVE src0_sel:WORD_1
	v_exp_f16_sdwa v19, v15 dst_sel:WORD_1 dst_unused:UNUSED_PRESERVE src0_sel:WORD_1
	v_exp_f16_sdwa v20, v16 dst_sel:WORD_1 dst_unused:UNUSED_PRESERVE src0_sel:WORD_1
	v_exp_f16_sdwa v21, v17 dst_sel:WORD_1 dst_unused:UNUSED_PRESERVE src0_sel:WORD_1
	v_pk_add_f16 v14, v73, v74 neg_lo:[0,1] neg_hi:[0,1]
	v_pk_add_f16 v10, v10, v18
	v_pk_add_f16 v11, v11, v19
	v_pk_add_f16 v12, v12, v20
	v_pk_add_f16 v13, v13, v21
	v_pk_fma_f16 v6, v38, v18, v6
	v_pk_fma_f16 v7, v39, v19, v7
	v_pk_fma_f16 v8, v40, v20, v8
	v_pk_fma_f16 v9, v41, v21, v9
	v_pk_add_f16 v15, v72, v75 neg_lo:[0,1] neg_hi:[0,1]
	v_pk_add_f16 v16, v71, v76 neg_lo:[0,1] neg_hi:[0,1]
	v_pk_add_f16 v17, v70, v77 neg_lo:[0,1] neg_hi:[0,1]
	v_exp_f16_sdwa v18, v14 dst_sel:WORD_0 dst_unused:UNUSED_PAD src0_sel:WORD_0
	v_exp_f16_sdwa v19, v15 dst_sel:WORD_0 dst_unused:UNUSED_PAD src0_sel:WORD_0
	v_exp_f16_sdwa v20, v16 dst_sel:WORD_0 dst_unused:UNUSED_PAD src0_sel:WORD_0
	v_exp_f16_sdwa v21, v17 dst_sel:WORD_0 dst_unused:UNUSED_PAD src0_sel:WORD_0
	v_exp_f16_sdwa v18, v14 dst_sel:WORD_1 dst_unused:UNUSED_PRESERVE src0_sel:WORD_1
	v_exp_f16_sdwa v19, v15 dst_sel:WORD_1 dst_unused:UNUSED_PRESERVE src0_sel:WORD_1
	v_exp_f16_sdwa v20, v16 dst_sel:WORD_1 dst_unused:UNUSED_PRESERVE src0_sel:WORD_1
	v_exp_f16_sdwa v21, v17 dst_sel:WORD_1 dst_unused:UNUSED_PRESERVE src0_sel:WORD_1
	v_pk_add_f16 v14, v30, v74 neg_lo:[0,1] neg_hi:[0,1]
	v_pk_add_f16 v13, v13, v21
	v_pk_add_f16 v12, v12, v20
	v_pk_add_f16 v11, v11, v19
	v_pk_add_f16 v10, v10, v18
	v_pk_fma_f16 v9, v61, v21, v9
	v_pk_fma_f16 v8, v60, v20, v8
	v_pk_fma_f16 v7, v59, v19, v7
	v_pk_fma_f16 v6, v58, v18, v6
	v_pk_add_f16 v15, v31, v75 neg_lo:[0,1] neg_hi:[0,1]
	v_pk_add_f16 v16, v32, v76 neg_lo:[0,1] neg_hi:[0,1]
	v_pk_add_f16 v17, v33, v77 neg_lo:[0,1] neg_hi:[0,1]
	v_exp_f16_sdwa v18, v14 dst_sel:WORD_0 dst_unused:UNUSED_PAD src0_sel:WORD_0
	v_exp_f16_sdwa v19, v15 dst_sel:WORD_0 dst_unused:UNUSED_PAD src0_sel:WORD_0
	v_exp_f16_sdwa v20, v16 dst_sel:WORD_0 dst_unused:UNUSED_PAD src0_sel:WORD_0
	v_exp_f16_sdwa v21, v17 dst_sel:WORD_0 dst_unused:UNUSED_PAD src0_sel:WORD_0
	v_exp_f16_sdwa v18, v14 dst_sel:WORD_1 dst_unused:UNUSED_PRESERVE src0_sel:WORD_1
	v_exp_f16_sdwa v19, v15 dst_sel:WORD_1 dst_unused:UNUSED_PRESERVE src0_sel:WORD_1
	v_exp_f16_sdwa v20, v16 dst_sel:WORD_1 dst_unused:UNUSED_PRESERVE src0_sel:WORD_1
	v_exp_f16_sdwa v21, v17 dst_sel:WORD_1 dst_unused:UNUSED_PRESERVE src0_sel:WORD_1
	v_pk_add_f16 v10, v10, v18
	v_pk_add_f16 v11, v11, v19
	v_pk_add_f16 v12, v12, v20
	v_pk_add_f16 v13, v13, v21
	v_pk_fma_f16 v14, v78, v18, v6
	v_pk_fma_f16 v15, v79, v19, v7
	v_pk_fma_f16 v16, v80, v20, v8
	v_pk_fma_f16 v17, v81, v21, v9
	v_pk_add_f16 v6, v46, v74 neg_lo:[0,1] neg_hi:[0,1]
	v_pk_add_f16 v7, v47, v75 neg_lo:[0,1] neg_hi:[0,1]
	v_pk_add_f16 v8, v48, v76 neg_lo:[0,1] neg_hi:[0,1]
	v_pk_add_f16 v9, v49, v77 neg_lo:[0,1] neg_hi:[0,1]
	v_exp_f16_sdwa v18, v6 dst_sel:WORD_0 dst_unused:UNUSED_PAD src0_sel:WORD_0
	v_exp_f16_sdwa v19, v7 dst_sel:WORD_0 dst_unused:UNUSED_PAD src0_sel:WORD_0
	v_exp_f16_sdwa v20, v8 dst_sel:WORD_0 dst_unused:UNUSED_PAD src0_sel:WORD_0
	v_exp_f16_sdwa v21, v9 dst_sel:WORD_0 dst_unused:UNUSED_PAD src0_sel:WORD_0
	v_exp_f16_sdwa v18, v6 dst_sel:WORD_1 dst_unused:UNUSED_PRESERVE src0_sel:WORD_1
	v_exp_f16_sdwa v19, v7 dst_sel:WORD_1 dst_unused:UNUSED_PRESERVE src0_sel:WORD_1
	v_exp_f16_sdwa v20, v8 dst_sel:WORD_1 dst_unused:UNUSED_PRESERVE src0_sel:WORD_1
	v_exp_f16_sdwa v21, v9 dst_sel:WORD_1 dst_unused:UNUSED_PRESERVE src0_sel:WORD_1
	s_nop 0
	v_pk_add_f16 v9, v13, v21
	v_pk_add_f16 v8, v12, v20
	v_pk_add_f16 v7, v11, v19
	v_pk_add_f16 v6, v10, v18
	v_pk_fma_f16 v13, v93, v21, v17
	v_pk_fma_f16 v12, v92, v20, v16
	v_pk_fma_f16 v11, v91, v19, v15
	v_pk_fma_f16 v10, v90, v18, v14
	v_pk_add_f16 v18, v50, v74 neg_lo:[0,1] neg_hi:[0,1]
	v_pk_add_f16 v19, v51, v75 neg_lo:[0,1] neg_hi:[0,1]
	v_pk_add_f16 v20, v52, v76 neg_lo:[0,1] neg_hi:[0,1]
	v_pk_add_f16 v21, v53, v77 neg_lo:[0,1] neg_hi:[0,1]
	v_exp_f16_sdwa v14, v18 dst_sel:WORD_0 dst_unused:UNUSED_PAD src0_sel:WORD_0
	v_exp_f16_sdwa v17, v19 dst_sel:WORD_0 dst_unused:UNUSED_PAD src0_sel:WORD_0
	v_exp_f16_sdwa v15, v20 dst_sel:WORD_0 dst_unused:UNUSED_PAD src0_sel:WORD_0
	v_exp_f16_sdwa v16, v21 dst_sel:WORD_0 dst_unused:UNUSED_PAD src0_sel:WORD_0
	v_exp_f16_sdwa v14, v18 dst_sel:WORD_1 dst_unused:UNUSED_PRESERVE src0_sel:WORD_1
	v_exp_f16_sdwa v17, v19 dst_sel:WORD_1 dst_unused:UNUSED_PRESERVE src0_sel:WORD_1
	v_exp_f16_sdwa v15, v20 dst_sel:WORD_1 dst_unused:UNUSED_PRESERVE src0_sel:WORD_1
	v_exp_f16_sdwa v16, v21 dst_sel:WORD_1 dst_unused:UNUSED_PRESERVE src0_sel:WORD_1
	s_nop 0

amdhsa.kernels:
  - .agpr_count:     0
    .args:
      - .actual_access:  read_only
        .address_space:  global
        .offset:         0
        .size:           8
        .value_kind:     global_buffer
      - .actual_access:  read_only
        .address_space:  global
        .offset:         8
        .size:           8
        .value_kind:     global_buffer
      - .actual_access:  read_only
        .address_space:  global
        .offset:         16
        .size:           8
        .value_kind:     global_buffer
      - .actual_access:  read_only
        .address_space:  global
        .offset:         24
        .size:           8
        .value_kind:     global_buffer
      - .actual_access:  read_only
        .address_space:  global
        .offset:         32
        .size:           8
        .value_kind:     global_buffer
      - .actual_access:  read_only
        .address_space:  global
        .offset:         40
        .size:           8
        .value_kind:     global_buffer
      - .actual_access:  read_only
        .address_space:  global
        .offset:         48
        .size:           8
        .value_kind:     global_buffer
      - .actual_access:  read_only
        .address_space:  global
        .offset:         56
        .size:           8
        .value_kind:     global_buffer
      - .actual_access:  write_only
        .address_space:  global
        .offset:         64
        .size:           8
        .value_kind:     global_buffer
      - .actual_access:  write_only
        .address_space:  global
        .offset:         72
        .size:           8
        .value_kind:     global_buffer
      - .actual_access:  write_only
        .address_space:  global
        .offset:         80
        .size:           8
        .value_kind:     global_buffer
      - .actual_access:  write_only
        .address_space:  global
        .offset:         88
        .size:           8
        .value_kind:     global_buffer
    .group_segment_fixed_size: 0
    .kernarg_segment_align: 8
    .kernarg_segment_size: 96
    .language:       OpenCL C
    .language_version:
      - 2
      - 0
    .max_flat_workgroup_size: 256
    .name:           _Z8k_prep_wPKfS0_S0_S0_S0_S0_S0_S0_PDF16_PfS1_S1_
    .private_segment_fixed_size: 0
    .sgpr_count:     23
    .sgpr_spill_count: 0
    .symbol:         _Z8k_prep_wPKfS0_S0_S0_S0_S0_S0_S0_PDF16_PfS1_S1_.kd
    .uniform_work_group_size: 1
    .uses_dynamic_stack: false
    .vgpr_count:     15
    .vgpr_spill_count: 0
    .wavefront_size: 64
  - .agpr_count:     0
    .args:
      - .actual_access:  read_only
        .address_space:  global
        .offset:         0
        .size:           8
        .value_kind:     global_buffer
      - .actual_access:  read_only
        .address_space:  global
        .offset:         8
        .size:           8
        .value_kind:     global_buffer
      - .actual_access:  read_only
        .address_space:  global
        .offset:         16
        .size:           8
        .value_kind:     global_buffer
      - .actual_access:  read_only
        .address_space:  global
        .offset:         24
        .size:           8
        .value_kind:     global_buffer
      - .actual_access:  write_only
        .address_space:  global
        .offset:         32
        .size:           8
        .value_kind:     global_buffer
      - .actual_access:  read_only
        .address_space:  global
        .offset:         40
        .size:           8
        .value_kind:     global_buffer
      - .actual_access:  read_only
        .address_space:  global
        .offset:         48
        .size:           8
        .value_kind:     global_buffer
      - .actual_access:  write_only
        .address_space:  global
        .offset:         56
        .size:           8
        .value_kind:     global_buffer
      - .offset:         64
        .size:           4
        .value_kind:     by_value
      - .offset:         68
        .size:           4
        .value_kind:     by_value
    .group_segment_fixed_size: 115712
    .kernarg_segment_align: 8
    .kernarg_segment_size: 72
    .language:       OpenCL C
    .language_version:
      - 2
      - 0
    .max_flat_workgroup_size: 512
    .name:           _Z8k_stageAPKfS0_S0_S0_PDF16_PKDF16_S0_S1_ii
    .private_segment_fixed_size: 0
    .sgpr_count:     28
    .sgpr_spill_count: 0
    .symbol:         _Z8k_stageAPKfS0_S0_S0_PDF16_PKDF16_S0_S1_ii.kd
    .uniform_work_group_size: 1
    .uses_dynamic_stack: false
    .vgpr_count:     251
    .vgpr_spill_count: 0
    .wavefront_size: 64
  - .agpr_count:     112
    .args:
      - .actual_access:  read_only
        .address_space:  global
        .offset:         0
        .size:           8
        .value_kind:     global_buffer
      - .actual_access:  read_only
        .address_space:  global
        .offset:         8
        .size:           8
        .value_kind:     global_buffer
      - .actual_access:  read_only
        .address_space:  global
        .offset:         16
        .size:           8
        .value_kind:     global_buffer
      - .actual_access:  read_only
        .address_space:  global
        .offset:         24
        .size:           8
        .value_kind:     global_buffer
      - .actual_access:  read_only
        .address_space:  global
        .offset:         32
        .size:           8
        .value_kind:     global_buffer
      - .actual_access:  write_only
        .address_space:  global
        .offset:         40
        .size:           8
        .value_kind:     global_buffer
    .group_segment_fixed_size: 107712
    .kernarg_segment_align: 8
    .kernarg_segment_size: 48
    .language:       OpenCL C
    .language_version:
      - 2
      - 0
    .max_flat_workgroup_size: 256
    .name:           _Z7k_conv4PKDF16_S0_S0_PKfS2_Pf
    .private_segment_fixed_size: 0
    .sgpr_count:     36
    .sgpr_spill_count: 0
    .symbol:         _Z7k_conv4PKDF16_S0_S0_PKfS2_Pf.kd
    .uniform_work_group_size: 1
    .uses_dynamic_stack: false
    .vgpr_count:     328
    .vgpr_spill_count: 0
    .wavefront_size: 64
  - .agpr_count:     0
    .args:
      - .offset:         0
        .size:           112
        .value_kind:     by_value
      - .actual_access:  read_only
        .address_space:  global
        .offset:         112
        .size:           8
        .value_kind:     global_buffer
      - .actual_access:  read_only
        .address_space:  global
        .offset:         120
        .size:           8
        .value_kind:     global_buffer
      - .actual_access:  write_only
        .address_space:  global
        .offset:         128
        .size:           8
        .value_kind:     global_buffer
      - .offset:         136
        .size:           4
        .value_kind:     by_value
      - .offset:         140
        .size:           4
        .value_kind:     by_value
      - .offset:         144
        .size:           4
        .value_kind:     by_value
    .group_segment_fixed_size: 115712
    .kernarg_segment_align: 8
    .kernarg_segment_size: 148
    .language:       OpenCL C
    .language_version:
      - 2
      - 0
    .max_flat_workgroup_size: 512
    .name:           _Z7k_stageILi0ELi8EEv8AttnArgsPKDF16_PKfPDF16_iii
    .private_segment_fixed_size: 0
    .sgpr_count:     41
    .sgpr_spill_count: 0
    .symbol:         _Z7k_stageILi0ELi8EEv8AttnArgsPKDF16_PKfPDF16_iii.kd
    .uniform_work_group_size: 1
    .uses_dynamic_stack: false
    .vgpr_count:     256
    .vgpr_spill_count: 0
    .wavefront_size: 64
  - .agpr_count:     0
    .args:
      - .offset:         0
        .size:           112
        .value_kind:     by_value
      - .actual_access:  read_only
        .address_space:  global
        .offset:         112
        .size:           8
        .value_kind:     global_buffer
      - .actual_access:  read_only
        .address_space:  global
        .offset:         120
        .size:           8
        .value_kind:     global_buffer
      - .actual_access:  write_only
        .address_space:  global
        .offset:         128
        .size:           8
        .value_kind:     global_buffer
      - .offset:         136
        .size:           4
        .value_kind:     by_value
      - .offset:         140
        .size:           4
        .value_kind:     by_value
      - .offset:         144
        .size:           4
        .value_kind:     by_value
    .group_segment_fixed_size: 82944
    .kernarg_segment_align: 8
    .kernarg_segment_size: 148
    .language:       OpenCL C
    .language_version:
      - 2
      - 0
    .max_flat_workgroup_size: 512
    .name:           _Z7k_stageILi1ELi4EEv8AttnArgsPKDF16_PKfPDF16_iii
    .private_segment_fixed_size: 0
    .sgpr_count:     55
    .sgpr_spill_count: 0
    .symbol:         _Z7k_stageILi1ELi4EEv8AttnArgsPKDF16_PKfPDF16_iii.kd
    .uniform_work_group_size: 1
    .uses_dynamic_stack: false
    .vgpr_count:     256
    .vgpr_spill_count: 0
    .wavefront_size: 64
  - .agpr_count:     0
    .args:
      - .offset:         0
        .size:           112
        .value_kind:     by_value
      - .actual_access:  read_only
        .address_space:  global
        .offset:         112
        .size:           8
        .value_kind:     global_buffer
      - .actual_access:  read_only
        .address_space:  global
        .offset:         120
        .size:           8
        .value_kind:     global_buffer
      - .actual_access:  write_only
        .address_space:  global
        .offset:         128
        .size:           8
        .value_kind:     global_buffer
      - .offset:         136
        .size:           4
        .value_kind:     by_value
      - .offset:         140
        .size:           4
        .value_kind:     by_value
      - .offset:         144
        .size:           4
        .value_kind:     by_value
    .group_segment_fixed_size: 82944
    .kernarg_segment_align: 8
    .kernarg_segment_size: 148
    .language:       OpenCL C
    .language_version:
      - 2
      - 0
    .max_flat_workgroup_size: 512
    .name:           _Z7k_stageILi0ELi4EEv8AttnArgsPKDF16_PKfPDF16_iii
    .private_segment_fixed_size: 0
    .sgpr_count:     38
    .sgpr_spill_count: 0
    .symbol:         _Z7k_stageILi0ELi4EEv8AttnArgsPKDF16_PKfPDF16_iii.kd
    .uniform_work_group_size: 1
    .uses_dynamic_stack: false
    .vgpr_count:     256
    .vgpr_spill_count: 0
    .wavefront_size: 64
  - .agpr_count:     0
    .args:
      - .offset:         0
        .size:           112
        .value_kind:     by_value
    .group_segment_fixed_size: 0
    .kernarg_segment_align: 8
    .kernarg_segment_size: 112
    .language:       OpenCL C
    .language_version:
      - 2
      - 0
    .max_flat_workgroup_size: 512
    .name:           _Z7k_attn2ILi2EEv8AttnArgs
    .private_segment_fixed_size: 0
    .sgpr_count:     102
    .sgpr_spill_count: 0
    .symbol:         _Z7k_attn2ILi2EEv8AttnArgs.kd
    .uniform_work_group_size: 1
    .uses_dynamic_stack: false
    .vgpr_count:     252
    .vgpr_spill_count: 0
    .wavefront_size: 64
